# v56 + cache policy: in-phase weight conversion f32 loads marked nt (stores unchanged)
# speedup vs baseline: 1.0097x; 1.0049x over previous
; #define GAS __attribute__((address_space(1)))
; #define LAS __attribute__((address_space(3)))
; #define LDS_WAIT() asm volatile("s_waitcnt lgkmcnt(0)" ::: "memory")
; __device__ __forceinline__ unsigned pk2(float lo, float hi) { unsigned r; asm("v_cvt_pk_bf16_f32 %0, %1, %2" : "=v"(r) : "v"(lo), "v"(hi)); return r; }
; __device__ __forceinline__ void transpose_item(const float* W, int K, int N, bf16* WT, int drow0, int kb, int n0, LAS float* scr, int lane) {
;     const int k0 = 64 * kb; const int c4 = 4 * (lane & 7); const bool ok = (n0 + c4) < N;
;     f32x4 v[8];
; #pragma unroll
;     for (int i = 0; i < 8; ++i) { const int kk = 8 * i + (lane >> 3); v[i] = ok ? *(const f32x4*)(W + (size_t)(k0 + kk) * N + n0 + c4) : (f32x4){0.f, 0.f, 0.f, 0.f}; }
; #pragma unroll
;     for (int i = 0; i < 8; ++i) { const int kk = 8 * i + (lane >> 3); LAS float* d = scr + kk * 33 + c4; d[0] = v[i][0]; d[1] = v[i][1]; d[2] = v[i][2]; d[3] = v[i][3]; }
;     LDS_WAIT(); asm volatile("" ::: "memory");
;     const int c = lane & 7;
; #pragma unroll
;     for (int j = 0; j < 4; ++j) { const int n = (lane >> 3) + 8 * j; const LAS float* s = scr + (8 * c) * 33 + n;
;         v4u o; o.x = pk2(s[0 * 33], s[1 * 33]); o.y = pk2(s[2 * 33], s[3 * 33]); o.z = pk2(s[4 * 33], s[5 * 33]); o.w = pk2(s[6 * 33], s[7 * 33]);
;         *(GAS v4u*)(WT + (size_t)(drow0 + n) * K + k0 + 8 * c) = o; }
;     LDS_WAIT(); asm volatile("" ::: "memory");
; }
; __device__ __forceinline__ void convert_item(const In& I, unsigned char* ws, int it, LAS float* scr, int lane) {
;     ...
;     { const int jk = r >> 3; r &= 7; const int kb = r >> 1, nb = r & 1;
;         transpose_item(I.nsa_w2 + (size_t)jk * 256 * 64, 256, 64, W2t + (size_t)jk * 64 * 256, 32 * nb, kb, 32 * nb, scr, lane); }
.LBB0_167:
	s_add_i32 s45, s40, 0xa800
	s_cmp_gt_i32 s45, 0x83ff
	s_mov_b64 s[2:3], -1
	s_cbranch_scc0 .LBB0_221
	s_cmpk_gt_u32 s45, 0x8eff
	s_cbranch_scc0 .LBB0_202
	s_cmpk_gt_u32 s45, 0x92ff
	s_cbranch_scc0 .LBB0_199
	s_cmpk_gt_u32 s45, 0x9fff
	s_cbranch_scc0 .LBB0_180
	s_cmpk_gt_u32 s45, 0xa3ff
	s_cbranch_scc0 .LBB0_177
	s_cmpk_gt_u32 s45, 0xa7ff
	s_cbranch_scc0 .LBB0_174
	s_lshr_b32 s68, s40, 3
	v_readlane_b32 s48, v253, 16
	s_lshl_b64 s[2:3], s[68:69], 16
	v_readlane_b32 s52, v253, 20
	v_readlane_b32 s53, v253, 21
	s_add_u32 s6, s52, s2
	s_addc_u32 s7, s53, s3
	s_lshl_b64 s[2:3], s[68:69], 15
	s_add_u32 s8, s35, s2
	s_addc_u32 s3, s39, s3
	s_and_b32 s2, s42, 32
	s_and_b32 s9, s42, 0xc0
	s_lshl_b32 s10, s2, 2
	s_add_u32 s6, s6, s10
	v_or_b32_e32 v6, s9, v39
	s_addc_u32 s7, s7, 0
	v_lshlrev_b32_e32 v2, 2, v36
	v_lshl_add_u64 v[4:5], s[6:7], 0, v[2:3]
	v_lshlrev_b32_e32 v2, 8, v6
	v_lshl_add_u64 v[28:29], v[4:5], 0, v[2:3]
	global_load_dwordx4 v[4:7], v[28:29], off nt
	global_load_dwordx4 v[8:11], v[28:29], off offset:2048 nt
	v_add_co_u32_e32 v16, vcc, s84, v28
	s_movk_i32 s6, 0x3000
	s_nop 0
	v_addc_co_u32_e32 v17, vcc, 0, v29, vcc
	v_add_co_u32_e32 v24, vcc, s74, v28
	v_add_u32_e32 v2, v44, v45
	s_nop 0
	v_addc_co_u32_e32 v25, vcc, 0, v29, vcc
	global_load_dwordx4 v[12:15], v[24:25], off offset:-4096 nt
	s_nop 0
	global_load_dwordx4 v[16:19], v[16:17], off offset:2048 nt
	s_nop 0
	global_load_dwordx4 v[20:23], v[24:25], off nt
	s_nop 0
	global_load_dwordx4 v[24:27], v[24:25], off offset:2048 nt
	v_add_co_u32_e32 v32, vcc, s6, v28
	s_lshl_b32 s6, s9, 1
	s_nop 0
	v_addc_co_u32_e32 v33, vcc, 0, v29, vcc
	global_load_dwordx4 v[28:31], v[32:33], off nt
	s_nop 0
	global_load_dwordx4 v[32:35], v[32:33], off offset:2048 nt
	s_add_u32 s6, s8, s6
	s_addc_u32 s7, s3, 0
	v_readlane_b32 s49, v253, 17
	v_readlane_b32 s50, v253, 18
	v_readlane_b32 s51, v253, 19
	v_readlane_b32 s54, v253, 22
	v_readlane_b32 s55, v253, 23
	v_readlane_b32 s56, v253, 24
	v_readlane_b32 s57, v253, 25
	v_readlane_b32 s58, v253, 26
	v_readlane_b32 s59, v253, 27
	v_readlane_b32 s60, v253, 28
	v_readlane_b32 s61, v253, 29
	v_readlane_b32 s62, v253, 30
	v_readlane_b32 s63, v253, 31
	s_waitcnt vmcnt(0)
	ds_write2_b32 v2, v4, v5 offset1:1
	ds_write2_b32 v2, v6, v7 offset0:2 offset1:3
	v_add_u32_e32 v4, 0x420, v2
	ds_write2_b32 v4, v8, v9 offset1:1
	v_add_u32_e32 v4, 0x428, v2
	ds_write2_b32 v4, v10, v11 offset1:1
	v_add_u32_e32 v4, 0x840, v2
	ds_write2_b32 v4, v12, v13 offset1:1
	v_add_u32_e32 v4, 0x848, v2
	ds_write2_b32 v4, v14, v15 offset1:1
	v_add_u32_e32 v4, 0xc60, v2
	ds_write2_b32 v4, v16, v17 offset1:1
	v_add_u32_e32 v4, 0xc68, v2
	ds_write2_b32 v4, v18, v19 offset1:1
	v_add_u32_e32 v4, 0x1080, v2
	ds_write2_b32 v4, v20, v21 offset1:1
	v_add_u32_e32 v4, 0x1088, v2
	ds_write2_b32 v4, v22, v23 offset1:1
	v_add_u32_e32 v4, 0x14a0, v2
	ds_write2_b32 v4, v24, v25 offset1:1
	v_add_u32_e32 v4, 0x14a8, v2
	ds_write2_b32 v4, v26, v27 offset1:1
	v_add_u32_e32 v4, 0x18c0, v2
	ds_write2_b32 v4, v28, v29 offset1:1
	v_add_u32_e32 v4, 0x18c8, v2
	ds_write2_b32 v4, v30, v31 offset1:1
	v_add_u32_e32 v4, 0x1ce0, v2
	v_add_u32_e32 v2, 0x1ce8, v2
	ds_write2_b32 v4, v32, v33 offset1:1
	ds_write2_b32 v2, v34, v35 offset1:1
	s_waitcnt lgkmcnt(0)
	ds_read2_b32 v[10:11], v49 offset0:33 offset1:41
	ds_read2_b32 v[12:13], v49 offset1:8
	v_lshlrev_b32_e32 v2, 1, v38
	ds_read2_b32 v[14:15], v49 offset0:66 offset1:74
	ds_read2_b32 v[16:17], v49 offset0:99 offset1:107
	ds_read2_b32 v[18:19], v49 offset0:132 offset1:140
	ds_read2_b32 v[20:21], v49 offset0:165 offset1:173
	ds_read2_b32 v[22:23], v49 offset0:198 offset1:206
	ds_read2_b32 v[24:25], v49 offset0:231 offset1:239
	v_lshl_add_u64 v[4:5], s[6:7], 0, v[2:3]
	v_or_b32_e32 v2, s2, v39
	v_lshlrev_b32_e32 v2, 9, v2
	v_lshl_add_u64 v[26:27], v[4:5], 0, v[2:3]
	v_or_b32_e32 v2, s2, v46
	s_waitcnt lgkmcnt(0)
	v_cvt_pk_bf16_f32 v6, v12, v10
	v_lshlrev_b32_e32 v2, 9, v2
	v_cvt_pk_bf16_f32 v7, v14, v16
	v_cvt_pk_bf16_f32 v8, v18, v20
	v_cvt_pk_bf16_f32 v9, v22, v24
	global_store_dwordx4 v[26:27], v[6:9], off sc1
	s_nop 1
	v_cvt_pk_bf16_f32 v6, v13, v11
	v_lshl_add_u64 v[10:11], v[4:5], 0, v[2:3]
	v_cvt_pk_bf16_f32 v7, v15, v17
	v_cvt_pk_bf16_f32 v8, v19, v21
	v_cvt_pk_bf16_f32 v9, v23, v25
	global_store_dwordx4 v[10:11], v[6:9], off sc1
	ds_read2_b32 v[10:11], v49 offset0:16 offset1:24
	ds_read2_b32 v[12:13], v49 offset0:49 offset1:57
	ds_read2_b32 v[14:15], v49 offset0:82 offset1:90
	ds_read2_b32 v[16:17], v49 offset0:115 offset1:123
	ds_read2_b32 v[18:19], v49 offset0:148 offset1:156
	ds_read2_b32 v[20:21], v49 offset0:181 offset1:189
	ds_read2_b32 v[22:23], v49 offset0:214 offset1:222
	ds_read2_b32 v[24:25], v49 offset0:247 offset1:255
	v_or_b32_e32 v2, s2, v47
	v_lshlrev_b32_e32 v2, 9, v2
	v_lshl_add_u64 v[26:27], v[4:5], 0, v[2:3]
	v_or_b32_e32 v2, s2, v48
	v_lshlrev_b32_e32 v2, 9, v2
	s_waitcnt lgkmcnt(6)
	v_cvt_pk_bf16_f32 v6, v10, v12
	s_waitcnt lgkmcnt(4)
	v_cvt_pk_bf16_f32 v7, v14, v16
	s_waitcnt lgkmcnt(2)
	v_cvt_pk_bf16_f32 v8, v18, v20
	s_waitcnt lgkmcnt(0)
	v_cvt_pk_bf16_f32 v9, v22, v24
	v_lshl_add_u64 v[4:5], v[4:5], 0, v[2:3]
	global_store_dwordx4 v[26:27], v[6:9], off sc1
	s_mov_b64 s[2:3], 0
	s_nop 0
	v_cvt_pk_bf16_f32 v6, v11, v13
	v_cvt_pk_bf16_f32 v7, v15, v17
	v_cvt_pk_bf16_f32 v8, v19, v21
	v_cvt_pk_bf16_f32 v9, v23, v25
	global_store_dwordx4 v[4:5], v[6:9], off sc1
	s_waitcnt lgkmcnt(0)
; #define GAS __attribute__((address_space(1)))
; #define LAS __attribute__((address_space(3)))
; #define LDS_WAIT() asm volatile("s_waitcnt lgkmcnt(0)" ::: "memory")
; __device__ __forceinline__ unsigned pk2(float lo, float hi) { unsigned r; asm("v_cvt_pk_bf16_f32 %0, %1, %2" : "=v"(r) : "v"(lo), "v"(hi)); return r; }
; __device__ __forceinline__ void transpose_item(const float* W, int K, int N, bf16* WT, int drow0, int kb, int n0, LAS float* scr, int lane) {
;     const int k0 = 64 * kb; const int c4 = 4 * (lane & 7); const bool ok = (n0 + c4) < N;
;     f32x4 v[8];
; #pragma unroll
;     for (int i = 0; i < 8; ++i) { const int kk = 8 * i + (lane >> 3); v[i] = ok ? *(const f32x4*)(W + (size_t)(k0 + kk) * N + n0 + c4) : (f32x4){0.f, 0.f, 0.f, 0.f}; }
; #pragma unroll
;     for (int i = 0; i < 8; ++i) { const int kk = 8 * i + (lane >> 3); LAS float* d = scr + kk * 33 + c4; d[0] = v[i][0]; d[1] = v[i][1]; d[2] = v[i][2]; d[3] = v[i][3]; }
;     LDS_WAIT(); asm volatile("" ::: "memory");
;     const int c = lane & 7;
; #pragma unroll
;     for (int j = 0; j < 4; ++j) { const int n = (lane >> 3) + 8 * j; const LAS float* s = scr + (8 * c) * 33 + n;
;         v4u o; o.x = pk2(s[0 * 33], s[1 * 33]); o.y = pk2(s[2 * 33], s[3 * 33]); o.z = pk2(s[4 * 33], s[5 * 33]); o.w = pk2(s[6 * 33], s[7 * 33]);
;         *(GAS v4u*)(WT + (size_t)(drow0 + n) * K + k0 + 8 * c) = o; }
;     LDS_WAIT(); asm volatile("" ::: "memory");
; }
; __device__ __forceinline__ void convert_item(const In& I, unsigned char* ws, int it, LAS float* scr, int lane) {
;     ...
;     if (r < 4 * I_W1) { const int jk = r / I_W1; r -= jk * I_W1; const int kb = r / 8, nb = r % 8;
;         transpose_item(I.nsa_w1 + (size_t)jk * 2048 * 256, 2048, 256, W1t + (size_t)jk * 256 * 2048, 32 * nb, kb, 32 * nb, scr, lane); return; }
.LBB0_174:
	s_andn2_b64 vcc, exec, s[2:3]
	s_cbranch_vccnz .LBB0_176
	s_add_i32 s2, s40, 0x400
	s_lshr_b32 s68, s2, 8
	s_lshl_b64 s[2:3], s[68:69], 21
	v_readlane_b32 s48, v253, 16
	v_readlane_b32 s49, v253, 17
	s_add_u32 s6, s48, s2
	s_addc_u32 s7, s49, s3
	s_lshl_b64 s[2:3], s[68:69], 20
	s_add_u32 s8, s33, s2
	s_addc_u32 s3, s34, s3
	s_and_b32 s2, s42, 0xe0
	s_and_b32 s9, s41, 0x7c0
	s_lshl_b32 s10, s2, 2
	s_add_u32 s6, s6, s10
	v_or_b32_e32 v6, s9, v39
	s_addc_u32 s7, s7, 0
	v_lshlrev_b32_e32 v2, 2, v36
	v_lshl_add_u64 v[4:5], s[6:7], 0, v[2:3]
	v_lshlrev_b32_e32 v2, 10, v6
	v_lshl_add_u64 v[32:33], v[4:5], 0, v[2:3]
	v_add_co_u32_e32 v8, vcc, s74, v32
	global_load_dwordx4 v[4:7], v[32:33], off nt
	s_nop 0
	v_addc_co_u32_e32 v9, vcc, 0, v33, vcc
	s_movk_i32 s6, 0x4000
	global_load_dwordx4 v[8:11], v[8:9], off nt
	v_add_co_u32_e32 v12, vcc, s6, v32
	s_movk_i32 s6, 0x6000
	s_nop 0
	v_addc_co_u32_e32 v13, vcc, 0, v33, vcc
	global_load_dwordx4 v[12:15], v[12:13], off nt
	v_add_co_u32_e32 v16, vcc, s6, v32
	s_mov_b32 s6, 0xa000
	s_nop 0
	v_addc_co_u32_e32 v17, vcc, 0, v33, vcc
	global_load_dwordx4 v[16:19], v[16:17], off nt
	v_add_co_u32_e32 v20, vcc, s81, v32
	v_add_u32_e32 v2, v44, v45
	s_nop 0
	v_addc_co_u32_e32 v21, vcc, 0, v33, vcc
	global_load_dwordx4 v[20:23], v[20:21], off nt
	v_add_co_u32_e32 v24, vcc, s6, v32
	s_mov_b32 s6, 0xc000
	s_nop 0
	v_addc_co_u32_e32 v25, vcc, 0, v33, vcc
	global_load_dwordx4 v[24:27], v[24:25], off nt
	v_add_co_u32_e32 v28, vcc, s6, v32
	s_mov_b32 s6, 0xe000
	s_nop 0
	v_addc_co_u32_e32 v29, vcc, 0, v33, vcc
	global_load_dwordx4 v[28:31], v[28:29], off nt
	v_add_co_u32_e32 v32, vcc, s6, v32
	s_lshl_b32 s6, s9, 1
	s_nop 0
	v_addc_co_u32_e32 v33, vcc, 0, v33, vcc
	global_load_dwordx4 v[32:35], v[32:33], off nt
	s_add_u32 s6, s8, s6
	s_addc_u32 s7, s3, 0
	v_readlane_b32 s50, v253, 18
	v_readlane_b32 s51, v253, 19
	v_readlane_b32 s52, v253, 20
	v_readlane_b32 s53, v253, 21
	v_readlane_b32 s54, v253, 22
	v_readlane_b32 s55, v253, 23
	v_readlane_b32 s56, v253, 24
	v_readlane_b32 s57, v253, 25
	v_readlane_b32 s58, v253, 26
	v_readlane_b32 s59, v253, 27
	v_readlane_b32 s60, v253, 28
	v_readlane_b32 s61, v253, 29
	v_readlane_b32 s62, v253, 30
	v_readlane_b32 s63, v253, 31
	s_waitcnt vmcnt(0)
	ds_write2_b32 v2, v4, v5 offset1:1
	ds_write2_b32 v2, v6, v7 offset0:2 offset1:3
	v_add_u32_e32 v4, 0x420, v2
	ds_write2_b32 v4, v8, v9 offset1:1
	v_add_u32_e32 v4, 0x428, v2
	ds_write2_b32 v4, v10, v11 offset1:1
	v_add_u32_e32 v4, 0x840, v2
	ds_write2_b32 v4, v12, v13 offset1:1
	v_add_u32_e32 v4, 0x848, v2
	ds_write2_b32 v4, v14, v15 offset1:1
	v_add_u32_e32 v4, 0xc60, v2
	ds_write2_b32 v4, v16, v17 offset1:1
	v_add_u32_e32 v4, 0xc68, v2
	ds_write2_b32 v4, v18, v19 offset1:1
	v_add_u32_e32 v4, 0x1080, v2
	ds_write2_b32 v4, v20, v21 offset1:1
	v_add_u32_e32 v4, 0x1088, v2
	ds_write2_b32 v4, v22, v23 offset1:1
	v_add_u32_e32 v4, 0x14a0, v2
	ds_write2_b32 v4, v24, v25 offset1:1
	v_add_u32_e32 v4, 0x14a8, v2
	ds_write2_b32 v4, v26, v27 offset1:1
	v_add_u32_e32 v4, 0x18c0, v2
	ds_write2_b32 v4, v28, v29 offset1:1
	v_add_u32_e32 v4, 0x18c8, v2
	ds_write2_b32 v4, v30, v31 offset1:1
	v_add_u32_e32 v4, 0x1ce0, v2
	v_add_u32_e32 v2, 0x1ce8, v2
	ds_write2_b32 v4, v32, v33 offset1:1
	ds_write2_b32 v2, v34, v35 offset1:1
	s_waitcnt lgkmcnt(0)
	ds_read2_b32 v[10:11], v49 offset0:33 offset1:41
	ds_read2_b32 v[12:13], v49 offset1:8
	v_lshlrev_b32_e32 v2, 1, v38
	ds_read2_b32 v[14:15], v49 offset0:66 offset1:74
	ds_read2_b32 v[16:17], v49 offset0:99 offset1:107
	ds_read2_b32 v[18:19], v49 offset0:132 offset1:140
	ds_read2_b32 v[20:21], v49 offset0:165 offset1:173
	ds_read2_b32 v[22:23], v49 offset0:198 offset1:206
	ds_read2_b32 v[24:25], v49 offset0:231 offset1:239
	v_lshl_add_u64 v[8:9], s[6:7], 0, v[2:3]
	v_or_b32_e32 v2, s2, v39
	v_lshlrev_b32_e32 v2, 12, v2
	v_lshl_add_u64 v[26:27], v[8:9], 0, v[2:3]
	v_or_b32_e32 v2, s2, v46
	s_waitcnt lgkmcnt(0)
	v_cvt_pk_bf16_f32 v4, v12, v10
	v_lshlrev_b32_e32 v2, 12, v2
	v_cvt_pk_bf16_f32 v5, v14, v16
	v_cvt_pk_bf16_f32 v6, v18, v20
	v_cvt_pk_bf16_f32 v7, v22, v24
	global_store_dwordx4 v[26:27], v[4:7], off sc1
	s_nop 1
	v_cvt_pk_bf16_f32 v4, v13, v11
	v_lshl_add_u64 v[10:11], v[8:9], 0, v[2:3]
	v_cvt_pk_bf16_f32 v5, v15, v17
	v_cvt_pk_bf16_f32 v6, v19, v21
	v_cvt_pk_bf16_f32 v7, v23, v25
	global_store_dwordx4 v[10:11], v[4:7], off sc1
	ds_read2_b32 v[10:11], v49 offset0:16 offset1:24
	ds_read2_b32 v[12:13], v49 offset0:49 offset1:57
	ds_read2_b32 v[14:15], v49 offset0:82 offset1:90
	ds_read2_b32 v[16:17], v49 offset0:115 offset1:123
	ds_read2_b32 v[18:19], v49 offset0:148 offset1:156
	ds_read2_b32 v[20:21], v49 offset0:181 offset1:189
	ds_read2_b32 v[22:23], v49 offset0:214 offset1:222
	ds_read2_b32 v[24:25], v49 offset0:247 offset1:255
	v_or_b32_e32 v2, s2, v47
	v_lshlrev_b32_e32 v2, 12, v2
	v_lshl_add_u64 v[26:27], v[8:9], 0, v[2:3]
	v_or_b32_e32 v2, s2, v48
	v_lshlrev_b32_e32 v2, 12, v2
	s_waitcnt lgkmcnt(6)
	v_cvt_pk_bf16_f32 v4, v10, v12
	s_waitcnt lgkmcnt(4)
	v_cvt_pk_bf16_f32 v5, v14, v16
	s_waitcnt lgkmcnt(2)
	v_cvt_pk_bf16_f32 v6, v18, v20
	s_waitcnt lgkmcnt(0)
	v_cvt_pk_bf16_f32 v7, v22, v24
	v_lshl_add_u64 v[8:9], v[8:9], 0, v[2:3]
	global_store_dwordx4 v[26:27], v[4:7], off sc1
	s_nop 1
	v_cvt_pk_bf16_f32 v4, v11, v13
	v_cvt_pk_bf16_f32 v5, v15, v17
	v_cvt_pk_bf16_f32 v6, v19, v21
	v_cvt_pk_bf16_f32 v7, v23, v25
	global_store_dwordx4 v[8:9], v[4:7], off sc1
	s_waitcnt lgkmcnt(0)

; #define GAS __attribute__((address_space(1)))
; #define LAS __attribute__((address_space(3)))
; #define LDS_WAIT() asm volatile("s_waitcnt lgkmcnt(0)" ::: "memory")
; __device__ __forceinline__ unsigned pk2(float lo, float hi) { unsigned r; asm("v_cvt_pk_bf16_f32 %0, %1, %2" : "=v"(r) : "v"(lo), "v"(hi)); return r; }
; __device__ __forceinline__ void transpose_item(const float* W, int K, int N, bf16* WT, int drow0, int kb, int n0, LAS float* scr, int lane) {
;     const int k0 = 64 * kb; const int c4 = 4 * (lane & 7); const bool ok = (n0 + c4) < N;
;     f32x4 v[8];
; #pragma unroll
;     for (int i = 0; i < 8; ++i) { const int kk = 8 * i + (lane >> 3); v[i] = ok ? *(const f32x4*)(W + (size_t)(k0 + kk) * N + n0 + c4) : (f32x4){0.f, 0.f, 0.f, 0.f}; }
; #pragma unroll
;     for (int i = 0; i < 8; ++i) { const int kk = 8 * i + (lane >> 3); LAS float* d = scr + kk * 33 + c4; d[0] = v[i][0]; d[1] = v[i][1]; d[2] = v[i][2]; d[3] = v[i][3]; }
;     LDS_WAIT(); asm volatile("" ::: "memory");
;     const int c = lane & 7;
; #pragma unroll
;     for (int j = 0; j < 4; ++j) { const int n = (lane >> 3) + 8 * j; const LAS float* s = scr + (8 * c) * 33 + n;
;         v4u o; o.x = pk2(s[0 * 33], s[1 * 33]); o.y = pk2(s[2 * 33], s[3 * 33]); o.z = pk2(s[4 * 33], s[5 * 33]); o.w = pk2(s[6 * 33], s[7 * 33]);
;         *(GAS v4u*)(WT + (size_t)(drow0 + n) * K + k0 + 8 * c) = o; }
;     LDS_WAIT(); asm volatile("" ::: "memory");
; }
; __device__ __forceinline__ void convert_item(const In& I, unsigned char* ws, int it, LAS float* scr, int lane) {
;     ...
;     if (r < 2 * I_SQ) { const int j = r / I_SQ; r -= j * I_SQ; const int kb = r / 32, nb = r % 32;
;         transpose_item(I.fox_w_out + (size_t)j * D * D, D, D, Wfout + (size_t)j * D * D, 32 * nb, kb, 32 * nb, scr, lane); return; }
.LBB0_177:
	s_andn2_b64 vcc, exec, s[2:3]
	s_cbranch_vccnz .LBB0_179
	s_add_i32 s2, s40, 0x800
	s_lshr_b32 s68, s2, 9
	v_readlane_b32 s48, v253, 16
	s_lshl_b64 s[2:3], s[68:69], 22
	v_readlane_b32 s60, v253, 28
	v_readlane_b32 s61, v253, 29
	s_add_u32 s6, s60, s2
	s_addc_u32 s7, s61, s3
	s_lshl_b64 s[2:3], s[68:69], 21
	s_add_u32 s8, s27, s2
	s_addc_u32 s3, s31, s3
	s_and_b32 s2, s42, 0x3e0
	s_add_i32 s9, s43, s44
	s_and_b32 s9, s9, 0x3c0
	s_lshl_b32 s10, s2, 2
	s_add_u32 s6, s6, s10
	v_or_b32_e32 v6, s9, v39
	s_addc_u32 s7, s7, 0
	v_lshlrev_b32_e32 v2, 2, v36
	v_lshl_add_u64 v[4:5], s[6:7], 0, v[2:3]
	v_lshlrev_b32_e32 v2, 12, v6
	v_lshl_add_u64 v[32:33], v[4:5], 0, v[2:3]
	v_add_co_u32_e32 v8, vcc, s81, v32
	global_load_dwordx4 v[4:7], v[32:33], off nt
	s_nop 0
	v_addc_co_u32_e32 v9, vcc, 0, v33, vcc
	global_load_dwordx4 v[8:11], v[8:9], off nt
	v_add_co_u32_e32 v12, vcc, s79, v32
	v_add_u32_e32 v2, v44, v45
	s_nop 0
	v_addc_co_u32_e32 v13, vcc, 0, v33, vcc
	global_load_dwordx4 v[12:15], v[12:13], off nt
	v_add_co_u32_e32 v16, vcc, s80, v32
	s_lshl_b32 s6, s9, 1
	s_nop 0
	v_addc_co_u32_e32 v17, vcc, 0, v33, vcc
	global_load_dwordx4 v[16:19], v[16:17], off nt
	v_add_co_u32_e32 v20, vcc, s85, v32
	s_add_u32 s6, s8, s6
	s_nop 0
	v_addc_co_u32_e32 v21, vcc, 0, v33, vcc
	global_load_dwordx4 v[20:23], v[20:21], off nt
	v_add_co_u32_e32 v24, vcc, s86, v32
	s_addc_u32 s7, s3, 0
	s_nop 0
	v_addc_co_u32_e32 v25, vcc, 0, v33, vcc
	global_load_dwordx4 v[24:27], v[24:25], off nt
	v_add_co_u32_e32 v28, vcc, s87, v32
	v_readlane_b32 s49, v253, 17
	s_nop 0
	v_addc_co_u32_e32 v29, vcc, 0, v33, vcc
	global_load_dwordx4 v[28:31], v[28:29], off nt
	v_add_co_u32_e32 v32, vcc, s89, v32
	v_readlane_b32 s50, v253, 18
	s_nop 0
	v_addc_co_u32_e32 v33, vcc, 0, v33, vcc
	global_load_dwordx4 v[32:35], v[32:33], off nt
	v_readlane_b32 s51, v253, 19
	v_readlane_b32 s52, v253, 20
	v_readlane_b32 s53, v253, 21
	v_readlane_b32 s54, v253, 22
	v_readlane_b32 s55, v253, 23
	v_readlane_b32 s56, v253, 24
	v_readlane_b32 s57, v253, 25
	v_readlane_b32 s58, v253, 26
	v_readlane_b32 s59, v253, 27
	v_readlane_b32 s62, v253, 30
	v_readlane_b32 s63, v253, 31
	s_waitcnt vmcnt(0)
	ds_write2_b32 v2, v4, v5 offset1:1
	ds_write2_b32 v2, v6, v7 offset0:2 offset1:3
	v_add_u32_e32 v4, 0x420, v2
	ds_write2_b32 v4, v8, v9 offset1:1
	v_add_u32_e32 v4, 0x428, v2
	ds_write2_b32 v4, v10, v11 offset1:1
	v_add_u32_e32 v4, 0x840, v2
	ds_write2_b32 v4, v12, v13 offset1:1
	v_add_u32_e32 v4, 0x848, v2
	ds_write2_b32 v4, v14, v15 offset1:1
	v_add_u32_e32 v4, 0xc60, v2
	ds_write2_b32 v4, v16, v17 offset1:1
	v_add_u32_e32 v4, 0xc68, v2
	ds_write2_b32 v4, v18, v19 offset1:1
	v_add_u32_e32 v4, 0x1080, v2
	ds_write2_b32 v4, v20, v21 offset1:1
	v_add_u32_e32 v4, 0x1088, v2
	ds_write2_b32 v4, v22, v23 offset1:1
	v_add_u32_e32 v4, 0x14a0, v2
	ds_write2_b32 v4, v24, v25 offset1:1
	v_add_u32_e32 v4, 0x14a8, v2
	ds_write2_b32 v4, v26, v27 offset1:1
	v_add_u32_e32 v4, 0x18c0, v2
	ds_write2_b32 v4, v28, v29 offset1:1
	v_add_u32_e32 v4, 0x18c8, v2
	ds_write2_b32 v4, v30, v31 offset1:1
	v_add_u32_e32 v4, 0x1ce0, v2
	v_add_u32_e32 v2, 0x1ce8, v2
	ds_write2_b32 v4, v32, v33 offset1:1
	ds_write2_b32 v2, v34, v35 offset1:1
	s_waitcnt lgkmcnt(0)
	ds_read2_b32 v[10:11], v49 offset0:33 offset1:41
	ds_read2_b32 v[12:13], v49 offset1:8
	v_lshlrev_b32_e32 v2, 1, v38
	ds_read2_b32 v[14:15], v49 offset0:66 offset1:74
	ds_read2_b32 v[16:17], v49 offset0:99 offset1:107
	ds_read2_b32 v[18:19], v49 offset0:132 offset1:140
	ds_read2_b32 v[20:21], v49 offset0:165 offset1:173
	ds_read2_b32 v[22:23], v49 offset0:198 offset1:206
	ds_read2_b32 v[24:25], v49 offset0:231 offset1:239
	v_lshl_add_u64 v[8:9], s[6:7], 0, v[2:3]
	v_or_b32_e32 v2, s2, v39
	v_lshlrev_b32_e32 v2, 11, v2
	v_lshl_add_u64 v[26:27], v[8:9], 0, v[2:3]
	v_or_b32_e32 v2, s2, v46
	s_waitcnt lgkmcnt(0)
	v_cvt_pk_bf16_f32 v4, v12, v10
	v_lshlrev_b32_e32 v2, 11, v2
	v_cvt_pk_bf16_f32 v5, v14, v16
	v_cvt_pk_bf16_f32 v6, v18, v20
	v_cvt_pk_bf16_f32 v7, v22, v24
	global_store_dwordx4 v[26:27], v[4:7], off sc1
	s_nop 1
	v_cvt_pk_bf16_f32 v4, v13, v11
	v_lshl_add_u64 v[10:11], v[8:9], 0, v[2:3]
	v_cvt_pk_bf16_f32 v5, v15, v17
	v_cvt_pk_bf16_f32 v6, v19, v21
	v_cvt_pk_bf16_f32 v7, v23, v25
	global_store_dwordx4 v[10:11], v[4:7], off sc1
	ds_read2_b32 v[10:11], v49 offset0:16 offset1:24
	ds_read2_b32 v[12:13], v49 offset0:49 offset1:57
	ds_read2_b32 v[14:15], v49 offset0:82 offset1:90
	ds_read2_b32 v[16:17], v49 offset0:115 offset1:123
	ds_read2_b32 v[18:19], v49 offset0:148 offset1:156
	ds_read2_b32 v[20:21], v49 offset0:181 offset1:189
	ds_read2_b32 v[22:23], v49 offset0:214 offset1:222
	ds_read2_b32 v[24:25], v49 offset0:247 offset1:255
	v_or_b32_e32 v2, s2, v47
	v_lshlrev_b32_e32 v2, 11, v2
	v_lshl_add_u64 v[26:27], v[8:9], 0, v[2:3]
	v_or_b32_e32 v2, s2, v48
	v_lshlrev_b32_e32 v2, 11, v2
	s_waitcnt lgkmcnt(6)
	v_cvt_pk_bf16_f32 v4, v10, v12
	s_waitcnt lgkmcnt(4)
	v_cvt_pk_bf16_f32 v5, v14, v16
	s_waitcnt lgkmcnt(2)
	v_cvt_pk_bf16_f32 v6, v18, v20
	s_waitcnt lgkmcnt(0)
	v_cvt_pk_bf16_f32 v7, v22, v24
	v_lshl_add_u64 v[8:9], v[8:9], 0, v[2:3]
	global_store_dwordx4 v[26:27], v[4:7], off sc1
	s_nop 1
	v_cvt_pk_bf16_f32 v4, v11, v13
	v_cvt_pk_bf16_f32 v5, v15, v17
	v_cvt_pk_bf16_f32 v6, v19, v21
	v_cvt_pk_bf16_f32 v7, v23, v25
	global_store_dwordx4 v[8:9], v[4:7], off sc1
	s_waitcnt lgkmcnt(0)

; #define GAS __attribute__((address_space(1)))
; #define LAS __attribute__((address_space(3)))
; #define LDS_WAIT() asm volatile("s_waitcnt lgkmcnt(0)" ::: "memory")
; __device__ __forceinline__ unsigned pk2(float lo, float hi) { unsigned r; asm("v_cvt_pk_bf16_f32 %0, %1, %2" : "=v"(r) : "v"(lo), "v"(hi)); return r; }
; __device__ __forceinline__ void transpose_item(const float* W, int K, int N, bf16* WT, int drow0, int kb, int n0, LAS float* scr, int lane) {
;     const int k0 = 64 * kb; const int c4 = 4 * (lane & 7); const bool ok = (n0 + c4) < N;
;     f32x4 v[8];
; #pragma unroll
;     for (int i = 0; i < 8; ++i) { const int kk = 8 * i + (lane >> 3); v[i] = ok ? *(const f32x4*)(W + (size_t)(k0 + kk) * N + n0 + c4) : (f32x4){0.f, 0.f, 0.f, 0.f}; }
; #pragma unroll
;     for (int i = 0; i < 8; ++i) { const int kk = 8 * i + (lane >> 3); LAS float* d = scr + kk * 33 + c4; d[0] = v[i][0]; d[1] = v[i][1]; d[2] = v[i][2]; d[3] = v[i][3]; }
;     LDS_WAIT(); asm volatile("" ::: "memory");
;     const int c = lane & 7;
; #pragma unroll
;     for (int j = 0; j < 4; ++j) { const int n = (lane >> 3) + 8 * j; const LAS float* s = scr + (8 * c) * 33 + n;
;         v4u o; o.x = pk2(s[0 * 33], s[1 * 33]); o.y = pk2(s[2 * 33], s[3 * 33]); o.z = pk2(s[4 * 33], s[5 * 33]); o.w = pk2(s[6 * 33], s[7 * 33]);
;         *(GAS v4u*)(WT + (size_t)(drow0 + n) * K + k0 + 8 * c) = o; }
;     LDS_WAIT(); asm volatile("" ::: "memory");
; }
; __device__ __forceinline__ void convert_item(const In& I, unsigned char* ws, int it, LAS float* scr, int lane) {
;     ...
;     if (r < 2 * I_SQ) { const int j = r / I_SQ; r -= j * I_SQ; const int kb = r / 32, nb = r % 32;
;         transpose_item(I.nsa_w_out + (size_t)j * D * D, D, D, Wnout + (size_t)j * D * D, 32 * nb, kb, 32 * nb, scr, lane); return; }
.LBB0_199:
	s_andn2_b64 vcc, exec, s[2:3]
	s_cbranch_vccnz .LBB0_201
	s_add_i32 s2, s40, 0x1900
	s_lshr_b32 s68, s2, 9
	v_readlane_b32 s48, v253, 16
	s_lshl_b64 s[2:3], s[68:69], 22
	v_readlane_b32 s54, v253, 22
	v_readlane_b32 s55, v253, 23
	s_add_u32 s6, s54, s2
	s_addc_u32 s7, s55, s3
	s_lshl_b64 s[2:3], s[68:69], 21
	s_add_u32 s8, s23, s2
	s_addc_u32 s3, s24, s3
	s_add_i32 s9, s43, s44
	s_and_b32 s2, s42, 0x3e0
	s_add_i32 s9, s9, 0xfffee200
	s_and_b32 s9, s9, 0x3c0
	s_lshl_b32 s10, s2, 2
	s_add_u32 s6, s6, s10
	v_or_b32_e32 v6, s9, v39
	s_addc_u32 s7, s7, 0
	v_lshlrev_b32_e32 v2, 2, v36
	v_lshl_add_u64 v[4:5], s[6:7], 0, v[2:3]
	v_lshlrev_b32_e32 v2, 12, v6
	v_lshl_add_u64 v[32:33], v[4:5], 0, v[2:3]
	v_add_co_u32_e32 v8, vcc, s81, v32
	global_load_dwordx4 v[4:7], v[32:33], off nt
	s_nop 0
	v_addc_co_u32_e32 v9, vcc, 0, v33, vcc
	global_load_dwordx4 v[8:11], v[8:9], off nt
	v_add_co_u32_e32 v12, vcc, s79, v32
	v_add_u32_e32 v2, v44, v45
	s_nop 0
	v_addc_co_u32_e32 v13, vcc, 0, v33, vcc
	global_load_dwordx4 v[12:15], v[12:13], off nt
	v_add_co_u32_e32 v16, vcc, s80, v32
	s_lshl_b32 s6, s9, 1
	s_nop 0
	v_addc_co_u32_e32 v17, vcc, 0, v33, vcc
	global_load_dwordx4 v[16:19], v[16:17], off nt
	v_add_co_u32_e32 v20, vcc, s85, v32
	s_add_u32 s6, s8, s6
	s_nop 0
	v_addc_co_u32_e32 v21, vcc, 0, v33, vcc
	global_load_dwordx4 v[20:23], v[20:21], off nt
	v_add_co_u32_e32 v24, vcc, s86, v32
	s_addc_u32 s7, s3, 0
	s_nop 0
	v_addc_co_u32_e32 v25, vcc, 0, v33, vcc
	global_load_dwordx4 v[24:27], v[24:25], off nt
	v_add_co_u32_e32 v28, vcc, s87, v32
	v_readlane_b32 s49, v253, 17
	s_nop 0
	v_addc_co_u32_e32 v29, vcc, 0, v33, vcc
	global_load_dwordx4 v[28:31], v[28:29], off nt
	v_add_co_u32_e32 v32, vcc, s89, v32
	v_readlane_b32 s50, v253, 18
	s_nop 0
	v_addc_co_u32_e32 v33, vcc, 0, v33, vcc
	global_load_dwordx4 v[32:35], v[32:33], off nt
	v_readlane_b32 s51, v253, 19
	v_readlane_b32 s52, v253, 20
	v_readlane_b32 s53, v253, 21
	v_readlane_b32 s56, v253, 24
	v_readlane_b32 s57, v253, 25
	v_readlane_b32 s58, v253, 26
	v_readlane_b32 s59, v253, 27
	v_readlane_b32 s60, v253, 28
	v_readlane_b32 s61, v253, 29
	v_readlane_b32 s62, v253, 30
	v_readlane_b32 s63, v253, 31
	s_waitcnt vmcnt(0)
	ds_write2_b32 v2, v4, v5 offset1:1
	ds_write2_b32 v2, v6, v7 offset0:2 offset1:3
	v_add_u32_e32 v4, 0x420, v2
	ds_write2_b32 v4, v8, v9 offset1:1
	v_add_u32_e32 v4, 0x428, v2
	ds_write2_b32 v4, v10, v11 offset1:1
	v_add_u32_e32 v4, 0x840, v2
	ds_write2_b32 v4, v12, v13 offset1:1
	v_add_u32_e32 v4, 0x848, v2
	ds_write2_b32 v4, v14, v15 offset1:1
	v_add_u32_e32 v4, 0xc60, v2
	ds_write2_b32 v4, v16, v17 offset1:1
	v_add_u32_e32 v4, 0xc68, v2
	ds_write2_b32 v4, v18, v19 offset1:1
	v_add_u32_e32 v4, 0x1080, v2
	ds_write2_b32 v4, v20, v21 offset1:1
	v_add_u32_e32 v4, 0x1088, v2
	ds_write2_b32 v4, v22, v23 offset1:1
	v_add_u32_e32 v4, 0x14a0, v2
	ds_write2_b32 v4, v24, v25 offset1:1
	v_add_u32_e32 v4, 0x14a8, v2
	ds_write2_b32 v4, v26, v27 offset1:1
	v_add_u32_e32 v4, 0x18c0, v2
	ds_write2_b32 v4, v28, v29 offset1:1
	v_add_u32_e32 v4, 0x18c8, v2
	ds_write2_b32 v4, v30, v31 offset1:1
	v_add_u32_e32 v4, 0x1ce0, v2
	v_add_u32_e32 v2, 0x1ce8, v2
	ds_write2_b32 v4, v32, v33 offset1:1
	ds_write2_b32 v2, v34, v35 offset1:1
	s_waitcnt lgkmcnt(0)
	ds_read2_b32 v[10:11], v49 offset0:33 offset1:41
	ds_read2_b32 v[12:13], v49 offset1:8
	v_lshlrev_b32_e32 v2, 1, v38
	ds_read2_b32 v[14:15], v49 offset0:66 offset1:74
	ds_read2_b32 v[16:17], v49 offset0:99 offset1:107
	ds_read2_b32 v[18:19], v49 offset0:132 offset1:140
	ds_read2_b32 v[20:21], v49 offset0:165 offset1:173
	ds_read2_b32 v[22:23], v49 offset0:198 offset1:206
	ds_read2_b32 v[24:25], v49 offset0:231 offset1:239
	v_lshl_add_u64 v[8:9], s[6:7], 0, v[2:3]
	v_or_b32_e32 v2, s2, v39
	v_lshlrev_b32_e32 v2, 11, v2
	v_lshl_add_u64 v[26:27], v[8:9], 0, v[2:3]
	v_or_b32_e32 v2, s2, v46
	s_waitcnt lgkmcnt(0)
	v_cvt_pk_bf16_f32 v4, v12, v10
	v_lshlrev_b32_e32 v2, 11, v2
	v_cvt_pk_bf16_f32 v5, v14, v16
	v_cvt_pk_bf16_f32 v6, v18, v20
	v_cvt_pk_bf16_f32 v7, v22, v24
	global_store_dwordx4 v[26:27], v[4:7], off sc1
	s_nop 1
	v_cvt_pk_bf16_f32 v4, v13, v11
	v_lshl_add_u64 v[10:11], v[8:9], 0, v[2:3]
	v_cvt_pk_bf16_f32 v5, v15, v17
	v_cvt_pk_bf16_f32 v6, v19, v21
	v_cvt_pk_bf16_f32 v7, v23, v25
	global_store_dwordx4 v[10:11], v[4:7], off sc1
	ds_read2_b32 v[10:11], v49 offset0:16 offset1:24
	ds_read2_b32 v[12:13], v49 offset0:49 offset1:57
	ds_read2_b32 v[14:15], v49 offset0:82 offset1:90
	ds_read2_b32 v[16:17], v49 offset0:115 offset1:123
	ds_read2_b32 v[18:19], v49 offset0:148 offset1:156
	ds_read2_b32 v[20:21], v49 offset0:181 offset1:189
	ds_read2_b32 v[22:23], v49 offset0:214 offset1:222
	ds_read2_b32 v[24:25], v49 offset0:247 offset1:255
	v_or_b32_e32 v2, s2, v47
	v_lshlrev_b32_e32 v2, 11, v2
	v_lshl_add_u64 v[26:27], v[8:9], 0, v[2:3]
	v_or_b32_e32 v2, s2, v48
	v_lshlrev_b32_e32 v2, 11, v2
	s_waitcnt lgkmcnt(6)
	v_cvt_pk_bf16_f32 v4, v10, v12
	s_waitcnt lgkmcnt(4)
	v_cvt_pk_bf16_f32 v5, v14, v16
	s_waitcnt lgkmcnt(2)
	v_cvt_pk_bf16_f32 v6, v18, v20
	s_waitcnt lgkmcnt(0)
	v_cvt_pk_bf16_f32 v7, v22, v24
	v_lshl_add_u64 v[8:9], v[8:9], 0, v[2:3]
	global_store_dwordx4 v[26:27], v[4:7], off sc1
	s_nop 1
	v_cvt_pk_bf16_f32 v4, v11, v13
	v_cvt_pk_bf16_f32 v5, v15, v17
	v_cvt_pk_bf16_f32 v6, v19, v21
	v_cvt_pk_bf16_f32 v7, v23, v25
	global_store_dwordx4 v[8:9], v[4:7], off sc1
	s_waitcnt lgkmcnt(0)

; #define GAS __attribute__((address_space(1)))
; #define LAS __attribute__((address_space(3)))
; #define LDS_WAIT() asm volatile("s_waitcnt lgkmcnt(0)" ::: "memory")
; __device__ __forceinline__ unsigned pk2(float lo, float hi) { unsigned r; asm("v_cvt_pk_bf16_f32 %0, %1, %2" : "=v"(r) : "v"(lo), "v"(hi)); return r; }
; __device__ __forceinline__ void transpose_item(const float* W, int K, int N, bf16* WT, int drow0, int kb, int n0, LAS float* scr, int lane) {
;     const int k0 = 64 * kb; const int c4 = 4 * (lane & 7); const bool ok = (n0 + c4) < N;
;     f32x4 v[8];
; #pragma unroll
;     for (int i = 0; i < 8; ++i) { const int kk = 8 * i + (lane >> 3); v[i] = ok ? *(const f32x4*)(W + (size_t)(k0 + kk) * N + n0 + c4) : (f32x4){0.f, 0.f, 0.f, 0.f}; }
; #pragma unroll
;     for (int i = 0; i < 8; ++i) { const int kk = 8 * i + (lane >> 3); LAS float* d = scr + kk * 33 + c4; d[0] = v[i][0]; d[1] = v[i][1]; d[2] = v[i][2]; d[3] = v[i][3]; }
;     LDS_WAIT(); asm volatile("" ::: "memory");
;     const int c = lane & 7;
; #pragma unroll
;     for (int j = 0; j < 4; ++j) { const int n = (lane >> 3) + 8 * j; const LAS float* s = scr + (8 * c) * 33 + n;
;         v4u o; o.x = pk2(s[0 * 33], s[1 * 33]); o.y = pk2(s[2 * 33], s[3 * 33]); o.z = pk2(s[4 * 33], s[5 * 33]); o.w = pk2(s[6 * 33], s[7 * 33]);
;         *(GAS v4u*)(WT + (size_t)(drow0 + n) * K + k0 + 8 * c) = o; }
;     LDS_WAIT(); asm volatile("" ::: "memory");
; }
; __device__ __forceinline__ void convert_item(const In& I, unsigned char* ws, int it, LAS float* scr, int lane) {
;     ...
;     if (r < T0) { const int f = r / I_FFN; r -= f * I_FFN;
;         if (r < 2 * I_G) { const int up = r >= I_G; r -= up * I_G; const int kb = r / 88, nb = r % 88;
;             transpose_item((up ? I.w_up : I.w_gate) + (size_t)f * D * FF, D, FF, Wgu + (size_t)f * NGU * D, 256 * (nb >> 2) + 32 * (nb & 3) + 128 * up, kb, 32 * nb, scr, lane); }
;         else { r -= 2 * I_G; const int kb = r / 32, nb = r % 32; transpose_item(I.w_down + (size_t)f * FF * D, FF, D, Wd + (size_t)f * D * FF, 32 * nb, kb, 32 * nb, scr, lane); }
.LBB0_221:
	s_andn2_b64 vcc, exec, s[2:3]
	s_cbranch_vccnz .LBB0_166
	s_mul_hi_i32 s2, s45, 0x3e0f83e1
	s_lshr_b32 s3, s2, 31
	s_ashr_i32 s6, s2, 10
	s_add_i32 s6, s6, s3
	s_mul_i32 s2, s6, 0xffffef80
	s_add_i32 s7, s40, s2
	s_add_i32 s7, s7, 0xa800
	s_cmpk_gt_i32 s7, 0xaff
	s_mov_b64 s[2:3], -1
	s_cbranch_scc0 .LBB0_224
	v_readlane_b32 s48, v253, 0
	v_readlane_b32 s49, v253, 1
	v_readlane_b32 s50, v253, 2
	v_readlane_b32 s51, v253, 3
	v_readlane_b32 s52, v253, 4
	v_readlane_b32 s53, v253, 5
	v_readlane_b32 s54, v253, 6
	v_readlane_b32 s55, v253, 7
	v_readlane_b32 s56, v253, 8
	v_readlane_b32 s57, v253, 9
	s_mov_b64 s[48:49], s[52:53]
	s_mul_i32 s3, s6, 0xb00000
	s_mov_b64 s[50:51], s[54:55]
	s_mov_b64 s[52:53], s[56:57]
	s_mul_hi_i32 s2, s6, 0xb00000
	s_add_u32 s9, s52, s3
	s_addc_u32 s11, s53, s2
	s_mul_i32 s3, s6, 0x580000
	s_mul_hi_i32 s2, s6, 0x580000
	s_add_u32 s3, s19, s3
	s_addc_u32 s8, s20, s2
	s_mul_i32 s10, s6, 0xffffdf00
	s_add_i32 s12, s43, s44
	s_add_i32 s10, s12, s10
	s_and_b32 s2, s42, 0x3e0
	s_andn2_b32 s10, s10, 63
	s_add_i32 s68, s10, 0xffffea00
	s_lshl_b32 s10, s2, 2
	v_or_b32_e32 v32, s68, v39
	s_add_u32 s10, s9, s10
	s_addc_u32 s11, s11, 0
	v_lshlrev_b32_e32 v2, 2, v36
	v_ashrrev_i32_e32 v33, 31, v32
	v_or_b32_e32 v8, 8, v32
	v_lshl_add_u64 v[34:35], s[10:11], 0, v[2:3]
	v_lshlrev_b64 v[4:5], 12, v[32:33]
	v_ashrrev_i32_e32 v9, 31, v8
	v_lshl_add_u64 v[4:5], v[34:35], 0, v[4:5]
	v_lshlrev_b64 v[8:9], 12, v[8:9]
	v_or_b32_e32 v12, 16, v32
	global_load_dwordx4 v[4:7], v[4:5], off nt
	v_lshl_add_u64 v[8:9], v[34:35], 0, v[8:9]
	v_ashrrev_i32_e32 v13, 31, v12
	global_load_dwordx4 v[8:11], v[8:9], off nt
	v_lshlrev_b64 v[12:13], 12, v[12:13]
	v_or_b32_e32 v16, 24, v32
	v_lshl_add_u64 v[12:13], v[34:35], 0, v[12:13]
	v_ashrrev_i32_e32 v17, 31, v16
	global_load_dwordx4 v[12:15], v[12:13], off nt
	v_lshlrev_b64 v[16:17], 12, v[16:17]
	v_or_b32_e32 v20, 32, v32
	v_lshl_add_u64 v[16:17], v[34:35], 0, v[16:17]
	v_ashrrev_i32_e32 v21, 31, v20
	global_load_dwordx4 v[16:19], v[16:17], off nt
	v_lshlrev_b64 v[20:21], 12, v[20:21]
	v_or_b32_e32 v24, 40, v32
	v_lshl_add_u64 v[20:21], v[34:35], 0, v[20:21]
	v_ashrrev_i32_e32 v25, 31, v24
	global_load_dwordx4 v[20:23], v[20:21], off nt
	v_lshlrev_b64 v[24:25], 12, v[24:25]
	v_or_b32_e32 v28, 48, v32
	v_lshl_add_u64 v[24:25], v[34:35], 0, v[24:25]
	v_ashrrev_i32_e32 v29, 31, v28
	global_load_dwordx4 v[24:27], v[24:25], off nt
	v_lshlrev_b64 v[28:29], 12, v[28:29]
	v_or_b32_e32 v32, 56, v32
	v_lshl_add_u64 v[28:29], v[34:35], 0, v[28:29]
	v_ashrrev_i32_e32 v33, 31, v32
	global_load_dwordx4 v[28:31], v[28:29], off nt
	v_lshlrev_b64 v[32:33], 12, v[32:33]
	v_lshl_add_u64 v[32:33], v[34:35], 0, v[32:33]
	global_load_dwordx4 v[32:35], v[32:33], off nt
	v_add_u32_e32 v2, v44, v45
	s_lshl_b64 s[10:11], s[68:69], 1
	s_add_u32 s10, s3, s10
	s_addc_u32 s11, s8, s11
	v_readlane_b32 s58, v253, 10
	v_readlane_b32 s59, v253, 11
	v_readlane_b32 s60, v253, 12
	v_readlane_b32 s61, v253, 13
	v_readlane_b32 s62, v253, 14
	v_readlane_b32 s63, v253, 15
	s_waitcnt vmcnt(0)
	ds_write2_b32 v2, v4, v5 offset1:1
	ds_write2_b32 v2, v6, v7 offset0:2 offset1:3
	v_add_u32_e32 v4, 0x420, v2
	ds_write2_b32 v4, v8, v9 offset1:1
	v_add_u32_e32 v4, 0x428, v2
	ds_write2_b32 v4, v10, v11 offset1:1
	v_add_u32_e32 v4, 0x840, v2
	ds_write2_b32 v4, v12, v13 offset1:1
	v_add_u32_e32 v4, 0x848, v2
	ds_write2_b32 v4, v14, v15 offset1:1
	v_add_u32_e32 v4, 0xc60, v2
	ds_write2_b32 v4, v16, v17 offset1:1
	v_add_u32_e32 v4, 0xc68, v2
	ds_write2_b32 v4, v18, v19 offset1:1
	v_add_u32_e32 v4, 0x1080, v2
	ds_write2_b32 v4, v20, v21 offset1:1
	v_add_u32_e32 v4, 0x1088, v2
	ds_write2_b32 v4, v22, v23 offset1:1
	v_add_u32_e32 v4, 0x14a0, v2
	ds_write2_b32 v4, v24, v25 offset1:1
	v_add_u32_e32 v4, 0x14a8, v2
	ds_write2_b32 v4, v26, v27 offset1:1
	v_add_u32_e32 v4, 0x18c0, v2
	ds_write2_b32 v4, v28, v29 offset1:1
	v_add_u32_e32 v4, 0x18c8, v2
	ds_write2_b32 v4, v30, v31 offset1:1
	v_add_u32_e32 v4, 0x1ce0, v2
	v_add_u32_e32 v2, 0x1ce8, v2
	ds_write2_b32 v4, v32, v33 offset1:1
	ds_write2_b32 v2, v34, v35 offset1:1
	s_waitcnt lgkmcnt(0)
	ds_read2_b32 v[10:11], v49 offset0:33 offset1:41
	ds_read2_b32 v[12:13], v49 offset1:8
	v_lshlrev_b32_e32 v2, 1, v38
	ds_read2_b32 v[14:15], v49 offset0:66 offset1:74
	ds_read2_b32 v[16:17], v49 offset0:99 offset1:107
	ds_read2_b32 v[18:19], v49 offset0:132 offset1:140
	ds_read2_b32 v[20:21], v49 offset0:165 offset1:173
	ds_read2_b32 v[22:23], v49 offset0:198 offset1:206
	ds_read2_b32 v[24:25], v49 offset0:231 offset1:239
	v_lshl_add_u64 v[8:9], s[10:11], 0, v[2:3]
	v_or_b32_e32 v2, s2, v39
	v_mul_u32_u24_e32 v2, 0x1600, v2
	v_lshl_add_u64 v[26:27], v[8:9], 0, v[2:3]
	v_or_b32_e32 v2, s2, v46
	s_waitcnt lgkmcnt(0)
	v_cvt_pk_bf16_f32 v4, v12, v10
	v_mul_u32_u24_e32 v2, 0x1600, v2
	v_cvt_pk_bf16_f32 v5, v14, v16
	v_cvt_pk_bf16_f32 v6, v18, v20
	v_cvt_pk_bf16_f32 v7, v22, v24
	global_store_dwordx4 v[26:27], v[4:7], off sc1
	s_nop 1
	v_cvt_pk_bf16_f32 v4, v13, v11
	v_lshl_add_u64 v[10:11], v[8:9], 0, v[2:3]
	v_cvt_pk_bf16_f32 v5, v15, v17
	v_cvt_pk_bf16_f32 v6, v19, v21
	v_cvt_pk_bf16_f32 v7, v23, v25
	global_store_dwordx4 v[10:11], v[4:7], off sc1
	ds_read2_b32 v[10:11], v49 offset0:16 offset1:24
	ds_read2_b32 v[12:13], v49 offset0:49 offset1:57
	ds_read2_b32 v[14:15], v49 offset0:82 offset1:90
	ds_read2_b32 v[16:17], v49 offset0:115 offset1:123
	ds_read2_b32 v[18:19], v49 offset0:148 offset1:156
	ds_read2_b32 v[20:21], v49 offset0:181 offset1:189
	ds_read2_b32 v[22:23], v49 offset0:214 offset1:222
	ds_read2_b32 v[24:25], v49 offset0:247 offset1:255
	v_or_b32_e32 v2, s2, v47
	v_mul_u32_u24_e32 v2, 0x1600, v2
	v_lshl_add_u64 v[26:27], v[8:9], 0, v[2:3]
	v_or_b32_e32 v2, s2, v48
	v_mul_u32_u24_e32 v2, 0x1600, v2
	s_waitcnt lgkmcnt(6)
	v_cvt_pk_bf16_f32 v4, v10, v12
	s_waitcnt lgkmcnt(4)
	v_cvt_pk_bf16_f32 v5, v14, v16
	s_waitcnt lgkmcnt(2)
	v_cvt_pk_bf16_f32 v6, v18, v20
	s_waitcnt lgkmcnt(0)
	v_cvt_pk_bf16_f32 v7, v22, v24
	v_lshl_add_u64 v[8:9], v[8:9], 0, v[2:3]
	global_store_dwordx4 v[26:27], v[4:7], off sc1
	s_mov_b64 s[2:3], 0
	s_nop 0
	v_cvt_pk_bf16_f32 v4, v11, v13
	v_cvt_pk_bf16_f32 v5, v15, v17
	v_cvt_pk_bf16_f32 v6, v19, v21
	v_cvt_pk_bf16_f32 v7, v23, v25
	global_store_dwordx4 v[8:9], v[4:7], off sc1
	s_waitcnt lgkmcnt(0)
; #define GAS __attribute__((address_space(1)))
; #define LAS __attribute__((address_space(3)))
; #define LDS_WAIT() asm volatile("s_waitcnt lgkmcnt(0)" ::: "memory")
; __device__ __forceinline__ unsigned pk2(float lo, float hi) { unsigned r; asm("v_cvt_pk_bf16_f32 %0, %1, %2" : "=v"(r) : "v"(lo), "v"(hi)); return r; }
; __device__ __forceinline__ void transpose_item(const float* W, int K, int N, bf16* WT, int drow0, int kb, int n0, LAS float* scr, int lane) {
;     const int k0 = 64 * kb; const int c4 = 4 * (lane & 7); const bool ok = (n0 + c4) < N;
;     f32x4 v[8];
; #pragma unroll
;     for (int i = 0; i < 8; ++i) { const int kk = 8 * i + (lane >> 3); v[i] = ok ? *(const f32x4*)(W + (size_t)(k0 + kk) * N + n0 + c4) : (f32x4){0.f, 0.f, 0.f, 0.f}; }
; #pragma unroll
;     for (int i = 0; i < 8; ++i) { const int kk = 8 * i + (lane >> 3); LAS float* d = scr + kk * 33 + c4; d[0] = v[i][0]; d[1] = v[i][1]; d[2] = v[i][2]; d[3] = v[i][3]; }
;     LDS_WAIT(); asm volatile("" ::: "memory");
;     const int c = lane & 7;
; #pragma unroll
;     for (int j = 0; j < 4; ++j) { const int n = (lane >> 3) + 8 * j; const LAS float* s = scr + (8 * c) * 33 + n;
;         v4u o; o.x = pk2(s[0 * 33], s[1 * 33]); o.y = pk2(s[2 * 33], s[3 * 33]); o.z = pk2(s[4 * 33], s[5 * 33]); o.w = pk2(s[6 * 33], s[7 * 33]);
;         *(GAS v4u*)(WT + (size_t)(drow0 + n) * K + k0 + 8 * c) = o; }
;     LDS_WAIT(); asm volatile("" ::: "memory");
; }
; __device__ __forceinline__ void convert_item(const In& I, unsigned char* ws, int it, LAS float* scr, int lane) {
;     ...
;         if (r < 2 * I_G) { const int up = r >= I_G; r -= up * I_G; const int kb = r / 88, nb = r % 88;
;             transpose_item((up ? I.w_up : I.w_gate) + (size_t)f * D * FF, D, FF, Wgu + (size_t)f * NGU * D, 256 * (nb >> 2) + 32 * (nb & 3) + 128 * up, kb, 32 * nb, scr, lane); }
.LBB0_224:
	s_andn2_b64 vcc, exec, s[2:3]
	s_cbranch_vccnz .LBB0_166
	v_readlane_b32 s48, v253, 0
	v_readlane_b32 s49, v253, 1
	v_readlane_b32 s50, v253, 2
	v_readlane_b32 s51, v253, 3
	v_readlane_b32 s52, v253, 4
	v_readlane_b32 s53, v253, 5
	s_cmpk_gt_i32 s7, 0x57f
	v_readlane_b32 s54, v253, 6
	v_readlane_b32 s55, v253, 7
	v_readlane_b32 s56, v253, 8
	v_readlane_b32 s57, v253, 9
	s_mov_b64 s[48:49], s[52:53]
	s_cselect_b32 s2, 0xfffffa80, 0
	s_mul_i32 s3, s6, 0x1080
	s_mov_b64 s[50:51], s[54:55]
	s_cselect_b32 s7, 0x80, 0
	s_cselect_b32 s8, s50, s48
	s_cselect_b32 s9, s51, s49
	s_sub_i32 s2, s2, s3
	s_add_i32 s2, s40, s2
	s_add_i32 s2, s2, 0xa800
	s_mul_hi_i32 s3, s2, 0x2e8ba2e9
	s_lshr_b32 s10, s3, 31
	s_ashr_i32 s3, s3, 4
	s_add_i32 s3, s3, s10
	s_mul_i32 s10, s3, 0x58
	s_sub_i32 s2, s2, s10
	s_mul_hi_i32 s10, s6, 0xb00000
	s_mul_i32 s6, s6, 0xb00000
	s_add_u32 s11, s8, s6
	s_addc_u32 s12, s9, s10
	s_add_u32 s13, s28, s6
	s_addc_u32 s10, s29, s10
	s_lshl_b32 s8, s2, 5
	s_lshl_b32 s6, s2, 6
	s_and_b32 s2, s8, 0x60
	s_and_b32 s6, s6, 0xffffff00
	s_or_b32 s2, s2, s7
	s_ashr_i32 s9, s8, 31
	s_or_b32 s6, s2, s6
	s_lshl_b32 s2, s3, 6
	s_lshl_b64 s[8:9], s[8:9], 2
	s_add_u32 s8, s11, s8
	s_addc_u32 s9, s12, s9
	v_lshlrev_b32_e32 v2, 2, v36
	v_or_b32_e32 v34, s2, v39
	v_lshl_add_u64 v[32:33], s[8:9], 0, v[2:3]
	s_movk_i32 s3, 0x2c00
	v_mad_i64_i32 v[4:5], s[8:9], v34, s3, v[32:33]
	v_or_b32_e32 v2, 8, v34
	global_load_dwordx4 v[4:7], v[4:5], off nt
	v_mad_i64_i32 v[8:9], s[8:9], v2, s3, v[32:33]
	global_load_dwordx4 v[8:11], v[8:9], off nt
	v_or_b32_e32 v2, 16, v34
	v_mad_i64_i32 v[12:13], s[8:9], v2, s3, v[32:33]
	global_load_dwordx4 v[12:15], v[12:13], off nt
	v_or_b32_e32 v2, 24, v34
	v_mad_i64_i32 v[16:17], s[8:9], v2, s3, v[32:33]
	global_load_dwordx4 v[16:19], v[16:17], off nt
	v_or_b32_e32 v2, 32, v34
	v_mad_i64_i32 v[20:21], s[8:9], v2, s3, v[32:33]
	global_load_dwordx4 v[20:23], v[20:21], off nt
	v_or_b32_e32 v2, 40, v34
	v_mad_i64_i32 v[24:25], s[8:9], v2, s3, v[32:33]
	global_load_dwordx4 v[24:27], v[24:25], off nt
	v_or_b32_e32 v2, 48, v34
	v_mad_i64_i32 v[28:29], s[8:9], v2, s3, v[32:33]
	global_load_dwordx4 v[28:31], v[28:29], off nt
	v_or_b32_e32 v2, 56, v34
	v_mad_i64_i32 v[32:33], s[8:9], v2, s3, v[32:33]
	global_load_dwordx4 v[32:35], v[32:33], off nt
	v_add_u32_e32 v2, v44, v45
	s_ashr_i32 s3, s2, 31
	s_lshl_b64 s[2:3], s[2:3], 1
	s_add_u32 s2, s13, s2
	s_addc_u32 s3, s10, s3
	v_readlane_b32 s58, v253, 10
	v_readlane_b32 s59, v253, 11
	v_readlane_b32 s60, v253, 12
	v_readlane_b32 s61, v253, 13
	v_readlane_b32 s62, v253, 14
	v_readlane_b32 s63, v253, 15
	s_mov_b64 s[52:53], s[56:57]
	s_waitcnt vmcnt(0)
	ds_write2_b32 v2, v4, v5 offset1:1
	ds_write2_b32 v2, v6, v7 offset0:2 offset1:3
	v_add_u32_e32 v4, 0x420, v2
	ds_write2_b32 v4, v8, v9 offset1:1
	v_add_u32_e32 v4, 0x428, v2
	ds_write2_b32 v4, v10, v11 offset1:1
	v_add_u32_e32 v4, 0x840, v2
	ds_write2_b32 v4, v12, v13 offset1:1
	v_add_u32_e32 v4, 0x848, v2
	ds_write2_b32 v4, v14, v15 offset1:1
	v_add_u32_e32 v4, 0xc60, v2
	ds_write2_b32 v4, v16, v17 offset1:1
	v_add_u32_e32 v4, 0xc68, v2
	ds_write2_b32 v4, v18, v19 offset1:1
	v_add_u32_e32 v4, 0x1080, v2
	ds_write2_b32 v4, v20, v21 offset1:1
	v_add_u32_e32 v4, 0x1088, v2
	ds_write2_b32 v4, v22, v23 offset1:1
	v_add_u32_e32 v4, 0x14a0, v2
	ds_write2_b32 v4, v24, v25 offset1:1
	v_add_u32_e32 v4, 0x14a8, v2
	ds_write2_b32 v4, v26, v27 offset1:1
	v_add_u32_e32 v4, 0x18c0, v2
	ds_write2_b32 v4, v28, v29 offset1:1
	v_add_u32_e32 v4, 0x18c8, v2
	ds_write2_b32 v4, v30, v31 offset1:1
	v_add_u32_e32 v4, 0x1ce0, v2
	v_add_u32_e32 v2, 0x1ce8, v2
	ds_write2_b32 v4, v32, v33 offset1:1
	ds_write2_b32 v2, v34, v35 offset1:1
	s_waitcnt lgkmcnt(0)
	ds_read2_b32 v[10:11], v49 offset0:33 offset1:41
	ds_read2_b32 v[12:13], v49 offset1:8
	ds_read2_b32 v[14:15], v49 offset0:66 offset1:74
	ds_read2_b32 v[16:17], v49 offset0:99 offset1:107
	ds_read2_b32 v[18:19], v49 offset0:132 offset1:140
	ds_read2_b32 v[20:21], v49 offset0:165 offset1:173
	ds_read2_b32 v[22:23], v49 offset0:198 offset1:206
	ds_read2_b32 v[24:25], v49 offset0:231 offset1:239
	v_or_b32_e32 v26, s6, v39
	v_lshlrev_b32_e32 v2, 1, v38
	v_ashrrev_i32_e32 v27, 31, v26
	v_lshl_add_u64 v[8:9], s[2:3], 0, v[2:3]
	v_lshlrev_b64 v[26:27], 11, v[26:27]
	s_waitcnt lgkmcnt(0)
	v_cvt_pk_bf16_f32 v4, v12, v10
	v_lshl_add_u64 v[26:27], v[8:9], 0, v[26:27]
	v_or_b32_e32 v10, s6, v46
	v_cvt_pk_bf16_f32 v5, v14, v16
	v_cvt_pk_bf16_f32 v6, v18, v20
	v_cvt_pk_bf16_f32 v7, v22, v24
	global_store_dwordx4 v[26:27], v[4:7], off sc1
	v_or_b32_e32 v26, s6, v47
	v_ashrrev_i32_e32 v27, 31, v26
	v_cvt_pk_bf16_f32 v4, v13, v11
	v_ashrrev_i32_e32 v11, 31, v10
	v_lshlrev_b64 v[10:11], 11, v[10:11]
	v_lshl_add_u64 v[10:11], v[8:9], 0, v[10:11]
	v_cvt_pk_bf16_f32 v5, v15, v17
	v_cvt_pk_bf16_f32 v6, v19, v21
	v_cvt_pk_bf16_f32 v7, v23, v25
	global_store_dwordx4 v[10:11], v[4:7], off sc1
	ds_read2_b32 v[10:11], v49 offset0:16 offset1:24
	ds_read2_b32 v[12:13], v49 offset0:49 offset1:57
	ds_read2_b32 v[14:15], v49 offset0:82 offset1:90
	ds_read2_b32 v[16:17], v49 offset0:115 offset1:123
	ds_read2_b32 v[18:19], v49 offset0:148 offset1:156
	ds_read2_b32 v[20:21], v49 offset0:181 offset1:189
	ds_read2_b32 v[22:23], v49 offset0:214 offset1:222
	ds_read2_b32 v[24:25], v49 offset0:247 offset1:255
	v_lshlrev_b64 v[26:27], 11, v[26:27]
	s_waitcnt lgkmcnt(6)
	v_cvt_pk_bf16_f32 v4, v10, v12
	v_lshl_add_u64 v[26:27], v[8:9], 0, v[26:27]
	v_or_b32_e32 v10, s6, v48
	s_waitcnt lgkmcnt(4)
	v_cvt_pk_bf16_f32 v5, v14, v16
	s_waitcnt lgkmcnt(2)
	v_cvt_pk_bf16_f32 v6, v18, v20
	s_waitcnt lgkmcnt(0)
	v_cvt_pk_bf16_f32 v7, v22, v24
	global_store_dwordx4 v[26:27], v[4:7], off sc1
	s_nop 1
	v_cvt_pk_bf16_f32 v4, v11, v13
	v_ashrrev_i32_e32 v11, 31, v10
	v_lshlrev_b64 v[10:11], 11, v[10:11]
	v_lshl_add_u64 v[8:9], v[8:9], 0, v[10:11]
	v_cvt_pk_bf16_f32 v5, v15, v17
	v_cvt_pk_bf16_f32 v6, v19, v21
	v_cvt_pk_bf16_f32 v7, v23, v25
	global_store_dwordx4 v[8:9], v[4:7], off sc1
	s_waitcnt lgkmcnt(0)
	s_branch .LBB0_166

; #define GAS __attribute__((address_space(1)))
; #define LAS __attribute__((address_space(3)))
; #define LDS_WAIT() asm volatile("s_waitcnt lgkmcnt(0)" ::: "memory")
; __device__ __forceinline__ unsigned pk2(float lo, float hi) { unsigned r; asm("v_cvt_pk_bf16_f32 %0, %1, %2" : "=v"(r) : "v"(lo), "v"(hi)); return r; }
; __device__ __forceinline__ void transpose_item(const float* W, int K, int N, bf16* WT, int drow0, int kb, int n0, LAS float* scr, int lane) {
;     const int k0 = 64 * kb; const int c4 = 4 * (lane & 7); const bool ok = (n0 + c4) < N;
;     f32x4 v[8];
; #pragma unroll
;     for (int i = 0; i < 8; ++i) { const int kk = 8 * i + (lane >> 3); v[i] = ok ? *(const f32x4*)(W + (size_t)(k0 + kk) * N + n0 + c4) : (f32x4){0.f, 0.f, 0.f, 0.f}; }
; #pragma unroll
;     for (int i = 0; i < 8; ++i) { const int kk = 8 * i + (lane >> 3); LAS float* d = scr + kk * 33 + c4; d[0] = v[i][0]; d[1] = v[i][1]; d[2] = v[i][2]; d[3] = v[i][3]; }
;     LDS_WAIT(); asm volatile("" ::: "memory");
;     const int c = lane & 7;
; #pragma unroll
;     for (int j = 0; j < 4; ++j) { const int n = (lane >> 3) + 8 * j; const LAS float* s = scr + (8 * c) * 33 + n;
;         v4u o; o.x = pk2(s[0 * 33], s[1 * 33]); o.y = pk2(s[2 * 33], s[3 * 33]); o.z = pk2(s[4 * 33], s[5 * 33]); o.w = pk2(s[6 * 33], s[7 * 33]);
;         *(GAS v4u*)(WT + (size_t)(drow0 + n) * K + k0 + 8 * c) = o; }
;     LDS_WAIT(); asm volatile("" ::: "memory");
; }
; __device__ __forceinline__ void convert_item(const In& I, unsigned char* ws, int it, LAS float* scr, int lane) {
;     ...
;     { const int jk = r >> 3; r &= 7; const int kb = r >> 1, nb = r & 1;
;         transpose_item(I.nsa_w2 + (size_t)jk * 256 * 64, 256, 64, W2t + (size_t)jk * 64 * 256, 32 * nb, kb, 32 * nb, scr, lane); }
.LBB0_229:
	s_add_i32 s44, s40, 0xa800
	s_cmp_gt_i32 s44, 0x83ff
	s_mov_b64 s[2:3], -1
	s_cbranch_scc0 .LBB0_283
	s_cmpk_gt_u32 s44, 0x8eff
	s_cbranch_scc0 .LBB0_264
	s_cmpk_gt_u32 s44, 0x92ff
	s_cbranch_scc0 .LBB0_261
	s_cmpk_gt_u32 s44, 0x9fff
	s_cbranch_scc0 .LBB0_242
	s_cmpk_gt_u32 s44, 0xa3ff
	s_cbranch_scc0 .LBB0_239
	s_cmpk_gt_u32 s44, 0xa7ff
	s_cbranch_scc0 .LBB0_236
	s_lshr_b32 s68, s40, 3
	v_readlane_b32 s48, v253, 16
	s_lshl_b64 s[2:3], s[68:69], 16
	v_readlane_b32 s52, v253, 20
	v_readlane_b32 s53, v253, 21
	s_add_u32 s6, s52, s2
	s_addc_u32 s7, s53, s3
	s_lshl_b64 s[2:3], s[68:69], 15
	s_add_u32 s8, s35, s2
	s_addc_u32 s3, s39, s3
	s_and_b32 s2, s42, 32
	s_and_b32 s9, s42, 0xc0
	s_lshl_b32 s10, s2, 2
	s_add_u32 s6, s6, s10
	v_or_b32_e32 v6, s9, v39
	s_addc_u32 s7, s7, 0
	v_lshlrev_b32_e32 v2, 2, v36
	v_lshl_add_u64 v[4:5], s[6:7], 0, v[2:3]
	v_lshlrev_b32_e32 v2, 8, v6
	v_lshl_add_u64 v[28:29], v[4:5], 0, v[2:3]
	global_load_dwordx4 v[4:7], v[28:29], off nt
	global_load_dwordx4 v[8:11], v[28:29], off offset:2048 nt
	v_add_co_u32_e32 v16, vcc, s84, v28
	s_movk_i32 s6, 0x3000
	s_nop 0
	v_addc_co_u32_e32 v17, vcc, 0, v29, vcc
	v_add_co_u32_e32 v24, vcc, s74, v28
	v_add_u32_e32 v2, v44, v45
	s_nop 0
	v_addc_co_u32_e32 v25, vcc, 0, v29, vcc
	global_load_dwordx4 v[12:15], v[24:25], off offset:-4096 nt
	s_nop 0
	global_load_dwordx4 v[16:19], v[16:17], off offset:2048 nt
	s_nop 0
	global_load_dwordx4 v[20:23], v[24:25], off nt
	s_nop 0
	global_load_dwordx4 v[24:27], v[24:25], off offset:2048 nt
	v_add_co_u32_e32 v32, vcc, s6, v28
	s_lshl_b32 s6, s9, 1
	s_nop 0
	v_addc_co_u32_e32 v33, vcc, 0, v29, vcc
	global_load_dwordx4 v[28:31], v[32:33], off nt
	s_nop 0
	global_load_dwordx4 v[32:35], v[32:33], off offset:2048 nt
	s_add_u32 s6, s8, s6
	s_addc_u32 s7, s3, 0
	v_readlane_b32 s49, v253, 17
	v_readlane_b32 s50, v253, 18
	v_readlane_b32 s51, v253, 19
	v_readlane_b32 s54, v253, 22
	v_readlane_b32 s55, v253, 23
	v_readlane_b32 s56, v253, 24
	v_readlane_b32 s57, v253, 25
	v_readlane_b32 s58, v253, 26
	v_readlane_b32 s59, v253, 27
	v_readlane_b32 s60, v253, 28
	v_readlane_b32 s61, v253, 29
	v_readlane_b32 s62, v253, 30
	v_readlane_b32 s63, v253, 31
	s_waitcnt vmcnt(0)
	ds_write2_b32 v2, v4, v5 offset1:1
	ds_write2_b32 v2, v6, v7 offset0:2 offset1:3
	v_add_u32_e32 v4, 0x420, v2
	ds_write2_b32 v4, v8, v9 offset1:1
	v_add_u32_e32 v4, 0x428, v2
	ds_write2_b32 v4, v10, v11 offset1:1
	v_add_u32_e32 v4, 0x840, v2
	ds_write2_b32 v4, v12, v13 offset1:1
	v_add_u32_e32 v4, 0x848, v2
	ds_write2_b32 v4, v14, v15 offset1:1
	v_add_u32_e32 v4, 0xc60, v2
	ds_write2_b32 v4, v16, v17 offset1:1
	v_add_u32_e32 v4, 0xc68, v2
	ds_write2_b32 v4, v18, v19 offset1:1
	v_add_u32_e32 v4, 0x1080, v2
	ds_write2_b32 v4, v20, v21 offset1:1
	v_add_u32_e32 v4, 0x1088, v2
	ds_write2_b32 v4, v22, v23 offset1:1
	v_add_u32_e32 v4, 0x14a0, v2
	ds_write2_b32 v4, v24, v25 offset1:1
	v_add_u32_e32 v4, 0x14a8, v2
	ds_write2_b32 v4, v26, v27 offset1:1
	v_add_u32_e32 v4, 0x18c0, v2
	ds_write2_b32 v4, v28, v29 offset1:1
	v_add_u32_e32 v4, 0x18c8, v2
	ds_write2_b32 v4, v30, v31 offset1:1
	v_add_u32_e32 v4, 0x1ce0, v2
	v_add_u32_e32 v2, 0x1ce8, v2
	ds_write2_b32 v4, v32, v33 offset1:1
	ds_write2_b32 v2, v34, v35 offset1:1
	s_waitcnt lgkmcnt(0)
	ds_read2_b32 v[10:11], v49 offset0:33 offset1:41
	ds_read2_b32 v[12:13], v49 offset1:8
	v_lshlrev_b32_e32 v2, 1, v38
	ds_read2_b32 v[14:15], v49 offset0:66 offset1:74
	ds_read2_b32 v[16:17], v49 offset0:99 offset1:107
	ds_read2_b32 v[18:19], v49 offset0:132 offset1:140
	ds_read2_b32 v[20:21], v49 offset0:165 offset1:173
	ds_read2_b32 v[22:23], v49 offset0:198 offset1:206
	ds_read2_b32 v[24:25], v49 offset0:231 offset1:239
	v_lshl_add_u64 v[4:5], s[6:7], 0, v[2:3]
	v_or_b32_e32 v2, s2, v39
	v_lshlrev_b32_e32 v2, 9, v2
	v_lshl_add_u64 v[26:27], v[4:5], 0, v[2:3]
	v_or_b32_e32 v2, s2, v46
	s_waitcnt lgkmcnt(0)
	v_cvt_pk_bf16_f32 v6, v12, v10
	v_lshlrev_b32_e32 v2, 9, v2
	v_cvt_pk_bf16_f32 v7, v14, v16
	v_cvt_pk_bf16_f32 v8, v18, v20
	v_cvt_pk_bf16_f32 v9, v22, v24
	global_store_dwordx4 v[26:27], v[6:9], off sc1
	s_nop 1
	v_cvt_pk_bf16_f32 v6, v13, v11
	v_lshl_add_u64 v[10:11], v[4:5], 0, v[2:3]
	v_cvt_pk_bf16_f32 v7, v15, v17
	v_cvt_pk_bf16_f32 v8, v19, v21
	v_cvt_pk_bf16_f32 v9, v23, v25
	global_store_dwordx4 v[10:11], v[6:9], off sc1
	ds_read2_b32 v[10:11], v49 offset0:16 offset1:24
	ds_read2_b32 v[12:13], v49 offset0:49 offset1:57
	ds_read2_b32 v[14:15], v49 offset0:82 offset1:90
	ds_read2_b32 v[16:17], v49 offset0:115 offset1:123
	ds_read2_b32 v[18:19], v49 offset0:148 offset1:156
	ds_read2_b32 v[20:21], v49 offset0:181 offset1:189
	ds_read2_b32 v[22:23], v49 offset0:214 offset1:222
	ds_read2_b32 v[24:25], v49 offset0:247 offset1:255
	v_or_b32_e32 v2, s2, v47
	v_lshlrev_b32_e32 v2, 9, v2
	v_lshl_add_u64 v[26:27], v[4:5], 0, v[2:3]
	v_or_b32_e32 v2, s2, v48
	v_lshlrev_b32_e32 v2, 9, v2
	s_waitcnt lgkmcnt(6)
	v_cvt_pk_bf16_f32 v6, v10, v12
	s_waitcnt lgkmcnt(4)
	v_cvt_pk_bf16_f32 v7, v14, v16
	s_waitcnt lgkmcnt(2)
	v_cvt_pk_bf16_f32 v8, v18, v20
	s_waitcnt lgkmcnt(0)
	v_cvt_pk_bf16_f32 v9, v22, v24
	v_lshl_add_u64 v[4:5], v[4:5], 0, v[2:3]
	global_store_dwordx4 v[26:27], v[6:9], off sc1
	s_mov_b64 s[2:3], 0
	s_nop 0
	v_cvt_pk_bf16_f32 v6, v11, v13
	v_cvt_pk_bf16_f32 v7, v15, v17
	v_cvt_pk_bf16_f32 v8, v19, v21
	v_cvt_pk_bf16_f32 v9, v23, v25
	global_store_dwordx4 v[4:5], v[6:9], off sc1
	s_waitcnt lgkmcnt(0)

; #define GAS __attribute__((address_space(1)))
; #define LAS __attribute__((address_space(3)))
; #define LDS_WAIT() asm volatile("s_waitcnt lgkmcnt(0)" ::: "memory")
; __device__ __forceinline__ unsigned pk2(float lo, float hi) { unsigned r; asm("v_cvt_pk_bf16_f32 %0, %1, %2" : "=v"(r) : "v"(lo), "v"(hi)); return r; }
; __device__ __forceinline__ void transpose_item(const float* W, int K, int N, bf16* WT, int drow0, int kb, int n0, LAS float* scr, int lane) {
;     const int k0 = 64 * kb; const int c4 = 4 * (lane & 7); const bool ok = (n0 + c4) < N;
;     f32x4 v[8];
; #pragma unroll
;     for (int i = 0; i < 8; ++i) { const int kk = 8 * i + (lane >> 3); v[i] = ok ? *(const f32x4*)(W + (size_t)(k0 + kk) * N + n0 + c4) : (f32x4){0.f, 0.f, 0.f, 0.f}; }
; #pragma unroll
;     for (int i = 0; i < 8; ++i) { const int kk = 8 * i + (lane >> 3); LAS float* d = scr + kk * 33 + c4; d[0] = v[i][0]; d[1] = v[i][1]; d[2] = v[i][2]; d[3] = v[i][3]; }
;     LDS_WAIT(); asm volatile("" ::: "memory");
;     const int c = lane & 7;
; #pragma unroll
;     for (int j = 0; j < 4; ++j) { const int n = (lane >> 3) + 8 * j; const LAS float* s = scr + (8 * c) * 33 + n;
;         v4u o; o.x = pk2(s[0 * 33], s[1 * 33]); o.y = pk2(s[2 * 33], s[3 * 33]); o.z = pk2(s[4 * 33], s[5 * 33]); o.w = pk2(s[6 * 33], s[7 * 33]);
;         *(GAS v4u*)(WT + (size_t)(drow0 + n) * K + k0 + 8 * c) = o; }
;     LDS_WAIT(); asm volatile("" ::: "memory");
; }
; __device__ __forceinline__ void convert_item(const In& I, unsigned char* ws, int it, LAS float* scr, int lane) {
;     ...
;     if (r < 2 * I_SQ) { const int j = r / I_SQ; r -= j * I_SQ; const int kb = r / 32, nb = r % 32;
;         transpose_item(I.fox_w_out + (size_t)j * D * D, D, D, Wfout + (size_t)j * D * D, 32 * nb, kb, 32 * nb, scr, lane); return; }
.LBB0_239:
	s_andn2_b64 vcc, exec, s[2:3]
	s_cbranch_vccnz .LBB0_241
	s_add_i32 s2, s40, 0x800
	s_lshr_b32 s68, s2, 9
	v_readlane_b32 s48, v253, 16
	s_lshl_b64 s[2:3], s[68:69], 22
	v_readlane_b32 s60, v253, 28
	v_readlane_b32 s61, v253, 29
	s_add_u32 s6, s60, s2
	s_addc_u32 s7, s61, s3
	s_lshl_b64 s[2:3], s[68:69], 21
	s_add_u32 s8, s27, s2
	s_addc_u32 s3, s31, s3
	s_and_b32 s2, s42, 0x3e0
	s_add_i32 s9, s43, 0x13800
	s_and_b32 s9, s9, 0x3c0
	s_lshl_b32 s10, s2, 2
	s_add_u32 s6, s6, s10
	v_or_b32_e32 v6, s9, v39
	s_addc_u32 s7, s7, 0
	v_lshlrev_b32_e32 v2, 2, v36
	v_lshl_add_u64 v[4:5], s[6:7], 0, v[2:3]
	v_lshlrev_b32_e32 v2, 12, v6
	v_lshl_add_u64 v[32:33], v[4:5], 0, v[2:3]
	v_add_co_u32_e32 v8, vcc, s81, v32
	global_load_dwordx4 v[4:7], v[32:33], off nt
	s_nop 0
	v_addc_co_u32_e32 v9, vcc, 0, v33, vcc
	global_load_dwordx4 v[8:11], v[8:9], off nt
	v_add_co_u32_e32 v12, vcc, s79, v32
	v_add_u32_e32 v2, v44, v45
	s_nop 0
	v_addc_co_u32_e32 v13, vcc, 0, v33, vcc
	global_load_dwordx4 v[12:15], v[12:13], off nt
	v_add_co_u32_e32 v16, vcc, s80, v32
	s_lshl_b32 s6, s9, 1
	s_nop 0
	v_addc_co_u32_e32 v17, vcc, 0, v33, vcc
	global_load_dwordx4 v[16:19], v[16:17], off nt
	v_add_co_u32_e32 v20, vcc, s85, v32
	s_add_u32 s6, s8, s6
	s_nop 0
	v_addc_co_u32_e32 v21, vcc, 0, v33, vcc
	global_load_dwordx4 v[20:23], v[20:21], off nt
	v_add_co_u32_e32 v24, vcc, s86, v32
	s_addc_u32 s7, s3, 0
	s_nop 0
	v_addc_co_u32_e32 v25, vcc, 0, v33, vcc
	global_load_dwordx4 v[24:27], v[24:25], off nt
	v_add_co_u32_e32 v28, vcc, s87, v32
	v_readlane_b32 s49, v253, 17
	s_nop 0
	v_addc_co_u32_e32 v29, vcc, 0, v33, vcc
	global_load_dwordx4 v[28:31], v[28:29], off nt
	v_add_co_u32_e32 v32, vcc, s89, v32
	v_readlane_b32 s50, v253, 18
	s_nop 0
	v_addc_co_u32_e32 v33, vcc, 0, v33, vcc
	global_load_dwordx4 v[32:35], v[32:33], off nt
	v_readlane_b32 s51, v253, 19
	v_readlane_b32 s52, v253, 20
	v_readlane_b32 s53, v253, 21
	v_readlane_b32 s54, v253, 22
	v_readlane_b32 s55, v253, 23
	v_readlane_b32 s56, v253, 24
	v_readlane_b32 s57, v253, 25
	v_readlane_b32 s58, v253, 26
	v_readlane_b32 s59, v253, 27
	v_readlane_b32 s62, v253, 30
	v_readlane_b32 s63, v253, 31
	s_waitcnt vmcnt(0)
	ds_write2_b32 v2, v4, v5 offset1:1
	ds_write2_b32 v2, v6, v7 offset0:2 offset1:3
	v_add_u32_e32 v4, 0x420, v2
	ds_write2_b32 v4, v8, v9 offset1:1
	v_add_u32_e32 v4, 0x428, v2
	ds_write2_b32 v4, v10, v11 offset1:1
	v_add_u32_e32 v4, 0x840, v2
	ds_write2_b32 v4, v12, v13 offset1:1
	v_add_u32_e32 v4, 0x848, v2
	ds_write2_b32 v4, v14, v15 offset1:1
	v_add_u32_e32 v4, 0xc60, v2
	ds_write2_b32 v4, v16, v17 offset1:1
	v_add_u32_e32 v4, 0xc68, v2
	ds_write2_b32 v4, v18, v19 offset1:1
	v_add_u32_e32 v4, 0x1080, v2
	ds_write2_b32 v4, v20, v21 offset1:1
	v_add_u32_e32 v4, 0x1088, v2
	ds_write2_b32 v4, v22, v23 offset1:1
	v_add_u32_e32 v4, 0x14a0, v2
	ds_write2_b32 v4, v24, v25 offset1:1
	v_add_u32_e32 v4, 0x14a8, v2
	ds_write2_b32 v4, v26, v27 offset1:1
	v_add_u32_e32 v4, 0x18c0, v2
	ds_write2_b32 v4, v28, v29 offset1:1
	v_add_u32_e32 v4, 0x18c8, v2
	ds_write2_b32 v4, v30, v31 offset1:1
	v_add_u32_e32 v4, 0x1ce0, v2
	v_add_u32_e32 v2, 0x1ce8, v2
	ds_write2_b32 v4, v32, v33 offset1:1
	ds_write2_b32 v2, v34, v35 offset1:1
	s_waitcnt lgkmcnt(0)
	ds_read2_b32 v[10:11], v49 offset0:33 offset1:41
	ds_read2_b32 v[12:13], v49 offset1:8
	v_lshlrev_b32_e32 v2, 1, v38
	ds_read2_b32 v[14:15], v49 offset0:66 offset1:74
	ds_read2_b32 v[16:17], v49 offset0:99 offset1:107
	ds_read2_b32 v[18:19], v49 offset0:132 offset1:140
	ds_read2_b32 v[20:21], v49 offset0:165 offset1:173
	ds_read2_b32 v[22:23], v49 offset0:198 offset1:206
	ds_read2_b32 v[24:25], v49 offset0:231 offset1:239
	v_lshl_add_u64 v[8:9], s[6:7], 0, v[2:3]
	v_or_b32_e32 v2, s2, v39
	v_lshlrev_b32_e32 v2, 11, v2
	v_lshl_add_u64 v[26:27], v[8:9], 0, v[2:3]
	v_or_b32_e32 v2, s2, v46
	s_waitcnt lgkmcnt(0)
	v_cvt_pk_bf16_f32 v4, v12, v10
	v_lshlrev_b32_e32 v2, 11, v2
	v_cvt_pk_bf16_f32 v5, v14, v16
	v_cvt_pk_bf16_f32 v6, v18, v20
	v_cvt_pk_bf16_f32 v7, v22, v24
	global_store_dwordx4 v[26:27], v[4:7], off sc1
	s_nop 1
	v_cvt_pk_bf16_f32 v4, v13, v11
	v_lshl_add_u64 v[10:11], v[8:9], 0, v[2:3]
	v_cvt_pk_bf16_f32 v5, v15, v17
	v_cvt_pk_bf16_f32 v6, v19, v21
	v_cvt_pk_bf16_f32 v7, v23, v25
	global_store_dwordx4 v[10:11], v[4:7], off sc1
	ds_read2_b32 v[10:11], v49 offset0:16 offset1:24
	ds_read2_b32 v[12:13], v49 offset0:49 offset1:57
	ds_read2_b32 v[14:15], v49 offset0:82 offset1:90
	ds_read2_b32 v[16:17], v49 offset0:115 offset1:123
	ds_read2_b32 v[18:19], v49 offset0:148 offset1:156
	ds_read2_b32 v[20:21], v49 offset0:181 offset1:189
	ds_read2_b32 v[22:23], v49 offset0:214 offset1:222
	ds_read2_b32 v[24:25], v49 offset0:247 offset1:255
	v_or_b32_e32 v2, s2, v47
	v_lshlrev_b32_e32 v2, 11, v2
	v_lshl_add_u64 v[26:27], v[8:9], 0, v[2:3]
	v_or_b32_e32 v2, s2, v48
	v_lshlrev_b32_e32 v2, 11, v2
	s_waitcnt lgkmcnt(6)
	v_cvt_pk_bf16_f32 v4, v10, v12
	s_waitcnt lgkmcnt(4)
	v_cvt_pk_bf16_f32 v5, v14, v16
	s_waitcnt lgkmcnt(2)
	v_cvt_pk_bf16_f32 v6, v18, v20
	s_waitcnt lgkmcnt(0)
	v_cvt_pk_bf16_f32 v7, v22, v24
	v_lshl_add_u64 v[8:9], v[8:9], 0, v[2:3]
	global_store_dwordx4 v[26:27], v[4:7], off sc1
	s_nop 1
	v_cvt_pk_bf16_f32 v4, v11, v13
	v_cvt_pk_bf16_f32 v5, v15, v17
	v_cvt_pk_bf16_f32 v6, v19, v21
	v_cvt_pk_bf16_f32 v7, v23, v25
	global_store_dwordx4 v[8:9], v[4:7], off sc1
	s_waitcnt lgkmcnt(0)

; #define GAS __attribute__((address_space(1)))
; #define LAS __attribute__((address_space(3)))
; #define LDS_WAIT() asm volatile("s_waitcnt lgkmcnt(0)" ::: "memory")
; __device__ __forceinline__ unsigned pk2(float lo, float hi) { unsigned r; asm("v_cvt_pk_bf16_f32 %0, %1, %2" : "=v"(r) : "v"(lo), "v"(hi)); return r; }
; __device__ __forceinline__ void transpose_item(const float* W, int K, int N, bf16* WT, int drow0, int kb, int n0, LAS float* scr, int lane) {
;     const int k0 = 64 * kb; const int c4 = 4 * (lane & 7); const bool ok = (n0 + c4) < N;
;     f32x4 v[8];
; #pragma unroll
;     for (int i = 0; i < 8; ++i) { const int kk = 8 * i + (lane >> 3); v[i] = ok ? *(const f32x4*)(W + (size_t)(k0 + kk) * N + n0 + c4) : (f32x4){0.f, 0.f, 0.f, 0.f}; }
; #pragma unroll
;     for (int i = 0; i < 8; ++i) { const int kk = 8 * i + (lane >> 3); LAS float* d = scr + kk * 33 + c4; d[0] = v[i][0]; d[1] = v[i][1]; d[2] = v[i][2]; d[3] = v[i][3]; }
;     LDS_WAIT(); asm volatile("" ::: "memory");
;     const int c = lane & 7;
; #pragma unroll
;     for (int j = 0; j < 4; ++j) { const int n = (lane >> 3) + 8 * j; const LAS float* s = scr + (8 * c) * 33 + n;
;         v4u o; o.x = pk2(s[0 * 33], s[1 * 33]); o.y = pk2(s[2 * 33], s[3 * 33]); o.z = pk2(s[4 * 33], s[5 * 33]); o.w = pk2(s[6 * 33], s[7 * 33]);
;         *(GAS v4u*)(WT + (size_t)(drow0 + n) * K + k0 + 8 * c) = o; }
;     LDS_WAIT(); asm volatile("" ::: "memory");
; }
; __device__ __forceinline__ void convert_item(const In& I, unsigned char* ws, int it, LAS float* scr, int lane) {
;     ...
;     if (r < 2 * I_SQ) { const int j = r / I_SQ; r -= j * I_SQ; const int kb = r / 32, nb = r % 32;
;         transpose_item(I.nsa_w_out + (size_t)j * D * D, D, D, Wnout + (size_t)j * D * D, 32 * nb, kb, 32 * nb, scr, lane); return; }
.LBB0_261:
	s_andn2_b64 vcc, exec, s[2:3]
	s_cbranch_vccnz .LBB0_263
	s_add_i32 s2, s40, 0x1900
	s_lshr_b32 s68, s2, 9
	v_readlane_b32 s48, v253, 16
	s_lshl_b64 s[2:3], s[68:69], 22
	v_readlane_b32 s54, v253, 22
	v_readlane_b32 s55, v253, 23
	s_add_u32 s6, s54, s2
	s_addc_u32 s7, s55, s3
	s_lshl_b64 s[2:3], s[68:69], 21
	s_add_u32 s8, s23, s2
	s_addc_u32 s3, s24, s3
	s_and_b32 s2, s42, 0x3e0
	s_add_i32 s9, s43, 0x1a00
	s_and_b32 s9, s9, 0x3c0
	s_lshl_b32 s10, s2, 2
	s_add_u32 s6, s6, s10
	v_or_b32_e32 v6, s9, v39
	s_addc_u32 s7, s7, 0
	v_lshlrev_b32_e32 v2, 2, v36
	v_lshl_add_u64 v[4:5], s[6:7], 0, v[2:3]
	v_lshlrev_b32_e32 v2, 12, v6
	v_lshl_add_u64 v[32:33], v[4:5], 0, v[2:3]
	v_add_co_u32_e32 v8, vcc, s81, v32
	global_load_dwordx4 v[4:7], v[32:33], off nt
	s_nop 0
	v_addc_co_u32_e32 v9, vcc, 0, v33, vcc
	global_load_dwordx4 v[8:11], v[8:9], off nt
	v_add_co_u32_e32 v12, vcc, s79, v32
	v_add_u32_e32 v2, v44, v45
	s_nop 0
	v_addc_co_u32_e32 v13, vcc, 0, v33, vcc
	global_load_dwordx4 v[12:15], v[12:13], off nt
	v_add_co_u32_e32 v16, vcc, s80, v32
	s_lshl_b32 s6, s9, 1
	s_nop 0
	v_addc_co_u32_e32 v17, vcc, 0, v33, vcc
	global_load_dwordx4 v[16:19], v[16:17], off nt
	v_add_co_u32_e32 v20, vcc, s85, v32
	s_add_u32 s6, s8, s6
	s_nop 0
	v_addc_co_u32_e32 v21, vcc, 0, v33, vcc
	global_load_dwordx4 v[20:23], v[20:21], off nt
	v_add_co_u32_e32 v24, vcc, s86, v32
	s_addc_u32 s7, s3, 0
	s_nop 0
	v_addc_co_u32_e32 v25, vcc, 0, v33, vcc
	global_load_dwordx4 v[24:27], v[24:25], off nt
	v_add_co_u32_e32 v28, vcc, s87, v32
	v_readlane_b32 s49, v253, 17
	s_nop 0
	v_addc_co_u32_e32 v29, vcc, 0, v33, vcc
	global_load_dwordx4 v[28:31], v[28:29], off nt
	v_add_co_u32_e32 v32, vcc, s89, v32
	v_readlane_b32 s50, v253, 18
	s_nop 0
	v_addc_co_u32_e32 v33, vcc, 0, v33, vcc
	global_load_dwordx4 v[32:35], v[32:33], off nt
	v_readlane_b32 s51, v253, 19
	v_readlane_b32 s52, v253, 20
	v_readlane_b32 s53, v253, 21
	v_readlane_b32 s56, v253, 24
	v_readlane_b32 s57, v253, 25
	v_readlane_b32 s58, v253, 26
	v_readlane_b32 s59, v253, 27
	v_readlane_b32 s60, v253, 28
	v_readlane_b32 s61, v253, 29
	v_readlane_b32 s62, v253, 30
	v_readlane_b32 s63, v253, 31
	s_waitcnt vmcnt(0)
	ds_write2_b32 v2, v4, v5 offset1:1
	ds_write2_b32 v2, v6, v7 offset0:2 offset1:3
	v_add_u32_e32 v4, 0x420, v2
	ds_write2_b32 v4, v8, v9 offset1:1
	v_add_u32_e32 v4, 0x428, v2
	ds_write2_b32 v4, v10, v11 offset1:1
	v_add_u32_e32 v4, 0x840, v2
	ds_write2_b32 v4, v12, v13 offset1:1
	v_add_u32_e32 v4, 0x848, v2
	ds_write2_b32 v4, v14, v15 offset1:1
	v_add_u32_e32 v4, 0xc60, v2
	ds_write2_b32 v4, v16, v17 offset1:1
	v_add_u32_e32 v4, 0xc68, v2
	ds_write2_b32 v4, v18, v19 offset1:1
	v_add_u32_e32 v4, 0x1080, v2
	ds_write2_b32 v4, v20, v21 offset1:1
	v_add_u32_e32 v4, 0x1088, v2
	ds_write2_b32 v4, v22, v23 offset1:1
	v_add_u32_e32 v4, 0x14a0, v2
	ds_write2_b32 v4, v24, v25 offset1:1
	v_add_u32_e32 v4, 0x14a8, v2
	ds_write2_b32 v4, v26, v27 offset1:1
	v_add_u32_e32 v4, 0x18c0, v2
	ds_write2_b32 v4, v28, v29 offset1:1
	v_add_u32_e32 v4, 0x18c8, v2
	ds_write2_b32 v4, v30, v31 offset1:1
	v_add_u32_e32 v4, 0x1ce0, v2
	v_add_u32_e32 v2, 0x1ce8, v2
	ds_write2_b32 v4, v32, v33 offset1:1
	ds_write2_b32 v2, v34, v35 offset1:1
	s_waitcnt lgkmcnt(0)
	ds_read2_b32 v[10:11], v49 offset0:33 offset1:41
	ds_read2_b32 v[12:13], v49 offset1:8
	v_lshlrev_b32_e32 v2, 1, v38
	ds_read2_b32 v[14:15], v49 offset0:66 offset1:74
	ds_read2_b32 v[16:17], v49 offset0:99 offset1:107
	ds_read2_b32 v[18:19], v49 offset0:132 offset1:140
	ds_read2_b32 v[20:21], v49 offset0:165 offset1:173
	ds_read2_b32 v[22:23], v49 offset0:198 offset1:206
	ds_read2_b32 v[24:25], v49 offset0:231 offset1:239
	v_lshl_add_u64 v[8:9], s[6:7], 0, v[2:3]
	v_or_b32_e32 v2, s2, v39
	v_lshlrev_b32_e32 v2, 11, v2
	v_lshl_add_u64 v[26:27], v[8:9], 0, v[2:3]
	v_or_b32_e32 v2, s2, v46
	s_waitcnt lgkmcnt(0)
	v_cvt_pk_bf16_f32 v4, v12, v10
	v_lshlrev_b32_e32 v2, 11, v2
	v_cvt_pk_bf16_f32 v5, v14, v16
	v_cvt_pk_bf16_f32 v6, v18, v20
	v_cvt_pk_bf16_f32 v7, v22, v24
	global_store_dwordx4 v[26:27], v[4:7], off sc1
	s_nop 1
	v_cvt_pk_bf16_f32 v4, v13, v11
	v_lshl_add_u64 v[10:11], v[8:9], 0, v[2:3]
	v_cvt_pk_bf16_f32 v5, v15, v17
	v_cvt_pk_bf16_f32 v6, v19, v21
	v_cvt_pk_bf16_f32 v7, v23, v25
	global_store_dwordx4 v[10:11], v[4:7], off sc1
	ds_read2_b32 v[10:11], v49 offset0:16 offset1:24
	ds_read2_b32 v[12:13], v49 offset0:49 offset1:57
	ds_read2_b32 v[14:15], v49 offset0:82 offset1:90
	ds_read2_b32 v[16:17], v49 offset0:115 offset1:123
	ds_read2_b32 v[18:19], v49 offset0:148 offset1:156
	ds_read2_b32 v[20:21], v49 offset0:181 offset1:189
	ds_read2_b32 v[22:23], v49 offset0:214 offset1:222
	ds_read2_b32 v[24:25], v49 offset0:247 offset1:255
	v_or_b32_e32 v2, s2, v47
	v_lshlrev_b32_e32 v2, 11, v2
	v_lshl_add_u64 v[26:27], v[8:9], 0, v[2:3]
	v_or_b32_e32 v2, s2, v48
	v_lshlrev_b32_e32 v2, 11, v2
	s_waitcnt lgkmcnt(6)
	v_cvt_pk_bf16_f32 v4, v10, v12
	s_waitcnt lgkmcnt(4)
	v_cvt_pk_bf16_f32 v5, v14, v16
	s_waitcnt lgkmcnt(2)
	v_cvt_pk_bf16_f32 v6, v18, v20
	s_waitcnt lgkmcnt(0)
	v_cvt_pk_bf16_f32 v7, v22, v24
	v_lshl_add_u64 v[8:9], v[8:9], 0, v[2:3]
	global_store_dwordx4 v[26:27], v[4:7], off sc1
	s_nop 1
	v_cvt_pk_bf16_f32 v4, v11, v13
	v_cvt_pk_bf16_f32 v5, v15, v17
	v_cvt_pk_bf16_f32 v6, v19, v21
	v_cvt_pk_bf16_f32 v7, v23, v25
	global_store_dwordx4 v[8:9], v[4:7], off sc1
	s_waitcnt lgkmcnt(0)

; #define GAS __attribute__((address_space(1)))
; #define LAS __attribute__((address_space(3)))
; #define LDS_WAIT() asm volatile("s_waitcnt lgkmcnt(0)" ::: "memory")
; __device__ __forceinline__ unsigned pk2(float lo, float hi) { unsigned r; asm("v_cvt_pk_bf16_f32 %0, %1, %2" : "=v"(r) : "v"(lo), "v"(hi)); return r; }
; __device__ __forceinline__ void transpose_item(const float* W, int K, int N, bf16* WT, int drow0, int kb, int n0, LAS float* scr, int lane) {
;     const int k0 = 64 * kb; const int c4 = 4 * (lane & 7); const bool ok = (n0 + c4) < N;
;     f32x4 v[8];
; #pragma unroll
;     for (int i = 0; i < 8; ++i) { const int kk = 8 * i + (lane >> 3); v[i] = ok ? *(const f32x4*)(W + (size_t)(k0 + kk) * N + n0 + c4) : (f32x4){0.f, 0.f, 0.f, 0.f}; }
; #pragma unroll
;     for (int i = 0; i < 8; ++i) { const int kk = 8 * i + (lane >> 3); LAS float* d = scr + kk * 33 + c4; d[0] = v[i][0]; d[1] = v[i][1]; d[2] = v[i][2]; d[3] = v[i][3]; }
;     LDS_WAIT(); asm volatile("" ::: "memory");
;     const int c = lane & 7;
; #pragma unroll
;     for (int j = 0; j < 4; ++j) { const int n = (lane >> 3) + 8 * j; const LAS float* s = scr + (8 * c) * 33 + n;
;         v4u o; o.x = pk2(s[0 * 33], s[1 * 33]); o.y = pk2(s[2 * 33], s[3 * 33]); o.z = pk2(s[4 * 33], s[5 * 33]); o.w = pk2(s[6 * 33], s[7 * 33]);
;         *(GAS v4u*)(WT + (size_t)(drow0 + n) * K + k0 + 8 * c) = o; }
;     LDS_WAIT(); asm volatile("" ::: "memory");
; }
; __device__ __forceinline__ void convert_item(const In& I, unsigned char* ws, int it, LAS float* scr, int lane) {
;     ...
;     if (r < T0) { const int f = r / I_FFN; r -= f * I_FFN;
;         if (r < 2 * I_G) { const int up = r >= I_G; r -= up * I_G; const int kb = r / 88, nb = r % 88;
;             transpose_item((up ? I.w_up : I.w_gate) + (size_t)f * D * FF, D, FF, Wgu + (size_t)f * NGU * D, 256 * (nb >> 2) + 32 * (nb & 3) + 128 * up, kb, 32 * nb, scr, lane); }
;         else { r -= 2 * I_G; const int kb = r / 32, nb = r % 32; transpose_item(I.w_down + (size_t)f * FF * D, FF, D, Wd + (size_t)f * D * FF, 32 * nb, kb, 32 * nb, scr, lane); }
.LBB0_283:
	s_andn2_b64 vcc, exec, s[2:3]
	s_cbranch_vccnz .LBB0_228
	s_mul_hi_i32 s2, s44, 0x3e0f83e1
	s_lshr_b32 s3, s2, 31
	s_ashr_i32 s6, s2, 10
	s_add_i32 s6, s6, s3
	s_mul_i32 s2, s6, 0xffffef80
	s_add_i32 s7, s40, s2
	s_add_i32 s7, s7, 0xa800
	s_cmpk_gt_i32 s7, 0xaff
	s_mov_b64 s[2:3], -1
	s_cbranch_scc0 .LBB0_286
	v_readlane_b32 s48, v253, 0
	v_readlane_b32 s49, v253, 1
	v_readlane_b32 s50, v253, 2
	v_readlane_b32 s51, v253, 3
	v_readlane_b32 s52, v253, 4
	v_readlane_b32 s53, v253, 5
	v_readlane_b32 s54, v253, 6
	v_readlane_b32 s55, v253, 7
	v_readlane_b32 s56, v253, 8
	v_readlane_b32 s57, v253, 9
	s_mov_b64 s[48:49], s[52:53]
	s_mul_i32 s3, s6, 0xb00000
	s_mov_b64 s[50:51], s[54:55]
	s_mov_b64 s[52:53], s[56:57]
	s_mul_hi_i32 s2, s6, 0xb00000
	s_add_u32 s9, s52, s3
	s_addc_u32 s11, s53, s2
	s_mul_i32 s3, s6, 0x580000
	s_mul_hi_i32 s2, s6, 0x580000
	s_add_u32 s3, s19, s3
	s_mul_i32 s10, s6, 0xffffdf00
	s_addc_u32 s8, s20, s2
	s_add_i32 s10, s43, s10
	s_add_i32 s10, s10, 0x13800
	s_and_b32 s2, s42, 0x3e0
	s_andn2_b32 s10, s10, 63
	s_add_i32 s68, s10, 0xffffea00
	s_lshl_b32 s10, s2, 2
	v_or_b32_e32 v32, s68, v39
	s_add_u32 s10, s9, s10
	s_addc_u32 s11, s11, 0
	v_lshlrev_b32_e32 v2, 2, v36
	v_ashrrev_i32_e32 v33, 31, v32
	v_or_b32_e32 v8, 8, v32
	v_lshl_add_u64 v[34:35], s[10:11], 0, v[2:3]
	v_lshlrev_b64 v[4:5], 12, v[32:33]
	v_ashrrev_i32_e32 v9, 31, v8
	v_lshl_add_u64 v[4:5], v[34:35], 0, v[4:5]
	v_lshlrev_b64 v[8:9], 12, v[8:9]
	v_or_b32_e32 v12, 16, v32
	global_load_dwordx4 v[4:7], v[4:5], off nt
	v_lshl_add_u64 v[8:9], v[34:35], 0, v[8:9]
	v_ashrrev_i32_e32 v13, 31, v12
	global_load_dwordx4 v[8:11], v[8:9], off nt
	v_lshlrev_b64 v[12:13], 12, v[12:13]
	v_or_b32_e32 v16, 24, v32
	v_lshl_add_u64 v[12:13], v[34:35], 0, v[12:13]
	v_ashrrev_i32_e32 v17, 31, v16
	global_load_dwordx4 v[12:15], v[12:13], off nt
	v_lshlrev_b64 v[16:17], 12, v[16:17]
	v_or_b32_e32 v20, 32, v32
	v_lshl_add_u64 v[16:17], v[34:35], 0, v[16:17]
	v_ashrrev_i32_e32 v21, 31, v20
	global_load_dwordx4 v[16:19], v[16:17], off nt
	v_lshlrev_b64 v[20:21], 12, v[20:21]
	v_or_b32_e32 v24, 40, v32
	v_lshl_add_u64 v[20:21], v[34:35], 0, v[20:21]
	v_ashrrev_i32_e32 v25, 31, v24
	global_load_dwordx4 v[20:23], v[20:21], off nt
	v_lshlrev_b64 v[24:25], 12, v[24:25]
	v_or_b32_e32 v28, 48, v32
	v_lshl_add_u64 v[24:25], v[34:35], 0, v[24:25]
	v_ashrrev_i32_e32 v29, 31, v28
	global_load_dwordx4 v[24:27], v[24:25], off nt
	v_lshlrev_b64 v[28:29], 12, v[28:29]
	v_or_b32_e32 v32, 56, v32
	v_lshl_add_u64 v[28:29], v[34:35], 0, v[28:29]
	v_ashrrev_i32_e32 v33, 31, v32
	global_load_dwordx4 v[28:31], v[28:29], off nt
	v_lshlrev_b64 v[32:33], 12, v[32:33]
	v_lshl_add_u64 v[32:33], v[34:35], 0, v[32:33]
	global_load_dwordx4 v[32:35], v[32:33], off nt
	v_add_u32_e32 v2, v44, v45
	s_lshl_b64 s[10:11], s[68:69], 1
	s_add_u32 s10, s3, s10
	s_addc_u32 s11, s8, s11
	v_readlane_b32 s58, v253, 10
	v_readlane_b32 s59, v253, 11
	v_readlane_b32 s60, v253, 12
	v_readlane_b32 s61, v253, 13
	v_readlane_b32 s62, v253, 14
	v_readlane_b32 s63, v253, 15
	s_waitcnt vmcnt(0)
	ds_write2_b32 v2, v4, v5 offset1:1
	ds_write2_b32 v2, v6, v7 offset0:2 offset1:3
	v_add_u32_e32 v4, 0x420, v2
	ds_write2_b32 v4, v8, v9 offset1:1
	v_add_u32_e32 v4, 0x428, v2
	ds_write2_b32 v4, v10, v11 offset1:1
	v_add_u32_e32 v4, 0x840, v2
	ds_write2_b32 v4, v12, v13 offset1:1
	v_add_u32_e32 v4, 0x848, v2
	ds_write2_b32 v4, v14, v15 offset1:1
	v_add_u32_e32 v4, 0xc60, v2
	ds_write2_b32 v4, v16, v17 offset1:1
	v_add_u32_e32 v4, 0xc68, v2
	ds_write2_b32 v4, v18, v19 offset1:1
	v_add_u32_e32 v4, 0x1080, v2
	ds_write2_b32 v4, v20, v21 offset1:1
	v_add_u32_e32 v4, 0x1088, v2
	ds_write2_b32 v4, v22, v23 offset1:1
	v_add_u32_e32 v4, 0x14a0, v2
	ds_write2_b32 v4, v24, v25 offset1:1
	v_add_u32_e32 v4, 0x14a8, v2
	ds_write2_b32 v4, v26, v27 offset1:1
	v_add_u32_e32 v4, 0x18c0, v2
	ds_write2_b32 v4, v28, v29 offset1:1
	v_add_u32_e32 v4, 0x18c8, v2
	ds_write2_b32 v4, v30, v31 offset1:1
	v_add_u32_e32 v4, 0x1ce0, v2
	v_add_u32_e32 v2, 0x1ce8, v2
	ds_write2_b32 v4, v32, v33 offset1:1
	ds_write2_b32 v2, v34, v35 offset1:1
	s_waitcnt lgkmcnt(0)
	ds_read2_b32 v[10:11], v49 offset0:33 offset1:41
	ds_read2_b32 v[12:13], v49 offset1:8
	v_lshlrev_b32_e32 v2, 1, v38
	ds_read2_b32 v[14:15], v49 offset0:66 offset1:74
	ds_read2_b32 v[16:17], v49 offset0:99 offset1:107
	ds_read2_b32 v[18:19], v49 offset0:132 offset1:140
	ds_read2_b32 v[20:21], v49 offset0:165 offset1:173
	ds_read2_b32 v[22:23], v49 offset0:198 offset1:206
	ds_read2_b32 v[24:25], v49 offset0:231 offset1:239
	v_lshl_add_u64 v[8:9], s[10:11], 0, v[2:3]
	v_or_b32_e32 v2, s2, v39
	v_mul_u32_u24_e32 v2, 0x1600, v2
	v_lshl_add_u64 v[26:27], v[8:9], 0, v[2:3]
	v_or_b32_e32 v2, s2, v46
	s_waitcnt lgkmcnt(0)
	v_cvt_pk_bf16_f32 v4, v12, v10
	v_mul_u32_u24_e32 v2, 0x1600, v2
	v_cvt_pk_bf16_f32 v5, v14, v16
	v_cvt_pk_bf16_f32 v6, v18, v20
	v_cvt_pk_bf16_f32 v7, v22, v24
	global_store_dwordx4 v[26:27], v[4:7], off sc1
	s_nop 1
	v_cvt_pk_bf16_f32 v4, v13, v11
	v_lshl_add_u64 v[10:11], v[8:9], 0, v[2:3]
	v_cvt_pk_bf16_f32 v5, v15, v17
	v_cvt_pk_bf16_f32 v6, v19, v21
	v_cvt_pk_bf16_f32 v7, v23, v25
	global_store_dwordx4 v[10:11], v[4:7], off sc1
	ds_read2_b32 v[10:11], v49 offset0:16 offset1:24
	ds_read2_b32 v[12:13], v49 offset0:49 offset1:57
	ds_read2_b32 v[14:15], v49 offset0:82 offset1:90
	ds_read2_b32 v[16:17], v49 offset0:115 offset1:123
	ds_read2_b32 v[18:19], v49 offset0:148 offset1:156
	ds_read2_b32 v[20:21], v49 offset0:181 offset1:189
	ds_read2_b32 v[22:23], v49 offset0:214 offset1:222
	ds_read2_b32 v[24:25], v49 offset0:247 offset1:255
	v_or_b32_e32 v2, s2, v47
	v_mul_u32_u24_e32 v2, 0x1600, v2
	v_lshl_add_u64 v[26:27], v[8:9], 0, v[2:3]
	v_or_b32_e32 v2, s2, v48
	v_mul_u32_u24_e32 v2, 0x1600, v2
	s_waitcnt lgkmcnt(6)
	v_cvt_pk_bf16_f32 v4, v10, v12
	s_waitcnt lgkmcnt(4)
	v_cvt_pk_bf16_f32 v5, v14, v16
	s_waitcnt lgkmcnt(2)
	v_cvt_pk_bf16_f32 v6, v18, v20
	s_waitcnt lgkmcnt(0)
	v_cvt_pk_bf16_f32 v7, v22, v24
	v_lshl_add_u64 v[8:9], v[8:9], 0, v[2:3]
	global_store_dwordx4 v[26:27], v[4:7], off sc1
	s_mov_b64 s[2:3], 0
	s_nop 0
	v_cvt_pk_bf16_f32 v4, v11, v13
	v_cvt_pk_bf16_f32 v5, v15, v17
	v_cvt_pk_bf16_f32 v6, v19, v21
	v_cvt_pk_bf16_f32 v7, v23, v25
	global_store_dwordx4 v[8:9], v[4:7], off sc1
	s_waitcnt lgkmcnt(0)

; #define GAS __attribute__((address_space(1)))
; #define LAS __attribute__((address_space(3)))
; #define LDS_WAIT() asm volatile("s_waitcnt lgkmcnt(0)" ::: "memory")
; __device__ __forceinline__ unsigned pk2(float lo, float hi) { unsigned r; asm("v_cvt_pk_bf16_f32 %0, %1, %2" : "=v"(r) : "v"(lo), "v"(hi)); return r; }
; __device__ __forceinline__ void transpose_item(const float* W, int K, int N, bf16* WT, int drow0, int kb, int n0, LAS float* scr, int lane) {
;     const int k0 = 64 * kb; const int c4 = 4 * (lane & 7); const bool ok = (n0 + c4) < N;
;     f32x4 v[8];
; #pragma unroll
;     for (int i = 0; i < 8; ++i) { const int kk = 8 * i + (lane >> 3); v[i] = ok ? *(const f32x4*)(W + (size_t)(k0 + kk) * N + n0 + c4) : (f32x4){0.f, 0.f, 0.f, 0.f}; }
; #pragma unroll
;     for (int i = 0; i < 8; ++i) { const int kk = 8 * i + (lane >> 3); LAS float* d = scr + kk * 33 + c4; d[0] = v[i][0]; d[1] = v[i][1]; d[2] = v[i][2]; d[3] = v[i][3]; }
;     LDS_WAIT(); asm volatile("" ::: "memory");
;     const int c = lane & 7;
; #pragma unroll
;     for (int j = 0; j < 4; ++j) { const int n = (lane >> 3) + 8 * j; const LAS float* s = scr + (8 * c) * 33 + n;
;         v4u o; o.x = pk2(s[0 * 33], s[1 * 33]); o.y = pk2(s[2 * 33], s[3 * 33]); o.z = pk2(s[4 * 33], s[5 * 33]); o.w = pk2(s[6 * 33], s[7 * 33]);
;         *(GAS v4u*)(WT + (size_t)(drow0 + n) * K + k0 + 8 * c) = o; }
;     LDS_WAIT(); asm volatile("" ::: "memory");
; }
; __device__ __forceinline__ void convert_item(const In& I, unsigned char* ws, int it, LAS float* scr, int lane) {
;     ...
;     if (r < 2 * I_SQ) { const int j = r / I_SQ; r -= j * I_SQ; const int kb = r / 32, nb = r % 32;
;         transpose_item(I.fox_w_out + (size_t)j * D * D, D, D, Wfout + (size_t)j * D * D, 32 * nb, kb, 32 * nb, scr, lane); return; }
.LBB0_303:
	s_andn2_b64 vcc, exec, s[2:3]
	s_cbranch_vccnz .LBB0_305
	s_add_i32 s2, s40, 0x800
	s_lshr_b32 s68, s2, 9
	v_readlane_b32 s48, v253, 16
	s_lshl_b64 s[2:3], s[68:69], 22
	v_readlane_b32 s60, v253, 28
	v_readlane_b32 s61, v253, 29
	s_add_u32 s6, s60, s2
	s_addc_u32 s7, s61, s3
	s_lshl_b64 s[2:3], s[68:69], 21
	s_add_u32 s8, s27, s2
	s_addc_u32 s3, s31, s3
	s_and_b32 s2, s42, 0x3e0
	s_add_i32 s9, s43, 0x10000
	s_and_b32 s9, s9, 0x3c0
	s_lshl_b32 s10, s2, 2
	s_add_u32 s6, s6, s10
	v_or_b32_e32 v6, s9, v39
	s_addc_u32 s7, s7, 0
	v_lshlrev_b32_e32 v2, 2, v36
	v_lshl_add_u64 v[4:5], s[6:7], 0, v[2:3]
	v_lshlrev_b32_e32 v2, 12, v6
	v_lshl_add_u64 v[32:33], v[4:5], 0, v[2:3]
	v_add_co_u32_e32 v8, vcc, s81, v32
	global_load_dwordx4 v[4:7], v[32:33], off nt
	s_nop 0
	v_addc_co_u32_e32 v9, vcc, 0, v33, vcc
	global_load_dwordx4 v[8:11], v[8:9], off nt
	v_add_co_u32_e32 v12, vcc, s79, v32
	v_add_u32_e32 v2, v44, v45
	s_nop 0
	v_addc_co_u32_e32 v13, vcc, 0, v33, vcc
	global_load_dwordx4 v[12:15], v[12:13], off nt
	v_add_co_u32_e32 v16, vcc, s80, v32
	s_lshl_b32 s6, s9, 1
	s_nop 0
	v_addc_co_u32_e32 v17, vcc, 0, v33, vcc
	global_load_dwordx4 v[16:19], v[16:17], off nt
	v_add_co_u32_e32 v20, vcc, s85, v32
	s_add_u32 s6, s8, s6
	s_nop 0
	v_addc_co_u32_e32 v21, vcc, 0, v33, vcc
	global_load_dwordx4 v[20:23], v[20:21], off nt
	v_add_co_u32_e32 v24, vcc, s86, v32
	s_addc_u32 s7, s3, 0
	s_nop 0
	v_addc_co_u32_e32 v25, vcc, 0, v33, vcc
	global_load_dwordx4 v[24:27], v[24:25], off nt
	v_add_co_u32_e32 v28, vcc, s87, v32
	v_readlane_b32 s49, v253, 17
	s_nop 0
	v_addc_co_u32_e32 v29, vcc, 0, v33, vcc
	global_load_dwordx4 v[28:31], v[28:29], off nt
	v_add_co_u32_e32 v32, vcc, s89, v32
	v_readlane_b32 s50, v253, 18
	s_nop 0
	v_addc_co_u32_e32 v33, vcc, 0, v33, vcc
	global_load_dwordx4 v[32:35], v[32:33], off nt
	v_readlane_b32 s51, v253, 19
	v_readlane_b32 s52, v253, 20
	v_readlane_b32 s53, v253, 21
	v_readlane_b32 s54, v253, 22
	v_readlane_b32 s55, v253, 23
	v_readlane_b32 s56, v253, 24
	v_readlane_b32 s57, v253, 25
	v_readlane_b32 s58, v253, 26
	v_readlane_b32 s59, v253, 27
	v_readlane_b32 s62, v253, 30
	v_readlane_b32 s63, v253, 31
	s_waitcnt vmcnt(0)
	ds_write2_b32 v2, v4, v5 offset1:1
	ds_write2_b32 v2, v6, v7 offset0:2 offset1:3
	v_add_u32_e32 v4, 0x420, v2
	ds_write2_b32 v4, v8, v9 offset1:1
	v_add_u32_e32 v4, 0x428, v2
	ds_write2_b32 v4, v10, v11 offset1:1
	v_add_u32_e32 v4, 0x840, v2
	ds_write2_b32 v4, v12, v13 offset1:1
	v_add_u32_e32 v4, 0x848, v2
	ds_write2_b32 v4, v14, v15 offset1:1
	v_add_u32_e32 v4, 0xc60, v2
	ds_write2_b32 v4, v16, v17 offset1:1
	v_add_u32_e32 v4, 0xc68, v2
	ds_write2_b32 v4, v18, v19 offset1:1
	v_add_u32_e32 v4, 0x1080, v2
	ds_write2_b32 v4, v20, v21 offset1:1
	v_add_u32_e32 v4, 0x1088, v2
	ds_write2_b32 v4, v22, v23 offset1:1
	v_add_u32_e32 v4, 0x14a0, v2
	ds_write2_b32 v4, v24, v25 offset1:1
	v_add_u32_e32 v4, 0x14a8, v2
	ds_write2_b32 v4, v26, v27 offset1:1
	v_add_u32_e32 v4, 0x18c0, v2
	ds_write2_b32 v4, v28, v29 offset1:1
	v_add_u32_e32 v4, 0x18c8, v2
	ds_write2_b32 v4, v30, v31 offset1:1
	v_add_u32_e32 v4, 0x1ce0, v2
	v_add_u32_e32 v2, 0x1ce8, v2
	ds_write2_b32 v4, v32, v33 offset1:1
	ds_write2_b32 v2, v34, v35 offset1:1
	s_waitcnt lgkmcnt(0)
	ds_read2_b32 v[10:11], v49 offset0:33 offset1:41
	ds_read2_b32 v[12:13], v49 offset1:8
	v_lshlrev_b32_e32 v2, 1, v38
	ds_read2_b32 v[14:15], v49 offset0:66 offset1:74
	ds_read2_b32 v[16:17], v49 offset0:99 offset1:107
	ds_read2_b32 v[18:19], v49 offset0:132 offset1:140
	ds_read2_b32 v[20:21], v49 offset0:165 offset1:173
	ds_read2_b32 v[22:23], v49 offset0:198 offset1:206
	ds_read2_b32 v[24:25], v49 offset0:231 offset1:239
	v_lshl_add_u64 v[8:9], s[6:7], 0, v[2:3]
	v_or_b32_e32 v2, s2, v39
	v_lshlrev_b32_e32 v2, 11, v2
	v_lshl_add_u64 v[26:27], v[8:9], 0, v[2:3]
	v_or_b32_e32 v2, s2, v46
	s_waitcnt lgkmcnt(0)
	v_cvt_pk_bf16_f32 v4, v12, v10
	v_lshlrev_b32_e32 v2, 11, v2
	v_cvt_pk_bf16_f32 v5, v14, v16
	v_cvt_pk_bf16_f32 v6, v18, v20
	v_cvt_pk_bf16_f32 v7, v22, v24
	global_store_dwordx4 v[26:27], v[4:7], off sc1
	s_nop 1
	v_cvt_pk_bf16_f32 v4, v13, v11
	v_lshl_add_u64 v[10:11], v[8:9], 0, v[2:3]
	v_cvt_pk_bf16_f32 v5, v15, v17
	v_cvt_pk_bf16_f32 v6, v19, v21
	v_cvt_pk_bf16_f32 v7, v23, v25
	global_store_dwordx4 v[10:11], v[4:7], off sc1
	ds_read2_b32 v[10:11], v49 offset0:16 offset1:24
	ds_read2_b32 v[12:13], v49 offset0:49 offset1:57
	ds_read2_b32 v[14:15], v49 offset0:82 offset1:90
	ds_read2_b32 v[16:17], v49 offset0:115 offset1:123
	ds_read2_b32 v[18:19], v49 offset0:148 offset1:156
	ds_read2_b32 v[20:21], v49 offset0:181 offset1:189
	ds_read2_b32 v[22:23], v49 offset0:214 offset1:222
	ds_read2_b32 v[24:25], v49 offset0:247 offset1:255
	v_or_b32_e32 v2, s2, v47
	v_lshlrev_b32_e32 v2, 11, v2
	v_lshl_add_u64 v[26:27], v[8:9], 0, v[2:3]
	v_or_b32_e32 v2, s2, v48
	v_lshlrev_b32_e32 v2, 11, v2
	s_waitcnt lgkmcnt(6)
	v_cvt_pk_bf16_f32 v4, v10, v12
	s_waitcnt lgkmcnt(4)
	v_cvt_pk_bf16_f32 v5, v14, v16
	s_waitcnt lgkmcnt(2)
	v_cvt_pk_bf16_f32 v6, v18, v20
	s_waitcnt lgkmcnt(0)
	v_cvt_pk_bf16_f32 v7, v22, v24
	v_lshl_add_u64 v[8:9], v[8:9], 0, v[2:3]
	global_store_dwordx4 v[26:27], v[4:7], off sc1
	s_nop 1
	v_cvt_pk_bf16_f32 v4, v11, v13
	v_cvt_pk_bf16_f32 v5, v15, v17
	v_cvt_pk_bf16_f32 v6, v19, v21
	v_cvt_pk_bf16_f32 v7, v23, v25
	global_store_dwordx4 v[8:9], v[4:7], off sc1
	s_waitcnt lgkmcnt(0)

; #define GAS __attribute__((address_space(1)))
; #define LAS __attribute__((address_space(3)))
; #define LDS_WAIT() asm volatile("s_waitcnt lgkmcnt(0)" ::: "memory")
; __device__ __forceinline__ unsigned pk2(float lo, float hi) { unsigned r; asm("v_cvt_pk_bf16_f32 %0, %1, %2" : "=v"(r) : "v"(lo), "v"(hi)); return r; }
; __device__ __forceinline__ void transpose_item(const float* W, int K, int N, bf16* WT, int drow0, int kb, int n0, LAS float* scr, int lane) {
;     const int k0 = 64 * kb; const int c4 = 4 * (lane & 7); const bool ok = (n0 + c4) < N;
;     f32x4 v[8];
; #pragma unroll
;     for (int i = 0; i < 8; ++i) { const int kk = 8 * i + (lane >> 3); v[i] = ok ? *(const f32x4*)(W + (size_t)(k0 + kk) * N + n0 + c4) : (f32x4){0.f, 0.f, 0.f, 0.f}; }
; #pragma unroll
;     for (int i = 0; i < 8; ++i) { const int kk = 8 * i + (lane >> 3); LAS float* d = scr + kk * 33 + c4; d[0] = v[i][0]; d[1] = v[i][1]; d[2] = v[i][2]; d[3] = v[i][3]; }
;     LDS_WAIT(); asm volatile("" ::: "memory");
;     const int c = lane & 7;
; #pragma unroll
;     for (int j = 0; j < 4; ++j) { const int n = (lane >> 3) + 8 * j; const LAS float* s = scr + (8 * c) * 33 + n;
;         v4u o; o.x = pk2(s[0 * 33], s[1 * 33]); o.y = pk2(s[2 * 33], s[3 * 33]); o.z = pk2(s[4 * 33], s[5 * 33]); o.w = pk2(s[6 * 33], s[7 * 33]);
;         *(GAS v4u*)(WT + (size_t)(drow0 + n) * K + k0 + 8 * c) = o; }
;     LDS_WAIT(); asm volatile("" ::: "memory");
; }
; __device__ __forceinline__ void convert_item(const In& I, unsigned char* ws, int it, LAS float* scr, int lane) {
;     ...
;     if (r < 2 * I_SQ) { const int j = r / I_SQ; r -= j * I_SQ; const int kb = r / 32, nb = r % 32;
;         transpose_item(I.nsa_w_out + (size_t)j * D * D, D, D, Wnout + (size_t)j * D * D, 32 * nb, kb, 32 * nb, scr, lane); return; }
.LBB0_325:
	s_andn2_b64 vcc, exec, s[2:3]
	s_cbranch_vccnz .LBB0_327
	s_add_i32 s2, s40, 0x1900
	s_lshr_b32 s68, s2, 9
	v_readlane_b32 s48, v253, 16
	s_lshl_b64 s[2:3], s[68:69], 22
	v_readlane_b32 s54, v253, 22
	v_readlane_b32 s55, v253, 23
	s_add_u32 s6, s54, s2
	s_addc_u32 s7, s55, s3
	s_lshl_b64 s[2:3], s[68:69], 21
	s_add_u32 s8, s23, s2
	s_addc_u32 s3, s24, s3
	s_and_b32 s2, s42, 0x3e0
	s_add_i32 s9, s43, 0xffffe200
	s_and_b32 s9, s9, 0x3c0
	s_lshl_b32 s10, s2, 2
	s_add_u32 s6, s6, s10
	v_or_b32_e32 v6, s9, v39
	s_addc_u32 s7, s7, 0
	v_lshlrev_b32_e32 v2, 2, v36
	v_lshl_add_u64 v[4:5], s[6:7], 0, v[2:3]
	v_lshlrev_b32_e32 v2, 12, v6
	v_lshl_add_u64 v[32:33], v[4:5], 0, v[2:3]
	v_add_co_u32_e32 v8, vcc, s81, v32
	global_load_dwordx4 v[4:7], v[32:33], off nt
	s_nop 0
	v_addc_co_u32_e32 v9, vcc, 0, v33, vcc
	global_load_dwordx4 v[8:11], v[8:9], off nt
	v_add_co_u32_e32 v12, vcc, s79, v32
	v_add_u32_e32 v2, v44, v45
	s_nop 0
	v_addc_co_u32_e32 v13, vcc, 0, v33, vcc
	global_load_dwordx4 v[12:15], v[12:13], off nt
	v_add_co_u32_e32 v16, vcc, s80, v32
	s_lshl_b32 s6, s9, 1
	s_nop 0
	v_addc_co_u32_e32 v17, vcc, 0, v33, vcc
	global_load_dwordx4 v[16:19], v[16:17], off nt
	v_add_co_u32_e32 v20, vcc, s85, v32
	s_add_u32 s6, s8, s6
	s_nop 0
	v_addc_co_u32_e32 v21, vcc, 0, v33, vcc
	global_load_dwordx4 v[20:23], v[20:21], off nt
	v_add_co_u32_e32 v24, vcc, s86, v32
	s_addc_u32 s7, s3, 0
	s_nop 0
	v_addc_co_u32_e32 v25, vcc, 0, v33, vcc
	global_load_dwordx4 v[24:27], v[24:25], off nt
	v_add_co_u32_e32 v28, vcc, s87, v32
	v_readlane_b32 s49, v253, 17
	s_nop 0
	v_addc_co_u32_e32 v29, vcc, 0, v33, vcc
	global_load_dwordx4 v[28:31], v[28:29], off nt
	v_add_co_u32_e32 v32, vcc, s89, v32
	v_readlane_b32 s50, v253, 18
	s_nop 0
	v_addc_co_u32_e32 v33, vcc, 0, v33, vcc
	global_load_dwordx4 v[32:35], v[32:33], off nt
	v_readlane_b32 s51, v253, 19
	v_readlane_b32 s52, v253, 20
	v_readlane_b32 s53, v253, 21
	v_readlane_b32 s56, v253, 24
	v_readlane_b32 s57, v253, 25
	v_readlane_b32 s58, v253, 26
	v_readlane_b32 s59, v253, 27
	v_readlane_b32 s60, v253, 28
	v_readlane_b32 s61, v253, 29
	v_readlane_b32 s62, v253, 30
	v_readlane_b32 s63, v253, 31
	s_waitcnt vmcnt(0)
	ds_write2_b32 v2, v4, v5 offset1:1
	ds_write2_b32 v2, v6, v7 offset0:2 offset1:3
	v_add_u32_e32 v4, 0x420, v2
	ds_write2_b32 v4, v8, v9 offset1:1
	v_add_u32_e32 v4, 0x428, v2
	ds_write2_b32 v4, v10, v11 offset1:1
	v_add_u32_e32 v4, 0x840, v2
	ds_write2_b32 v4, v12, v13 offset1:1
	v_add_u32_e32 v4, 0x848, v2
	ds_write2_b32 v4, v14, v15 offset1:1
	v_add_u32_e32 v4, 0xc60, v2
	ds_write2_b32 v4, v16, v17 offset1:1
	v_add_u32_e32 v4, 0xc68, v2
	ds_write2_b32 v4, v18, v19 offset1:1
	v_add_u32_e32 v4, 0x1080, v2
	ds_write2_b32 v4, v20, v21 offset1:1
	v_add_u32_e32 v4, 0x1088, v2
	ds_write2_b32 v4, v22, v23 offset1:1
	v_add_u32_e32 v4, 0x14a0, v2
	ds_write2_b32 v4, v24, v25 offset1:1
	v_add_u32_e32 v4, 0x14a8, v2
	ds_write2_b32 v4, v26, v27 offset1:1
	v_add_u32_e32 v4, 0x18c0, v2
	ds_write2_b32 v4, v28, v29 offset1:1
	v_add_u32_e32 v4, 0x18c8, v2
	ds_write2_b32 v4, v30, v31 offset1:1
	v_add_u32_e32 v4, 0x1ce0, v2
	v_add_u32_e32 v2, 0x1ce8, v2
	ds_write2_b32 v4, v32, v33 offset1:1
	ds_write2_b32 v2, v34, v35 offset1:1
	s_waitcnt lgkmcnt(0)
	ds_read2_b32 v[10:11], v49 offset0:33 offset1:41
	ds_read2_b32 v[12:13], v49 offset1:8
	v_lshlrev_b32_e32 v2, 1, v38
	ds_read2_b32 v[14:15], v49 offset0:66 offset1:74
	ds_read2_b32 v[16:17], v49 offset0:99 offset1:107
	ds_read2_b32 v[18:19], v49 offset0:132 offset1:140
	ds_read2_b32 v[20:21], v49 offset0:165 offset1:173
	ds_read2_b32 v[22:23], v49 offset0:198 offset1:206
	ds_read2_b32 v[24:25], v49 offset0:231 offset1:239
	v_lshl_add_u64 v[8:9], s[6:7], 0, v[2:3]
	v_or_b32_e32 v2, s2, v39
	v_lshlrev_b32_e32 v2, 11, v2
	v_lshl_add_u64 v[26:27], v[8:9], 0, v[2:3]
	v_or_b32_e32 v2, s2, v46
	s_waitcnt lgkmcnt(0)
	v_cvt_pk_bf16_f32 v4, v12, v10
	v_lshlrev_b32_e32 v2, 11, v2
	v_cvt_pk_bf16_f32 v5, v14, v16
	v_cvt_pk_bf16_f32 v6, v18, v20
	v_cvt_pk_bf16_f32 v7, v22, v24
	global_store_dwordx4 v[26:27], v[4:7], off sc1
	s_nop 1
	v_cvt_pk_bf16_f32 v4, v13, v11
	v_lshl_add_u64 v[10:11], v[8:9], 0, v[2:3]
	v_cvt_pk_bf16_f32 v5, v15, v17
	v_cvt_pk_bf16_f32 v6, v19, v21
	v_cvt_pk_bf16_f32 v7, v23, v25
	global_store_dwordx4 v[10:11], v[4:7], off sc1
	ds_read2_b32 v[10:11], v49 offset0:16 offset1:24
	ds_read2_b32 v[12:13], v49 offset0:49 offset1:57
	ds_read2_b32 v[14:15], v49 offset0:82 offset1:90
	ds_read2_b32 v[16:17], v49 offset0:115 offset1:123
	ds_read2_b32 v[18:19], v49 offset0:148 offset1:156
	ds_read2_b32 v[20:21], v49 offset0:181 offset1:189
	ds_read2_b32 v[22:23], v49 offset0:214 offset1:222
	ds_read2_b32 v[24:25], v49 offset0:247 offset1:255
	v_or_b32_e32 v2, s2, v47
	v_lshlrev_b32_e32 v2, 11, v2
	v_lshl_add_u64 v[26:27], v[8:9], 0, v[2:3]
	v_or_b32_e32 v2, s2, v48
	v_lshlrev_b32_e32 v2, 11, v2
	s_waitcnt lgkmcnt(6)
	v_cvt_pk_bf16_f32 v4, v10, v12
	s_waitcnt lgkmcnt(4)
	v_cvt_pk_bf16_f32 v5, v14, v16
	s_waitcnt lgkmcnt(2)
	v_cvt_pk_bf16_f32 v6, v18, v20
	s_waitcnt lgkmcnt(0)
	v_cvt_pk_bf16_f32 v7, v22, v24
	v_lshl_add_u64 v[8:9], v[8:9], 0, v[2:3]
	global_store_dwordx4 v[26:27], v[4:7], off sc1
	s_nop 1
	v_cvt_pk_bf16_f32 v4, v11, v13
	v_cvt_pk_bf16_f32 v5, v15, v17
	v_cvt_pk_bf16_f32 v6, v19, v21
	v_cvt_pk_bf16_f32 v7, v23, v25
	global_store_dwordx4 v[8:9], v[4:7], off sc1
	s_waitcnt lgkmcnt(0)

; #define GAS __attribute__((address_space(1)))
; #define LAS __attribute__((address_space(3)))
; #define LDS_WAIT() asm volatile("s_waitcnt lgkmcnt(0)" ::: "memory")
; __device__ __forceinline__ unsigned pk2(float lo, float hi) { unsigned r; asm("v_cvt_pk_bf16_f32 %0, %1, %2" : "=v"(r) : "v"(lo), "v"(hi)); return r; }
; __device__ __forceinline__ void transpose_item(const float* W, int K, int N, bf16* WT, int drow0, int kb, int n0, LAS float* scr, int lane) {
;     const int k0 = 64 * kb; const int c4 = 4 * (lane & 7); const bool ok = (n0 + c4) < N;
;     f32x4 v[8];
; #pragma unroll
;     for (int i = 0; i < 8; ++i) { const int kk = 8 * i + (lane >> 3); v[i] = ok ? *(const f32x4*)(W + (size_t)(k0 + kk) * N + n0 + c4) : (f32x4){0.f, 0.f, 0.f, 0.f}; }
; #pragma unroll
;     for (int i = 0; i < 8; ++i) { const int kk = 8 * i + (lane >> 3); LAS float* d = scr + kk * 33 + c4; d[0] = v[i][0]; d[1] = v[i][1]; d[2] = v[i][2]; d[3] = v[i][3]; }
;     LDS_WAIT(); asm volatile("" ::: "memory");
;     const int c = lane & 7;
; #pragma unroll
;     for (int j = 0; j < 4; ++j) { const int n = (lane >> 3) + 8 * j; const LAS float* s = scr + (8 * c) * 33 + n;
;         v4u o; o.x = pk2(s[0 * 33], s[1 * 33]); o.y = pk2(s[2 * 33], s[3 * 33]); o.z = pk2(s[4 * 33], s[5 * 33]); o.w = pk2(s[6 * 33], s[7 * 33]);
;         *(GAS v4u*)(WT + (size_t)(drow0 + n) * K + k0 + 8 * c) = o; }
;     LDS_WAIT(); asm volatile("" ::: "memory");
; }
; __device__ __forceinline__ void convert_item(const In& I, unsigned char* ws, int it, LAS float* scr, int lane) {
;     ...
;     if (r < T0) { const int f = r / I_FFN; r -= f * I_FFN;
;         if (r < 2 * I_G) { const int up = r >= I_G; r -= up * I_G; const int kb = r / 88, nb = r % 88;
;             transpose_item((up ? I.w_up : I.w_gate) + (size_t)f * D * FF, D, FF, Wgu + (size_t)f * NGU * D, 256 * (nb >> 2) + 32 * (nb & 3) + 128 * up, kb, 32 * nb, scr, lane); }
;         else { r -= 2 * I_G; const int kb = r / 32, nb = r % 32; transpose_item(I.w_down + (size_t)f * FF * D, FF, D, Wd + (size_t)f * D * FF, 32 * nb, kb, 32 * nb, scr, lane); }
.LBB0_347:
	s_andn2_b64 vcc, exec, s[2:3]
	s_cbranch_vccnz .LBB0_292
	s_mul_hi_i32 s2, s44, 0x3e0f83e1
	s_lshr_b32 s3, s2, 31
	s_ashr_i32 s6, s2, 10
	s_add_i32 s6, s6, s3
	s_mul_i32 s2, s6, 0xffffef80
	s_add_i32 s7, s40, s2
	s_add_i32 s7, s7, 0xa800
	s_cmpk_gt_i32 s7, 0xaff
	s_mov_b64 s[2:3], -1
	s_cbranch_scc0 .LBB0_350
	v_readlane_b32 s48, v253, 0
	v_readlane_b32 s49, v253, 1
	v_readlane_b32 s50, v253, 2
	v_readlane_b32 s51, v253, 3
	v_readlane_b32 s52, v253, 4
	v_readlane_b32 s53, v253, 5
	v_readlane_b32 s54, v253, 6
	v_readlane_b32 s55, v253, 7
	v_readlane_b32 s56, v253, 8
	v_readlane_b32 s57, v253, 9
	s_mov_b64 s[48:49], s[52:53]
	s_mul_i32 s3, s6, 0xb00000
	s_mov_b64 s[50:51], s[54:55]
	s_mov_b64 s[52:53], s[56:57]
	s_mul_hi_i32 s2, s6, 0xb00000
	s_add_u32 s9, s52, s3
	s_addc_u32 s11, s53, s2
	s_mul_i32 s3, s6, 0x580000
	s_mul_hi_i32 s2, s6, 0x580000
	s_add_u32 s3, s19, s3
	s_mul_i32 s10, s6, 0xffffdf00
	s_addc_u32 s8, s20, s2
	s_add_i32 s10, s43, s10
	s_add_i32 s10, s10, 0x10000
	s_and_b32 s2, s42, 0x3e0
	s_andn2_b32 s10, s10, 63
	s_add_i32 s68, s10, 0xffffea00
	s_lshl_b32 s10, s2, 2
	v_or_b32_e32 v32, s68, v39
	s_add_u32 s10, s9, s10
	s_addc_u32 s11, s11, 0
	v_lshlrev_b32_e32 v2, 2, v36
	v_ashrrev_i32_e32 v33, 31, v32
	v_or_b32_e32 v8, 8, v32
	v_lshl_add_u64 v[34:35], s[10:11], 0, v[2:3]
	v_lshlrev_b64 v[4:5], 12, v[32:33]
	v_ashrrev_i32_e32 v9, 31, v8
	v_lshl_add_u64 v[4:5], v[34:35], 0, v[4:5]
	v_lshlrev_b64 v[8:9], 12, v[8:9]
	v_or_b32_e32 v12, 16, v32
	global_load_dwordx4 v[4:7], v[4:5], off nt
	v_lshl_add_u64 v[8:9], v[34:35], 0, v[8:9]
	v_ashrrev_i32_e32 v13, 31, v12
	global_load_dwordx4 v[8:11], v[8:9], off nt
	v_lshlrev_b64 v[12:13], 12, v[12:13]
	v_or_b32_e32 v16, 24, v32
	v_lshl_add_u64 v[12:13], v[34:35], 0, v[12:13]
	v_ashrrev_i32_e32 v17, 31, v16
	global_load_dwordx4 v[12:15], v[12:13], off nt
	v_lshlrev_b64 v[16:17], 12, v[16:17]
	v_or_b32_e32 v20, 32, v32
	v_lshl_add_u64 v[16:17], v[34:35], 0, v[16:17]
	v_ashrrev_i32_e32 v21, 31, v20
	global_load_dwordx4 v[16:19], v[16:17], off nt
	v_lshlrev_b64 v[20:21], 12, v[20:21]
	v_or_b32_e32 v24, 40, v32
	v_lshl_add_u64 v[20:21], v[34:35], 0, v[20:21]
	v_ashrrev_i32_e32 v25, 31, v24
	global_load_dwordx4 v[20:23], v[20:21], off nt
	v_lshlrev_b64 v[24:25], 12, v[24:25]
	v_or_b32_e32 v28, 48, v32
	v_lshl_add_u64 v[24:25], v[34:35], 0, v[24:25]
	v_ashrrev_i32_e32 v29, 31, v28
	global_load_dwordx4 v[24:27], v[24:25], off nt
	v_lshlrev_b64 v[28:29], 12, v[28:29]
	v_or_b32_e32 v32, 56, v32
	v_lshl_add_u64 v[28:29], v[34:35], 0, v[28:29]
	v_ashrrev_i32_e32 v33, 31, v32
	global_load_dwordx4 v[28:31], v[28:29], off nt
	v_lshlrev_b64 v[32:33], 12, v[32:33]
	v_lshl_add_u64 v[32:33], v[34:35], 0, v[32:33]
	global_load_dwordx4 v[32:35], v[32:33], off nt
	v_add_u32_e32 v2, v44, v45
	s_lshl_b64 s[10:11], s[68:69], 1
	s_add_u32 s10, s3, s10
	s_addc_u32 s11, s8, s11
	v_readlane_b32 s58, v253, 10
	v_readlane_b32 s59, v253, 11
	v_readlane_b32 s60, v253, 12
	v_readlane_b32 s61, v253, 13
	v_readlane_b32 s62, v253, 14
	v_readlane_b32 s63, v253, 15
	s_waitcnt vmcnt(0)
	ds_write2_b32 v2, v4, v5 offset1:1
	ds_write2_b32 v2, v6, v7 offset0:2 offset1:3
	v_add_u32_e32 v4, 0x420, v2
	ds_write2_b32 v4, v8, v9 offset1:1
	v_add_u32_e32 v4, 0x428, v2
	ds_write2_b32 v4, v10, v11 offset1:1
	v_add_u32_e32 v4, 0x840, v2
	ds_write2_b32 v4, v12, v13 offset1:1
	v_add_u32_e32 v4, 0x848, v2
	ds_write2_b32 v4, v14, v15 offset1:1
	v_add_u32_e32 v4, 0xc60, v2
	ds_write2_b32 v4, v16, v17 offset1:1
	v_add_u32_e32 v4, 0xc68, v2
	ds_write2_b32 v4, v18, v19 offset1:1
	v_add_u32_e32 v4, 0x1080, v2
	ds_write2_b32 v4, v20, v21 offset1:1
	v_add_u32_e32 v4, 0x1088, v2
	ds_write2_b32 v4, v22, v23 offset1:1
	v_add_u32_e32 v4, 0x14a0, v2
	ds_write2_b32 v4, v24, v25 offset1:1
	v_add_u32_e32 v4, 0x14a8, v2
	ds_write2_b32 v4, v26, v27 offset1:1
	v_add_u32_e32 v4, 0x18c0, v2
	ds_write2_b32 v4, v28, v29 offset1:1
	v_add_u32_e32 v4, 0x18c8, v2
	ds_write2_b32 v4, v30, v31 offset1:1
	v_add_u32_e32 v4, 0x1ce0, v2
	v_add_u32_e32 v2, 0x1ce8, v2
	ds_write2_b32 v4, v32, v33 offset1:1
	ds_write2_b32 v2, v34, v35 offset1:1
	s_waitcnt lgkmcnt(0)
	ds_read2_b32 v[10:11], v49 offset0:33 offset1:41
	ds_read2_b32 v[12:13], v49 offset1:8
	v_lshlrev_b32_e32 v2, 1, v38
	ds_read2_b32 v[14:15], v49 offset0:66 offset1:74
	ds_read2_b32 v[16:17], v49 offset0:99 offset1:107
	ds_read2_b32 v[18:19], v49 offset0:132 offset1:140
	ds_read2_b32 v[20:21], v49 offset0:165 offset1:173
	ds_read2_b32 v[22:23], v49 offset0:198 offset1:206
	ds_read2_b32 v[24:25], v49 offset0:231 offset1:239
	v_lshl_add_u64 v[8:9], s[10:11], 0, v[2:3]
	v_or_b32_e32 v2, s2, v39
	v_mul_u32_u24_e32 v2, 0x1600, v2
	v_lshl_add_u64 v[26:27], v[8:9], 0, v[2:3]
	v_or_b32_e32 v2, s2, v46
	s_waitcnt lgkmcnt(0)
	v_cvt_pk_bf16_f32 v4, v12, v10
	v_mul_u32_u24_e32 v2, 0x1600, v2
	v_cvt_pk_bf16_f32 v5, v14, v16
	v_cvt_pk_bf16_f32 v6, v18, v20
	v_cvt_pk_bf16_f32 v7, v22, v24
	global_store_dwordx4 v[26:27], v[4:7], off sc1
	s_nop 1
	v_cvt_pk_bf16_f32 v4, v13, v11
	v_lshl_add_u64 v[10:11], v[8:9], 0, v[2:3]
	v_cvt_pk_bf16_f32 v5, v15, v17
	v_cvt_pk_bf16_f32 v6, v19, v21
	v_cvt_pk_bf16_f32 v7, v23, v25
	global_store_dwordx4 v[10:11], v[4:7], off sc1
	ds_read2_b32 v[10:11], v49 offset0:16 offset1:24
	ds_read2_b32 v[12:13], v49 offset0:49 offset1:57
	ds_read2_b32 v[14:15], v49 offset0:82 offset1:90
	ds_read2_b32 v[16:17], v49 offset0:115 offset1:123
	ds_read2_b32 v[18:19], v49 offset0:148 offset1:156
	ds_read2_b32 v[20:21], v49 offset0:181 offset1:189
	ds_read2_b32 v[22:23], v49 offset0:214 offset1:222
	ds_read2_b32 v[24:25], v49 offset0:247 offset1:255
	v_or_b32_e32 v2, s2, v47
	v_mul_u32_u24_e32 v2, 0x1600, v2
	v_lshl_add_u64 v[26:27], v[8:9], 0, v[2:3]
	v_or_b32_e32 v2, s2, v48
	v_mul_u32_u24_e32 v2, 0x1600, v2
	s_waitcnt lgkmcnt(6)
	v_cvt_pk_bf16_f32 v4, v10, v12
	s_waitcnt lgkmcnt(4)
	v_cvt_pk_bf16_f32 v5, v14, v16
	s_waitcnt lgkmcnt(2)
	v_cvt_pk_bf16_f32 v6, v18, v20
	s_waitcnt lgkmcnt(0)
	v_cvt_pk_bf16_f32 v7, v22, v24
	v_lshl_add_u64 v[8:9], v[8:9], 0, v[2:3]
	global_store_dwordx4 v[26:27], v[4:7], off sc1
	s_mov_b64 s[2:3], 0
	s_nop 0
	v_cvt_pk_bf16_f32 v4, v11, v13
	v_cvt_pk_bf16_f32 v5, v15, v17
	v_cvt_pk_bf16_f32 v6, v19, v21
	v_cvt_pk_bf16_f32 v7, v23, v25
	global_store_dwordx4 v[8:9], v[4:7], off sc1
	s_waitcnt lgkmcnt(0)

; #define GAS __attribute__((address_space(1)))
; #define LAS __attribute__((address_space(3)))
; #define LDS_WAIT() asm volatile("s_waitcnt lgkmcnt(0)" ::: "memory")
; __device__ __forceinline__ unsigned pk2(float lo, float hi) { unsigned r; asm("v_cvt_pk_bf16_f32 %0, %1, %2" : "=v"(r) : "v"(lo), "v"(hi)); return r; }
; __device__ __forceinline__ void transpose_item(const float* W, int K, int N, bf16* WT, int drow0, int kb, int n0, LAS float* scr, int lane) {
;     const int k0 = 64 * kb; const int c4 = 4 * (lane & 7); const bool ok = (n0 + c4) < N;
;     f32x4 v[8];
; #pragma unroll
;     for (int i = 0; i < 8; ++i) { const int kk = 8 * i + (lane >> 3); v[i] = ok ? *(const f32x4*)(W + (size_t)(k0 + kk) * N + n0 + c4) : (f32x4){0.f, 0.f, 0.f, 0.f}; }
; #pragma unroll
;     for (int i = 0; i < 8; ++i) { const int kk = 8 * i + (lane >> 3); LAS float* d = scr + kk * 33 + c4; d[0] = v[i][0]; d[1] = v[i][1]; d[2] = v[i][2]; d[3] = v[i][3]; }
;     LDS_WAIT(); asm volatile("" ::: "memory");
;     const int c = lane & 7;
; #pragma unroll
;     for (int j = 0; j < 4; ++j) { const int n = (lane >> 3) + 8 * j; const LAS float* s = scr + (8 * c) * 33 + n;
;         v4u o; o.x = pk2(s[0 * 33], s[1 * 33]); o.y = pk2(s[2 * 33], s[3 * 33]); o.z = pk2(s[4 * 33], s[5 * 33]); o.w = pk2(s[6 * 33], s[7 * 33]);
;         *(GAS v4u*)(WT + (size_t)(drow0 + n) * K + k0 + 8 * c) = o; }
;     LDS_WAIT(); asm volatile("" ::: "memory");
; }
; __device__ __forceinline__ void convert_item(const In& I, unsigned char* ws, int it, LAS float* scr, int lane) {
;     ...
;     { const int jk = r >> 3; r &= 7; const int kb = r >> 1, nb = r & 1;
;         transpose_item(I.nsa_w2 + (size_t)jk * 256 * 64, 256, 64, W2t + (size_t)jk * 64 * 256, 32 * nb, kb, 32 * nb, scr, lane); }
.LBB0_355:
	s_add_i32 s45, s41, 0xa800
	s_cmp_gt_i32 s45, 0x83ff
	s_mov_b64 s[2:3], -1
	s_cbranch_scc0 .LBB0_409
	s_cmpk_gt_u32 s45, 0x8eff
	s_cbranch_scc0 .LBB0_390
	s_cmpk_gt_u32 s45, 0x92ff
	s_cbranch_scc0 .LBB0_387
	s_cmpk_gt_u32 s45, 0x9fff
	s_cbranch_scc0 .LBB0_368
	s_cmpk_gt_u32 s45, 0xa3ff
	s_cbranch_scc0 .LBB0_365
	s_cmpk_gt_u32 s45, 0xa7ff
	s_cbranch_scc0 .LBB0_362
	s_lshr_b32 s68, s41, 3
	v_readlane_b32 s48, v253, 16
	s_lshl_b64 s[2:3], s[68:69], 16
	v_readlane_b32 s52, v253, 20
	v_readlane_b32 s53, v253, 21
	s_add_u32 s6, s52, s2
	s_addc_u32 s7, s53, s3
	s_lshl_b64 s[2:3], s[68:69], 15
	s_add_u32 s8, s34, s2
	s_addc_u32 s3, s35, s3
	s_and_b32 s2, s43, 32
	s_and_b32 s9, s43, 0xc0
	s_lshl_b32 s10, s2, 2
	s_add_u32 s6, s6, s10
	v_or_b32_e32 v6, s9, v39
	s_addc_u32 s7, s7, 0
	v_lshlrev_b32_e32 v2, 2, v36
	v_lshl_add_u64 v[4:5], s[6:7], 0, v[2:3]
	v_lshlrev_b32_e32 v2, 8, v6
	v_lshl_add_u64 v[28:29], v[4:5], 0, v[2:3]
	v_add_co_u32_e32 v16, vcc, s84, v28
	global_load_dwordx4 v[4:7], v[28:29], off nt
	global_load_dwordx4 v[8:11], v[28:29], off offset:2048 nt
	v_addc_co_u32_e32 v17, vcc, 0, v29, vcc
	v_add_co_u32_e32 v24, vcc, s74, v28
	s_movk_i32 s6, 0x3000
	s_nop 0
	v_addc_co_u32_e32 v25, vcc, 0, v29, vcc
	global_load_dwordx4 v[12:15], v[24:25], off offset:-4096 nt
	s_nop 0
	global_load_dwordx4 v[16:19], v[16:17], off offset:2048 nt
	s_nop 0
	global_load_dwordx4 v[20:23], v[24:25], off nt
	s_nop 0
	global_load_dwordx4 v[24:27], v[24:25], off offset:2048 nt
	v_add_co_u32_e32 v32, vcc, s6, v28
	v_add_u32_e32 v2, v44, v47
	s_nop 0
	v_addc_co_u32_e32 v33, vcc, 0, v29, vcc
	global_load_dwordx4 v[28:31], v[32:33], off nt
	s_nop 0
	global_load_dwordx4 v[32:35], v[32:33], off offset:2048 nt
	s_lshl_b32 s6, s9, 1
	s_add_u32 s6, s8, s6
	s_addc_u32 s7, s3, 0
	v_readlane_b32 s49, v253, 17
	v_readlane_b32 s50, v253, 18
	v_readlane_b32 s51, v253, 19
	v_readlane_b32 s54, v253, 22
	v_readlane_b32 s55, v253, 23
	v_readlane_b32 s56, v253, 24
	v_readlane_b32 s57, v253, 25
	v_readlane_b32 s58, v253, 26
	v_readlane_b32 s59, v253, 27
	v_readlane_b32 s60, v253, 28
	v_readlane_b32 s61, v253, 29
	v_readlane_b32 s62, v253, 30
	v_readlane_b32 s63, v253, 31
	s_waitcnt vmcnt(0)
	ds_write2_b32 v45, v4, v5 offset1:1
	ds_write2_b32 v45, v6, v7 offset0:2 offset1:3
	v_add_u32_e32 v4, 0x420, v2
	ds_write2_b32 v2, v8, v9 offset1:1
	ds_write2_b32 v2, v10, v11 offset0:2 offset1:3
	ds_write2_b32 v4, v12, v13 offset1:1
	v_add_u32_e32 v4, 0x428, v2
	ds_write2_b32 v4, v14, v15 offset1:1
	v_add_u32_e32 v4, 0x840, v2
	v_add_u32_e32 v2, 0x848, v2
	ds_write2_b32 v2, v18, v19 offset1:1
	v_add_u32_e32 v2, 0x1080, v45
	ds_write2_b32 v2, v20, v21 offset1:1
	v_add_u32_e32 v2, 0x1088, v45
	ds_write2_b32 v2, v22, v23 offset1:1
	v_add_u32_e32 v2, 0x14a0, v45
	ds_write2_b32 v2, v24, v25 offset1:1
	v_add_u32_e32 v2, 0x14a8, v45
	ds_write2_b32 v2, v26, v27 offset1:1
	v_add_u32_e32 v2, 0x18c0, v45
	ds_write2_b32 v2, v28, v29 offset1:1
	v_add_u32_e32 v2, 0x18c8, v45
	ds_write2_b32 v2, v30, v31 offset1:1
	v_add_u32_e32 v2, 0x1ce0, v45
	ds_write2_b32 v2, v32, v33 offset1:1
	v_add_u32_e32 v2, 0x1ce8, v45
	ds_write2_b32 v4, v16, v17 offset1:1
	ds_write2_b32 v2, v34, v35 offset1:1
	s_waitcnt lgkmcnt(0)
	ds_read2_b32 v[10:11], v50 offset0:33 offset1:41
	ds_read2_b32 v[12:13], v50 offset1:8
	v_lshlrev_b32_e32 v2, 1, v38
	ds_read2_b32 v[14:15], v50 offset0:66 offset1:74
	ds_read2_b32 v[16:17], v50 offset0:99 offset1:107
	ds_read2_b32 v[18:19], v50 offset0:132 offset1:140
	ds_read2_b32 v[20:21], v50 offset0:165 offset1:173
	ds_read2_b32 v[22:23], v50 offset0:198 offset1:206
	ds_read2_b32 v[24:25], v50 offset0:231 offset1:239
	v_lshl_add_u64 v[4:5], s[6:7], 0, v[2:3]
	v_or_b32_e32 v2, s2, v39
	v_lshlrev_b32_e32 v2, 9, v2
	v_lshl_add_u64 v[26:27], v[4:5], 0, v[2:3]
	v_or_b32_e32 v2, s2, v46
	s_waitcnt lgkmcnt(0)
	v_cvt_pk_bf16_f32 v6, v12, v10
	v_lshlrev_b32_e32 v2, 9, v2
	v_cvt_pk_bf16_f32 v7, v14, v16
	v_cvt_pk_bf16_f32 v8, v18, v20
	v_cvt_pk_bf16_f32 v9, v22, v24
	global_store_dwordx4 v[26:27], v[6:9], off sc1
	s_nop 1
	v_cvt_pk_bf16_f32 v6, v13, v11
	v_lshl_add_u64 v[10:11], v[4:5], 0, v[2:3]
	v_cvt_pk_bf16_f32 v7, v15, v17
	v_cvt_pk_bf16_f32 v8, v19, v21
	v_cvt_pk_bf16_f32 v9, v23, v25
	global_store_dwordx4 v[10:11], v[6:9], off sc1
	ds_read2_b32 v[10:11], v50 offset0:16 offset1:24
	ds_read2_b32 v[12:13], v50 offset0:49 offset1:57
	ds_read2_b32 v[14:15], v50 offset0:82 offset1:90
	ds_read2_b32 v[16:17], v50 offset0:115 offset1:123
	ds_read2_b32 v[18:19], v50 offset0:148 offset1:156
	ds_read2_b32 v[20:21], v50 offset0:181 offset1:189
	ds_read2_b32 v[22:23], v50 offset0:214 offset1:222
	ds_read2_b32 v[24:25], v50 offset0:247 offset1:255
	v_or_b32_e32 v2, s2, v48
	v_lshlrev_b32_e32 v2, 9, v2
	v_lshl_add_u64 v[26:27], v[4:5], 0, v[2:3]
	v_or_b32_e32 v2, s2, v49
	v_lshlrev_b32_e32 v2, 9, v2
	s_waitcnt lgkmcnt(6)
	v_cvt_pk_bf16_f32 v6, v10, v12
	s_waitcnt lgkmcnt(4)
	v_cvt_pk_bf16_f32 v7, v14, v16
	s_waitcnt lgkmcnt(2)
	v_cvt_pk_bf16_f32 v8, v18, v20
	s_waitcnt lgkmcnt(0)
	v_cvt_pk_bf16_f32 v9, v22, v24
	v_lshl_add_u64 v[4:5], v[4:5], 0, v[2:3]
	global_store_dwordx4 v[26:27], v[6:9], off sc1
	s_mov_b64 s[2:3], 0
	s_nop 0
	v_cvt_pk_bf16_f32 v6, v11, v13
	v_cvt_pk_bf16_f32 v7, v15, v17
	v_cvt_pk_bf16_f32 v8, v19, v21
	v_cvt_pk_bf16_f32 v9, v23, v25
	global_store_dwordx4 v[4:5], v[6:9], off sc1
	s_waitcnt lgkmcnt(0)
; #define GAS __attribute__((address_space(1)))
; #define LAS __attribute__((address_space(3)))
; #define LDS_WAIT() asm volatile("s_waitcnt lgkmcnt(0)" ::: "memory")
; __device__ __forceinline__ unsigned pk2(float lo, float hi) { unsigned r; asm("v_cvt_pk_bf16_f32 %0, %1, %2" : "=v"(r) : "v"(lo), "v"(hi)); return r; }
; __device__ __forceinline__ void transpose_item(const float* W, int K, int N, bf16* WT, int drow0, int kb, int n0, LAS float* scr, int lane) {
;     const int k0 = 64 * kb; const int c4 = 4 * (lane & 7); const bool ok = (n0 + c4) < N;
;     f32x4 v[8];
; #pragma unroll
;     for (int i = 0; i < 8; ++i) { const int kk = 8 * i + (lane >> 3); v[i] = ok ? *(const f32x4*)(W + (size_t)(k0 + kk) * N + n0 + c4) : (f32x4){0.f, 0.f, 0.f, 0.f}; }
; #pragma unroll
;     for (int i = 0; i < 8; ++i) { const int kk = 8 * i + (lane >> 3); LAS float* d = scr + kk * 33 + c4; d[0] = v[i][0]; d[1] = v[i][1]; d[2] = v[i][2]; d[3] = v[i][3]; }
;     LDS_WAIT(); asm volatile("" ::: "memory");
;     const int c = lane & 7;
; #pragma unroll
;     for (int j = 0; j < 4; ++j) { const int n = (lane >> 3) + 8 * j; const LAS float* s = scr + (8 * c) * 33 + n;
;         v4u o; o.x = pk2(s[0 * 33], s[1 * 33]); o.y = pk2(s[2 * 33], s[3 * 33]); o.z = pk2(s[4 * 33], s[5 * 33]); o.w = pk2(s[6 * 33], s[7 * 33]);
;         *(GAS v4u*)(WT + (size_t)(drow0 + n) * K + k0 + 8 * c) = o; }
;     LDS_WAIT(); asm volatile("" ::: "memory");
; }
; __device__ __forceinline__ void convert_item(const In& I, unsigned char* ws, int it, LAS float* scr, int lane) {
;     ...
;     if (r < 4 * I_W1) { const int jk = r / I_W1; r -= jk * I_W1; const int kb = r / 8, nb = r % 8;
;         transpose_item(I.nsa_w1 + (size_t)jk * 2048 * 256, 2048, 256, W1t + (size_t)jk * 256 * 2048, 32 * nb, kb, 32 * nb, scr, lane); return; }
.LBB0_362:
	s_andn2_b64 vcc, exec, s[2:3]
	s_cbranch_vccnz .LBB0_364
	s_add_i32 s2, s41, 0x400
	s_lshr_b32 s68, s2, 8
	s_lshl_b64 s[2:3], s[68:69], 21
	v_readlane_b32 s48, v253, 16
	v_readlane_b32 s49, v253, 17
	s_add_u32 s6, s48, s2
	s_addc_u32 s7, s49, s3
	s_lshl_b64 s[2:3], s[68:69], 20
	s_add_u32 s8, s31, s2
	s_addc_u32 s3, s33, s3
	s_and_b32 s2, s43, 0xe0
	s_and_b32 s9, s42, 0x7c0
	s_lshl_b32 s10, s2, 2
	s_add_u32 s6, s6, s10
	v_or_b32_e32 v6, s9, v39
	s_addc_u32 s7, s7, 0
	v_lshlrev_b32_e32 v2, 2, v36
	v_lshl_add_u64 v[4:5], s[6:7], 0, v[2:3]
	v_lshlrev_b32_e32 v2, 10, v6
	v_lshl_add_u64 v[32:33], v[4:5], 0, v[2:3]
	v_add_co_u32_e32 v8, vcc, s74, v32
	s_movk_i32 s6, 0x4000
	s_nop 0
	v_addc_co_u32_e32 v9, vcc, 0, v33, vcc
	v_add_co_u32_e32 v12, vcc, s6, v32
	s_movk_i32 s6, 0x6000
	s_nop 0
	v_addc_co_u32_e32 v13, vcc, 0, v33, vcc
	global_load_dwordx4 v[4:7], v[32:33], off nt
	v_add_co_u32_e32 v16, vcc, s6, v32
	global_load_dwordx4 v[8:11], v[8:9], off nt
	s_nop 0
	v_addc_co_u32_e32 v17, vcc, 0, v33, vcc
	global_load_dwordx4 v[12:15], v[12:13], off nt
	v_add_co_u32_e32 v20, vcc, s81, v32
	global_load_dwordx4 v[16:19], v[16:17], off nt
	s_nop 0
	v_addc_co_u32_e32 v21, vcc, 0, v33, vcc
	s_mov_b32 s6, 0xa000
	global_load_dwordx4 v[20:23], v[20:21], off nt
	v_add_co_u32_e32 v24, vcc, s6, v32
	s_mov_b32 s6, 0xc000
	s_nop 0
	v_addc_co_u32_e32 v25, vcc, 0, v33, vcc
	global_load_dwordx4 v[24:27], v[24:25], off nt
	v_add_co_u32_e32 v28, vcc, s6, v32
	s_mov_b32 s6, 0xe000
	s_nop 0
	v_addc_co_u32_e32 v29, vcc, 0, v33, vcc
	global_load_dwordx4 v[28:31], v[28:29], off nt
	v_add_co_u32_e32 v32, vcc, s6, v32
	v_add_u32_e32 v2, v44, v47
	s_nop 0
	v_addc_co_u32_e32 v33, vcc, 0, v33, vcc
	global_load_dwordx4 v[32:35], v[32:33], off nt
	s_lshl_b32 s6, s9, 1
	s_add_u32 s6, s8, s6
	s_addc_u32 s7, s3, 0
	v_readlane_b32 s50, v253, 18
	v_readlane_b32 s51, v253, 19
	v_readlane_b32 s52, v253, 20
	v_readlane_b32 s53, v253, 21
	v_readlane_b32 s54, v253, 22
	v_readlane_b32 s55, v253, 23
	v_readlane_b32 s56, v253, 24
	v_readlane_b32 s57, v253, 25
	v_readlane_b32 s58, v253, 26
	v_readlane_b32 s59, v253, 27
	v_readlane_b32 s60, v253, 28
	v_readlane_b32 s61, v253, 29
	v_readlane_b32 s62, v253, 30
	v_readlane_b32 s63, v253, 31
	s_waitcnt vmcnt(0)
	ds_write2_b32 v45, v4, v5 offset1:1
	ds_write2_b32 v45, v6, v7 offset0:2 offset1:3
	v_add_u32_e32 v4, 0x420, v2
	ds_write2_b32 v2, v8, v9 offset1:1
	ds_write2_b32 v2, v10, v11 offset0:2 offset1:3
	ds_write2_b32 v4, v12, v13 offset1:1
	v_add_u32_e32 v4, 0x428, v2
	ds_write2_b32 v4, v14, v15 offset1:1
	v_add_u32_e32 v4, 0x840, v2
	v_add_u32_e32 v2, 0x848, v2
	ds_write2_b32 v2, v18, v19 offset1:1
	v_add_u32_e32 v2, 0x1080, v45
	ds_write2_b32 v2, v20, v21 offset1:1
	v_add_u32_e32 v2, 0x1088, v45
	ds_write2_b32 v2, v22, v23 offset1:1
	v_add_u32_e32 v2, 0x14a0, v45
	ds_write2_b32 v4, v16, v17 offset1:1
	ds_write2_b32 v2, v24, v25 offset1:1
	v_add_u32_e32 v2, 0x14a8, v45
	ds_write2_b32 v2, v26, v27 offset1:1
	v_add_u32_e32 v2, 0x18c0, v45
	ds_write2_b32 v2, v28, v29 offset1:1
	v_add_u32_e32 v2, 0x18c8, v45
	ds_write2_b32 v2, v30, v31 offset1:1
	v_add_u32_e32 v2, 0x1ce0, v45
	ds_write2_b32 v2, v32, v33 offset1:1
	v_add_u32_e32 v2, 0x1ce8, v45
	ds_write2_b32 v2, v34, v35 offset1:1
	s_waitcnt lgkmcnt(0)
	ds_read2_b32 v[10:11], v50 offset0:33 offset1:41
	ds_read2_b32 v[12:13], v50 offset1:8
	v_lshlrev_b32_e32 v2, 1, v38
	ds_read2_b32 v[14:15], v50 offset0:66 offset1:74
	ds_read2_b32 v[16:17], v50 offset0:99 offset1:107
	ds_read2_b32 v[18:19], v50 offset0:132 offset1:140
	ds_read2_b32 v[20:21], v50 offset0:165 offset1:173
	ds_read2_b32 v[22:23], v50 offset0:198 offset1:206
	ds_read2_b32 v[24:25], v50 offset0:231 offset1:239
	v_lshl_add_u64 v[4:5], s[6:7], 0, v[2:3]
	v_or_b32_e32 v2, s2, v39
	v_lshlrev_b32_e32 v2, 12, v2
	v_lshl_add_u64 v[26:27], v[4:5], 0, v[2:3]
	v_or_b32_e32 v2, s2, v46
	s_waitcnt lgkmcnt(0)
	v_cvt_pk_bf16_f32 v6, v12, v10
	v_lshlrev_b32_e32 v2, 12, v2
	v_cvt_pk_bf16_f32 v7, v14, v16
	v_cvt_pk_bf16_f32 v8, v18, v20
	v_cvt_pk_bf16_f32 v9, v22, v24
	global_store_dwordx4 v[26:27], v[6:9], off sc1
	s_nop 1
	v_cvt_pk_bf16_f32 v6, v13, v11
	v_lshl_add_u64 v[10:11], v[4:5], 0, v[2:3]
	v_cvt_pk_bf16_f32 v7, v15, v17
	v_cvt_pk_bf16_f32 v8, v19, v21
	v_cvt_pk_bf16_f32 v9, v23, v25
	global_store_dwordx4 v[10:11], v[6:9], off sc1
	ds_read2_b32 v[10:11], v50 offset0:16 offset1:24
	ds_read2_b32 v[12:13], v50 offset0:49 offset1:57
	ds_read2_b32 v[14:15], v50 offset0:82 offset1:90
	ds_read2_b32 v[16:17], v50 offset0:115 offset1:123
	ds_read2_b32 v[18:19], v50 offset0:148 offset1:156
	ds_read2_b32 v[20:21], v50 offset0:181 offset1:189
	ds_read2_b32 v[22:23], v50 offset0:214 offset1:222
	ds_read2_b32 v[24:25], v50 offset0:247 offset1:255
	v_or_b32_e32 v2, s2, v48
	v_lshlrev_b32_e32 v2, 12, v2
	v_lshl_add_u64 v[26:27], v[4:5], 0, v[2:3]
	v_or_b32_e32 v2, s2, v49
	v_lshlrev_b32_e32 v2, 12, v2
	s_waitcnt lgkmcnt(6)
	v_cvt_pk_bf16_f32 v6, v10, v12
	s_waitcnt lgkmcnt(4)
	v_cvt_pk_bf16_f32 v7, v14, v16
	s_waitcnt lgkmcnt(2)
	v_cvt_pk_bf16_f32 v8, v18, v20
	s_waitcnt lgkmcnt(0)
	v_cvt_pk_bf16_f32 v9, v22, v24
	v_lshl_add_u64 v[4:5], v[4:5], 0, v[2:3]
	global_store_dwordx4 v[26:27], v[6:9], off sc1
	s_nop 1
	v_cvt_pk_bf16_f32 v6, v11, v13
	v_cvt_pk_bf16_f32 v7, v15, v17
	v_cvt_pk_bf16_f32 v8, v19, v21
	v_cvt_pk_bf16_f32 v9, v23, v25
	global_store_dwordx4 v[4:5], v[6:9], off sc1
	s_waitcnt lgkmcnt(0)

; #define GAS __attribute__((address_space(1)))
; #define LAS __attribute__((address_space(3)))
; #define LDS_WAIT() asm volatile("s_waitcnt lgkmcnt(0)" ::: "memory")
; __device__ __forceinline__ unsigned pk2(float lo, float hi) { unsigned r; asm("v_cvt_pk_bf16_f32 %0, %1, %2" : "=v"(r) : "v"(lo), "v"(hi)); return r; }
; __device__ __forceinline__ void transpose_item(const float* W, int K, int N, bf16* WT, int drow0, int kb, int n0, LAS float* scr, int lane) {
;     const int k0 = 64 * kb; const int c4 = 4 * (lane & 7); const bool ok = (n0 + c4) < N;
;     f32x4 v[8];
; #pragma unroll
;     for (int i = 0; i < 8; ++i) { const int kk = 8 * i + (lane >> 3); v[i] = ok ? *(const f32x4*)(W + (size_t)(k0 + kk) * N + n0 + c4) : (f32x4){0.f, 0.f, 0.f, 0.f}; }
; #pragma unroll
;     for (int i = 0; i < 8; ++i) { const int kk = 8 * i + (lane >> 3); LAS float* d = scr + kk * 33 + c4; d[0] = v[i][0]; d[1] = v[i][1]; d[2] = v[i][2]; d[3] = v[i][3]; }
;     LDS_WAIT(); asm volatile("" ::: "memory");
;     const int c = lane & 7;
; #pragma unroll
;     for (int j = 0; j < 4; ++j) { const int n = (lane >> 3) + 8 * j; const LAS float* s = scr + (8 * c) * 33 + n;
;         v4u o; o.x = pk2(s[0 * 33], s[1 * 33]); o.y = pk2(s[2 * 33], s[3 * 33]); o.z = pk2(s[4 * 33], s[5 * 33]); o.w = pk2(s[6 * 33], s[7 * 33]);
;         *(GAS v4u*)(WT + (size_t)(drow0 + n) * K + k0 + 8 * c) = o; }
;     LDS_WAIT(); asm volatile("" ::: "memory");
; }
; __device__ __forceinline__ void convert_item(const In& I, unsigned char* ws, int it, LAS float* scr, int lane) {
;     ...
;     if (r < 2 * I_SQ) { const int j = r / I_SQ; r -= j * I_SQ; const int kb = r / 32, nb = r % 32;
;         transpose_item(I.fox_w_out + (size_t)j * D * D, D, D, Wfout + (size_t)j * D * D, 32 * nb, kb, 32 * nb, scr, lane); return; }
.LBB0_365:
	s_andn2_b64 vcc, exec, s[2:3]
	s_cbranch_vccnz .LBB0_367
	s_add_i32 s2, s41, 0x800
	s_lshr_b32 s68, s2, 9
	v_readlane_b32 s48, v253, 16
	s_lshl_b64 s[2:3], s[68:69], 22
	v_readlane_b32 s60, v253, 28
	v_readlane_b32 s61, v253, 29
	s_add_u32 s8, s60, s2
	s_addc_u32 s9, s61, s3
	s_lshl_b64 s[6:7], s[68:69], 21
	s_add_u32 s3, s26, s6
	s_addc_u32 s6, s27, s7
	s_and_b32 s2, s43, 0x3e0
	s_add_i32 s7, s44, 0x11600
	s_and_b32 s7, s7, 0x3c0
	s_lshl_b32 s10, s2, 2
	s_add_u32 s8, s8, s10
	v_or_b32_e32 v6, s7, v39
	s_addc_u32 s9, s9, 0
	v_lshlrev_b32_e32 v2, 2, v36
	v_lshl_add_u64 v[4:5], s[8:9], 0, v[2:3]
	v_lshlrev_b32_e32 v2, 12, v6
	v_lshl_add_u64 v[32:33], v[4:5], 0, v[2:3]
	v_add_co_u32_e32 v8, vcc, s81, v32
	global_load_dwordx4 v[4:7], v[32:33], off nt
	s_nop 0
	v_addc_co_u32_e32 v9, vcc, 0, v33, vcc
	v_add_co_u32_e32 v12, vcc, s79, v32
	global_load_dwordx4 v[8:11], v[8:9], off nt
	s_nop 0
	v_addc_co_u32_e32 v13, vcc, 0, v33, vcc
	v_add_co_u32_e32 v16, vcc, s80, v32
	global_load_dwordx4 v[12:15], v[12:13], off nt
	s_nop 0
	v_addc_co_u32_e32 v17, vcc, 0, v33, vcc
	v_add_co_u32_e32 v20, vcc, s85, v32
	global_load_dwordx4 v[16:19], v[16:17], off nt
	s_nop 0
	v_addc_co_u32_e32 v21, vcc, 0, v33, vcc
	global_load_dwordx4 v[20:23], v[20:21], off nt
	v_add_co_u32_e32 v24, vcc, s86, v32
	v_add_u32_e32 v2, v44, v47
	s_nop 0
	v_addc_co_u32_e32 v25, vcc, 0, v33, vcc
	global_load_dwordx4 v[24:27], v[24:25], off nt
	v_add_co_u32_e32 v28, vcc, s87, v32
	s_lshl_b32 s7, s7, 1
	s_nop 0
	v_addc_co_u32_e32 v29, vcc, 0, v33, vcc
	global_load_dwordx4 v[28:31], v[28:29], off nt
	v_add_co_u32_e32 v32, vcc, s89, v32
	s_add_u32 s8, s3, s7
	s_nop 0
	v_addc_co_u32_e32 v33, vcc, 0, v33, vcc
	global_load_dwordx4 v[32:35], v[32:33], off nt
	s_addc_u32 s9, s6, 0
	v_readlane_b32 s49, v253, 17
	v_readlane_b32 s50, v253, 18
	v_readlane_b32 s51, v253, 19
	v_readlane_b32 s52, v253, 20
	v_readlane_b32 s53, v253, 21
	v_readlane_b32 s54, v253, 22
	v_readlane_b32 s55, v253, 23
	v_readlane_b32 s56, v253, 24
	v_readlane_b32 s57, v253, 25
	v_readlane_b32 s58, v253, 26
	v_readlane_b32 s59, v253, 27
	v_readlane_b32 s62, v253, 30
	v_readlane_b32 s63, v253, 31
	s_waitcnt vmcnt(0)
	ds_write2_b32 v45, v4, v5 offset1:1
	ds_write2_b32 v45, v6, v7 offset0:2 offset1:3
	v_add_u32_e32 v4, 0x420, v2
	ds_write2_b32 v2, v8, v9 offset1:1
	ds_write2_b32 v2, v10, v11 offset0:2 offset1:3
	ds_write2_b32 v4, v12, v13 offset1:1
	v_add_u32_e32 v4, 0x428, v2
	ds_write2_b32 v4, v14, v15 offset1:1
	v_add_u32_e32 v4, 0x840, v2
	v_add_u32_e32 v2, 0x848, v2
	ds_write2_b32 v2, v18, v19 offset1:1
	v_add_u32_e32 v2, 0x1080, v45
	ds_write2_b32 v4, v16, v17 offset1:1
	ds_write2_b32 v2, v20, v21 offset1:1
	v_add_u32_e32 v2, 0x1088, v45
	ds_write2_b32 v2, v22, v23 offset1:1
	v_add_u32_e32 v2, 0x14a0, v45
	ds_write2_b32 v2, v24, v25 offset1:1
	v_add_u32_e32 v2, 0x14a8, v45
	ds_write2_b32 v2, v26, v27 offset1:1
	v_add_u32_e32 v2, 0x18c0, v45
	ds_write2_b32 v2, v28, v29 offset1:1
	v_add_u32_e32 v2, 0x18c8, v45
	ds_write2_b32 v2, v30, v31 offset1:1
	v_add_u32_e32 v2, 0x1ce0, v45
	ds_write2_b32 v2, v32, v33 offset1:1
	v_add_u32_e32 v2, 0x1ce8, v45
	ds_write2_b32 v2, v34, v35 offset1:1
	s_waitcnt lgkmcnt(0)
	ds_read2_b32 v[10:11], v50 offset0:33 offset1:41
	ds_read2_b32 v[12:13], v50 offset1:8
	v_lshlrev_b32_e32 v2, 1, v38
	ds_read2_b32 v[14:15], v50 offset0:66 offset1:74
	ds_read2_b32 v[16:17], v50 offset0:99 offset1:107
	ds_read2_b32 v[18:19], v50 offset0:132 offset1:140
	ds_read2_b32 v[20:21], v50 offset0:165 offset1:173
	ds_read2_b32 v[22:23], v50 offset0:198 offset1:206
	ds_read2_b32 v[24:25], v50 offset0:231 offset1:239
	v_lshl_add_u64 v[8:9], s[8:9], 0, v[2:3]
	v_or_b32_e32 v2, s2, v39
	v_lshlrev_b32_e32 v2, 11, v2
	v_lshl_add_u64 v[26:27], v[8:9], 0, v[2:3]
	v_or_b32_e32 v2, s2, v46
	s_waitcnt lgkmcnt(0)
	v_cvt_pk_bf16_f32 v4, v12, v10
	v_lshlrev_b32_e32 v2, 11, v2
	v_cvt_pk_bf16_f32 v5, v14, v16
	v_cvt_pk_bf16_f32 v6, v18, v20
	v_cvt_pk_bf16_f32 v7, v22, v24
	global_store_dwordx4 v[26:27], v[4:7], off sc1
	s_nop 1
	v_cvt_pk_bf16_f32 v4, v13, v11
	v_lshl_add_u64 v[10:11], v[8:9], 0, v[2:3]
	v_cvt_pk_bf16_f32 v5, v15, v17
	v_cvt_pk_bf16_f32 v6, v19, v21
	v_cvt_pk_bf16_f32 v7, v23, v25
	global_store_dwordx4 v[10:11], v[4:7], off sc1
	ds_read2_b32 v[10:11], v50 offset0:16 offset1:24
	ds_read2_b32 v[12:13], v50 offset0:49 offset1:57
	ds_read2_b32 v[14:15], v50 offset0:82 offset1:90
	ds_read2_b32 v[16:17], v50 offset0:115 offset1:123
	ds_read2_b32 v[18:19], v50 offset0:148 offset1:156
	ds_read2_b32 v[20:21], v50 offset0:181 offset1:189
	ds_read2_b32 v[22:23], v50 offset0:214 offset1:222
	ds_read2_b32 v[24:25], v50 offset0:247 offset1:255
	v_or_b32_e32 v2, s2, v48
	v_lshlrev_b32_e32 v2, 11, v2
	v_lshl_add_u64 v[26:27], v[8:9], 0, v[2:3]
	v_or_b32_e32 v2, s2, v49
	v_lshlrev_b32_e32 v2, 11, v2
	s_waitcnt lgkmcnt(6)
	v_cvt_pk_bf16_f32 v4, v10, v12
	s_waitcnt lgkmcnt(4)
	v_cvt_pk_bf16_f32 v5, v14, v16
	s_waitcnt lgkmcnt(2)
	v_cvt_pk_bf16_f32 v6, v18, v20
	s_waitcnt lgkmcnt(0)
	v_cvt_pk_bf16_f32 v7, v22, v24
	v_lshl_add_u64 v[8:9], v[8:9], 0, v[2:3]
	global_store_dwordx4 v[26:27], v[4:7], off sc1
	s_nop 1
	v_cvt_pk_bf16_f32 v4, v11, v13
	v_cvt_pk_bf16_f32 v5, v15, v17
	v_cvt_pk_bf16_f32 v6, v19, v21
	v_cvt_pk_bf16_f32 v7, v23, v25
	global_store_dwordx4 v[8:9], v[4:7], off sc1
	s_waitcnt lgkmcnt(0)

; #define GAS __attribute__((address_space(1)))
; #define LAS __attribute__((address_space(3)))
; #define LDS_WAIT() asm volatile("s_waitcnt lgkmcnt(0)" ::: "memory")
; __device__ __forceinline__ unsigned pk2(float lo, float hi) { unsigned r; asm("v_cvt_pk_bf16_f32 %0, %1, %2" : "=v"(r) : "v"(lo), "v"(hi)); return r; }
; __device__ __forceinline__ void transpose_item(const float* W, int K, int N, bf16* WT, int drow0, int kb, int n0, LAS float* scr, int lane) {
;     const int k0 = 64 * kb; const int c4 = 4 * (lane & 7); const bool ok = (n0 + c4) < N;
;     f32x4 v[8];
; #pragma unroll
;     for (int i = 0; i < 8; ++i) { const int kk = 8 * i + (lane >> 3); v[i] = ok ? *(const f32x4*)(W + (size_t)(k0 + kk) * N + n0 + c4) : (f32x4){0.f, 0.f, 0.f, 0.f}; }
; #pragma unroll
;     for (int i = 0; i < 8; ++i) { const int kk = 8 * i + (lane >> 3); LAS float* d = scr + kk * 33 + c4; d[0] = v[i][0]; d[1] = v[i][1]; d[2] = v[i][2]; d[3] = v[i][3]; }
;     LDS_WAIT(); asm volatile("" ::: "memory");
;     const int c = lane & 7;
; #pragma unroll
;     for (int j = 0; j < 4; ++j) { const int n = (lane >> 3) + 8 * j; const LAS float* s = scr + (8 * c) * 33 + n;
;         v4u o; o.x = pk2(s[0 * 33], s[1 * 33]); o.y = pk2(s[2 * 33], s[3 * 33]); o.z = pk2(s[4 * 33], s[5 * 33]); o.w = pk2(s[6 * 33], s[7 * 33]);
;         *(GAS v4u*)(WT + (size_t)(drow0 + n) * K + k0 + 8 * c) = o; }
;     LDS_WAIT(); asm volatile("" ::: "memory");
; }
; __device__ __forceinline__ void convert_item(const In& I, unsigned char* ws, int it, LAS float* scr, int lane) {
;     ...
;     if (r < 2 * I_SQ) { const int j = r / I_SQ; r -= j * I_SQ; const int kb = r / 32, nb = r % 32;
;         transpose_item(I.nsa_w_out + (size_t)j * D * D, D, D, Wnout + (size_t)j * D * D, 32 * nb, kb, 32 * nb, scr, lane); return; }
.LBB0_387:
	s_andn2_b64 vcc, exec, s[2:3]
	s_cbranch_vccnz .LBB0_389
	s_add_i32 s2, s41, 0x1900
	s_lshr_b32 s68, s2, 9
	v_readlane_b32 s48, v253, 16
	s_lshl_b64 s[2:3], s[68:69], 22
	v_readlane_b32 s54, v253, 22
	v_readlane_b32 s55, v253, 23
	s_add_u32 s8, s54, s2
	s_addc_u32 s9, s55, s3
	s_lshl_b64 s[6:7], s[68:69], 21
	s_add_u32 s3, s22, s6
	s_addc_u32 s6, s23, s7
	s_and_b32 s2, s43, 0x3e0
	s_add_i32 s7, s44, 0xfffff800
	s_and_b32 s7, s7, 0x3c0
	s_lshl_b32 s10, s2, 2
	s_add_u32 s8, s8, s10
	v_or_b32_e32 v6, s7, v39
	s_addc_u32 s9, s9, 0
	v_lshlrev_b32_e32 v2, 2, v36
	v_lshl_add_u64 v[4:5], s[8:9], 0, v[2:3]
	v_lshlrev_b32_e32 v2, 12, v6
	v_lshl_add_u64 v[32:33], v[4:5], 0, v[2:3]
	v_add_co_u32_e32 v8, vcc, s81, v32
	global_load_dwordx4 v[4:7], v[32:33], off nt
	s_nop 0
	v_addc_co_u32_e32 v9, vcc, 0, v33, vcc
	v_add_co_u32_e32 v12, vcc, s79, v32
	global_load_dwordx4 v[8:11], v[8:9], off nt
	s_nop 0
	v_addc_co_u32_e32 v13, vcc, 0, v33, vcc
	v_add_co_u32_e32 v16, vcc, s80, v32
	global_load_dwordx4 v[12:15], v[12:13], off nt
	s_nop 0
	v_addc_co_u32_e32 v17, vcc, 0, v33, vcc
	v_add_co_u32_e32 v20, vcc, s85, v32
	global_load_dwordx4 v[16:19], v[16:17], off nt
	s_nop 0
	v_addc_co_u32_e32 v21, vcc, 0, v33, vcc
	global_load_dwordx4 v[20:23], v[20:21], off nt
	v_add_co_u32_e32 v24, vcc, s86, v32
	v_add_u32_e32 v2, v44, v47
	s_nop 0
	v_addc_co_u32_e32 v25, vcc, 0, v33, vcc
	global_load_dwordx4 v[24:27], v[24:25], off nt
	v_add_co_u32_e32 v28, vcc, s87, v32
	s_lshl_b32 s7, s7, 1
	s_nop 0
	v_addc_co_u32_e32 v29, vcc, 0, v33, vcc
	global_load_dwordx4 v[28:31], v[28:29], off nt
	v_add_co_u32_e32 v32, vcc, s89, v32
	s_add_u32 s8, s3, s7
	s_nop 0
	v_addc_co_u32_e32 v33, vcc, 0, v33, vcc
	global_load_dwordx4 v[32:35], v[32:33], off nt
	s_addc_u32 s9, s6, 0
	v_readlane_b32 s49, v253, 17
	v_readlane_b32 s50, v253, 18
	v_readlane_b32 s51, v253, 19
	v_readlane_b32 s52, v253, 20
	v_readlane_b32 s53, v253, 21
	v_readlane_b32 s56, v253, 24
	v_readlane_b32 s57, v253, 25
	v_readlane_b32 s58, v253, 26
	v_readlane_b32 s59, v253, 27
	v_readlane_b32 s60, v253, 28
	v_readlane_b32 s61, v253, 29
	v_readlane_b32 s62, v253, 30
	v_readlane_b32 s63, v253, 31
	s_waitcnt vmcnt(0)
	ds_write2_b32 v45, v4, v5 offset1:1
	ds_write2_b32 v45, v6, v7 offset0:2 offset1:3
	v_add_u32_e32 v4, 0x420, v2
	ds_write2_b32 v2, v8, v9 offset1:1
	ds_write2_b32 v2, v10, v11 offset0:2 offset1:3
	ds_write2_b32 v4, v12, v13 offset1:1
	v_add_u32_e32 v4, 0x428, v2
	ds_write2_b32 v4, v14, v15 offset1:1
	v_add_u32_e32 v4, 0x840, v2
	v_add_u32_e32 v2, 0x848, v2
	ds_write2_b32 v2, v18, v19 offset1:1
	v_add_u32_e32 v2, 0x1080, v45
	ds_write2_b32 v4, v16, v17 offset1:1
	ds_write2_b32 v2, v20, v21 offset1:1
	v_add_u32_e32 v2, 0x1088, v45
	ds_write2_b32 v2, v22, v23 offset1:1
	v_add_u32_e32 v2, 0x14a0, v45
	ds_write2_b32 v2, v24, v25 offset1:1
	v_add_u32_e32 v2, 0x14a8, v45
	ds_write2_b32 v2, v26, v27 offset1:1
	v_add_u32_e32 v2, 0x18c0, v45
	ds_write2_b32 v2, v28, v29 offset1:1
	v_add_u32_e32 v2, 0x18c8, v45
	ds_write2_b32 v2, v30, v31 offset1:1
	v_add_u32_e32 v2, 0x1ce0, v45
	ds_write2_b32 v2, v32, v33 offset1:1
	v_add_u32_e32 v2, 0x1ce8, v45
	ds_write2_b32 v2, v34, v35 offset1:1
	s_waitcnt lgkmcnt(0)
	ds_read2_b32 v[10:11], v50 offset0:33 offset1:41
	ds_read2_b32 v[12:13], v50 offset1:8
	v_lshlrev_b32_e32 v2, 1, v38
	ds_read2_b32 v[14:15], v50 offset0:66 offset1:74
	ds_read2_b32 v[16:17], v50 offset0:99 offset1:107
	ds_read2_b32 v[18:19], v50 offset0:132 offset1:140
	ds_read2_b32 v[20:21], v50 offset0:165 offset1:173
	ds_read2_b32 v[22:23], v50 offset0:198 offset1:206
	ds_read2_b32 v[24:25], v50 offset0:231 offset1:239
	v_lshl_add_u64 v[8:9], s[8:9], 0, v[2:3]
	v_or_b32_e32 v2, s2, v39
	v_lshlrev_b32_e32 v2, 11, v2
	v_lshl_add_u64 v[26:27], v[8:9], 0, v[2:3]
	v_or_b32_e32 v2, s2, v46
	s_waitcnt lgkmcnt(0)
	v_cvt_pk_bf16_f32 v4, v12, v10
	v_lshlrev_b32_e32 v2, 11, v2
	v_cvt_pk_bf16_f32 v5, v14, v16
	v_cvt_pk_bf16_f32 v6, v18, v20
	v_cvt_pk_bf16_f32 v7, v22, v24
	global_store_dwordx4 v[26:27], v[4:7], off sc1
	s_nop 1
	v_cvt_pk_bf16_f32 v4, v13, v11
	v_lshl_add_u64 v[10:11], v[8:9], 0, v[2:3]
	v_cvt_pk_bf16_f32 v5, v15, v17
	v_cvt_pk_bf16_f32 v6, v19, v21
	v_cvt_pk_bf16_f32 v7, v23, v25
	global_store_dwordx4 v[10:11], v[4:7], off sc1
	ds_read2_b32 v[10:11], v50 offset0:16 offset1:24
	ds_read2_b32 v[12:13], v50 offset0:49 offset1:57
	ds_read2_b32 v[14:15], v50 offset0:82 offset1:90
	ds_read2_b32 v[16:17], v50 offset0:115 offset1:123
	ds_read2_b32 v[18:19], v50 offset0:148 offset1:156
	ds_read2_b32 v[20:21], v50 offset0:181 offset1:189
	ds_read2_b32 v[22:23], v50 offset0:214 offset1:222
	ds_read2_b32 v[24:25], v50 offset0:247 offset1:255
	v_or_b32_e32 v2, s2, v48
	v_lshlrev_b32_e32 v2, 11, v2
	v_lshl_add_u64 v[26:27], v[8:9], 0, v[2:3]
	v_or_b32_e32 v2, s2, v49
	v_lshlrev_b32_e32 v2, 11, v2
	s_waitcnt lgkmcnt(6)
	v_cvt_pk_bf16_f32 v4, v10, v12
	s_waitcnt lgkmcnt(4)
	v_cvt_pk_bf16_f32 v5, v14, v16
	s_waitcnt lgkmcnt(2)
	v_cvt_pk_bf16_f32 v6, v18, v20
	s_waitcnt lgkmcnt(0)
	v_cvt_pk_bf16_f32 v7, v22, v24
	v_lshl_add_u64 v[8:9], v[8:9], 0, v[2:3]
	global_store_dwordx4 v[26:27], v[4:7], off sc1
	s_nop 1
	v_cvt_pk_bf16_f32 v4, v11, v13
	v_cvt_pk_bf16_f32 v5, v15, v17
	v_cvt_pk_bf16_f32 v6, v19, v21
	v_cvt_pk_bf16_f32 v7, v23, v25
	global_store_dwordx4 v[8:9], v[4:7], off sc1
	s_waitcnt lgkmcnt(0)

; #define GAS __attribute__((address_space(1)))
; #define LAS __attribute__((address_space(3)))
; #define LDS_WAIT() asm volatile("s_waitcnt lgkmcnt(0)" ::: "memory")
; __device__ __forceinline__ unsigned pk2(float lo, float hi) { unsigned r; asm("v_cvt_pk_bf16_f32 %0, %1, %2" : "=v"(r) : "v"(lo), "v"(hi)); return r; }
; __device__ __forceinline__ void transpose_item(const float* W, int K, int N, bf16* WT, int drow0, int kb, int n0, LAS float* scr, int lane) {
;     const int k0 = 64 * kb; const int c4 = 4 * (lane & 7); const bool ok = (n0 + c4) < N;
;     f32x4 v[8];
; #pragma unroll
;     for (int i = 0; i < 8; ++i) { const int kk = 8 * i + (lane >> 3); v[i] = ok ? *(const f32x4*)(W + (size_t)(k0 + kk) * N + n0 + c4) : (f32x4){0.f, 0.f, 0.f, 0.f}; }
; #pragma unroll
;     for (int i = 0; i < 8; ++i) { const int kk = 8 * i + (lane >> 3); LAS float* d = scr + kk * 33 + c4; d[0] = v[i][0]; d[1] = v[i][1]; d[2] = v[i][2]; d[3] = v[i][3]; }
;     LDS_WAIT(); asm volatile("" ::: "memory");
;     const int c = lane & 7;
; #pragma unroll
;     for (int j = 0; j < 4; ++j) { const int n = (lane >> 3) + 8 * j; const LAS float* s = scr + (8 * c) * 33 + n;
;         v4u o; o.x = pk2(s[0 * 33], s[1 * 33]); o.y = pk2(s[2 * 33], s[3 * 33]); o.z = pk2(s[4 * 33], s[5 * 33]); o.w = pk2(s[6 * 33], s[7 * 33]);
;         *(GAS v4u*)(WT + (size_t)(drow0 + n) * K + k0 + 8 * c) = o; }
;     LDS_WAIT(); asm volatile("" ::: "memory");
; }
; __device__ __forceinline__ void convert_item(const In& I, unsigned char* ws, int it, LAS float* scr, int lane) {
;     ...
;     if (r < T0) { const int f = r / I_FFN; r -= f * I_FFN;
;         if (r < 2 * I_G) { const int up = r >= I_G; r -= up * I_G; const int kb = r / 88, nb = r % 88;
;             transpose_item((up ? I.w_up : I.w_gate) + (size_t)f * D * FF, D, FF, Wgu + (size_t)f * NGU * D, 256 * (nb >> 2) + 32 * (nb & 3) + 128 * up, kb, 32 * nb, scr, lane); }
;         else { r -= 2 * I_G; const int kb = r / 32, nb = r % 32; transpose_item(I.w_down + (size_t)f * FF * D, FF, D, Wd + (size_t)f * D * FF, 32 * nb, kb, 32 * nb, scr, lane); }
.LBB0_409:
	s_andn2_b64 vcc, exec, s[2:3]
	s_cbranch_vccnz .LBB0_354
	s_mul_hi_i32 s2, s45, 0x3e0f83e1
	s_lshr_b32 s3, s2, 31
	s_ashr_i32 s6, s2, 10
	s_add_i32 s6, s6, s3
	s_mul_i32 s2, s6, 0xffffef80
	s_add_i32 s7, s41, s2
	s_add_i32 s7, s7, 0xa800
	s_cmpk_gt_i32 s7, 0xaff
	s_mov_b64 s[2:3], -1
	s_cbranch_scc0 .LBB0_412
	v_readlane_b32 s48, v253, 0
	v_readlane_b32 s49, v253, 1
	v_readlane_b32 s50, v253, 2
	v_readlane_b32 s51, v253, 3
	v_readlane_b32 s52, v253, 4
	v_readlane_b32 s53, v253, 5
	v_readlane_b32 s54, v253, 6
	v_readlane_b32 s55, v253, 7
	v_readlane_b32 s56, v253, 8
	v_readlane_b32 s57, v253, 9
	s_mov_b64 s[48:49], s[52:53]
	s_mul_i32 s3, s6, 0xb00000
	s_mov_b64 s[50:51], s[54:55]
	s_mov_b64 s[52:53], s[56:57]
	s_mul_hi_i32 s2, s6, 0xb00000
	s_add_u32 s9, s52, s3
	s_addc_u32 s11, s53, s2
	s_mul_i32 s3, s6, 0x580000
	s_mul_hi_i32 s2, s6, 0x580000
	s_add_u32 s3, s1, s3
	s_mul_i32 s10, s6, 0xffffdf00
	s_addc_u32 s8, s19, s2
	s_add_i32 s10, s44, s10
	s_add_i32 s10, s10, 0x11600
	s_and_b32 s2, s43, 0x3e0
	s_andn2_b32 s10, s10, 63
	s_add_i32 s68, s10, 0xffffea00
	s_lshl_b32 s10, s2, 2
	v_or_b32_e32 v32, s68, v39
	s_add_u32 s10, s9, s10
	s_addc_u32 s11, s11, 0
	v_lshlrev_b32_e32 v2, 2, v36
	v_ashrrev_i32_e32 v33, 31, v32
	v_or_b32_e32 v8, 8, v32
	v_or_b32_e32 v12, 16, v32
	v_lshl_add_u64 v[34:35], s[10:11], 0, v[2:3]
	v_lshlrev_b64 v[4:5], 12, v[32:33]
	v_ashrrev_i32_e32 v9, 31, v8
	v_ashrrev_i32_e32 v13, 31, v12
	v_lshl_add_u64 v[4:5], v[34:35], 0, v[4:5]
	v_lshlrev_b64 v[8:9], 12, v[8:9]
	v_lshlrev_b64 v[12:13], 12, v[12:13]
	v_or_b32_e32 v16, 24, v32
	global_load_dwordx4 v[4:7], v[4:5], off nt
	v_lshl_add_u64 v[8:9], v[34:35], 0, v[8:9]
	v_lshl_add_u64 v[12:13], v[34:35], 0, v[12:13]
	v_ashrrev_i32_e32 v17, 31, v16
	v_or_b32_e32 v20, 32, v32
	global_load_dwordx4 v[8:11], v[8:9], off nt
	v_lshlrev_b64 v[16:17], 12, v[16:17]
	global_load_dwordx4 v[12:15], v[12:13], off nt
	v_ashrrev_i32_e32 v21, 31, v20
	v_lshl_add_u64 v[16:17], v[34:35], 0, v[16:17]
	v_lshlrev_b64 v[20:21], 12, v[20:21]
	v_or_b32_e32 v24, 40, v32
	global_load_dwordx4 v[16:19], v[16:17], off nt
	v_lshl_add_u64 v[20:21], v[34:35], 0, v[20:21]
	v_ashrrev_i32_e32 v25, 31, v24
	global_load_dwordx4 v[20:23], v[20:21], off nt
	v_lshlrev_b64 v[24:25], 12, v[24:25]
	v_or_b32_e32 v28, 48, v32
	v_lshl_add_u64 v[24:25], v[34:35], 0, v[24:25]
	v_ashrrev_i32_e32 v29, 31, v28
	global_load_dwordx4 v[24:27], v[24:25], off nt
	v_lshlrev_b64 v[28:29], 12, v[28:29]
	v_or_b32_e32 v32, 56, v32
	v_lshl_add_u64 v[28:29], v[34:35], 0, v[28:29]
	v_ashrrev_i32_e32 v33, 31, v32
	global_load_dwordx4 v[28:31], v[28:29], off nt
	v_lshlrev_b64 v[32:33], 12, v[32:33]
	v_lshl_add_u64 v[32:33], v[34:35], 0, v[32:33]
	global_load_dwordx4 v[32:35], v[32:33], off nt
	v_add_u32_e32 v2, v44, v47
	s_lshl_b64 s[10:11], s[68:69], 1
	s_add_u32 s10, s3, s10
	s_addc_u32 s11, s8, s11
	v_readlane_b32 s58, v253, 10
	v_readlane_b32 s59, v253, 11
	v_readlane_b32 s60, v253, 12
	v_readlane_b32 s61, v253, 13
	v_readlane_b32 s62, v253, 14
	v_readlane_b32 s63, v253, 15
	s_waitcnt vmcnt(0)
	ds_write2_b32 v45, v4, v5 offset1:1
	ds_write2_b32 v45, v6, v7 offset0:2 offset1:3
	v_add_u32_e32 v4, 0x420, v2
	ds_write2_b32 v2, v8, v9 offset1:1
	ds_write2_b32 v2, v10, v11 offset0:2 offset1:3
	ds_write2_b32 v4, v12, v13 offset1:1
	v_add_u32_e32 v4, 0x428, v2
	ds_write2_b32 v4, v14, v15 offset1:1
	v_add_u32_e32 v4, 0x840, v2
	v_add_u32_e32 v2, 0x848, v2
	ds_write2_b32 v2, v18, v19 offset1:1
	v_add_u32_e32 v2, 0x1080, v45
	ds_write2_b32 v4, v16, v17 offset1:1
	ds_write2_b32 v2, v20, v21 offset1:1
	v_add_u32_e32 v2, 0x1088, v45
	ds_write2_b32 v2, v22, v23 offset1:1
	v_add_u32_e32 v2, 0x14a0, v45
	ds_write2_b32 v2, v24, v25 offset1:1
	v_add_u32_e32 v2, 0x14a8, v45
	ds_write2_b32 v2, v26, v27 offset1:1
	v_add_u32_e32 v2, 0x18c0, v45
	ds_write2_b32 v2, v28, v29 offset1:1
	v_add_u32_e32 v2, 0x18c8, v45
	ds_write2_b32 v2, v30, v31 offset1:1
	v_add_u32_e32 v2, 0x1ce0, v45
	ds_write2_b32 v2, v32, v33 offset1:1
	v_add_u32_e32 v2, 0x1ce8, v45
	ds_write2_b32 v2, v34, v35 offset1:1
	s_waitcnt lgkmcnt(0)
	ds_read2_b32 v[10:11], v50 offset0:33 offset1:41
	ds_read2_b32 v[12:13], v50 offset1:8
	v_lshlrev_b32_e32 v2, 1, v38
	ds_read2_b32 v[14:15], v50 offset0:66 offset1:74
	ds_read2_b32 v[16:17], v50 offset0:99 offset1:107
	ds_read2_b32 v[18:19], v50 offset0:132 offset1:140
	ds_read2_b32 v[20:21], v50 offset0:165 offset1:173
	ds_read2_b32 v[22:23], v50 offset0:198 offset1:206
	ds_read2_b32 v[24:25], v50 offset0:231 offset1:239
	v_lshl_add_u64 v[8:9], s[10:11], 0, v[2:3]
	v_or_b32_e32 v2, s2, v39
	v_mul_u32_u24_e32 v2, 0x1600, v2
	v_lshl_add_u64 v[26:27], v[8:9], 0, v[2:3]
	v_or_b32_e32 v2, s2, v46
	s_waitcnt lgkmcnt(0)
	v_cvt_pk_bf16_f32 v4, v12, v10
	v_mul_u32_u24_e32 v2, 0x1600, v2
	v_cvt_pk_bf16_f32 v5, v14, v16
	v_cvt_pk_bf16_f32 v6, v18, v20
	v_cvt_pk_bf16_f32 v7, v22, v24
	global_store_dwordx4 v[26:27], v[4:7], off sc1
	s_nop 1
	v_cvt_pk_bf16_f32 v4, v13, v11
	v_lshl_add_u64 v[10:11], v[8:9], 0, v[2:3]
	v_cvt_pk_bf16_f32 v5, v15, v17
	v_cvt_pk_bf16_f32 v6, v19, v21
	v_cvt_pk_bf16_f32 v7, v23, v25
	global_store_dwordx4 v[10:11], v[4:7], off sc1
	ds_read2_b32 v[10:11], v50 offset0:16 offset1:24
	ds_read2_b32 v[12:13], v50 offset0:49 offset1:57
	ds_read2_b32 v[14:15], v50 offset0:82 offset1:90
	ds_read2_b32 v[16:17], v50 offset0:115 offset1:123
	ds_read2_b32 v[18:19], v50 offset0:148 offset1:156
	ds_read2_b32 v[20:21], v50 offset0:181 offset1:189
	ds_read2_b32 v[22:23], v50 offset0:214 offset1:222
	ds_read2_b32 v[24:25], v50 offset0:247 offset1:255
	v_or_b32_e32 v2, s2, v48
	v_mul_u32_u24_e32 v2, 0x1600, v2
	v_lshl_add_u64 v[26:27], v[8:9], 0, v[2:3]
	v_or_b32_e32 v2, s2, v49
	v_mul_u32_u24_e32 v2, 0x1600, v2
	s_waitcnt lgkmcnt(6)
	v_cvt_pk_bf16_f32 v4, v10, v12
	s_waitcnt lgkmcnt(4)
	v_cvt_pk_bf16_f32 v5, v14, v16
	s_waitcnt lgkmcnt(2)
	v_cvt_pk_bf16_f32 v6, v18, v20
	s_waitcnt lgkmcnt(0)
	v_cvt_pk_bf16_f32 v7, v22, v24
	v_lshl_add_u64 v[8:9], v[8:9], 0, v[2:3]
	global_store_dwordx4 v[26:27], v[4:7], off sc1
	s_mov_b64 s[2:3], 0
	s_nop 0
	v_cvt_pk_bf16_f32 v4, v11, v13
	v_cvt_pk_bf16_f32 v5, v15, v17
	v_cvt_pk_bf16_f32 v6, v19, v21
	v_cvt_pk_bf16_f32 v7, v23, v25
	global_store_dwordx4 v[8:9], v[4:7], off sc1
	s_waitcnt lgkmcnt(0)
; #define GAS __attribute__((address_space(1)))
; #define LAS __attribute__((address_space(3)))
; #define LDS_WAIT() asm volatile("s_waitcnt lgkmcnt(0)" ::: "memory")
; __device__ __forceinline__ unsigned pk2(float lo, float hi) { unsigned r; asm("v_cvt_pk_bf16_f32 %0, %1, %2" : "=v"(r) : "v"(lo), "v"(hi)); return r; }
; __device__ __forceinline__ void transpose_item(const float* W, int K, int N, bf16* WT, int drow0, int kb, int n0, LAS float* scr, int lane) {
;     const int k0 = 64 * kb; const int c4 = 4 * (lane & 7); const bool ok = (n0 + c4) < N;
;     f32x4 v[8];
; #pragma unroll
;     for (int i = 0; i < 8; ++i) { const int kk = 8 * i + (lane >> 3); v[i] = ok ? *(const f32x4*)(W + (size_t)(k0 + kk) * N + n0 + c4) : (f32x4){0.f, 0.f, 0.f, 0.f}; }
; #pragma unroll
;     for (int i = 0; i < 8; ++i) { const int kk = 8 * i + (lane >> 3); LAS float* d = scr + kk * 33 + c4; d[0] = v[i][0]; d[1] = v[i][1]; d[2] = v[i][2]; d[3] = v[i][3]; }
;     LDS_WAIT(); asm volatile("" ::: "memory");
;     const int c = lane & 7;
; #pragma unroll
;     for (int j = 0; j < 4; ++j) { const int n = (lane >> 3) + 8 * j; const LAS float* s = scr + (8 * c) * 33 + n;
;         v4u o; o.x = pk2(s[0 * 33], s[1 * 33]); o.y = pk2(s[2 * 33], s[3 * 33]); o.z = pk2(s[4 * 33], s[5 * 33]); o.w = pk2(s[6 * 33], s[7 * 33]);
;         *(GAS v4u*)(WT + (size_t)(drow0 + n) * K + k0 + 8 * c) = o; }
;     LDS_WAIT(); asm volatile("" ::: "memory");
; }
; __device__ __forceinline__ void convert_item(const In& I, unsigned char* ws, int it, LAS float* scr, int lane) {
;     ...
;         if (r < 2 * I_G) { const int up = r >= I_G; r -= up * I_G; const int kb = r / 88, nb = r % 88;
;             transpose_item((up ? I.w_up : I.w_gate) + (size_t)f * D * FF, D, FF, Wgu + (size_t)f * NGU * D, 256 * (nb >> 2) + 32 * (nb & 3) + 128 * up, kb, 32 * nb, scr, lane); }
.LBB0_412:
	s_andn2_b64 vcc, exec, s[2:3]
	s_cbranch_vccnz .LBB0_354
	v_readlane_b32 s48, v253, 0
	v_readlane_b32 s49, v253, 1
	v_readlane_b32 s50, v253, 2
	v_readlane_b32 s51, v253, 3
	v_readlane_b32 s52, v253, 4
	v_readlane_b32 s53, v253, 5
	s_cmpk_gt_i32 s7, 0x57f
	v_readlane_b32 s54, v253, 6
	v_readlane_b32 s55, v253, 7
	v_readlane_b32 s56, v253, 8
	v_readlane_b32 s57, v253, 9
	s_mov_b64 s[48:49], s[52:53]
	s_cselect_b32 s2, 0xfffffa80, 0
	s_mul_i32 s3, s6, 0x1080
	s_mov_b64 s[50:51], s[54:55]
	s_cselect_b32 s9, 0x80, 0
	s_cselect_b32 s7, s50, s48
	s_cselect_b32 s8, s51, s49
	s_sub_i32 s2, s2, s3
	s_add_i32 s2, s41, s2
	s_add_i32 s2, s2, 0xa800
	s_mul_hi_i32 s3, s2, 0x2e8ba2e9
	s_lshr_b32 s10, s3, 31
	s_ashr_i32 s3, s3, 4
	s_add_i32 s3, s3, s10
	s_mul_i32 s10, s3, 0x58
	s_sub_i32 s2, s2, s10
	s_mul_hi_i32 s10, s6, 0xb00000
	s_mul_i32 s6, s6, 0xb00000
	s_add_u32 s12, s7, s6
	s_addc_u32 s13, s8, s10
	s_add_u32 s7, s28, s6
	s_addc_u32 s8, s29, s10
	s_lshl_b32 s10, s2, 5
	s_lshl_b32 s6, s2, 6
	s_and_b32 s2, s10, 0x60
	s_and_b32 s6, s6, 0xffffff00
	s_or_b32 s2, s2, s9
	s_ashr_i32 s11, s10, 31
	s_or_b32 s6, s2, s6
	s_lshl_b32 s2, s3, 6
	s_lshl_b64 s[10:11], s[10:11], 2
	s_add_u32 s10, s12, s10
	v_or_b32_e32 v34, s2, v39
	s_addc_u32 s11, s13, s11
	v_lshlrev_b32_e32 v2, 2, v36
	v_lshl_add_u64 v[32:33], s[10:11], 0, v[2:3]
	s_movk_i32 s3, 0x2c00
	v_or_b32_e32 v2, 8, v34
	v_mad_i64_i32 v[4:5], s[10:11], v34, s3, v[32:33]
	v_mad_i64_i32 v[8:9], s[10:11], v2, s3, v[32:33]
	v_or_b32_e32 v2, 16, v34
	global_load_dwordx4 v[4:7], v[4:5], off nt
	v_mad_i64_i32 v[12:13], s[10:11], v2, s3, v[32:33]
	global_load_dwordx4 v[8:11], v[8:9], off nt
	v_or_b32_e32 v2, 24, v34
	global_load_dwordx4 v[12:15], v[12:13], off nt
	v_mad_i64_i32 v[16:17], s[10:11], v2, s3, v[32:33]
	v_or_b32_e32 v2, 32, v34
	global_load_dwordx4 v[16:19], v[16:17], off nt
	v_mad_i64_i32 v[20:21], s[10:11], v2, s3, v[32:33]
	global_load_dwordx4 v[20:23], v[20:21], off nt
	v_or_b32_e32 v2, 40, v34
	v_mad_i64_i32 v[24:25], s[10:11], v2, s3, v[32:33]
	global_load_dwordx4 v[24:27], v[24:25], off nt
	v_or_b32_e32 v2, 48, v34
	v_mad_i64_i32 v[28:29], s[10:11], v2, s3, v[32:33]
	global_load_dwordx4 v[28:31], v[28:29], off nt
	v_or_b32_e32 v2, 56, v34
	v_mad_i64_i32 v[32:33], s[10:11], v2, s3, v[32:33]
	global_load_dwordx4 v[32:35], v[32:33], off nt
	v_add_u32_e32 v2, v44, v47
	s_ashr_i32 s3, s2, 31
	s_lshl_b64 s[2:3], s[2:3], 1
	s_add_u32 s2, s7, s2
	s_addc_u32 s3, s8, s3
	v_readlane_b32 s58, v253, 10
	v_readlane_b32 s59, v253, 11
	v_readlane_b32 s60, v253, 12
	v_readlane_b32 s61, v253, 13
	v_readlane_b32 s62, v253, 14
	v_readlane_b32 s63, v253, 15
	s_mov_b64 s[52:53], s[56:57]
	s_waitcnt vmcnt(0)
	ds_write2_b32 v45, v4, v5 offset1:1
	ds_write2_b32 v45, v6, v7 offset0:2 offset1:3
	v_add_u32_e32 v4, 0x420, v2
	ds_write2_b32 v2, v8, v9 offset1:1
	ds_write2_b32 v2, v10, v11 offset0:2 offset1:3
	ds_write2_b32 v4, v12, v13 offset1:1
	v_add_u32_e32 v4, 0x428, v2
	ds_write2_b32 v4, v14, v15 offset1:1
	v_add_u32_e32 v4, 0x840, v2
	v_add_u32_e32 v2, 0x848, v2
	ds_write2_b32 v2, v18, v19 offset1:1
	v_add_u32_e32 v2, 0x1080, v45
	ds_write2_b32 v2, v20, v21 offset1:1
	v_add_u32_e32 v2, 0x1088, v45
	ds_write2_b32 v2, v22, v23 offset1:1
	v_add_u32_e32 v2, 0x14a0, v45
	ds_write2_b32 v2, v24, v25 offset1:1
	v_add_u32_e32 v2, 0x14a8, v45
	ds_write2_b32 v2, v26, v27 offset1:1
	v_add_u32_e32 v2, 0x18c0, v45
	ds_write2_b32 v2, v28, v29 offset1:1
	v_add_u32_e32 v2, 0x18c8, v45
	ds_write2_b32 v2, v30, v31 offset1:1
	v_add_u32_e32 v2, 0x1ce0, v45
	ds_write2_b32 v2, v32, v33 offset1:1
	v_add_u32_e32 v2, 0x1ce8, v45
	ds_write2_b32 v4, v16, v17 offset1:1
	ds_write2_b32 v2, v34, v35 offset1:1
	s_waitcnt lgkmcnt(0)
	ds_read2_b32 v[10:11], v50 offset0:33 offset1:41
	ds_read2_b32 v[12:13], v50 offset1:8
	ds_read2_b32 v[14:15], v50 offset0:66 offset1:74
	ds_read2_b32 v[16:17], v50 offset0:99 offset1:107
	ds_read2_b32 v[18:19], v50 offset0:132 offset1:140
	ds_read2_b32 v[20:21], v50 offset0:165 offset1:173
	ds_read2_b32 v[22:23], v50 offset0:198 offset1:206
	ds_read2_b32 v[24:25], v50 offset0:231 offset1:239
	v_or_b32_e32 v26, s6, v39
	v_lshlrev_b32_e32 v2, 1, v38
	v_ashrrev_i32_e32 v27, 31, v26
	v_lshl_add_u64 v[8:9], s[2:3], 0, v[2:3]
	v_lshlrev_b64 v[26:27], 11, v[26:27]
	s_waitcnt lgkmcnt(0)
	v_cvt_pk_bf16_f32 v4, v12, v10
	v_lshl_add_u64 v[26:27], v[8:9], 0, v[26:27]
	v_or_b32_e32 v10, s6, v46
	v_cvt_pk_bf16_f32 v5, v14, v16
	v_cvt_pk_bf16_f32 v6, v18, v20
	v_cvt_pk_bf16_f32 v7, v22, v24
	global_store_dwordx4 v[26:27], v[4:7], off sc1
	v_or_b32_e32 v26, s6, v48
	v_ashrrev_i32_e32 v27, 31, v26
	v_cvt_pk_bf16_f32 v4, v13, v11
	v_ashrrev_i32_e32 v11, 31, v10
	v_lshlrev_b64 v[10:11], 11, v[10:11]
	v_lshl_add_u64 v[10:11], v[8:9], 0, v[10:11]
	v_cvt_pk_bf16_f32 v5, v15, v17
	v_cvt_pk_bf16_f32 v6, v19, v21
	v_cvt_pk_bf16_f32 v7, v23, v25
	global_store_dwordx4 v[10:11], v[4:7], off sc1
	ds_read2_b32 v[10:11], v50 offset0:16 offset1:24
	ds_read2_b32 v[12:13], v50 offset0:49 offset1:57
	ds_read2_b32 v[14:15], v50 offset0:82 offset1:90
	ds_read2_b32 v[16:17], v50 offset0:115 offset1:123
	ds_read2_b32 v[18:19], v50 offset0:148 offset1:156
	ds_read2_b32 v[20:21], v50 offset0:181 offset1:189
	ds_read2_b32 v[22:23], v50 offset0:214 offset1:222
	ds_read2_b32 v[24:25], v50 offset0:247 offset1:255
	v_lshlrev_b64 v[26:27], 11, v[26:27]
	s_waitcnt lgkmcnt(6)
	v_cvt_pk_bf16_f32 v4, v10, v12
	v_lshl_add_u64 v[26:27], v[8:9], 0, v[26:27]
	v_or_b32_e32 v10, s6, v49
	s_waitcnt lgkmcnt(4)
	v_cvt_pk_bf16_f32 v5, v14, v16
	s_waitcnt lgkmcnt(2)
	v_cvt_pk_bf16_f32 v6, v18, v20
	s_waitcnt lgkmcnt(0)
	v_cvt_pk_bf16_f32 v7, v22, v24
	global_store_dwordx4 v[26:27], v[4:7], off sc1
	s_nop 1
	v_cvt_pk_bf16_f32 v4, v11, v13
	v_ashrrev_i32_e32 v11, 31, v10
	v_lshlrev_b64 v[10:11], 11, v[10:11]
	v_lshl_add_u64 v[8:9], v[8:9], 0, v[10:11]
	v_cvt_pk_bf16_f32 v5, v15, v17
	v_cvt_pk_bf16_f32 v6, v19, v21
	v_cvt_pk_bf16_f32 v7, v23, v25
	global_store_dwordx4 v[8:9], v[4:7], off sc1
	s_waitcnt lgkmcnt(0)
	s_branch .LBB0_354

; #define GAS __attribute__((address_space(1)))
; __device__ __forceinline__ void transpose_item(const float* W, int K, int N, bf16* WT, int drow0, int kb, int n0, LAS float* scr, int lane) {
;     const int k0 = 64 * kb; const int c4 = 4 * (lane & 7); const bool ok = (n0 + c4) < N;
;     f32x4 v[8];
; #pragma unroll
;     for (int i = 0; i < 8; ++i) { const int kk = 8 * i + (lane >> 3); v[i] = ok ? *(const f32x4*)(W + (size_t)(k0 + kk) * N + n0 + c4) : (f32x4){0.f, 0.f, 0.f, 0.f}; }
; #pragma unroll
;     for (int i = 0; i < 8; ++i) { const int kk = 8 * i + (lane >> 3); LAS float* d = scr + kk * 33 + c4; d[0] = v[i][0]; d[1] = v[i][1]; d[2] = v[i][2]; d[3] = v[i][3]; }
;     LDS_WAIT(); asm volatile("" ::: "memory");
;     const int c = lane & 7;
; #pragma unroll
;     for (int j = 0; j < 4; ++j) { const int n = (lane >> 3) + 8 * j; const LAS float* s = scr + (8 * c) * 33 + n;
;         v4u o; o.x = pk2(s[0 * 33], s[1 * 33]); o.y = pk2(s[2 * 33], s[3 * 33]); o.z = pk2(s[4 * 33], s[5 * 33]); o.w = pk2(s[6 * 33], s[7 * 33]);
;         *(GAS v4u*)(WT + (size_t)(drow0 + n) * K + k0 + 8 * c) = o; }
;     LDS_WAIT(); asm volatile("" ::: "memory");
; }
; __device__ __forceinline__ void convert_item(const In& I, unsigned char* ws, int it, LAS float* scr, int lane) {
;     ...
;     int r = it;
;     if (r < T0) { const int f = r / I_FFN; r -= f * I_FFN;
;         if (r < 2 * I_G) { const int up = r >= I_G; r -= up * I_G; const int kb = r / 88, nb = r % 88;
;             transpose_item((up ? I.w_up : I.w_gate) + (size_t)f * D * FF, D, FF, Wgu + (size_t)f * NGU * D, 256 * (nb >> 2) + 32 * (nb & 3) + 128 * up, kb, 32 * nb, scr, lane); }
;         else { r -= 2 * I_G; const int kb = r / 32, nb = r % 32; transpose_item(I.w_down + (size_t)f * FF * D, FF, D, Wd + (size_t)f * D * FF, 32 * nb, kb, 32 * nb, scr, lane); }
;         return; }
;     r -= T0;
;     if (r < 2 * I_NIN) { const int j = r / I_NIN; r -= j * I_NIN; const int kb = r / 88, nb = r % 88;
;         transpose_item(I.nsa_w_in + (size_t)j * D * NSA_IN, D, NSA_IN, Wnin + (size_t)j * NSA_IN_PAD * D, 32 * nb, kb, 32 * nb, scr, lane); return; }
;     r -= 2 * I_NIN;
;     if (r < 2 * I_SQ) { const int j = r / I_SQ; r -= j * I_SQ; const int kb = r / 32, nb = r % 32;
;         transpose_item(I.nsa_w_out + (size_t)j * D * D, D, D, Wnout + (size_t)j * D * D, 32 * nb, kb, 32 * nb, scr, lane); return; }
;     r -= 2 * I_SQ;
.LBB0_416:
	s_add_i32 s43, s41, 0xa800
	s_cmp_gt_i32 s43, 0x83ff
	s_mov_b64 s[2:3], -1
	s_cbranch_scc0 .LBB0_470
	s_cmpk_gt_u32 s43, 0x8eff
	s_cbranch_scc0 .LBB0_451
	s_cmpk_gt_u32 s43, 0x92ff
	s_cbranch_scc0 .LBB0_448
	s_cmpk_gt_u32 s43, 0x9fff
	s_cbranch_scc0 .LBB0_429
	s_cmpk_gt_u32 s43, 0xa3ff
	s_cbranch_scc0 .LBB0_426
	s_cmpk_gt_u32 s43, 0xa7ff
	s_cbranch_scc0 .LBB0_423
	s_lshr_b32 s68, s41, 3
	v_readlane_b32 s44, v253, 16
	s_lshl_b64 s[2:3], s[68:69], 16
	v_readlane_b32 s48, v253, 20
	v_readlane_b32 s49, v253, 21
	s_add_u32 s6, s48, s2
	s_addc_u32 s7, s49, s3
	s_lshl_b64 s[2:3], s[68:69], 15
	s_add_u32 s8, s34, s2
	s_addc_u32 s3, s35, s3
	s_and_b32 s2, s42, 32
	s_and_b32 s9, s42, 0xc0
	s_lshl_b32 s10, s2, 2
	s_add_u32 s6, s6, s10
	v_or_b32_e32 v6, s9, v39
	s_addc_u32 s7, s7, 0
	v_lshlrev_b32_e32 v2, 2, v36
	v_lshl_add_u64 v[4:5], s[6:7], 0, v[2:3]
	v_lshlrev_b32_e32 v2, 8, v6
	v_lshl_add_u64 v[28:29], v[4:5], 0, v[2:3]
	v_add_co_u32_e32 v16, vcc, s84, v28
	global_load_dwordx4 v[4:7], v[28:29], off nt
	global_load_dwordx4 v[8:11], v[28:29], off offset:2048 nt
	v_addc_co_u32_e32 v17, vcc, 0, v29, vcc
	v_add_co_u32_e32 v24, vcc, s74, v28
	s_movk_i32 s6, 0x3000
	s_nop 0
	v_addc_co_u32_e32 v25, vcc, 0, v29, vcc
	global_load_dwordx4 v[12:15], v[24:25], off offset:-4096 nt
	s_nop 0
	global_load_dwordx4 v[16:19], v[16:17], off offset:2048 nt
	s_nop 0
	global_load_dwordx4 v[20:23], v[24:25], off nt
	s_nop 0
	global_load_dwordx4 v[24:27], v[24:25], off offset:2048 nt
	v_add_co_u32_e32 v32, vcc, s6, v28
	v_add_u32_e32 v2, v44, v47
	s_nop 0
	v_addc_co_u32_e32 v33, vcc, 0, v29, vcc
	global_load_dwordx4 v[28:31], v[32:33], off nt
	s_nop 0
	global_load_dwordx4 v[32:35], v[32:33], off offset:2048 nt
	s_lshl_b32 s6, s9, 1
	s_add_u32 s6, s8, s6
	s_addc_u32 s7, s3, 0
	v_readlane_b32 s45, v253, 17
	v_readlane_b32 s46, v253, 18
	v_readlane_b32 s47, v253, 19
	v_readlane_b32 s50, v253, 22
	v_readlane_b32 s51, v253, 23
	v_readlane_b32 s52, v253, 24
	v_readlane_b32 s53, v253, 25
	v_readlane_b32 s54, v253, 26
	v_readlane_b32 s55, v253, 27
	v_readlane_b32 s56, v253, 28
	v_readlane_b32 s57, v253, 29
	v_readlane_b32 s58, v253, 30
	v_readlane_b32 s59, v253, 31
	s_waitcnt vmcnt(0)
	ds_write2_b32 v45, v4, v5 offset1:1
	ds_write2_b32 v45, v6, v7 offset0:2 offset1:3
	v_add_u32_e32 v4, 0x420, v2
	ds_write2_b32 v2, v8, v9 offset1:1
	ds_write2_b32 v2, v10, v11 offset0:2 offset1:3
	ds_write2_b32 v4, v12, v13 offset1:1
	v_add_u32_e32 v4, 0x428, v2
	ds_write2_b32 v4, v14, v15 offset1:1
	v_add_u32_e32 v4, 0x840, v2
	v_add_u32_e32 v2, 0x848, v2
	ds_write2_b32 v2, v18, v19 offset1:1
	v_add_u32_e32 v2, 0x1080, v45
	ds_write2_b32 v2, v20, v21 offset1:1
	v_add_u32_e32 v2, 0x1088, v45
	ds_write2_b32 v2, v22, v23 offset1:1
	v_add_u32_e32 v2, 0x14a0, v45
	ds_write2_b32 v2, v24, v25 offset1:1
	v_add_u32_e32 v2, 0x14a8, v45
	ds_write2_b32 v2, v26, v27 offset1:1
	v_add_u32_e32 v2, 0x18c0, v45
	ds_write2_b32 v2, v28, v29 offset1:1
	v_add_u32_e32 v2, 0x18c8, v45
	ds_write2_b32 v2, v30, v31 offset1:1
	v_add_u32_e32 v2, 0x1ce0, v45
	ds_write2_b32 v2, v32, v33 offset1:1
	v_add_u32_e32 v2, 0x1ce8, v45
	ds_write2_b32 v4, v16, v17 offset1:1
	ds_write2_b32 v2, v34, v35 offset1:1
	s_waitcnt lgkmcnt(0)
	ds_read2_b32 v[10:11], v50 offset0:33 offset1:41
	ds_read2_b32 v[12:13], v50 offset1:8
	v_lshlrev_b32_e32 v2, 1, v38
	ds_read2_b32 v[14:15], v50 offset0:66 offset1:74
	ds_read2_b32 v[16:17], v50 offset0:99 offset1:107
	ds_read2_b32 v[18:19], v50 offset0:132 offset1:140
	ds_read2_b32 v[20:21], v50 offset0:165 offset1:173
	ds_read2_b32 v[22:23], v50 offset0:198 offset1:206
	ds_read2_b32 v[24:25], v50 offset0:231 offset1:239
	v_lshl_add_u64 v[4:5], s[6:7], 0, v[2:3]
	v_or_b32_e32 v2, s2, v39
	v_lshlrev_b32_e32 v2, 9, v2
	v_lshl_add_u64 v[26:27], v[4:5], 0, v[2:3]
	v_or_b32_e32 v2, s2, v46
	s_waitcnt lgkmcnt(0)
	v_cvt_pk_bf16_f32 v6, v12, v10
	v_lshlrev_b32_e32 v2, 9, v2
	v_cvt_pk_bf16_f32 v7, v14, v16
	v_cvt_pk_bf16_f32 v8, v18, v20
	v_cvt_pk_bf16_f32 v9, v22, v24
	global_store_dwordx4 v[26:27], v[6:9], off sc1
	s_nop 1
	v_cvt_pk_bf16_f32 v6, v13, v11
	v_lshl_add_u64 v[10:11], v[4:5], 0, v[2:3]
	v_cvt_pk_bf16_f32 v7, v15, v17
	v_cvt_pk_bf16_f32 v8, v19, v21
	v_cvt_pk_bf16_f32 v9, v23, v25
	global_store_dwordx4 v[10:11], v[6:9], off sc1
	ds_read2_b32 v[10:11], v50 offset0:16 offset1:24
	ds_read2_b32 v[12:13], v50 offset0:49 offset1:57
	ds_read2_b32 v[14:15], v50 offset0:82 offset1:90
	ds_read2_b32 v[16:17], v50 offset0:115 offset1:123
	ds_read2_b32 v[18:19], v50 offset0:148 offset1:156
	ds_read2_b32 v[20:21], v50 offset0:181 offset1:189
	ds_read2_b32 v[22:23], v50 offset0:214 offset1:222
	ds_read2_b32 v[24:25], v50 offset0:247 offset1:255
	v_or_b32_e32 v2, s2, v48
	v_lshlrev_b32_e32 v2, 9, v2
	v_lshl_add_u64 v[26:27], v[4:5], 0, v[2:3]
	v_or_b32_e32 v2, s2, v49
	v_lshlrev_b32_e32 v2, 9, v2
	s_waitcnt lgkmcnt(6)
	v_cvt_pk_bf16_f32 v6, v10, v12
	s_waitcnt lgkmcnt(4)
	v_cvt_pk_bf16_f32 v7, v14, v16
	s_waitcnt lgkmcnt(2)
	v_cvt_pk_bf16_f32 v8, v18, v20
	s_waitcnt lgkmcnt(0)
	v_cvt_pk_bf16_f32 v9, v22, v24
	v_lshl_add_u64 v[4:5], v[4:5], 0, v[2:3]
	global_store_dwordx4 v[26:27], v[6:9], off sc1
	s_mov_b64 s[2:3], 0
	s_nop 0
	v_cvt_pk_bf16_f32 v6, v11, v13
	v_cvt_pk_bf16_f32 v7, v15, v17
	v_cvt_pk_bf16_f32 v8, v19, v21
	v_cvt_pk_bf16_f32 v9, v23, v25
	global_store_dwordx4 v[4:5], v[6:9], off sc1
	s_waitcnt lgkmcnt(0)
; #define GAS __attribute__((address_space(1)))
; #define LAS __attribute__((address_space(3)))
; #define LDS_WAIT() asm volatile("s_waitcnt lgkmcnt(0)" ::: "memory")
; __device__ __forceinline__ unsigned pk2(float lo, float hi) { unsigned r; asm("v_cvt_pk_bf16_f32 %0, %1, %2" : "=v"(r) : "v"(lo), "v"(hi)); return r; }
; __device__ __forceinline__ void transpose_item(const float* W, int K, int N, bf16* WT, int drow0, int kb, int n0, LAS float* scr, int lane) {
;     const int k0 = 64 * kb; const int c4 = 4 * (lane & 7); const bool ok = (n0 + c4) < N;
;     f32x4 v[8];
; #pragma unroll
;     for (int i = 0; i < 8; ++i) { const int kk = 8 * i + (lane >> 3); v[i] = ok ? *(const f32x4*)(W + (size_t)(k0 + kk) * N + n0 + c4) : (f32x4){0.f, 0.f, 0.f, 0.f}; }
; #pragma unroll
;     for (int i = 0; i < 8; ++i) { const int kk = 8 * i + (lane >> 3); LAS float* d = scr + kk * 33 + c4; d[0] = v[i][0]; d[1] = v[i][1]; d[2] = v[i][2]; d[3] = v[i][3]; }
;     LDS_WAIT(); asm volatile("" ::: "memory");
;     const int c = lane & 7;
; #pragma unroll
;     for (int j = 0; j < 4; ++j) { const int n = (lane >> 3) + 8 * j; const LAS float* s = scr + (8 * c) * 33 + n;
;         v4u o; o.x = pk2(s[0 * 33], s[1 * 33]); o.y = pk2(s[2 * 33], s[3 * 33]); o.z = pk2(s[4 * 33], s[5 * 33]); o.w = pk2(s[6 * 33], s[7 * 33]);
;         *(GAS v4u*)(WT + (size_t)(drow0 + n) * K + k0 + 8 * c) = o; }
;     LDS_WAIT(); asm volatile("" ::: "memory");
; }
; __device__ __forceinline__ void convert_item(const In& I, unsigned char* ws, int it, LAS float* scr, int lane) {
;     ...
;     if (r < 4 * I_W1) { const int jk = r / I_W1; r -= jk * I_W1; const int kb = r / 8, nb = r % 8;
;         transpose_item(I.nsa_w1 + (size_t)jk * 2048 * 256, 2048, 256, W1t + (size_t)jk * 256 * 2048, 32 * nb, kb, 32 * nb, scr, lane); return; }
.LBB0_423:
	s_andn2_b64 vcc, exec, s[2:3]
	s_cbranch_vccnz .LBB0_425
	s_add_i32 s2, s41, 0x400
	s_lshr_b32 s68, s2, 8
	s_lshl_b64 s[2:3], s[68:69], 21
	v_readlane_b32 s44, v253, 16
	v_readlane_b32 s45, v253, 17
	s_add_u32 s6, s44, s2
	s_addc_u32 s7, s45, s3
	s_lshl_b64 s[2:3], s[68:69], 20
	s_add_u32 s8, s31, s2
	s_addc_u32 s3, s33, s3
	s_and_b32 s2, s42, 0xe0
	s_and_b32 s9, s40, 0x7c0
	s_lshl_b32 s10, s2, 2
	s_add_u32 s6, s6, s10
	v_or_b32_e32 v6, s9, v39
	s_addc_u32 s7, s7, 0
	v_lshlrev_b32_e32 v2, 2, v36
	v_lshl_add_u64 v[4:5], s[6:7], 0, v[2:3]
	v_lshlrev_b32_e32 v2, 10, v6
	v_lshl_add_u64 v[32:33], v[4:5], 0, v[2:3]
	v_add_co_u32_e32 v8, vcc, s74, v32
	s_movk_i32 s6, 0x4000
	s_nop 0
	v_addc_co_u32_e32 v9, vcc, 0, v33, vcc
	v_add_co_u32_e32 v12, vcc, s6, v32
	s_movk_i32 s6, 0x6000
	s_nop 0
	v_addc_co_u32_e32 v13, vcc, 0, v33, vcc
	global_load_dwordx4 v[4:7], v[32:33], off nt
	v_add_co_u32_e32 v16, vcc, s6, v32
	global_load_dwordx4 v[8:11], v[8:9], off nt
	s_nop 0
	v_addc_co_u32_e32 v17, vcc, 0, v33, vcc
	global_load_dwordx4 v[12:15], v[12:13], off nt
	v_add_co_u32_e32 v20, vcc, s81, v32
	global_load_dwordx4 v[16:19], v[16:17], off nt
	s_nop 0
	v_addc_co_u32_e32 v21, vcc, 0, v33, vcc
	s_mov_b32 s6, 0xa000
	global_load_dwordx4 v[20:23], v[20:21], off nt
	v_add_co_u32_e32 v24, vcc, s6, v32
	s_mov_b32 s6, 0xc000
	s_nop 0
	v_addc_co_u32_e32 v25, vcc, 0, v33, vcc
	global_load_dwordx4 v[24:27], v[24:25], off nt
	v_add_co_u32_e32 v28, vcc, s6, v32
	s_mov_b32 s6, 0xe000
	s_nop 0
	v_addc_co_u32_e32 v29, vcc, 0, v33, vcc
	global_load_dwordx4 v[28:31], v[28:29], off nt
	v_add_co_u32_e32 v32, vcc, s6, v32
	v_add_u32_e32 v2, v44, v47
	s_nop 0
	v_addc_co_u32_e32 v33, vcc, 0, v33, vcc
	global_load_dwordx4 v[32:35], v[32:33], off nt
	s_lshl_b32 s6, s9, 1
	s_add_u32 s6, s8, s6
	s_addc_u32 s7, s3, 0
	v_readlane_b32 s46, v253, 18
	v_readlane_b32 s47, v253, 19
	v_readlane_b32 s48, v253, 20
	v_readlane_b32 s49, v253, 21
	v_readlane_b32 s50, v253, 22
	v_readlane_b32 s51, v253, 23
	v_readlane_b32 s52, v253, 24
	v_readlane_b32 s53, v253, 25
	v_readlane_b32 s54, v253, 26
	v_readlane_b32 s55, v253, 27
	v_readlane_b32 s56, v253, 28
	v_readlane_b32 s57, v253, 29
	v_readlane_b32 s58, v253, 30
	v_readlane_b32 s59, v253, 31
	s_waitcnt vmcnt(0)
	ds_write2_b32 v45, v4, v5 offset1:1
	ds_write2_b32 v45, v6, v7 offset0:2 offset1:3
	v_add_u32_e32 v4, 0x420, v2
	ds_write2_b32 v2, v8, v9 offset1:1
	ds_write2_b32 v2, v10, v11 offset0:2 offset1:3
	ds_write2_b32 v4, v12, v13 offset1:1
	v_add_u32_e32 v4, 0x428, v2
	ds_write2_b32 v4, v14, v15 offset1:1
	v_add_u32_e32 v4, 0x840, v2
	v_add_u32_e32 v2, 0x848, v2
	ds_write2_b32 v2, v18, v19 offset1:1
	v_add_u32_e32 v2, 0x1080, v45
	ds_write2_b32 v2, v20, v21 offset1:1
	v_add_u32_e32 v2, 0x1088, v45
	ds_write2_b32 v2, v22, v23 offset1:1
	v_add_u32_e32 v2, 0x14a0, v45
	ds_write2_b32 v4, v16, v17 offset1:1
	ds_write2_b32 v2, v24, v25 offset1:1
	v_add_u32_e32 v2, 0x14a8, v45
	ds_write2_b32 v2, v26, v27 offset1:1
	v_add_u32_e32 v2, 0x18c0, v45
	ds_write2_b32 v2, v28, v29 offset1:1
	v_add_u32_e32 v2, 0x18c8, v45
	ds_write2_b32 v2, v30, v31 offset1:1
	v_add_u32_e32 v2, 0x1ce0, v45
	ds_write2_b32 v2, v32, v33 offset1:1
	v_add_u32_e32 v2, 0x1ce8, v45
	ds_write2_b32 v2, v34, v35 offset1:1
	s_waitcnt lgkmcnt(0)
	ds_read2_b32 v[10:11], v50 offset0:33 offset1:41
	ds_read2_b32 v[12:13], v50 offset1:8
	v_lshlrev_b32_e32 v2, 1, v38
	ds_read2_b32 v[14:15], v50 offset0:66 offset1:74
	ds_read2_b32 v[16:17], v50 offset0:99 offset1:107
	ds_read2_b32 v[18:19], v50 offset0:132 offset1:140
	ds_read2_b32 v[20:21], v50 offset0:165 offset1:173
	ds_read2_b32 v[22:23], v50 offset0:198 offset1:206
	ds_read2_b32 v[24:25], v50 offset0:231 offset1:239
	v_lshl_add_u64 v[4:5], s[6:7], 0, v[2:3]
	v_or_b32_e32 v2, s2, v39
	v_lshlrev_b32_e32 v2, 12, v2
	v_lshl_add_u64 v[26:27], v[4:5], 0, v[2:3]
	v_or_b32_e32 v2, s2, v46
	s_waitcnt lgkmcnt(0)
	v_cvt_pk_bf16_f32 v6, v12, v10
	v_lshlrev_b32_e32 v2, 12, v2
	v_cvt_pk_bf16_f32 v7, v14, v16
	v_cvt_pk_bf16_f32 v8, v18, v20
	v_cvt_pk_bf16_f32 v9, v22, v24
	global_store_dwordx4 v[26:27], v[6:9], off sc1
	s_nop 1
	v_cvt_pk_bf16_f32 v6, v13, v11
	v_lshl_add_u64 v[10:11], v[4:5], 0, v[2:3]
	v_cvt_pk_bf16_f32 v7, v15, v17
	v_cvt_pk_bf16_f32 v8, v19, v21
	v_cvt_pk_bf16_f32 v9, v23, v25
	global_store_dwordx4 v[10:11], v[6:9], off sc1
	ds_read2_b32 v[10:11], v50 offset0:16 offset1:24
	ds_read2_b32 v[12:13], v50 offset0:49 offset1:57
	ds_read2_b32 v[14:15], v50 offset0:82 offset1:90
	ds_read2_b32 v[16:17], v50 offset0:115 offset1:123
	ds_read2_b32 v[18:19], v50 offset0:148 offset1:156
	ds_read2_b32 v[20:21], v50 offset0:181 offset1:189
	ds_read2_b32 v[22:23], v50 offset0:214 offset1:222
	ds_read2_b32 v[24:25], v50 offset0:247 offset1:255
	v_or_b32_e32 v2, s2, v48
	v_lshlrev_b32_e32 v2, 12, v2
	v_lshl_add_u64 v[26:27], v[4:5], 0, v[2:3]
	v_or_b32_e32 v2, s2, v49
	v_lshlrev_b32_e32 v2, 12, v2
	s_waitcnt lgkmcnt(6)
	v_cvt_pk_bf16_f32 v6, v10, v12
	s_waitcnt lgkmcnt(4)
	v_cvt_pk_bf16_f32 v7, v14, v16
	s_waitcnt lgkmcnt(2)
	v_cvt_pk_bf16_f32 v8, v18, v20
	s_waitcnt lgkmcnt(0)
	v_cvt_pk_bf16_f32 v9, v22, v24
	v_lshl_add_u64 v[4:5], v[4:5], 0, v[2:3]
	global_store_dwordx4 v[26:27], v[6:9], off sc1
	s_nop 1
	v_cvt_pk_bf16_f32 v6, v11, v13
	v_cvt_pk_bf16_f32 v7, v15, v17
	v_cvt_pk_bf16_f32 v8, v19, v21
	v_cvt_pk_bf16_f32 v9, v23, v25
	global_store_dwordx4 v[4:5], v[6:9], off sc1
	s_waitcnt lgkmcnt(0)

; #define GAS __attribute__((address_space(1)))
; #define LAS __attribute__((address_space(3)))
; #define LDS_WAIT() asm volatile("s_waitcnt lgkmcnt(0)" ::: "memory")
; __device__ __forceinline__ unsigned pk2(float lo, float hi) { unsigned r; asm("v_cvt_pk_bf16_f32 %0, %1, %2" : "=v"(r) : "v"(lo), "v"(hi)); return r; }
; __device__ __forceinline__ void transpose_item(const float* W, int K, int N, bf16* WT, int drow0, int kb, int n0, LAS float* scr, int lane) {
;     const int k0 = 64 * kb; const int c4 = 4 * (lane & 7); const bool ok = (n0 + c4) < N;
;     f32x4 v[8];
; #pragma unroll
;     for (int i = 0; i < 8; ++i) { const int kk = 8 * i + (lane >> 3); v[i] = ok ? *(const f32x4*)(W + (size_t)(k0 + kk) * N + n0 + c4) : (f32x4){0.f, 0.f, 0.f, 0.f}; }
; #pragma unroll
;     for (int i = 0; i < 8; ++i) { const int kk = 8 * i + (lane >> 3); LAS float* d = scr + kk * 33 + c4; d[0] = v[i][0]; d[1] = v[i][1]; d[2] = v[i][2]; d[3] = v[i][3]; }
;     LDS_WAIT(); asm volatile("" ::: "memory");
;     const int c = lane & 7;
; #pragma unroll
;     for (int j = 0; j < 4; ++j) { const int n = (lane >> 3) + 8 * j; const LAS float* s = scr + (8 * c) * 33 + n;
;         v4u o; o.x = pk2(s[0 * 33], s[1 * 33]); o.y = pk2(s[2 * 33], s[3 * 33]); o.z = pk2(s[4 * 33], s[5 * 33]); o.w = pk2(s[6 * 33], s[7 * 33]);
;         *(GAS v4u*)(WT + (size_t)(drow0 + n) * K + k0 + 8 * c) = o; }
;     LDS_WAIT(); asm volatile("" ::: "memory");
; }
; __device__ __forceinline__ void convert_item(const In& I, unsigned char* ws, int it, LAS float* scr, int lane) {
;     ...
;     if (r < 2 * I_SQ) { const int j = r / I_SQ; r -= j * I_SQ; const int kb = r / 32, nb = r % 32;
;         transpose_item(I.fox_w_out + (size_t)j * D * D, D, D, Wfout + (size_t)j * D * D, 32 * nb, kb, 32 * nb, scr, lane); return; }
.LBB0_426:
	s_andn2_b64 vcc, exec, s[2:3]
	s_cbranch_vccnz .LBB0_428
	s_add_i32 s2, s41, 0x800
	s_lshr_b32 s68, s2, 9
	v_readlane_b32 s44, v253, 16
	s_lshl_b64 s[2:3], s[68:69], 22
	v_readlane_b32 s56, v253, 28
	v_readlane_b32 s57, v253, 29
	s_add_u32 s8, s56, s2
	s_addc_u32 s9, s57, s3
	s_lshl_b64 s[6:7], s[68:69], 21
	s_add_u32 s3, s26, s6
	s_addc_u32 s6, s27, s7
	s_and_b32 s2, s42, 0x3e0
	s_add_i32 s7, s0, 0x14000
	s_and_b32 s7, s7, 0x3c0
	s_lshl_b32 s10, s2, 2
	s_add_u32 s8, s8, s10
	v_or_b32_e32 v6, s7, v39
	s_addc_u32 s9, s9, 0
	v_lshlrev_b32_e32 v2, 2, v36
	v_lshl_add_u64 v[4:5], s[8:9], 0, v[2:3]
	v_lshlrev_b32_e32 v2, 12, v6
	v_lshl_add_u64 v[32:33], v[4:5], 0, v[2:3]
	v_add_co_u32_e32 v8, vcc, s81, v32
	global_load_dwordx4 v[4:7], v[32:33], off nt
	s_nop 0
	v_addc_co_u32_e32 v9, vcc, 0, v33, vcc
	v_add_co_u32_e32 v12, vcc, s79, v32
	global_load_dwordx4 v[8:11], v[8:9], off nt
	s_nop 0
	v_addc_co_u32_e32 v13, vcc, 0, v33, vcc
	v_add_co_u32_e32 v16, vcc, s80, v32
	global_load_dwordx4 v[12:15], v[12:13], off nt
	s_nop 0
	v_addc_co_u32_e32 v17, vcc, 0, v33, vcc
	v_add_co_u32_e32 v20, vcc, s85, v32
	global_load_dwordx4 v[16:19], v[16:17], off nt
	s_nop 0
	v_addc_co_u32_e32 v21, vcc, 0, v33, vcc
	global_load_dwordx4 v[20:23], v[20:21], off nt
	v_add_co_u32_e32 v24, vcc, s86, v32
	v_add_u32_e32 v2, v44, v47
	s_nop 0
	v_addc_co_u32_e32 v25, vcc, 0, v33, vcc
	global_load_dwordx4 v[24:27], v[24:25], off nt
	v_add_co_u32_e32 v28, vcc, s87, v32
	s_lshl_b32 s7, s7, 1
	s_nop 0
	v_addc_co_u32_e32 v29, vcc, 0, v33, vcc
	global_load_dwordx4 v[28:31], v[28:29], off nt
	v_add_co_u32_e32 v32, vcc, s89, v32
	s_add_u32 s8, s3, s7
	s_nop 0
	v_addc_co_u32_e32 v33, vcc, 0, v33, vcc
	global_load_dwordx4 v[32:35], v[32:33], off nt
	s_addc_u32 s9, s6, 0
	v_readlane_b32 s45, v253, 17
	v_readlane_b32 s46, v253, 18
	v_readlane_b32 s47, v253, 19
	v_readlane_b32 s48, v253, 20
	v_readlane_b32 s49, v253, 21
	v_readlane_b32 s50, v253, 22
	v_readlane_b32 s51, v253, 23
	v_readlane_b32 s52, v253, 24
	v_readlane_b32 s53, v253, 25
	v_readlane_b32 s54, v253, 26
	v_readlane_b32 s55, v253, 27
	v_readlane_b32 s58, v253, 30
	v_readlane_b32 s59, v253, 31
	s_waitcnt vmcnt(0)
	ds_write2_b32 v45, v4, v5 offset1:1
	ds_write2_b32 v45, v6, v7 offset0:2 offset1:3
	v_add_u32_e32 v4, 0x420, v2
	ds_write2_b32 v2, v8, v9 offset1:1
	ds_write2_b32 v2, v10, v11 offset0:2 offset1:3
	ds_write2_b32 v4, v12, v13 offset1:1
	v_add_u32_e32 v4, 0x428, v2
	ds_write2_b32 v4, v14, v15 offset1:1
	v_add_u32_e32 v4, 0x840, v2
	v_add_u32_e32 v2, 0x848, v2
	ds_write2_b32 v2, v18, v19 offset1:1
	v_add_u32_e32 v2, 0x1080, v45
	ds_write2_b32 v4, v16, v17 offset1:1
	ds_write2_b32 v2, v20, v21 offset1:1
	v_add_u32_e32 v2, 0x1088, v45
	ds_write2_b32 v2, v22, v23 offset1:1
	v_add_u32_e32 v2, 0x14a0, v45
	ds_write2_b32 v2, v24, v25 offset1:1
	v_add_u32_e32 v2, 0x14a8, v45
	ds_write2_b32 v2, v26, v27 offset1:1
	v_add_u32_e32 v2, 0x18c0, v45
	ds_write2_b32 v2, v28, v29 offset1:1
	v_add_u32_e32 v2, 0x18c8, v45
	ds_write2_b32 v2, v30, v31 offset1:1
	v_add_u32_e32 v2, 0x1ce0, v45
	ds_write2_b32 v2, v32, v33 offset1:1
	v_add_u32_e32 v2, 0x1ce8, v45
	ds_write2_b32 v2, v34, v35 offset1:1
	s_waitcnt lgkmcnt(0)
	ds_read2_b32 v[10:11], v50 offset0:33 offset1:41
	ds_read2_b32 v[12:13], v50 offset1:8
	v_lshlrev_b32_e32 v2, 1, v38
	ds_read2_b32 v[14:15], v50 offset0:66 offset1:74
	ds_read2_b32 v[16:17], v50 offset0:99 offset1:107
	ds_read2_b32 v[18:19], v50 offset0:132 offset1:140
	ds_read2_b32 v[20:21], v50 offset0:165 offset1:173
	ds_read2_b32 v[22:23], v50 offset0:198 offset1:206
	ds_read2_b32 v[24:25], v50 offset0:231 offset1:239
	v_lshl_add_u64 v[8:9], s[8:9], 0, v[2:3]
	v_or_b32_e32 v2, s2, v39
	v_lshlrev_b32_e32 v2, 11, v2
	v_lshl_add_u64 v[26:27], v[8:9], 0, v[2:3]
	v_or_b32_e32 v2, s2, v46
	s_waitcnt lgkmcnt(0)
	v_cvt_pk_bf16_f32 v4, v12, v10
	v_lshlrev_b32_e32 v2, 11, v2
	v_cvt_pk_bf16_f32 v5, v14, v16
	v_cvt_pk_bf16_f32 v6, v18, v20
	v_cvt_pk_bf16_f32 v7, v22, v24
	global_store_dwordx4 v[26:27], v[4:7], off sc1
	s_nop 1
	v_cvt_pk_bf16_f32 v4, v13, v11
	v_lshl_add_u64 v[10:11], v[8:9], 0, v[2:3]
	v_cvt_pk_bf16_f32 v5, v15, v17
	v_cvt_pk_bf16_f32 v6, v19, v21
	v_cvt_pk_bf16_f32 v7, v23, v25
	global_store_dwordx4 v[10:11], v[4:7], off sc1
	ds_read2_b32 v[10:11], v50 offset0:16 offset1:24
	ds_read2_b32 v[12:13], v50 offset0:49 offset1:57
	ds_read2_b32 v[14:15], v50 offset0:82 offset1:90
	ds_read2_b32 v[16:17], v50 offset0:115 offset1:123
	ds_read2_b32 v[18:19], v50 offset0:148 offset1:156
	ds_read2_b32 v[20:21], v50 offset0:181 offset1:189
	ds_read2_b32 v[22:23], v50 offset0:214 offset1:222
	ds_read2_b32 v[24:25], v50 offset0:247 offset1:255
	v_or_b32_e32 v2, s2, v48
	v_lshlrev_b32_e32 v2, 11, v2
	v_lshl_add_u64 v[26:27], v[8:9], 0, v[2:3]
	v_or_b32_e32 v2, s2, v49
	v_lshlrev_b32_e32 v2, 11, v2
	s_waitcnt lgkmcnt(6)
	v_cvt_pk_bf16_f32 v4, v10, v12
	s_waitcnt lgkmcnt(4)
	v_cvt_pk_bf16_f32 v5, v14, v16
	s_waitcnt lgkmcnt(2)
	v_cvt_pk_bf16_f32 v6, v18, v20
	s_waitcnt lgkmcnt(0)
	v_cvt_pk_bf16_f32 v7, v22, v24
	v_lshl_add_u64 v[8:9], v[8:9], 0, v[2:3]
	global_store_dwordx4 v[26:27], v[4:7], off sc1
	s_nop 1
	v_cvt_pk_bf16_f32 v4, v11, v13
	v_cvt_pk_bf16_f32 v5, v15, v17
	v_cvt_pk_bf16_f32 v6, v19, v21
	v_cvt_pk_bf16_f32 v7, v23, v25
	global_store_dwordx4 v[8:9], v[4:7], off sc1
	s_waitcnt lgkmcnt(0)

; #define GAS __attribute__((address_space(1)))
; #define LAS __attribute__((address_space(3)))
; #define LDS_WAIT() asm volatile("s_waitcnt lgkmcnt(0)" ::: "memory")
; __device__ __forceinline__ unsigned pk2(float lo, float hi) { unsigned r; asm("v_cvt_pk_bf16_f32 %0, %1, %2" : "=v"(r) : "v"(lo), "v"(hi)); return r; }
; __device__ __forceinline__ void transpose_item(const float* W, int K, int N, bf16* WT, int drow0, int kb, int n0, LAS float* scr, int lane) {
;     const int k0 = 64 * kb; const int c4 = 4 * (lane & 7); const bool ok = (n0 + c4) < N;
;     f32x4 v[8];
; #pragma unroll
;     for (int i = 0; i < 8; ++i) { const int kk = 8 * i + (lane >> 3); v[i] = ok ? *(const f32x4*)(W + (size_t)(k0 + kk) * N + n0 + c4) : (f32x4){0.f, 0.f, 0.f, 0.f}; }
; #pragma unroll
;     for (int i = 0; i < 8; ++i) { const int kk = 8 * i + (lane >> 3); LAS float* d = scr + kk * 33 + c4; d[0] = v[i][0]; d[1] = v[i][1]; d[2] = v[i][2]; d[3] = v[i][3]; }
;     LDS_WAIT(); asm volatile("" ::: "memory");
;     const int c = lane & 7;
; #pragma unroll
;     for (int j = 0; j < 4; ++j) { const int n = (lane >> 3) + 8 * j; const LAS float* s = scr + (8 * c) * 33 + n;
;         v4u o; o.x = pk2(s[0 * 33], s[1 * 33]); o.y = pk2(s[2 * 33], s[3 * 33]); o.z = pk2(s[4 * 33], s[5 * 33]); o.w = pk2(s[6 * 33], s[7 * 33]);
;         *(GAS v4u*)(WT + (size_t)(drow0 + n) * K + k0 + 8 * c) = o; }
;     LDS_WAIT(); asm volatile("" ::: "memory");
; }
; __device__ __forceinline__ void convert_item(const In& I, unsigned char* ws, int it, LAS float* scr, int lane) {
;     ...
;     if (r < 2 * I_SQ) { const int j = r / I_SQ; r -= j * I_SQ; const int kb = r / 32, nb = r % 32;
;         transpose_item(I.nsa_w_out + (size_t)j * D * D, D, D, Wnout + (size_t)j * D * D, 32 * nb, kb, 32 * nb, scr, lane); return; }
.LBB0_448:
	s_andn2_b64 vcc, exec, s[2:3]
	s_cbranch_vccnz .LBB0_450
	s_add_i32 s2, s41, 0x1900
	s_lshr_b32 s68, s2, 9
	v_readlane_b32 s44, v253, 16
	s_lshl_b64 s[2:3], s[68:69], 22
	v_readlane_b32 s50, v253, 22
	v_readlane_b32 s51, v253, 23
	s_add_u32 s8, s50, s2
	s_addc_u32 s9, s51, s3
	s_lshl_b64 s[6:7], s[68:69], 21
	s_add_u32 s3, s22, s6
	s_addc_u32 s6, s23, s7
	s_and_b32 s2, s42, 0x3e0
	s_add_i32 s7, s0, 0x2200
	s_and_b32 s7, s7, 0x3c0
	s_lshl_b32 s10, s2, 2
	s_add_u32 s8, s8, s10
	v_or_b32_e32 v6, s7, v39
	s_addc_u32 s9, s9, 0
	v_lshlrev_b32_e32 v2, 2, v36
	v_lshl_add_u64 v[4:5], s[8:9], 0, v[2:3]
	v_lshlrev_b32_e32 v2, 12, v6
	v_lshl_add_u64 v[32:33], v[4:5], 0, v[2:3]
	v_add_co_u32_e32 v8, vcc, s81, v32
	global_load_dwordx4 v[4:7], v[32:33], off nt
	s_nop 0
	v_addc_co_u32_e32 v9, vcc, 0, v33, vcc
	v_add_co_u32_e32 v12, vcc, s79, v32
	global_load_dwordx4 v[8:11], v[8:9], off nt
	s_nop 0
	v_addc_co_u32_e32 v13, vcc, 0, v33, vcc
	v_add_co_u32_e32 v16, vcc, s80, v32
	global_load_dwordx4 v[12:15], v[12:13], off nt
	s_nop 0
	v_addc_co_u32_e32 v17, vcc, 0, v33, vcc
	v_add_co_u32_e32 v20, vcc, s85, v32
	global_load_dwordx4 v[16:19], v[16:17], off nt
	s_nop 0
	v_addc_co_u32_e32 v21, vcc, 0, v33, vcc
	global_load_dwordx4 v[20:23], v[20:21], off nt
	v_add_co_u32_e32 v24, vcc, s86, v32
	v_add_u32_e32 v2, v44, v47
	s_nop 0
	v_addc_co_u32_e32 v25, vcc, 0, v33, vcc
	global_load_dwordx4 v[24:27], v[24:25], off nt
	v_add_co_u32_e32 v28, vcc, s87, v32
	s_lshl_b32 s7, s7, 1
	s_nop 0
	v_addc_co_u32_e32 v29, vcc, 0, v33, vcc
	global_load_dwordx4 v[28:31], v[28:29], off nt
	v_add_co_u32_e32 v32, vcc, s89, v32
	s_add_u32 s8, s3, s7
	s_nop 0
	v_addc_co_u32_e32 v33, vcc, 0, v33, vcc
	global_load_dwordx4 v[32:35], v[32:33], off nt
	s_addc_u32 s9, s6, 0
	v_readlane_b32 s45, v253, 17
	v_readlane_b32 s46, v253, 18
	v_readlane_b32 s47, v253, 19
	v_readlane_b32 s48, v253, 20
	v_readlane_b32 s49, v253, 21
	v_readlane_b32 s52, v253, 24
	v_readlane_b32 s53, v253, 25
	v_readlane_b32 s54, v253, 26
	v_readlane_b32 s55, v253, 27
	v_readlane_b32 s56, v253, 28
	v_readlane_b32 s57, v253, 29
	v_readlane_b32 s58, v253, 30
	v_readlane_b32 s59, v253, 31
	s_waitcnt vmcnt(0)
	ds_write2_b32 v45, v4, v5 offset1:1
	ds_write2_b32 v45, v6, v7 offset0:2 offset1:3
	v_add_u32_e32 v4, 0x420, v2
	ds_write2_b32 v2, v8, v9 offset1:1
	ds_write2_b32 v2, v10, v11 offset0:2 offset1:3
	ds_write2_b32 v4, v12, v13 offset1:1
	v_add_u32_e32 v4, 0x428, v2
	ds_write2_b32 v4, v14, v15 offset1:1
	v_add_u32_e32 v4, 0x840, v2
	v_add_u32_e32 v2, 0x848, v2
	ds_write2_b32 v2, v18, v19 offset1:1
	v_add_u32_e32 v2, 0x1080, v45
	ds_write2_b32 v4, v16, v17 offset1:1
	ds_write2_b32 v2, v20, v21 offset1:1
	v_add_u32_e32 v2, 0x1088, v45
	ds_write2_b32 v2, v22, v23 offset1:1
	v_add_u32_e32 v2, 0x14a0, v45
	ds_write2_b32 v2, v24, v25 offset1:1
	v_add_u32_e32 v2, 0x14a8, v45
	ds_write2_b32 v2, v26, v27 offset1:1
	v_add_u32_e32 v2, 0x18c0, v45
	ds_write2_b32 v2, v28, v29 offset1:1
	v_add_u32_e32 v2, 0x18c8, v45
	ds_write2_b32 v2, v30, v31 offset1:1
	v_add_u32_e32 v2, 0x1ce0, v45
	ds_write2_b32 v2, v32, v33 offset1:1
	v_add_u32_e32 v2, 0x1ce8, v45
	ds_write2_b32 v2, v34, v35 offset1:1
	s_waitcnt lgkmcnt(0)
	ds_read2_b32 v[10:11], v50 offset0:33 offset1:41
	ds_read2_b32 v[12:13], v50 offset1:8
	v_lshlrev_b32_e32 v2, 1, v38
	ds_read2_b32 v[14:15], v50 offset0:66 offset1:74
	ds_read2_b32 v[16:17], v50 offset0:99 offset1:107
	ds_read2_b32 v[18:19], v50 offset0:132 offset1:140
	ds_read2_b32 v[20:21], v50 offset0:165 offset1:173
	ds_read2_b32 v[22:23], v50 offset0:198 offset1:206
	ds_read2_b32 v[24:25], v50 offset0:231 offset1:239
	v_lshl_add_u64 v[8:9], s[8:9], 0, v[2:3]
	v_or_b32_e32 v2, s2, v39
	v_lshlrev_b32_e32 v2, 11, v2
	v_lshl_add_u64 v[26:27], v[8:9], 0, v[2:3]
	v_or_b32_e32 v2, s2, v46
	s_waitcnt lgkmcnt(0)
	v_cvt_pk_bf16_f32 v4, v12, v10
	v_lshlrev_b32_e32 v2, 11, v2
	v_cvt_pk_bf16_f32 v5, v14, v16
	v_cvt_pk_bf16_f32 v6, v18, v20
	v_cvt_pk_bf16_f32 v7, v22, v24
	global_store_dwordx4 v[26:27], v[4:7], off sc1
	s_nop 1
	v_cvt_pk_bf16_f32 v4, v13, v11
	v_lshl_add_u64 v[10:11], v[8:9], 0, v[2:3]
	v_cvt_pk_bf16_f32 v5, v15, v17
	v_cvt_pk_bf16_f32 v6, v19, v21
	v_cvt_pk_bf16_f32 v7, v23, v25
	global_store_dwordx4 v[10:11], v[4:7], off sc1
	ds_read2_b32 v[10:11], v50 offset0:16 offset1:24
	ds_read2_b32 v[12:13], v50 offset0:49 offset1:57
	ds_read2_b32 v[14:15], v50 offset0:82 offset1:90
	ds_read2_b32 v[16:17], v50 offset0:115 offset1:123
	ds_read2_b32 v[18:19], v50 offset0:148 offset1:156
	ds_read2_b32 v[20:21], v50 offset0:181 offset1:189
	ds_read2_b32 v[22:23], v50 offset0:214 offset1:222
	ds_read2_b32 v[24:25], v50 offset0:247 offset1:255
	v_or_b32_e32 v2, s2, v48
	v_lshlrev_b32_e32 v2, 11, v2
	v_lshl_add_u64 v[26:27], v[8:9], 0, v[2:3]
	v_or_b32_e32 v2, s2, v49
	v_lshlrev_b32_e32 v2, 11, v2
	s_waitcnt lgkmcnt(6)
	v_cvt_pk_bf16_f32 v4, v10, v12
	s_waitcnt lgkmcnt(4)
	v_cvt_pk_bf16_f32 v5, v14, v16
	s_waitcnt lgkmcnt(2)
	v_cvt_pk_bf16_f32 v6, v18, v20
	s_waitcnt lgkmcnt(0)
	v_cvt_pk_bf16_f32 v7, v22, v24
	v_lshl_add_u64 v[8:9], v[8:9], 0, v[2:3]
	global_store_dwordx4 v[26:27], v[4:7], off sc1
	s_nop 1
	v_cvt_pk_bf16_f32 v4, v11, v13
	v_cvt_pk_bf16_f32 v5, v15, v17
	v_cvt_pk_bf16_f32 v6, v19, v21
	v_cvt_pk_bf16_f32 v7, v23, v25
	global_store_dwordx4 v[8:9], v[4:7], off sc1
	s_waitcnt lgkmcnt(0)

; #define GAS __attribute__((address_space(1)))
; #define LAS __attribute__((address_space(3)))
; #define LDS_WAIT() asm volatile("s_waitcnt lgkmcnt(0)" ::: "memory")
; __device__ __forceinline__ unsigned pk2(float lo, float hi) { unsigned r; asm("v_cvt_pk_bf16_f32 %0, %1, %2" : "=v"(r) : "v"(lo), "v"(hi)); return r; }
; __device__ __forceinline__ void transpose_item(const float* W, int K, int N, bf16* WT, int drow0, int kb, int n0, LAS float* scr, int lane) {
;     const int k0 = 64 * kb; const int c4 = 4 * (lane & 7); const bool ok = (n0 + c4) < N;
;     f32x4 v[8];
; #pragma unroll
;     for (int i = 0; i < 8; ++i) { const int kk = 8 * i + (lane >> 3); v[i] = ok ? *(const f32x4*)(W + (size_t)(k0 + kk) * N + n0 + c4) : (f32x4){0.f, 0.f, 0.f, 0.f}; }
; #pragma unroll
;     for (int i = 0; i < 8; ++i) { const int kk = 8 * i + (lane >> 3); LAS float* d = scr + kk * 33 + c4; d[0] = v[i][0]; d[1] = v[i][1]; d[2] = v[i][2]; d[3] = v[i][3]; }
;     LDS_WAIT(); asm volatile("" ::: "memory");
;     const int c = lane & 7;
; #pragma unroll
;     for (int j = 0; j < 4; ++j) { const int n = (lane >> 3) + 8 * j; const LAS float* s = scr + (8 * c) * 33 + n;
;         v4u o; o.x = pk2(s[0 * 33], s[1 * 33]); o.y = pk2(s[2 * 33], s[3 * 33]); o.z = pk2(s[4 * 33], s[5 * 33]); o.w = pk2(s[6 * 33], s[7 * 33]);
;         *(GAS v4u*)(WT + (size_t)(drow0 + n) * K + k0 + 8 * c) = o; }
;     LDS_WAIT(); asm volatile("" ::: "memory");
; }
; __device__ __forceinline__ void convert_item(const In& I, unsigned char* ws, int it, LAS float* scr, int lane) {
;     ...
;     if (r < T0) { const int f = r / I_FFN; r -= f * I_FFN;
;         if (r < 2 * I_G) { const int up = r >= I_G; r -= up * I_G; const int kb = r / 88, nb = r % 88;
;             transpose_item((up ? I.w_up : I.w_gate) + (size_t)f * D * FF, D, FF, Wgu + (size_t)f * NGU * D, 256 * (nb >> 2) + 32 * (nb & 3) + 128 * up, kb, 32 * nb, scr, lane); }
;         else { r -= 2 * I_G; const int kb = r / 32, nb = r % 32; transpose_item(I.w_down + (size_t)f * FF * D, FF, D, Wd + (size_t)f * D * FF, 32 * nb, kb, 32 * nb, scr, lane); }
.LBB0_470:
	s_andn2_b64 vcc, exec, s[2:3]
	s_cbranch_vccnz .LBB0_415
	s_mul_hi_i32 s2, s43, 0x3e0f83e1
	s_lshr_b32 s3, s2, 31
	s_ashr_i32 s6, s2, 10
	s_add_i32 s6, s6, s3
	s_mul_i32 s2, s6, 0xffffef80
	s_add_i32 s7, s41, s2
	s_add_i32 s7, s7, 0xa800
	s_cmpk_gt_i32 s7, 0xaff
	s_mov_b64 s[2:3], -1
	s_cbranch_scc0 .LBB0_473
	v_readlane_b32 s44, v253, 0
	s_mul_i32 s3, s6, 0xb00000
	v_readlane_b32 s52, v253, 8
	s_mul_hi_i32 s2, s6, 0xb00000
	v_readlane_b32 s53, v253, 9
	s_add_u32 s9, s52, s3
	s_addc_u32 s11, s53, s2
	s_mul_i32 s3, s6, 0x580000
	s_mul_hi_i32 s2, s6, 0x580000
	s_add_u32 s3, s1, s3
	s_mul_i32 s10, s6, 0xffffdf00
	s_addc_u32 s8, s19, s2
	s_add_i32 s10, s0, s10
	s_add_i32 s10, s10, 0x14000
	s_and_b32 s2, s42, 0x3e0
	s_andn2_b32 s10, s10, 63
	s_add_i32 s68, s10, 0xffffea00
	s_lshl_b32 s10, s2, 2
	v_or_b32_e32 v32, s68, v39
	s_add_u32 s10, s9, s10
	s_addc_u32 s11, s11, 0
	v_lshlrev_b32_e32 v2, 2, v36
	v_ashrrev_i32_e32 v33, 31, v32
	v_or_b32_e32 v8, 8, v32
	v_or_b32_e32 v12, 16, v32
	v_lshl_add_u64 v[34:35], s[10:11], 0, v[2:3]
	v_lshlrev_b64 v[4:5], 12, v[32:33]
	v_ashrrev_i32_e32 v9, 31, v8
	v_ashrrev_i32_e32 v13, 31, v12
	v_lshl_add_u64 v[4:5], v[34:35], 0, v[4:5]
	v_lshlrev_b64 v[8:9], 12, v[8:9]
	v_lshlrev_b64 v[12:13], 12, v[12:13]
	v_or_b32_e32 v16, 24, v32
	global_load_dwordx4 v[4:7], v[4:5], off nt
	v_lshl_add_u64 v[8:9], v[34:35], 0, v[8:9]
	v_lshl_add_u64 v[12:13], v[34:35], 0, v[12:13]
	v_ashrrev_i32_e32 v17, 31, v16
	v_or_b32_e32 v20, 32, v32
	global_load_dwordx4 v[8:11], v[8:9], off nt
	v_lshlrev_b64 v[16:17], 12, v[16:17]
	global_load_dwordx4 v[12:15], v[12:13], off nt
	v_ashrrev_i32_e32 v21, 31, v20
	v_lshl_add_u64 v[16:17], v[34:35], 0, v[16:17]
	v_lshlrev_b64 v[20:21], 12, v[20:21]
	v_or_b32_e32 v24, 40, v32
	global_load_dwordx4 v[16:19], v[16:17], off nt
	v_lshl_add_u64 v[20:21], v[34:35], 0, v[20:21]
	v_ashrrev_i32_e32 v25, 31, v24
	global_load_dwordx4 v[20:23], v[20:21], off nt
	v_lshlrev_b64 v[24:25], 12, v[24:25]
	v_or_b32_e32 v28, 48, v32
	v_lshl_add_u64 v[24:25], v[34:35], 0, v[24:25]
	v_ashrrev_i32_e32 v29, 31, v28
	global_load_dwordx4 v[24:27], v[24:25], off nt
	v_lshlrev_b64 v[28:29], 12, v[28:29]
	v_or_b32_e32 v32, 56, v32
	v_lshl_add_u64 v[28:29], v[34:35], 0, v[28:29]
	v_ashrrev_i32_e32 v33, 31, v32
	global_load_dwordx4 v[28:31], v[28:29], off nt
	v_lshlrev_b64 v[32:33], 12, v[32:33]
	v_lshl_add_u64 v[32:33], v[34:35], 0, v[32:33]
	global_load_dwordx4 v[32:35], v[32:33], off nt
	v_add_u32_e32 v2, v44, v47
	s_lshl_b64 s[10:11], s[68:69], 1
	s_add_u32 s10, s3, s10
	s_addc_u32 s11, s8, s11
	v_readlane_b32 s45, v253, 1
	v_readlane_b32 s46, v253, 2
	v_readlane_b32 s47, v253, 3
	v_readlane_b32 s48, v253, 4
	v_readlane_b32 s49, v253, 5
	v_readlane_b32 s50, v253, 6
	v_readlane_b32 s51, v253, 7
	v_readlane_b32 s54, v253, 10
	v_readlane_b32 s55, v253, 11
	v_readlane_b32 s56, v253, 12
	v_readlane_b32 s57, v253, 13
	v_readlane_b32 s58, v253, 14
	v_readlane_b32 s59, v253, 15
	s_waitcnt vmcnt(0)
	ds_write2_b32 v45, v4, v5 offset1:1
	ds_write2_b32 v45, v6, v7 offset0:2 offset1:3
	v_add_u32_e32 v4, 0x420, v2
	ds_write2_b32 v2, v8, v9 offset1:1
	ds_write2_b32 v2, v10, v11 offset0:2 offset1:3
	ds_write2_b32 v4, v12, v13 offset1:1
	v_add_u32_e32 v4, 0x428, v2
	ds_write2_b32 v4, v14, v15 offset1:1
	v_add_u32_e32 v4, 0x840, v2
	v_add_u32_e32 v2, 0x848, v2
	ds_write2_b32 v2, v18, v19 offset1:1
	v_add_u32_e32 v2, 0x1080, v45
	ds_write2_b32 v4, v16, v17 offset1:1
	ds_write2_b32 v2, v20, v21 offset1:1
	v_add_u32_e32 v2, 0x1088, v45
	ds_write2_b32 v2, v22, v23 offset1:1
	v_add_u32_e32 v2, 0x14a0, v45
	ds_write2_b32 v2, v24, v25 offset1:1
	v_add_u32_e32 v2, 0x14a8, v45
	ds_write2_b32 v2, v26, v27 offset1:1
	v_add_u32_e32 v2, 0x18c0, v45
	ds_write2_b32 v2, v28, v29 offset1:1
	v_add_u32_e32 v2, 0x18c8, v45
	ds_write2_b32 v2, v30, v31 offset1:1
	v_add_u32_e32 v2, 0x1ce0, v45
	ds_write2_b32 v2, v32, v33 offset1:1
	v_add_u32_e32 v2, 0x1ce8, v45
	ds_write2_b32 v2, v34, v35 offset1:1
	s_waitcnt lgkmcnt(0)
	ds_read2_b32 v[10:11], v50 offset0:33 offset1:41
	ds_read2_b32 v[12:13], v50 offset1:8
	v_lshlrev_b32_e32 v2, 1, v38
	ds_read2_b32 v[14:15], v50 offset0:66 offset1:74
	ds_read2_b32 v[16:17], v50 offset0:99 offset1:107
	ds_read2_b32 v[18:19], v50 offset0:132 offset1:140
	ds_read2_b32 v[20:21], v50 offset0:165 offset1:173
	ds_read2_b32 v[22:23], v50 offset0:198 offset1:206
	ds_read2_b32 v[24:25], v50 offset0:231 offset1:239
	v_lshl_add_u64 v[8:9], s[10:11], 0, v[2:3]
	v_or_b32_e32 v2, s2, v39
	v_mul_u32_u24_e32 v2, 0x1600, v2
	v_lshl_add_u64 v[26:27], v[8:9], 0, v[2:3]
	v_or_b32_e32 v2, s2, v46
	s_waitcnt lgkmcnt(0)
	v_cvt_pk_bf16_f32 v4, v12, v10
	v_mul_u32_u24_e32 v2, 0x1600, v2
	v_cvt_pk_bf16_f32 v5, v14, v16
	v_cvt_pk_bf16_f32 v6, v18, v20
	v_cvt_pk_bf16_f32 v7, v22, v24
	global_store_dwordx4 v[26:27], v[4:7], off sc1
	s_nop 1
	v_cvt_pk_bf16_f32 v4, v13, v11
	v_lshl_add_u64 v[10:11], v[8:9], 0, v[2:3]
	v_cvt_pk_bf16_f32 v5, v15, v17
	v_cvt_pk_bf16_f32 v6, v19, v21
	v_cvt_pk_bf16_f32 v7, v23, v25
	global_store_dwordx4 v[10:11], v[4:7], off sc1
	ds_read2_b32 v[10:11], v50 offset0:16 offset1:24
	ds_read2_b32 v[12:13], v50 offset0:49 offset1:57
	ds_read2_b32 v[14:15], v50 offset0:82 offset1:90
	ds_read2_b32 v[16:17], v50 offset0:115 offset1:123
	ds_read2_b32 v[18:19], v50 offset0:148 offset1:156
	ds_read2_b32 v[20:21], v50 offset0:181 offset1:189
	ds_read2_b32 v[22:23], v50 offset0:214 offset1:222
	ds_read2_b32 v[24:25], v50 offset0:247 offset1:255
	v_or_b32_e32 v2, s2, v48
	v_mul_u32_u24_e32 v2, 0x1600, v2
	v_lshl_add_u64 v[26:27], v[8:9], 0, v[2:3]
	v_or_b32_e32 v2, s2, v49
	v_mul_u32_u24_e32 v2, 0x1600, v2
	s_waitcnt lgkmcnt(6)
	v_cvt_pk_bf16_f32 v4, v10, v12
	s_waitcnt lgkmcnt(4)
	v_cvt_pk_bf16_f32 v5, v14, v16
	s_waitcnt lgkmcnt(2)
	v_cvt_pk_bf16_f32 v6, v18, v20
	s_waitcnt lgkmcnt(0)
	v_cvt_pk_bf16_f32 v7, v22, v24
	v_lshl_add_u64 v[8:9], v[8:9], 0, v[2:3]
	global_store_dwordx4 v[26:27], v[4:7], off sc1
	s_mov_b64 s[2:3], 0
	s_nop 0
	v_cvt_pk_bf16_f32 v4, v11, v13
	v_cvt_pk_bf16_f32 v5, v15, v17
	v_cvt_pk_bf16_f32 v6, v19, v21
	v_cvt_pk_bf16_f32 v7, v23, v25
	global_store_dwordx4 v[8:9], v[4:7], off sc1
	s_waitcnt lgkmcnt(0)
; #define GAS __attribute__((address_space(1)))
; #define LAS __attribute__((address_space(3)))
; #define LDS_WAIT() asm volatile("s_waitcnt lgkmcnt(0)" ::: "memory")
; __device__ __forceinline__ unsigned pk2(float lo, float hi) { unsigned r; asm("v_cvt_pk_bf16_f32 %0, %1, %2" : "=v"(r) : "v"(lo), "v"(hi)); return r; }
; __device__ __forceinline__ void transpose_item(const float* W, int K, int N, bf16* WT, int drow0, int kb, int n0, LAS float* scr, int lane) {
;     const int k0 = 64 * kb; const int c4 = 4 * (lane & 7); const bool ok = (n0 + c4) < N;
;     f32x4 v[8];
; #pragma unroll
;     for (int i = 0; i < 8; ++i) { const int kk = 8 * i + (lane >> 3); v[i] = ok ? *(const f32x4*)(W + (size_t)(k0 + kk) * N + n0 + c4) : (f32x4){0.f, 0.f, 0.f, 0.f}; }
; #pragma unroll
;     for (int i = 0; i < 8; ++i) { const int kk = 8 * i + (lane >> 3); LAS float* d = scr + kk * 33 + c4; d[0] = v[i][0]; d[1] = v[i][1]; d[2] = v[i][2]; d[3] = v[i][3]; }
;     LDS_WAIT(); asm volatile("" ::: "memory");
;     const int c = lane & 7;
; #pragma unroll
;     for (int j = 0; j < 4; ++j) { const int n = (lane >> 3) + 8 * j; const LAS float* s = scr + (8 * c) * 33 + n;
;         v4u o; o.x = pk2(s[0 * 33], s[1 * 33]); o.y = pk2(s[2 * 33], s[3 * 33]); o.z = pk2(s[4 * 33], s[5 * 33]); o.w = pk2(s[6 * 33], s[7 * 33]);
;         *(GAS v4u*)(WT + (size_t)(drow0 + n) * K + k0 + 8 * c) = o; }
;     LDS_WAIT(); asm volatile("" ::: "memory");
; }
; __device__ __forceinline__ void convert_item(const In& I, unsigned char* ws, int it, LAS float* scr, int lane) {
;     ...
;     if (r < T0) { const int f = r / I_FFN; r -= f * I_FFN;
;         if (r < 2 * I_G) { const int up = r >= I_G; r -= up * I_G; const int kb = r / 88, nb = r % 88;
;             transpose_item((up ? I.w_up : I.w_gate) + (size_t)f * D * FF, D, FF, Wgu + (size_t)f * NGU * D, 256 * (nb >> 2) + 32 * (nb & 3) + 128 * up, kb, 32 * nb, scr, lane); }
.LBB0_473:
	s_andn2_b64 vcc, exec, s[2:3]
	s_cbranch_vccnz .LBB0_415
	s_cmpk_gt_i32 s7, 0x57f
	v_readlane_b32 s44, v253, 0
	s_cselect_b32 s2, 0xfffffa80, 0
	s_mul_i32 s3, s6, 0x1080
	v_readlane_b32 s48, v253, 4
	v_readlane_b32 s49, v253, 5
	v_readlane_b32 s50, v253, 6
	v_readlane_b32 s51, v253, 7
	s_cselect_b32 s9, 0x80, 0
	s_cselect_b32 s7, s50, s48
	s_cselect_b32 s8, s51, s49
	s_sub_i32 s2, s2, s3
	s_add_i32 s2, s41, s2
	s_add_i32 s2, s2, 0xa800
	s_mul_hi_i32 s3, s2, 0x2e8ba2e9
	s_lshr_b32 s10, s3, 31
	s_ashr_i32 s3, s3, 4
	s_add_i32 s3, s3, s10
	s_mul_i32 s10, s3, 0x58
	s_sub_i32 s2, s2, s10
	s_mul_hi_i32 s10, s6, 0xb00000
	s_mul_i32 s6, s6, 0xb00000
	s_add_u32 s12, s7, s6
	s_addc_u32 s13, s8, s10
	s_add_u32 s7, s28, s6
	s_addc_u32 s8, s29, s10
	s_lshl_b32 s10, s2, 5
	s_lshl_b32 s6, s2, 6
	s_and_b32 s2, s10, 0x60
	s_and_b32 s6, s6, 0xffffff00
	s_or_b32 s2, s2, s9
	s_ashr_i32 s11, s10, 31
	s_or_b32 s6, s2, s6
	s_lshl_b32 s2, s3, 6
	s_lshl_b64 s[10:11], s[10:11], 2
	s_add_u32 s10, s12, s10
	v_or_b32_e32 v34, s2, v39
	s_addc_u32 s11, s13, s11
	v_lshlrev_b32_e32 v2, 2, v36
	v_lshl_add_u64 v[32:33], s[10:11], 0, v[2:3]
	s_movk_i32 s3, 0x2c00
	v_or_b32_e32 v2, 8, v34
	v_mad_i64_i32 v[4:5], s[10:11], v34, s3, v[32:33]
	v_mad_i64_i32 v[8:9], s[10:11], v2, s3, v[32:33]
	v_or_b32_e32 v2, 16, v34
	global_load_dwordx4 v[4:7], v[4:5], off nt
	v_mad_i64_i32 v[12:13], s[10:11], v2, s3, v[32:33]
	global_load_dwordx4 v[8:11], v[8:9], off nt
	v_or_b32_e32 v2, 24, v34
	global_load_dwordx4 v[12:15], v[12:13], off nt
	v_mad_i64_i32 v[16:17], s[10:11], v2, s3, v[32:33]
	v_or_b32_e32 v2, 32, v34
	global_load_dwordx4 v[16:19], v[16:17], off nt
	v_mad_i64_i32 v[20:21], s[10:11], v2, s3, v[32:33]
	global_load_dwordx4 v[20:23], v[20:21], off nt
	v_or_b32_e32 v2, 40, v34
	v_mad_i64_i32 v[24:25], s[10:11], v2, s3, v[32:33]
	global_load_dwordx4 v[24:27], v[24:25], off nt
	v_or_b32_e32 v2, 48, v34
	v_mad_i64_i32 v[28:29], s[10:11], v2, s3, v[32:33]
	global_load_dwordx4 v[28:31], v[28:29], off nt
	v_or_b32_e32 v2, 56, v34
	v_mad_i64_i32 v[32:33], s[10:11], v2, s3, v[32:33]
	global_load_dwordx4 v[32:35], v[32:33], off nt
	v_add_u32_e32 v2, v44, v47
	s_ashr_i32 s3, s2, 31
	s_lshl_b64 s[2:3], s[2:3], 1
	s_add_u32 s2, s7, s2
	s_addc_u32 s3, s8, s3
	v_readlane_b32 s45, v253, 1
	v_readlane_b32 s46, v253, 2
	v_readlane_b32 s47, v253, 3
	v_readlane_b32 s52, v253, 8
	v_readlane_b32 s53, v253, 9
	v_readlane_b32 s54, v253, 10
	v_readlane_b32 s55, v253, 11
	v_readlane_b32 s56, v253, 12
	v_readlane_b32 s57, v253, 13
	v_readlane_b32 s58, v253, 14
	v_readlane_b32 s59, v253, 15
	s_waitcnt vmcnt(0)
	ds_write2_b32 v45, v4, v5 offset1:1
	ds_write2_b32 v45, v6, v7 offset0:2 offset1:3
	v_add_u32_e32 v4, 0x420, v2
	ds_write2_b32 v2, v8, v9 offset1:1
	ds_write2_b32 v2, v10, v11 offset0:2 offset1:3
	ds_write2_b32 v4, v12, v13 offset1:1
	v_add_u32_e32 v4, 0x428, v2
	ds_write2_b32 v4, v14, v15 offset1:1
	v_add_u32_e32 v4, 0x840, v2
	v_add_u32_e32 v2, 0x848, v2
	ds_write2_b32 v2, v18, v19 offset1:1
	v_add_u32_e32 v2, 0x1080, v45
	ds_write2_b32 v2, v20, v21 offset1:1
	v_add_u32_e32 v2, 0x1088, v45
	ds_write2_b32 v2, v22, v23 offset1:1
	v_add_u32_e32 v2, 0x14a0, v45
	ds_write2_b32 v2, v24, v25 offset1:1
	v_add_u32_e32 v2, 0x14a8, v45
	ds_write2_b32 v2, v26, v27 offset1:1
	v_add_u32_e32 v2, 0x18c0, v45
	ds_write2_b32 v2, v28, v29 offset1:1
	v_add_u32_e32 v2, 0x18c8, v45
	ds_write2_b32 v2, v30, v31 offset1:1
	v_add_u32_e32 v2, 0x1ce0, v45
	ds_write2_b32 v2, v32, v33 offset1:1
	v_add_u32_e32 v2, 0x1ce8, v45
	ds_write2_b32 v4, v16, v17 offset1:1
	ds_write2_b32 v2, v34, v35 offset1:1
	s_waitcnt lgkmcnt(0)
	ds_read2_b32 v[10:11], v50 offset0:33 offset1:41
	ds_read2_b32 v[12:13], v50 offset1:8
	ds_read2_b32 v[14:15], v50 offset0:66 offset1:74
	ds_read2_b32 v[16:17], v50 offset0:99 offset1:107
	ds_read2_b32 v[18:19], v50 offset0:132 offset1:140
	ds_read2_b32 v[20:21], v50 offset0:165 offset1:173
	ds_read2_b32 v[22:23], v50 offset0:198 offset1:206
	ds_read2_b32 v[24:25], v50 offset0:231 offset1:239
	v_or_b32_e32 v26, s6, v39
	v_lshlrev_b32_e32 v2, 1, v38
	v_ashrrev_i32_e32 v27, 31, v26
	v_lshl_add_u64 v[8:9], s[2:3], 0, v[2:3]
	v_lshlrev_b64 v[26:27], 11, v[26:27]
	s_waitcnt lgkmcnt(0)
	v_cvt_pk_bf16_f32 v4, v12, v10
	v_lshl_add_u64 v[26:27], v[8:9], 0, v[26:27]
	v_or_b32_e32 v10, s6, v46
	v_cvt_pk_bf16_f32 v5, v14, v16
	v_cvt_pk_bf16_f32 v6, v18, v20
	v_cvt_pk_bf16_f32 v7, v22, v24
	global_store_dwordx4 v[26:27], v[4:7], off sc1
	v_or_b32_e32 v26, s6, v48
	v_ashrrev_i32_e32 v27, 31, v26
	v_cvt_pk_bf16_f32 v4, v13, v11
	v_ashrrev_i32_e32 v11, 31, v10
	v_lshlrev_b64 v[10:11], 11, v[10:11]
	v_lshl_add_u64 v[10:11], v[8:9], 0, v[10:11]
	v_cvt_pk_bf16_f32 v5, v15, v17
	v_cvt_pk_bf16_f32 v6, v19, v21
	v_cvt_pk_bf16_f32 v7, v23, v25
	global_store_dwordx4 v[10:11], v[4:7], off sc1
	ds_read2_b32 v[10:11], v50 offset0:16 offset1:24
	ds_read2_b32 v[12:13], v50 offset0:49 offset1:57
	ds_read2_b32 v[14:15], v50 offset0:82 offset1:90
	ds_read2_b32 v[16:17], v50 offset0:115 offset1:123
	ds_read2_b32 v[18:19], v50 offset0:148 offset1:156
	ds_read2_b32 v[20:21], v50 offset0:181 offset1:189
	ds_read2_b32 v[22:23], v50 offset0:214 offset1:222
	ds_read2_b32 v[24:25], v50 offset0:247 offset1:255
	v_lshlrev_b64 v[26:27], 11, v[26:27]
	s_waitcnt lgkmcnt(6)
	v_cvt_pk_bf16_f32 v4, v10, v12
	v_lshl_add_u64 v[26:27], v[8:9], 0, v[26:27]
	v_or_b32_e32 v10, s6, v49
	s_waitcnt lgkmcnt(4)
	v_cvt_pk_bf16_f32 v5, v14, v16
	s_waitcnt lgkmcnt(2)
	v_cvt_pk_bf16_f32 v6, v18, v20
	s_waitcnt lgkmcnt(0)
	v_cvt_pk_bf16_f32 v7, v22, v24
	global_store_dwordx4 v[26:27], v[4:7], off sc1
	s_nop 1
	v_cvt_pk_bf16_f32 v4, v11, v13
	v_ashrrev_i32_e32 v11, 31, v10
	v_lshlrev_b64 v[10:11], 11, v[10:11]
	v_lshl_add_u64 v[8:9], v[8:9], 0, v[10:11]
	v_cvt_pk_bf16_f32 v5, v15, v17
	v_cvt_pk_bf16_f32 v6, v19, v21
	v_cvt_pk_bf16_f32 v7, v23, v25
	global_store_dwordx4 v[8:9], v[4:7], off sc1
	s_waitcnt lgkmcnt(0)
	s_branch .LBB0_415

; #define GAS __attribute__((address_space(1)))
; __device__ __forceinline__ void transpose_item(const float* W, int K, int N, bf16* WT, int drow0, int kb, int n0, LAS float* scr, int lane) {
;     const int k0 = 64 * kb; const int c4 = 4 * (lane & 7); const bool ok = (n0 + c4) < N;
;     f32x4 v[8];
; #pragma unroll
;     for (int i = 0; i < 8; ++i) { const int kk = 8 * i + (lane >> 3); v[i] = ok ? *(const f32x4*)(W + (size_t)(k0 + kk) * N + n0 + c4) : (f32x4){0.f, 0.f, 0.f, 0.f}; }
; #pragma unroll
;     for (int i = 0; i < 8; ++i) { const int kk = 8 * i + (lane >> 3); LAS float* d = scr + kk * 33 + c4; d[0] = v[i][0]; d[1] = v[i][1]; d[2] = v[i][2]; d[3] = v[i][3]; }
;     LDS_WAIT(); asm volatile("" ::: "memory");
;     const int c = lane & 7;
; #pragma unroll
;     for (int j = 0; j < 4; ++j) { const int n = (lane >> 3) + 8 * j; const LAS float* s = scr + (8 * c) * 33 + n;
;         v4u o; o.x = pk2(s[0 * 33], s[1 * 33]); o.y = pk2(s[2 * 33], s[3 * 33]); o.z = pk2(s[4 * 33], s[5 * 33]); o.w = pk2(s[6 * 33], s[7 * 33]);
;         *(GAS v4u*)(WT + (size_t)(drow0 + n) * K + k0 + 8 * c) = o; }
;     LDS_WAIT(); asm volatile("" ::: "memory");
; }
; __device__ __forceinline__ void convert_item(const In& I, unsigned char* ws, int it, LAS float* scr, int lane) {
;     ...
;     int r = it;
;     if (r < T0) { const int f = r / I_FFN; r -= f * I_FFN;
;         if (r < 2 * I_G) { const int up = r >= I_G; r -= up * I_G; const int kb = r / 88, nb = r % 88;
;             transpose_item((up ? I.w_up : I.w_gate) + (size_t)f * D * FF, D, FF, Wgu + (size_t)f * NGU * D, 256 * (nb >> 2) + 32 * (nb & 3) + 128 * up, kb, 32 * nb, scr, lane); }
;         else { r -= 2 * I_G; const int kb = r / 32, nb = r % 32; transpose_item(I.w_down + (size_t)f * FF * D, FF, D, Wd + (size_t)f * D * FF, 32 * nb, kb, 32 * nb, scr, lane); }
;         return; }
;     r -= T0;
;     if (r < 2 * I_NIN) { const int j = r / I_NIN; r -= j * I_NIN; const int kb = r / 88, nb = r % 88;
;         transpose_item(I.nsa_w_in + (size_t)j * D * NSA_IN, D, NSA_IN, Wnin + (size_t)j * NSA_IN_PAD * D, 32 * nb, kb, 32 * nb, scr, lane); return; }
;     r -= 2 * I_NIN;
;     if (r < 2 * I_SQ) { const int j = r / I_SQ; r -= j * I_SQ; const int kb = r / 32, nb = r % 32;
;         transpose_item(I.nsa_w_out + (size_t)j * D * D, D, D, Wnout + (size_t)j * D * D, 32 * nb, kb, 32 * nb, scr, lane); return; }
;     r -= 2 * I_SQ;
.LBB0_478:
	s_add_i32 s42, s18, 0xa800
	s_cmp_gt_i32 s42, 0x83ff
	s_mov_b64 s[2:3], -1
	s_cbranch_scc0 .LBB0_532
	s_cmpk_gt_u32 s42, 0x8eff
	s_cbranch_scc0 .LBB0_513
	s_cmpk_gt_u32 s42, 0x92ff
	s_cbranch_scc0 .LBB0_510
	s_cmpk_gt_u32 s42, 0x9fff
	s_cbranch_scc0 .LBB0_491
	s_cmpk_gt_u32 s42, 0xa3ff
	s_cbranch_scc0 .LBB0_488
	s_cmpk_gt_u32 s42, 0xa7ff
	s_cbranch_scc0 .LBB0_485
	s_lshr_b32 s68, s18, 3
	v_readlane_b32 s44, v253, 16
	s_lshl_b64 s[2:3], s[68:69], 16
	v_readlane_b32 s48, v253, 20
	v_readlane_b32 s49, v253, 21
	s_add_u32 s6, s48, s2
	s_addc_u32 s7, s49, s3
	s_lshl_b64 s[2:3], s[68:69], 15
	s_add_u32 s8, s34, s2
	s_addc_u32 s3, s35, s3
	s_and_b32 s2, s40, 32
	s_and_b32 s9, s40, 0xc0
	s_lshl_b32 s10, s2, 2
	s_add_u32 s6, s6, s10
	v_or_b32_e32 v6, s9, v39
	s_addc_u32 s7, s7, 0
	v_lshlrev_b32_e32 v2, 2, v36
	v_lshl_add_u64 v[4:5], s[6:7], 0, v[2:3]
	v_lshlrev_b32_e32 v2, 8, v6
	v_lshl_add_u64 v[28:29], v[4:5], 0, v[2:3]
	global_load_dwordx4 v[4:7], v[28:29], off nt
	global_load_dwordx4 v[8:11], v[28:29], off offset:2048 nt
	v_add_co_u32_e32 v16, vcc, s84, v28
	s_movk_i32 s6, 0x3000
	s_nop 0
	v_addc_co_u32_e32 v17, vcc, 0, v29, vcc
	v_add_co_u32_e32 v24, vcc, s74, v28
	v_add_u32_e32 v2, v44, v45
	s_nop 0
	v_addc_co_u32_e32 v25, vcc, 0, v29, vcc
	global_load_dwordx4 v[12:15], v[24:25], off offset:-4096 nt
	s_nop 0
	global_load_dwordx4 v[16:19], v[16:17], off offset:2048 nt
	s_nop 0
	global_load_dwordx4 v[20:23], v[24:25], off nt
	s_nop 0
	global_load_dwordx4 v[24:27], v[24:25], off offset:2048 nt
	v_add_co_u32_e32 v32, vcc, s6, v28
	s_lshl_b32 s6, s9, 1
	s_nop 0
	v_addc_co_u32_e32 v33, vcc, 0, v29, vcc
	global_load_dwordx4 v[28:31], v[32:33], off nt
	s_nop 0
	global_load_dwordx4 v[32:35], v[32:33], off offset:2048 nt
	s_add_u32 s6, s8, s6
	s_addc_u32 s7, s3, 0
	v_readlane_b32 s45, v253, 17
	v_readlane_b32 s46, v253, 18
	v_readlane_b32 s47, v253, 19
	v_readlane_b32 s50, v253, 22
	v_readlane_b32 s51, v253, 23
	v_readlane_b32 s52, v253, 24
	v_readlane_b32 s53, v253, 25
	v_readlane_b32 s54, v253, 26
	v_readlane_b32 s55, v253, 27
	v_readlane_b32 s56, v253, 28
	v_readlane_b32 s57, v253, 29
	v_readlane_b32 s58, v253, 30
	v_readlane_b32 s59, v253, 31
	s_waitcnt vmcnt(0)
	ds_write2_b32 v2, v4, v5 offset1:1
	ds_write2_b32 v2, v6, v7 offset0:2 offset1:3
	v_add_u32_e32 v4, 0x420, v2
	ds_write2_b32 v4, v8, v9 offset1:1
	v_add_u32_e32 v4, 0x428, v2
	ds_write2_b32 v4, v10, v11 offset1:1
	v_add_u32_e32 v4, 0x840, v2
	ds_write2_b32 v4, v12, v13 offset1:1
	v_add_u32_e32 v4, 0x848, v2
	ds_write2_b32 v4, v14, v15 offset1:1
	v_add_u32_e32 v4, 0xc60, v2
	ds_write2_b32 v4, v16, v17 offset1:1
	v_add_u32_e32 v4, 0xc68, v2
	ds_write2_b32 v4, v18, v19 offset1:1
	v_add_u32_e32 v4, 0x1080, v2
	ds_write2_b32 v4, v20, v21 offset1:1
	v_add_u32_e32 v4, 0x1088, v2
	ds_write2_b32 v4, v22, v23 offset1:1
	v_add_u32_e32 v4, 0x14a0, v2
	ds_write2_b32 v4, v24, v25 offset1:1
	v_add_u32_e32 v4, 0x14a8, v2
	ds_write2_b32 v4, v26, v27 offset1:1
	v_add_u32_e32 v4, 0x18c0, v2
	ds_write2_b32 v4, v28, v29 offset1:1
	v_add_u32_e32 v4, 0x18c8, v2
	ds_write2_b32 v4, v30, v31 offset1:1
	v_add_u32_e32 v4, 0x1ce0, v2
	v_add_u32_e32 v2, 0x1ce8, v2
	ds_write2_b32 v4, v32, v33 offset1:1
	ds_write2_b32 v2, v34, v35 offset1:1
	s_waitcnt lgkmcnt(0)
	ds_read2_b32 v[10:11], v49 offset0:33 offset1:41
	ds_read2_b32 v[12:13], v49 offset1:8
	v_lshlrev_b32_e32 v2, 1, v38
	ds_read2_b32 v[14:15], v49 offset0:66 offset1:74
	ds_read2_b32 v[16:17], v49 offset0:99 offset1:107
	ds_read2_b32 v[18:19], v49 offset0:132 offset1:140
	ds_read2_b32 v[20:21], v49 offset0:165 offset1:173
	ds_read2_b32 v[22:23], v49 offset0:198 offset1:206
	ds_read2_b32 v[24:25], v49 offset0:231 offset1:239
	v_lshl_add_u64 v[4:5], s[6:7], 0, v[2:3]
	v_or_b32_e32 v2, s2, v39
	v_lshlrev_b32_e32 v2, 9, v2
	v_lshl_add_u64 v[26:27], v[4:5], 0, v[2:3]
	v_or_b32_e32 v2, s2, v46
	s_waitcnt lgkmcnt(0)
	v_cvt_pk_bf16_f32 v6, v12, v10
	v_lshlrev_b32_e32 v2, 9, v2
	v_cvt_pk_bf16_f32 v7, v14, v16
	v_cvt_pk_bf16_f32 v8, v18, v20
	v_cvt_pk_bf16_f32 v9, v22, v24
	global_store_dwordx4 v[26:27], v[6:9], off sc1
	s_nop 1
	v_cvt_pk_bf16_f32 v6, v13, v11
	v_lshl_add_u64 v[10:11], v[4:5], 0, v[2:3]
	v_cvt_pk_bf16_f32 v7, v15, v17
	v_cvt_pk_bf16_f32 v8, v19, v21
	v_cvt_pk_bf16_f32 v9, v23, v25
	global_store_dwordx4 v[10:11], v[6:9], off sc1
	ds_read2_b32 v[10:11], v49 offset0:16 offset1:24
	ds_read2_b32 v[12:13], v49 offset0:49 offset1:57
	ds_read2_b32 v[14:15], v49 offset0:82 offset1:90
	ds_read2_b32 v[16:17], v49 offset0:115 offset1:123
	ds_read2_b32 v[18:19], v49 offset0:148 offset1:156
	ds_read2_b32 v[20:21], v49 offset0:181 offset1:189
	ds_read2_b32 v[22:23], v49 offset0:214 offset1:222
	ds_read2_b32 v[24:25], v49 offset0:247 offset1:255
	v_or_b32_e32 v2, s2, v47
	v_lshlrev_b32_e32 v2, 9, v2
	v_lshl_add_u64 v[26:27], v[4:5], 0, v[2:3]
	v_or_b32_e32 v2, s2, v48
	v_lshlrev_b32_e32 v2, 9, v2
	s_waitcnt lgkmcnt(6)
	v_cvt_pk_bf16_f32 v6, v10, v12
	s_waitcnt lgkmcnt(4)
	v_cvt_pk_bf16_f32 v7, v14, v16
	s_waitcnt lgkmcnt(2)
	v_cvt_pk_bf16_f32 v8, v18, v20
	s_waitcnt lgkmcnt(0)
	v_cvt_pk_bf16_f32 v9, v22, v24
	v_lshl_add_u64 v[4:5], v[4:5], 0, v[2:3]
	global_store_dwordx4 v[26:27], v[6:9], off sc1
	s_mov_b64 s[2:3], 0
	s_nop 0
	v_cvt_pk_bf16_f32 v6, v11, v13
	v_cvt_pk_bf16_f32 v7, v15, v17
	v_cvt_pk_bf16_f32 v8, v19, v21
	v_cvt_pk_bf16_f32 v9, v23, v25
	global_store_dwordx4 v[4:5], v[6:9], off sc1
	s_waitcnt lgkmcnt(0)
; #define GAS __attribute__((address_space(1)))
; #define LAS __attribute__((address_space(3)))
; #define LDS_WAIT() asm volatile("s_waitcnt lgkmcnt(0)" ::: "memory")
; __device__ __forceinline__ unsigned pk2(float lo, float hi) { unsigned r; asm("v_cvt_pk_bf16_f32 %0, %1, %2" : "=v"(r) : "v"(lo), "v"(hi)); return r; }
; __device__ __forceinline__ void transpose_item(const float* W, int K, int N, bf16* WT, int drow0, int kb, int n0, LAS float* scr, int lane) {
;     const int k0 = 64 * kb; const int c4 = 4 * (lane & 7); const bool ok = (n0 + c4) < N;
;     f32x4 v[8];
; #pragma unroll
;     for (int i = 0; i < 8; ++i) { const int kk = 8 * i + (lane >> 3); v[i] = ok ? *(const f32x4*)(W + (size_t)(k0 + kk) * N + n0 + c4) : (f32x4){0.f, 0.f, 0.f, 0.f}; }
; #pragma unroll
;     for (int i = 0; i < 8; ++i) { const int kk = 8 * i + (lane >> 3); LAS float* d = scr + kk * 33 + c4; d[0] = v[i][0]; d[1] = v[i][1]; d[2] = v[i][2]; d[3] = v[i][3]; }
;     LDS_WAIT(); asm volatile("" ::: "memory");
;     const int c = lane & 7;
; #pragma unroll
;     for (int j = 0; j < 4; ++j) { const int n = (lane >> 3) + 8 * j; const LAS float* s = scr + (8 * c) * 33 + n;
;         v4u o; o.x = pk2(s[0 * 33], s[1 * 33]); o.y = pk2(s[2 * 33], s[3 * 33]); o.z = pk2(s[4 * 33], s[5 * 33]); o.w = pk2(s[6 * 33], s[7 * 33]);
;         *(GAS v4u*)(WT + (size_t)(drow0 + n) * K + k0 + 8 * c) = o; }
;     LDS_WAIT(); asm volatile("" ::: "memory");
; }
; __device__ __forceinline__ void convert_item(const In& I, unsigned char* ws, int it, LAS float* scr, int lane) {
;     ...
;     if (r < 4 * I_W1) { const int jk = r / I_W1; r -= jk * I_W1; const int kb = r / 8, nb = r % 8;
;         transpose_item(I.nsa_w1 + (size_t)jk * 2048 * 256, 2048, 256, W1t + (size_t)jk * 256 * 2048, 32 * nb, kb, 32 * nb, scr, lane); return; }
.LBB0_485:
	s_andn2_b64 vcc, exec, s[2:3]
	s_cbranch_vccnz .LBB0_487
	s_add_i32 s2, s18, 0x400
	s_lshr_b32 s68, s2, 8
	s_lshl_b64 s[2:3], s[68:69], 21
	v_readlane_b32 s44, v253, 16
	v_readlane_b32 s45, v253, 17
	s_add_u32 s6, s44, s2
	s_addc_u32 s7, s45, s3
	s_lshl_b64 s[2:3], s[68:69], 20
	s_add_u32 s8, s31, s2
	s_addc_u32 s3, s33, s3
	s_and_b32 s2, s40, 0xe0
	s_and_b32 s9, s39, 0x7c0
	s_lshl_b32 s10, s2, 2
	s_add_u32 s6, s6, s10
	v_or_b32_e32 v6, s9, v39
	s_addc_u32 s7, s7, 0
	v_lshlrev_b32_e32 v2, 2, v36
	v_lshl_add_u64 v[4:5], s[6:7], 0, v[2:3]
	v_lshlrev_b32_e32 v2, 10, v6
	v_lshl_add_u64 v[32:33], v[4:5], 0, v[2:3]
	v_add_co_u32_e32 v8, vcc, s74, v32
	global_load_dwordx4 v[4:7], v[32:33], off nt
	s_nop 0
	v_addc_co_u32_e32 v9, vcc, 0, v33, vcc
	s_movk_i32 s6, 0x4000
	global_load_dwordx4 v[8:11], v[8:9], off nt
	v_add_co_u32_e32 v12, vcc, s6, v32
	s_movk_i32 s6, 0x6000
	s_nop 0
	v_addc_co_u32_e32 v13, vcc, 0, v33, vcc
	global_load_dwordx4 v[12:15], v[12:13], off nt
	v_add_co_u32_e32 v16, vcc, s6, v32
	s_mov_b32 s6, 0xa000
	s_nop 0
	v_addc_co_u32_e32 v17, vcc, 0, v33, vcc
	global_load_dwordx4 v[16:19], v[16:17], off nt
	v_add_co_u32_e32 v20, vcc, s81, v32
	v_add_u32_e32 v2, v44, v45
	s_nop 0
	v_addc_co_u32_e32 v21, vcc, 0, v33, vcc
	global_load_dwordx4 v[20:23], v[20:21], off nt
	v_add_co_u32_e32 v24, vcc, s6, v32
	s_mov_b32 s6, 0xc000
	s_nop 0
	v_addc_co_u32_e32 v25, vcc, 0, v33, vcc
	global_load_dwordx4 v[24:27], v[24:25], off nt
	v_add_co_u32_e32 v28, vcc, s6, v32
	s_mov_b32 s6, 0xe000
	s_nop 0
	v_addc_co_u32_e32 v29, vcc, 0, v33, vcc
	global_load_dwordx4 v[28:31], v[28:29], off nt
	v_add_co_u32_e32 v32, vcc, s6, v32
	s_lshl_b32 s6, s9, 1
	s_nop 0
	v_addc_co_u32_e32 v33, vcc, 0, v33, vcc
	global_load_dwordx4 v[32:35], v[32:33], off nt
	s_add_u32 s6, s8, s6
	s_addc_u32 s7, s3, 0
	v_readlane_b32 s46, v253, 18
	v_readlane_b32 s47, v253, 19
	v_readlane_b32 s48, v253, 20
	v_readlane_b32 s49, v253, 21
	v_readlane_b32 s50, v253, 22
	v_readlane_b32 s51, v253, 23
	v_readlane_b32 s52, v253, 24
	v_readlane_b32 s53, v253, 25
	v_readlane_b32 s54, v253, 26
	v_readlane_b32 s55, v253, 27
	v_readlane_b32 s56, v253, 28
	v_readlane_b32 s57, v253, 29
	v_readlane_b32 s58, v253, 30
	v_readlane_b32 s59, v253, 31
	s_waitcnt vmcnt(0)
	ds_write2_b32 v2, v4, v5 offset1:1
	ds_write2_b32 v2, v6, v7 offset0:2 offset1:3
	v_add_u32_e32 v4, 0x420, v2
	ds_write2_b32 v4, v8, v9 offset1:1
	v_add_u32_e32 v4, 0x428, v2
	ds_write2_b32 v4, v10, v11 offset1:1
	v_add_u32_e32 v4, 0x840, v2
	ds_write2_b32 v4, v12, v13 offset1:1
	v_add_u32_e32 v4, 0x848, v2
	ds_write2_b32 v4, v14, v15 offset1:1
	v_add_u32_e32 v4, 0xc60, v2
	ds_write2_b32 v4, v16, v17 offset1:1
	v_add_u32_e32 v4, 0xc68, v2
	ds_write2_b32 v4, v18, v19 offset1:1
	v_add_u32_e32 v4, 0x1080, v2
	ds_write2_b32 v4, v20, v21 offset1:1
	v_add_u32_e32 v4, 0x1088, v2
	ds_write2_b32 v4, v22, v23 offset1:1
	v_add_u32_e32 v4, 0x14a0, v2
	ds_write2_b32 v4, v24, v25 offset1:1
	v_add_u32_e32 v4, 0x14a8, v2
	ds_write2_b32 v4, v26, v27 offset1:1
	v_add_u32_e32 v4, 0x18c0, v2
	ds_write2_b32 v4, v28, v29 offset1:1
	v_add_u32_e32 v4, 0x18c8, v2
	ds_write2_b32 v4, v30, v31 offset1:1
	v_add_u32_e32 v4, 0x1ce0, v2
	v_add_u32_e32 v2, 0x1ce8, v2
	ds_write2_b32 v4, v32, v33 offset1:1
	ds_write2_b32 v2, v34, v35 offset1:1
	s_waitcnt lgkmcnt(0)
	ds_read2_b32 v[10:11], v49 offset0:33 offset1:41
	ds_read2_b32 v[12:13], v49 offset1:8
	v_lshlrev_b32_e32 v2, 1, v38
	ds_read2_b32 v[14:15], v49 offset0:66 offset1:74
	ds_read2_b32 v[16:17], v49 offset0:99 offset1:107
	ds_read2_b32 v[18:19], v49 offset0:132 offset1:140
	ds_read2_b32 v[20:21], v49 offset0:165 offset1:173
	ds_read2_b32 v[22:23], v49 offset0:198 offset1:206
	ds_read2_b32 v[24:25], v49 offset0:231 offset1:239
	v_lshl_add_u64 v[8:9], s[6:7], 0, v[2:3]
	v_or_b32_e32 v2, s2, v39
	v_lshlrev_b32_e32 v2, 12, v2
	v_lshl_add_u64 v[26:27], v[8:9], 0, v[2:3]
	v_or_b32_e32 v2, s2, v46
	s_waitcnt lgkmcnt(0)
	v_cvt_pk_bf16_f32 v4, v12, v10
	v_lshlrev_b32_e32 v2, 12, v2
	v_cvt_pk_bf16_f32 v5, v14, v16
	v_cvt_pk_bf16_f32 v6, v18, v20
	v_cvt_pk_bf16_f32 v7, v22, v24
	global_store_dwordx4 v[26:27], v[4:7], off sc1
	s_nop 1
	v_cvt_pk_bf16_f32 v4, v13, v11
	v_lshl_add_u64 v[10:11], v[8:9], 0, v[2:3]
	v_cvt_pk_bf16_f32 v5, v15, v17
	v_cvt_pk_bf16_f32 v6, v19, v21
	v_cvt_pk_bf16_f32 v7, v23, v25
	global_store_dwordx4 v[10:11], v[4:7], off sc1
	ds_read2_b32 v[10:11], v49 offset0:16 offset1:24
	ds_read2_b32 v[12:13], v49 offset0:49 offset1:57
	ds_read2_b32 v[14:15], v49 offset0:82 offset1:90
	ds_read2_b32 v[16:17], v49 offset0:115 offset1:123
	ds_read2_b32 v[18:19], v49 offset0:148 offset1:156
	ds_read2_b32 v[20:21], v49 offset0:181 offset1:189
	ds_read2_b32 v[22:23], v49 offset0:214 offset1:222
	ds_read2_b32 v[24:25], v49 offset0:247 offset1:255
	v_or_b32_e32 v2, s2, v47
	v_lshlrev_b32_e32 v2, 12, v2
	v_lshl_add_u64 v[26:27], v[8:9], 0, v[2:3]
	v_or_b32_e32 v2, s2, v48
	v_lshlrev_b32_e32 v2, 12, v2
	s_waitcnt lgkmcnt(6)
	v_cvt_pk_bf16_f32 v4, v10, v12
	s_waitcnt lgkmcnt(4)
	v_cvt_pk_bf16_f32 v5, v14, v16
	s_waitcnt lgkmcnt(2)
	v_cvt_pk_bf16_f32 v6, v18, v20
	s_waitcnt lgkmcnt(0)
	v_cvt_pk_bf16_f32 v7, v22, v24
	v_lshl_add_u64 v[8:9], v[8:9], 0, v[2:3]
	global_store_dwordx4 v[26:27], v[4:7], off sc1
	s_nop 1
	v_cvt_pk_bf16_f32 v4, v11, v13
	v_cvt_pk_bf16_f32 v5, v15, v17
	v_cvt_pk_bf16_f32 v6, v19, v21
	v_cvt_pk_bf16_f32 v7, v23, v25
	global_store_dwordx4 v[8:9], v[4:7], off sc1
	s_waitcnt lgkmcnt(0)

; #define GAS __attribute__((address_space(1)))
; #define LAS __attribute__((address_space(3)))
; #define LDS_WAIT() asm volatile("s_waitcnt lgkmcnt(0)" ::: "memory")
; __device__ __forceinline__ unsigned pk2(float lo, float hi) { unsigned r; asm("v_cvt_pk_bf16_f32 %0, %1, %2" : "=v"(r) : "v"(lo), "v"(hi)); return r; }
; __device__ __forceinline__ void transpose_item(const float* W, int K, int N, bf16* WT, int drow0, int kb, int n0, LAS float* scr, int lane) {
;     const int k0 = 64 * kb; const int c4 = 4 * (lane & 7); const bool ok = (n0 + c4) < N;
;     f32x4 v[8];
; #pragma unroll
;     for (int i = 0; i < 8; ++i) { const int kk = 8 * i + (lane >> 3); v[i] = ok ? *(const f32x4*)(W + (size_t)(k0 + kk) * N + n0 + c4) : (f32x4){0.f, 0.f, 0.f, 0.f}; }
; #pragma unroll
;     for (int i = 0; i < 8; ++i) { const int kk = 8 * i + (lane >> 3); LAS float* d = scr + kk * 33 + c4; d[0] = v[i][0]; d[1] = v[i][1]; d[2] = v[i][2]; d[3] = v[i][3]; }
;     LDS_WAIT(); asm volatile("" ::: "memory");
;     const int c = lane & 7;
; #pragma unroll
;     for (int j = 0; j < 4; ++j) { const int n = (lane >> 3) + 8 * j; const LAS float* s = scr + (8 * c) * 33 + n;
;         v4u o; o.x = pk2(s[0 * 33], s[1 * 33]); o.y = pk2(s[2 * 33], s[3 * 33]); o.z = pk2(s[4 * 33], s[5 * 33]); o.w = pk2(s[6 * 33], s[7 * 33]);
;         *(GAS v4u*)(WT + (size_t)(drow0 + n) * K + k0 + 8 * c) = o; }
;     LDS_WAIT(); asm volatile("" ::: "memory");
; }
; __device__ __forceinline__ void convert_item(const In& I, unsigned char* ws, int it, LAS float* scr, int lane) {
;     ...
;     if (r < 2 * I_SQ) { const int j = r / I_SQ; r -= j * I_SQ; const int kb = r / 32, nb = r % 32;
;         transpose_item(I.fox_w_out + (size_t)j * D * D, D, D, Wfout + (size_t)j * D * D, 32 * nb, kb, 32 * nb, scr, lane); return; }
.LBB0_488:
	s_andn2_b64 vcc, exec, s[2:3]
	s_cbranch_vccnz .LBB0_490
	s_add_i32 s2, s18, 0x800
	s_lshr_b32 s68, s2, 9
	v_readlane_b32 s44, v253, 16
	s_lshl_b64 s[2:3], s[68:69], 22
	v_readlane_b32 s56, v253, 28
	v_readlane_b32 s57, v253, 29
	s_add_u32 s6, s56, s2
	s_addc_u32 s7, s57, s3
	s_lshl_b64 s[2:3], s[68:69], 21
	s_add_u32 s8, s26, s2
	s_addc_u32 s3, s27, s3
	s_and_b32 s2, s40, 0x3e0
	s_add_i32 s9, s41, 0x14800
	s_and_b32 s9, s9, 0x3c0
	s_lshl_b32 s10, s2, 2
	s_add_u32 s6, s6, s10
	v_or_b32_e32 v6, s9, v39
	s_addc_u32 s7, s7, 0
	v_lshlrev_b32_e32 v2, 2, v36
	v_lshl_add_u64 v[4:5], s[6:7], 0, v[2:3]
	v_lshlrev_b32_e32 v2, 12, v6
	v_lshl_add_u64 v[32:33], v[4:5], 0, v[2:3]
	v_add_co_u32_e32 v8, vcc, s81, v32
	global_load_dwordx4 v[4:7], v[32:33], off nt
	s_nop 0
	v_addc_co_u32_e32 v9, vcc, 0, v33, vcc
	global_load_dwordx4 v[8:11], v[8:9], off nt
	v_add_co_u32_e32 v12, vcc, s79, v32
	v_add_u32_e32 v2, v44, v45
	s_nop 0
	v_addc_co_u32_e32 v13, vcc, 0, v33, vcc
	global_load_dwordx4 v[12:15], v[12:13], off nt
	v_add_co_u32_e32 v16, vcc, s80, v32
	s_lshl_b32 s6, s9, 1
	s_nop 0
	v_addc_co_u32_e32 v17, vcc, 0, v33, vcc
	global_load_dwordx4 v[16:19], v[16:17], off nt
	v_add_co_u32_e32 v20, vcc, s85, v32
	s_add_u32 s6, s8, s6
	s_nop 0
	v_addc_co_u32_e32 v21, vcc, 0, v33, vcc
	global_load_dwordx4 v[20:23], v[20:21], off nt
	v_add_co_u32_e32 v24, vcc, s86, v32
	s_addc_u32 s7, s3, 0
	s_nop 0
	v_addc_co_u32_e32 v25, vcc, 0, v33, vcc
	global_load_dwordx4 v[24:27], v[24:25], off nt
	v_add_co_u32_e32 v28, vcc, s87, v32
	v_readlane_b32 s45, v253, 17
	s_nop 0
	v_addc_co_u32_e32 v29, vcc, 0, v33, vcc
	global_load_dwordx4 v[28:31], v[28:29], off nt
	v_add_co_u32_e32 v32, vcc, s89, v32
	v_readlane_b32 s46, v253, 18
	s_nop 0
	v_addc_co_u32_e32 v33, vcc, 0, v33, vcc
	global_load_dwordx4 v[32:35], v[32:33], off nt
	v_readlane_b32 s47, v253, 19
	v_readlane_b32 s48, v253, 20
	v_readlane_b32 s49, v253, 21
	v_readlane_b32 s50, v253, 22
	v_readlane_b32 s51, v253, 23
	v_readlane_b32 s52, v253, 24
	v_readlane_b32 s53, v253, 25
	v_readlane_b32 s54, v253, 26
	v_readlane_b32 s55, v253, 27
	v_readlane_b32 s58, v253, 30
	v_readlane_b32 s59, v253, 31
	s_waitcnt vmcnt(0)
	ds_write2_b32 v2, v4, v5 offset1:1
	ds_write2_b32 v2, v6, v7 offset0:2 offset1:3
	v_add_u32_e32 v4, 0x420, v2
	ds_write2_b32 v4, v8, v9 offset1:1
	v_add_u32_e32 v4, 0x428, v2
	ds_write2_b32 v4, v10, v11 offset1:1
	v_add_u32_e32 v4, 0x840, v2
	ds_write2_b32 v4, v12, v13 offset1:1
	v_add_u32_e32 v4, 0x848, v2
	ds_write2_b32 v4, v14, v15 offset1:1
	v_add_u32_e32 v4, 0xc60, v2
	ds_write2_b32 v4, v16, v17 offset1:1
	v_add_u32_e32 v4, 0xc68, v2
	ds_write2_b32 v4, v18, v19 offset1:1
	v_add_u32_e32 v4, 0x1080, v2
	ds_write2_b32 v4, v20, v21 offset1:1
	v_add_u32_e32 v4, 0x1088, v2
	ds_write2_b32 v4, v22, v23 offset1:1
	v_add_u32_e32 v4, 0x14a0, v2
	ds_write2_b32 v4, v24, v25 offset1:1
	v_add_u32_e32 v4, 0x14a8, v2
	ds_write2_b32 v4, v26, v27 offset1:1
	v_add_u32_e32 v4, 0x18c0, v2
	ds_write2_b32 v4, v28, v29 offset1:1
	v_add_u32_e32 v4, 0x18c8, v2
	ds_write2_b32 v4, v30, v31 offset1:1
	v_add_u32_e32 v4, 0x1ce0, v2
	v_add_u32_e32 v2, 0x1ce8, v2
	ds_write2_b32 v4, v32, v33 offset1:1
	ds_write2_b32 v2, v34, v35 offset1:1
	s_waitcnt lgkmcnt(0)
	ds_read2_b32 v[10:11], v49 offset0:33 offset1:41
	ds_read2_b32 v[12:13], v49 offset1:8
	v_lshlrev_b32_e32 v2, 1, v38
	ds_read2_b32 v[14:15], v49 offset0:66 offset1:74
	ds_read2_b32 v[16:17], v49 offset0:99 offset1:107
	ds_read2_b32 v[18:19], v49 offset0:132 offset1:140
	ds_read2_b32 v[20:21], v49 offset0:165 offset1:173
	ds_read2_b32 v[22:23], v49 offset0:198 offset1:206
	ds_read2_b32 v[24:25], v49 offset0:231 offset1:239
	v_lshl_add_u64 v[8:9], s[6:7], 0, v[2:3]
	v_or_b32_e32 v2, s2, v39
	v_lshlrev_b32_e32 v2, 11, v2
	v_lshl_add_u64 v[26:27], v[8:9], 0, v[2:3]
	v_or_b32_e32 v2, s2, v46
	s_waitcnt lgkmcnt(0)
	v_cvt_pk_bf16_f32 v4, v12, v10
	v_lshlrev_b32_e32 v2, 11, v2
	v_cvt_pk_bf16_f32 v5, v14, v16
	v_cvt_pk_bf16_f32 v6, v18, v20
	v_cvt_pk_bf16_f32 v7, v22, v24
	global_store_dwordx4 v[26:27], v[4:7], off sc1
	s_nop 1
	v_cvt_pk_bf16_f32 v4, v13, v11
	v_lshl_add_u64 v[10:11], v[8:9], 0, v[2:3]
	v_cvt_pk_bf16_f32 v5, v15, v17
	v_cvt_pk_bf16_f32 v6, v19, v21
	v_cvt_pk_bf16_f32 v7, v23, v25
	global_store_dwordx4 v[10:11], v[4:7], off sc1
	ds_read2_b32 v[10:11], v49 offset0:16 offset1:24
	ds_read2_b32 v[12:13], v49 offset0:49 offset1:57
	ds_read2_b32 v[14:15], v49 offset0:82 offset1:90
	ds_read2_b32 v[16:17], v49 offset0:115 offset1:123
	ds_read2_b32 v[18:19], v49 offset0:148 offset1:156
	ds_read2_b32 v[20:21], v49 offset0:181 offset1:189
	ds_read2_b32 v[22:23], v49 offset0:214 offset1:222
	ds_read2_b32 v[24:25], v49 offset0:247 offset1:255
	v_or_b32_e32 v2, s2, v47
	v_lshlrev_b32_e32 v2, 11, v2
	v_lshl_add_u64 v[26:27], v[8:9], 0, v[2:3]
	v_or_b32_e32 v2, s2, v48
	v_lshlrev_b32_e32 v2, 11, v2
	s_waitcnt lgkmcnt(6)
	v_cvt_pk_bf16_f32 v4, v10, v12
	s_waitcnt lgkmcnt(4)
	v_cvt_pk_bf16_f32 v5, v14, v16
	s_waitcnt lgkmcnt(2)
	v_cvt_pk_bf16_f32 v6, v18, v20
	s_waitcnt lgkmcnt(0)
	v_cvt_pk_bf16_f32 v7, v22, v24
	v_lshl_add_u64 v[8:9], v[8:9], 0, v[2:3]
	global_store_dwordx4 v[26:27], v[4:7], off sc1
	s_nop 1
	v_cvt_pk_bf16_f32 v4, v11, v13
	v_cvt_pk_bf16_f32 v5, v15, v17
	v_cvt_pk_bf16_f32 v6, v19, v21
	v_cvt_pk_bf16_f32 v7, v23, v25
	global_store_dwordx4 v[8:9], v[4:7], off sc1
	s_waitcnt lgkmcnt(0)

; #define GAS __attribute__((address_space(1)))
; #define LAS __attribute__((address_space(3)))
; #define LDS_WAIT() asm volatile("s_waitcnt lgkmcnt(0)" ::: "memory")
; __device__ __forceinline__ unsigned pk2(float lo, float hi) { unsigned r; asm("v_cvt_pk_bf16_f32 %0, %1, %2" : "=v"(r) : "v"(lo), "v"(hi)); return r; }
; __device__ __forceinline__ void transpose_item(const float* W, int K, int N, bf16* WT, int drow0, int kb, int n0, LAS float* scr, int lane) {
;     const int k0 = 64 * kb; const int c4 = 4 * (lane & 7); const bool ok = (n0 + c4) < N;
;     f32x4 v[8];
; #pragma unroll
;     for (int i = 0; i < 8; ++i) { const int kk = 8 * i + (lane >> 3); v[i] = ok ? *(const f32x4*)(W + (size_t)(k0 + kk) * N + n0 + c4) : (f32x4){0.f, 0.f, 0.f, 0.f}; }
; #pragma unroll
;     for (int i = 0; i < 8; ++i) { const int kk = 8 * i + (lane >> 3); LAS float* d = scr + kk * 33 + c4; d[0] = v[i][0]; d[1] = v[i][1]; d[2] = v[i][2]; d[3] = v[i][3]; }
;     LDS_WAIT(); asm volatile("" ::: "memory");
;     const int c = lane & 7;
; #pragma unroll
;     for (int j = 0; j < 4; ++j) { const int n = (lane >> 3) + 8 * j; const LAS float* s = scr + (8 * c) * 33 + n;
;         v4u o; o.x = pk2(s[0 * 33], s[1 * 33]); o.y = pk2(s[2 * 33], s[3 * 33]); o.z = pk2(s[4 * 33], s[5 * 33]); o.w = pk2(s[6 * 33], s[7 * 33]);
;         *(GAS v4u*)(WT + (size_t)(drow0 + n) * K + k0 + 8 * c) = o; }
;     LDS_WAIT(); asm volatile("" ::: "memory");
; }
; __device__ __forceinline__ void convert_item(const In& I, unsigned char* ws, int it, LAS float* scr, int lane) {
;     ...
;     if (r < 2 * I_SQ) { const int j = r / I_SQ; r -= j * I_SQ; const int kb = r / 32, nb = r % 32;
;         transpose_item(I.nsa_w_out + (size_t)j * D * D, D, D, Wnout + (size_t)j * D * D, 32 * nb, kb, 32 * nb, scr, lane); return; }
.LBB0_510:
	s_andn2_b64 vcc, exec, s[2:3]
	s_cbranch_vccnz .LBB0_512
	s_add_i32 s2, s18, 0x1900
	s_lshr_b32 s68, s2, 9
	v_readlane_b32 s44, v253, 16
	s_lshl_b64 s[2:3], s[68:69], 22
	v_readlane_b32 s50, v253, 22
	v_readlane_b32 s51, v253, 23
	s_add_u32 s6, s50, s2
	s_addc_u32 s7, s51, s3
	s_lshl_b64 s[2:3], s[68:69], 21
	s_add_u32 s8, s22, s2
	s_addc_u32 s3, s23, s3
	s_and_b32 s2, s40, 0x3e0
	s_add_i32 s9, s41, 0x2a00
	s_and_b32 s9, s9, 0x3c0
	s_lshl_b32 s10, s2, 2
	s_add_u32 s6, s6, s10
	v_or_b32_e32 v6, s9, v39
	s_addc_u32 s7, s7, 0
	v_lshlrev_b32_e32 v2, 2, v36
	v_lshl_add_u64 v[4:5], s[6:7], 0, v[2:3]
	v_lshlrev_b32_e32 v2, 12, v6
	v_lshl_add_u64 v[32:33], v[4:5], 0, v[2:3]
	v_add_co_u32_e32 v8, vcc, s81, v32
	global_load_dwordx4 v[4:7], v[32:33], off nt
	s_nop 0
	v_addc_co_u32_e32 v9, vcc, 0, v33, vcc
	global_load_dwordx4 v[8:11], v[8:9], off nt
	v_add_co_u32_e32 v12, vcc, s79, v32
	v_add_u32_e32 v2, v44, v45
	s_nop 0
	v_addc_co_u32_e32 v13, vcc, 0, v33, vcc
	global_load_dwordx4 v[12:15], v[12:13], off nt
	v_add_co_u32_e32 v16, vcc, s80, v32
	s_lshl_b32 s6, s9, 1
	s_nop 0
	v_addc_co_u32_e32 v17, vcc, 0, v33, vcc
	global_load_dwordx4 v[16:19], v[16:17], off nt
	v_add_co_u32_e32 v20, vcc, s85, v32
	s_add_u32 s6, s8, s6
	s_nop 0
	v_addc_co_u32_e32 v21, vcc, 0, v33, vcc
	global_load_dwordx4 v[20:23], v[20:21], off nt
	v_add_co_u32_e32 v24, vcc, s86, v32
	s_addc_u32 s7, s3, 0
	s_nop 0
	v_addc_co_u32_e32 v25, vcc, 0, v33, vcc
	global_load_dwordx4 v[24:27], v[24:25], off nt
	v_add_co_u32_e32 v28, vcc, s87, v32
	v_readlane_b32 s45, v253, 17
	s_nop 0
	v_addc_co_u32_e32 v29, vcc, 0, v33, vcc
	global_load_dwordx4 v[28:31], v[28:29], off nt
	v_add_co_u32_e32 v32, vcc, s89, v32
	v_readlane_b32 s46, v253, 18
	s_nop 0
	v_addc_co_u32_e32 v33, vcc, 0, v33, vcc
	global_load_dwordx4 v[32:35], v[32:33], off nt
	v_readlane_b32 s47, v253, 19
	v_readlane_b32 s48, v253, 20
	v_readlane_b32 s49, v253, 21
	v_readlane_b32 s52, v253, 24
	v_readlane_b32 s53, v253, 25
	v_readlane_b32 s54, v253, 26
	v_readlane_b32 s55, v253, 27
	v_readlane_b32 s56, v253, 28
	v_readlane_b32 s57, v253, 29
	v_readlane_b32 s58, v253, 30
	v_readlane_b32 s59, v253, 31
	s_waitcnt vmcnt(0)
	ds_write2_b32 v2, v4, v5 offset1:1
	ds_write2_b32 v2, v6, v7 offset0:2 offset1:3
	v_add_u32_e32 v4, 0x420, v2
	ds_write2_b32 v4, v8, v9 offset1:1
	v_add_u32_e32 v4, 0x428, v2
	ds_write2_b32 v4, v10, v11 offset1:1
	v_add_u32_e32 v4, 0x840, v2
	ds_write2_b32 v4, v12, v13 offset1:1
	v_add_u32_e32 v4, 0x848, v2
	ds_write2_b32 v4, v14, v15 offset1:1
	v_add_u32_e32 v4, 0xc60, v2
	ds_write2_b32 v4, v16, v17 offset1:1
	v_add_u32_e32 v4, 0xc68, v2
	ds_write2_b32 v4, v18, v19 offset1:1
	v_add_u32_e32 v4, 0x1080, v2
	ds_write2_b32 v4, v20, v21 offset1:1
	v_add_u32_e32 v4, 0x1088, v2
	ds_write2_b32 v4, v22, v23 offset1:1
	v_add_u32_e32 v4, 0x14a0, v2
	ds_write2_b32 v4, v24, v25 offset1:1
	v_add_u32_e32 v4, 0x14a8, v2
	ds_write2_b32 v4, v26, v27 offset1:1
	v_add_u32_e32 v4, 0x18c0, v2
	ds_write2_b32 v4, v28, v29 offset1:1
	v_add_u32_e32 v4, 0x18c8, v2
	ds_write2_b32 v4, v30, v31 offset1:1
	v_add_u32_e32 v4, 0x1ce0, v2
	v_add_u32_e32 v2, 0x1ce8, v2
	ds_write2_b32 v4, v32, v33 offset1:1
	ds_write2_b32 v2, v34, v35 offset1:1
	s_waitcnt lgkmcnt(0)
	ds_read2_b32 v[10:11], v49 offset0:33 offset1:41
	ds_read2_b32 v[12:13], v49 offset1:8
	v_lshlrev_b32_e32 v2, 1, v38
	ds_read2_b32 v[14:15], v49 offset0:66 offset1:74
	ds_read2_b32 v[16:17], v49 offset0:99 offset1:107
	ds_read2_b32 v[18:19], v49 offset0:132 offset1:140
	ds_read2_b32 v[20:21], v49 offset0:165 offset1:173
	ds_read2_b32 v[22:23], v49 offset0:198 offset1:206
	ds_read2_b32 v[24:25], v49 offset0:231 offset1:239
	v_lshl_add_u64 v[8:9], s[6:7], 0, v[2:3]
	v_or_b32_e32 v2, s2, v39
	v_lshlrev_b32_e32 v2, 11, v2
	v_lshl_add_u64 v[26:27], v[8:9], 0, v[2:3]
	v_or_b32_e32 v2, s2, v46
	s_waitcnt lgkmcnt(0)
	v_cvt_pk_bf16_f32 v4, v12, v10
	v_lshlrev_b32_e32 v2, 11, v2
	v_cvt_pk_bf16_f32 v5, v14, v16
	v_cvt_pk_bf16_f32 v6, v18, v20
	v_cvt_pk_bf16_f32 v7, v22, v24
	global_store_dwordx4 v[26:27], v[4:7], off sc1
	s_nop 1
	v_cvt_pk_bf16_f32 v4, v13, v11
	v_lshl_add_u64 v[10:11], v[8:9], 0, v[2:3]
	v_cvt_pk_bf16_f32 v5, v15, v17
	v_cvt_pk_bf16_f32 v6, v19, v21
	v_cvt_pk_bf16_f32 v7, v23, v25
	global_store_dwordx4 v[10:11], v[4:7], off sc1
	ds_read2_b32 v[10:11], v49 offset0:16 offset1:24
	ds_read2_b32 v[12:13], v49 offset0:49 offset1:57
	ds_read2_b32 v[14:15], v49 offset0:82 offset1:90
	ds_read2_b32 v[16:17], v49 offset0:115 offset1:123
	ds_read2_b32 v[18:19], v49 offset0:148 offset1:156
	ds_read2_b32 v[20:21], v49 offset0:181 offset1:189
	ds_read2_b32 v[22:23], v49 offset0:214 offset1:222
	ds_read2_b32 v[24:25], v49 offset0:247 offset1:255
	v_or_b32_e32 v2, s2, v47
	v_lshlrev_b32_e32 v2, 11, v2
	v_lshl_add_u64 v[26:27], v[8:9], 0, v[2:3]
	v_or_b32_e32 v2, s2, v48
	v_lshlrev_b32_e32 v2, 11, v2
	s_waitcnt lgkmcnt(6)
	v_cvt_pk_bf16_f32 v4, v10, v12
	s_waitcnt lgkmcnt(4)
	v_cvt_pk_bf16_f32 v5, v14, v16
	s_waitcnt lgkmcnt(2)
	v_cvt_pk_bf16_f32 v6, v18, v20
	s_waitcnt lgkmcnt(0)
	v_cvt_pk_bf16_f32 v7, v22, v24
	v_lshl_add_u64 v[8:9], v[8:9], 0, v[2:3]
	global_store_dwordx4 v[26:27], v[4:7], off sc1
	s_nop 1
	v_cvt_pk_bf16_f32 v4, v11, v13
	v_cvt_pk_bf16_f32 v5, v15, v17
	v_cvt_pk_bf16_f32 v6, v19, v21
	v_cvt_pk_bf16_f32 v7, v23, v25
	global_store_dwordx4 v[8:9], v[4:7], off sc1
	s_waitcnt lgkmcnt(0)

; #define GAS __attribute__((address_space(1)))
; #define LAS __attribute__((address_space(3)))
; #define LDS_WAIT() asm volatile("s_waitcnt lgkmcnt(0)" ::: "memory")
; __device__ __forceinline__ unsigned pk2(float lo, float hi) { unsigned r; asm("v_cvt_pk_bf16_f32 %0, %1, %2" : "=v"(r) : "v"(lo), "v"(hi)); return r; }
; __device__ __forceinline__ void transpose_item(const float* W, int K, int N, bf16* WT, int drow0, int kb, int n0, LAS float* scr, int lane) {
;     const int k0 = 64 * kb; const int c4 = 4 * (lane & 7); const bool ok = (n0 + c4) < N;
;     f32x4 v[8];
; #pragma unroll
;     for (int i = 0; i < 8; ++i) { const int kk = 8 * i + (lane >> 3); v[i] = ok ? *(const f32x4*)(W + (size_t)(k0 + kk) * N + n0 + c4) : (f32x4){0.f, 0.f, 0.f, 0.f}; }
; #pragma unroll
;     for (int i = 0; i < 8; ++i) { const int kk = 8 * i + (lane >> 3); LAS float* d = scr + kk * 33 + c4; d[0] = v[i][0]; d[1] = v[i][1]; d[2] = v[i][2]; d[3] = v[i][3]; }
;     LDS_WAIT(); asm volatile("" ::: "memory");
;     const int c = lane & 7;
; #pragma unroll
;     for (int j = 0; j < 4; ++j) { const int n = (lane >> 3) + 8 * j; const LAS float* s = scr + (8 * c) * 33 + n;
;         v4u o; o.x = pk2(s[0 * 33], s[1 * 33]); o.y = pk2(s[2 * 33], s[3 * 33]); o.z = pk2(s[4 * 33], s[5 * 33]); o.w = pk2(s[6 * 33], s[7 * 33]);
;         *(GAS v4u*)(WT + (size_t)(drow0 + n) * K + k0 + 8 * c) = o; }
;     LDS_WAIT(); asm volatile("" ::: "memory");
; }
; __device__ __forceinline__ void convert_item(const In& I, unsigned char* ws, int it, LAS float* scr, int lane) {
;     ...
;     if (r < T0) { const int f = r / I_FFN; r -= f * I_FFN;
;         if (r < 2 * I_G) { const int up = r >= I_G; r -= up * I_G; const int kb = r / 88, nb = r % 88;
;             transpose_item((up ? I.w_up : I.w_gate) + (size_t)f * D * FF, D, FF, Wgu + (size_t)f * NGU * D, 256 * (nb >> 2) + 32 * (nb & 3) + 128 * up, kb, 32 * nb, scr, lane); }
;         else { r -= 2 * I_G; const int kb = r / 32, nb = r % 32; transpose_item(I.w_down + (size_t)f * FF * D, FF, D, Wd + (size_t)f * D * FF, 32 * nb, kb, 32 * nb, scr, lane); }
.LBB0_532:
	s_andn2_b64 vcc, exec, s[2:3]
	s_cbranch_vccnz .LBB0_477
	s_mul_hi_i32 s2, s42, 0x3e0f83e1
	s_lshr_b32 s3, s2, 31
	s_ashr_i32 s6, s2, 10
	s_add_i32 s6, s6, s3
	s_mul_i32 s2, s6, 0xffffef80
	s_add_i32 s7, s18, s2
	s_add_i32 s7, s7, 0xa800
	s_cmpk_gt_i32 s7, 0xaff
	s_mov_b64 s[2:3], -1
	s_cbranch_scc0 .LBB0_535
	v_readlane_b32 s44, v253, 0
	s_mul_i32 s3, s6, 0xb00000
	v_readlane_b32 s52, v253, 8
	s_mul_hi_i32 s2, s6, 0xb00000
	v_readlane_b32 s53, v253, 9
	s_add_u32 s9, s52, s3
	s_addc_u32 s11, s53, s2
	s_mul_i32 s3, s6, 0x580000
	s_mul_hi_i32 s2, s6, 0x580000
	s_add_u32 s3, s1, s3
	s_mul_i32 s10, s6, 0xffffdf00
	s_addc_u32 s8, s19, s2
	s_add_i32 s10, s41, s10
	s_add_i32 s10, s10, 0x14800
	s_and_b32 s2, s40, 0x3e0
	s_andn2_b32 s10, s10, 63
	s_add_i32 s68, s10, 0xffffea00
	s_lshl_b32 s10, s2, 2
	v_or_b32_e32 v32, s68, v39
	s_add_u32 s10, s9, s10
	s_addc_u32 s11, s11, 0
	v_lshlrev_b32_e32 v2, 2, v36
	v_ashrrev_i32_e32 v33, 31, v32
	v_or_b32_e32 v8, 8, v32
	v_lshl_add_u64 v[34:35], s[10:11], 0, v[2:3]
	v_lshlrev_b64 v[4:5], 12, v[32:33]
	v_ashrrev_i32_e32 v9, 31, v8
	v_lshl_add_u64 v[4:5], v[34:35], 0, v[4:5]
	v_lshlrev_b64 v[8:9], 12, v[8:9]
	v_or_b32_e32 v12, 16, v32
	global_load_dwordx4 v[4:7], v[4:5], off nt
	v_lshl_add_u64 v[8:9], v[34:35], 0, v[8:9]
	v_ashrrev_i32_e32 v13, 31, v12
	global_load_dwordx4 v[8:11], v[8:9], off nt
	v_lshlrev_b64 v[12:13], 12, v[12:13]
	v_or_b32_e32 v16, 24, v32
	v_lshl_add_u64 v[12:13], v[34:35], 0, v[12:13]
	v_ashrrev_i32_e32 v17, 31, v16
	global_load_dwordx4 v[12:15], v[12:13], off nt
	v_lshlrev_b64 v[16:17], 12, v[16:17]
	v_or_b32_e32 v20, 32, v32
	v_lshl_add_u64 v[16:17], v[34:35], 0, v[16:17]
	v_ashrrev_i32_e32 v21, 31, v20
	global_load_dwordx4 v[16:19], v[16:17], off nt
	v_lshlrev_b64 v[20:21], 12, v[20:21]
	v_or_b32_e32 v24, 40, v32
	v_lshl_add_u64 v[20:21], v[34:35], 0, v[20:21]
	v_ashrrev_i32_e32 v25, 31, v24
	global_load_dwordx4 v[20:23], v[20:21], off nt
	v_lshlrev_b64 v[24:25], 12, v[24:25]
	v_or_b32_e32 v28, 48, v32
	v_lshl_add_u64 v[24:25], v[34:35], 0, v[24:25]
	v_ashrrev_i32_e32 v29, 31, v28
	global_load_dwordx4 v[24:27], v[24:25], off nt
	v_lshlrev_b64 v[28:29], 12, v[28:29]
	v_or_b32_e32 v32, 56, v32
	v_lshl_add_u64 v[28:29], v[34:35], 0, v[28:29]
	v_ashrrev_i32_e32 v33, 31, v32
	global_load_dwordx4 v[28:31], v[28:29], off nt
	v_lshlrev_b64 v[32:33], 12, v[32:33]
	v_lshl_add_u64 v[32:33], v[34:35], 0, v[32:33]
	global_load_dwordx4 v[32:35], v[32:33], off nt
	v_add_u32_e32 v2, v44, v45
	s_lshl_b64 s[10:11], s[68:69], 1
	s_add_u32 s10, s3, s10
	s_addc_u32 s11, s8, s11
	v_readlane_b32 s45, v253, 1
	v_readlane_b32 s46, v253, 2
	v_readlane_b32 s47, v253, 3
	v_readlane_b32 s48, v253, 4
	v_readlane_b32 s49, v253, 5
	v_readlane_b32 s50, v253, 6
	v_readlane_b32 s51, v253, 7
	v_readlane_b32 s54, v253, 10
	v_readlane_b32 s55, v253, 11
	v_readlane_b32 s56, v253, 12
	v_readlane_b32 s57, v253, 13
	v_readlane_b32 s58, v253, 14
	v_readlane_b32 s59, v253, 15
	s_waitcnt vmcnt(0)
	ds_write2_b32 v2, v4, v5 offset1:1
	ds_write2_b32 v2, v6, v7 offset0:2 offset1:3
	v_add_u32_e32 v4, 0x420, v2
	ds_write2_b32 v4, v8, v9 offset1:1
	v_add_u32_e32 v4, 0x428, v2
	ds_write2_b32 v4, v10, v11 offset1:1
	v_add_u32_e32 v4, 0x840, v2
	ds_write2_b32 v4, v12, v13 offset1:1
	v_add_u32_e32 v4, 0x848, v2
	ds_write2_b32 v4, v14, v15 offset1:1
	v_add_u32_e32 v4, 0xc60, v2
	ds_write2_b32 v4, v16, v17 offset1:1
	v_add_u32_e32 v4, 0xc68, v2
	ds_write2_b32 v4, v18, v19 offset1:1
	v_add_u32_e32 v4, 0x1080, v2
	ds_write2_b32 v4, v20, v21 offset1:1
	v_add_u32_e32 v4, 0x1088, v2
	ds_write2_b32 v4, v22, v23 offset1:1
	v_add_u32_e32 v4, 0x14a0, v2
	ds_write2_b32 v4, v24, v25 offset1:1
	v_add_u32_e32 v4, 0x14a8, v2
	ds_write2_b32 v4, v26, v27 offset1:1
	v_add_u32_e32 v4, 0x18c0, v2
	ds_write2_b32 v4, v28, v29 offset1:1
	v_add_u32_e32 v4, 0x18c8, v2
	ds_write2_b32 v4, v30, v31 offset1:1
	v_add_u32_e32 v4, 0x1ce0, v2
	v_add_u32_e32 v2, 0x1ce8, v2
	ds_write2_b32 v4, v32, v33 offset1:1
	ds_write2_b32 v2, v34, v35 offset1:1
	s_waitcnt lgkmcnt(0)
	ds_read2_b32 v[10:11], v49 offset0:33 offset1:41
	ds_read2_b32 v[12:13], v49 offset1:8
	v_lshlrev_b32_e32 v2, 1, v38
	ds_read2_b32 v[14:15], v49 offset0:66 offset1:74
	ds_read2_b32 v[16:17], v49 offset0:99 offset1:107
	ds_read2_b32 v[18:19], v49 offset0:132 offset1:140
	ds_read2_b32 v[20:21], v49 offset0:165 offset1:173
	ds_read2_b32 v[22:23], v49 offset0:198 offset1:206
	ds_read2_b32 v[24:25], v49 offset0:231 offset1:239
	v_lshl_add_u64 v[8:9], s[10:11], 0, v[2:3]
	v_or_b32_e32 v2, s2, v39
	v_mul_u32_u24_e32 v2, 0x1600, v2
	v_lshl_add_u64 v[26:27], v[8:9], 0, v[2:3]
	v_or_b32_e32 v2, s2, v46
	s_waitcnt lgkmcnt(0)
	v_cvt_pk_bf16_f32 v4, v12, v10
	v_mul_u32_u24_e32 v2, 0x1600, v2
	v_cvt_pk_bf16_f32 v5, v14, v16
	v_cvt_pk_bf16_f32 v6, v18, v20
	v_cvt_pk_bf16_f32 v7, v22, v24
	global_store_dwordx4 v[26:27], v[4:7], off sc1
	s_nop 1
	v_cvt_pk_bf16_f32 v4, v13, v11
	v_lshl_add_u64 v[10:11], v[8:9], 0, v[2:3]
	v_cvt_pk_bf16_f32 v5, v15, v17
	v_cvt_pk_bf16_f32 v6, v19, v21
	v_cvt_pk_bf16_f32 v7, v23, v25
	global_store_dwordx4 v[10:11], v[4:7], off sc1
	ds_read2_b32 v[10:11], v49 offset0:16 offset1:24
	ds_read2_b32 v[12:13], v49 offset0:49 offset1:57
	ds_read2_b32 v[14:15], v49 offset0:82 offset1:90
	ds_read2_b32 v[16:17], v49 offset0:115 offset1:123
	ds_read2_b32 v[18:19], v49 offset0:148 offset1:156
	ds_read2_b32 v[20:21], v49 offset0:181 offset1:189
	ds_read2_b32 v[22:23], v49 offset0:214 offset1:222
	ds_read2_b32 v[24:25], v49 offset0:247 offset1:255
	v_or_b32_e32 v2, s2, v47
	v_mul_u32_u24_e32 v2, 0x1600, v2
	v_lshl_add_u64 v[26:27], v[8:9], 0, v[2:3]
	v_or_b32_e32 v2, s2, v48
	v_mul_u32_u24_e32 v2, 0x1600, v2
	s_waitcnt lgkmcnt(6)
	v_cvt_pk_bf16_f32 v4, v10, v12
	s_waitcnt lgkmcnt(4)
	v_cvt_pk_bf16_f32 v5, v14, v16
	s_waitcnt lgkmcnt(2)
	v_cvt_pk_bf16_f32 v6, v18, v20
	s_waitcnt lgkmcnt(0)
	v_cvt_pk_bf16_f32 v7, v22, v24
	v_lshl_add_u64 v[8:9], v[8:9], 0, v[2:3]
	global_store_dwordx4 v[26:27], v[4:7], off sc1
	s_mov_b64 s[2:3], 0
	s_nop 0
	v_cvt_pk_bf16_f32 v4, v11, v13
	v_cvt_pk_bf16_f32 v5, v15, v17
	v_cvt_pk_bf16_f32 v6, v19, v21
	v_cvt_pk_bf16_f32 v7, v23, v25
	global_store_dwordx4 v[8:9], v[4:7], off sc1
	s_waitcnt lgkmcnt(0)
; #define GAS __attribute__((address_space(1)))
; #define LAS __attribute__((address_space(3)))
; #define LDS_WAIT() asm volatile("s_waitcnt lgkmcnt(0)" ::: "memory")
; __device__ __forceinline__ unsigned pk2(float lo, float hi) { unsigned r; asm("v_cvt_pk_bf16_f32 %0, %1, %2" : "=v"(r) : "v"(lo), "v"(hi)); return r; }
; __device__ __forceinline__ void transpose_item(const float* W, int K, int N, bf16* WT, int drow0, int kb, int n0, LAS float* scr, int lane) {
;     const int k0 = 64 * kb; const int c4 = 4 * (lane & 7); const bool ok = (n0 + c4) < N;
;     f32x4 v[8];
; #pragma unroll
;     for (int i = 0; i < 8; ++i) { const int kk = 8 * i + (lane >> 3); v[i] = ok ? *(const f32x4*)(W + (size_t)(k0 + kk) * N + n0 + c4) : (f32x4){0.f, 0.f, 0.f, 0.f}; }
; #pragma unroll
;     for (int i = 0; i < 8; ++i) { const int kk = 8 * i + (lane >> 3); LAS float* d = scr + kk * 33 + c4; d[0] = v[i][0]; d[1] = v[i][1]; d[2] = v[i][2]; d[3] = v[i][3]; }
;     LDS_WAIT(); asm volatile("" ::: "memory");
;     const int c = lane & 7;
; #pragma unroll
;     for (int j = 0; j < 4; ++j) { const int n = (lane >> 3) + 8 * j; const LAS float* s = scr + (8 * c) * 33 + n;
;         v4u o; o.x = pk2(s[0 * 33], s[1 * 33]); o.y = pk2(s[2 * 33], s[3 * 33]); o.z = pk2(s[4 * 33], s[5 * 33]); o.w = pk2(s[6 * 33], s[7 * 33]);
;         *(GAS v4u*)(WT + (size_t)(drow0 + n) * K + k0 + 8 * c) = o; }
;     LDS_WAIT(); asm volatile("" ::: "memory");
; }
; __device__ __forceinline__ void convert_item(const In& I, unsigned char* ws, int it, LAS float* scr, int lane) {
;     ...
;     if (r < T0) { const int f = r / I_FFN; r -= f * I_FFN;
;         if (r < 2 * I_G) { const int up = r >= I_G; r -= up * I_G; const int kb = r / 88, nb = r % 88;
;             transpose_item((up ? I.w_up : I.w_gate) + (size_t)f * D * FF, D, FF, Wgu + (size_t)f * NGU * D, 256 * (nb >> 2) + 32 * (nb & 3) + 128 * up, kb, 32 * nb, scr, lane); }
.LBB0_535:
	s_andn2_b64 vcc, exec, s[2:3]
	s_cbranch_vccnz .LBB0_477
	s_cmpk_gt_i32 s7, 0x57f
	v_readlane_b32 s44, v253, 0
	s_cselect_b32 s2, 0xfffffa80, 0
	s_mul_i32 s3, s6, 0x1080
	v_readlane_b32 s48, v253, 4
	v_readlane_b32 s49, v253, 5
	v_readlane_b32 s50, v253, 6
	v_readlane_b32 s51, v253, 7
	s_cselect_b32 s7, 0x80, 0
	s_cselect_b32 s8, s50, s48
	s_cselect_b32 s9, s51, s49
	s_sub_i32 s2, s2, s3
	s_add_i32 s2, s18, s2
	s_add_i32 s2, s2, 0xa800
	s_mul_hi_i32 s3, s2, 0x2e8ba2e9
	s_lshr_b32 s10, s3, 31
	s_ashr_i32 s3, s3, 4
	s_add_i32 s3, s3, s10
	s_mul_i32 s10, s3, 0x58
	s_sub_i32 s2, s2, s10
	s_mul_hi_i32 s10, s6, 0xb00000
	s_mul_i32 s6, s6, 0xb00000
	s_add_u32 s11, s8, s6
	s_addc_u32 s12, s9, s10
	s_add_u32 s13, s28, s6
	s_addc_u32 s10, s29, s10
	s_lshl_b32 s8, s2, 5
	s_lshl_b32 s6, s2, 6
	s_and_b32 s2, s8, 0x60
	s_and_b32 s6, s6, 0xffffff00
	s_or_b32 s2, s2, s7
	s_ashr_i32 s9, s8, 31
	s_or_b32 s6, s2, s6
	s_lshl_b32 s2, s3, 6
	s_lshl_b64 s[8:9], s[8:9], 2
	s_add_u32 s8, s11, s8
	s_addc_u32 s9, s12, s9
	v_lshlrev_b32_e32 v2, 2, v36
	v_or_b32_e32 v34, s2, v39
	v_lshl_add_u64 v[32:33], s[8:9], 0, v[2:3]
	s_movk_i32 s3, 0x2c00
	v_mad_i64_i32 v[4:5], s[8:9], v34, s3, v[32:33]
	v_or_b32_e32 v2, 8, v34
	global_load_dwordx4 v[4:7], v[4:5], off nt
	v_mad_i64_i32 v[8:9], s[8:9], v2, s3, v[32:33]
	global_load_dwordx4 v[8:11], v[8:9], off nt
	v_or_b32_e32 v2, 16, v34
	v_mad_i64_i32 v[12:13], s[8:9], v2, s3, v[32:33]
	global_load_dwordx4 v[12:15], v[12:13], off nt
	v_or_b32_e32 v2, 24, v34
	v_mad_i64_i32 v[16:17], s[8:9], v2, s3, v[32:33]
	global_load_dwordx4 v[16:19], v[16:17], off nt
	v_or_b32_e32 v2, 32, v34
	v_mad_i64_i32 v[20:21], s[8:9], v2, s3, v[32:33]
	global_load_dwordx4 v[20:23], v[20:21], off nt
	v_or_b32_e32 v2, 40, v34
	v_mad_i64_i32 v[24:25], s[8:9], v2, s3, v[32:33]
	global_load_dwordx4 v[24:27], v[24:25], off nt
	v_or_b32_e32 v2, 48, v34
	v_mad_i64_i32 v[28:29], s[8:9], v2, s3, v[32:33]
	global_load_dwordx4 v[28:31], v[28:29], off nt
	v_or_b32_e32 v2, 56, v34
	v_mad_i64_i32 v[32:33], s[8:9], v2, s3, v[32:33]
	global_load_dwordx4 v[32:35], v[32:33], off nt
	v_add_u32_e32 v2, v44, v45
	s_ashr_i32 s3, s2, 31
	s_lshl_b64 s[2:3], s[2:3], 1
	s_add_u32 s2, s13, s2
	s_addc_u32 s3, s10, s3
	v_readlane_b32 s45, v253, 1
	v_readlane_b32 s46, v253, 2
	v_readlane_b32 s47, v253, 3
	v_readlane_b32 s52, v253, 8
	v_readlane_b32 s53, v253, 9
	v_readlane_b32 s54, v253, 10
	v_readlane_b32 s55, v253, 11
	v_readlane_b32 s56, v253, 12
	v_readlane_b32 s57, v253, 13
	v_readlane_b32 s58, v253, 14
	v_readlane_b32 s59, v253, 15
	s_waitcnt vmcnt(0)
	ds_write2_b32 v2, v4, v5 offset1:1
	ds_write2_b32 v2, v6, v7 offset0:2 offset1:3
	v_add_u32_e32 v4, 0x420, v2
	ds_write2_b32 v4, v8, v9 offset1:1
	v_add_u32_e32 v4, 0x428, v2
	ds_write2_b32 v4, v10, v11 offset1:1
	v_add_u32_e32 v4, 0x840, v2
	ds_write2_b32 v4, v12, v13 offset1:1
	v_add_u32_e32 v4, 0x848, v2
	ds_write2_b32 v4, v14, v15 offset1:1
	v_add_u32_e32 v4, 0xc60, v2
	ds_write2_b32 v4, v16, v17 offset1:1
	v_add_u32_e32 v4, 0xc68, v2
	ds_write2_b32 v4, v18, v19 offset1:1
	v_add_u32_e32 v4, 0x1080, v2
	ds_write2_b32 v4, v20, v21 offset1:1
	v_add_u32_e32 v4, 0x1088, v2
	ds_write2_b32 v4, v22, v23 offset1:1
	v_add_u32_e32 v4, 0x14a0, v2
	ds_write2_b32 v4, v24, v25 offset1:1
	v_add_u32_e32 v4, 0x14a8, v2
	ds_write2_b32 v4, v26, v27 offset1:1
	v_add_u32_e32 v4, 0x18c0, v2
	ds_write2_b32 v4, v28, v29 offset1:1
	v_add_u32_e32 v4, 0x18c8, v2
	ds_write2_b32 v4, v30, v31 offset1:1
	v_add_u32_e32 v4, 0x1ce0, v2
	v_add_u32_e32 v2, 0x1ce8, v2
	ds_write2_b32 v4, v32, v33 offset1:1
	ds_write2_b32 v2, v34, v35 offset1:1
	s_waitcnt lgkmcnt(0)
	ds_read2_b32 v[10:11], v49 offset0:33 offset1:41
	ds_read2_b32 v[12:13], v49 offset1:8
	ds_read2_b32 v[14:15], v49 offset0:66 offset1:74
	ds_read2_b32 v[16:17], v49 offset0:99 offset1:107
	ds_read2_b32 v[18:19], v49 offset0:132 offset1:140
	ds_read2_b32 v[20:21], v49 offset0:165 offset1:173
	ds_read2_b32 v[22:23], v49 offset0:198 offset1:206
	ds_read2_b32 v[24:25], v49 offset0:231 offset1:239
	v_or_b32_e32 v26, s6, v39
	v_lshlrev_b32_e32 v2, 1, v38
	v_ashrrev_i32_e32 v27, 31, v26
	v_lshl_add_u64 v[8:9], s[2:3], 0, v[2:3]
	v_lshlrev_b64 v[26:27], 11, v[26:27]
	s_waitcnt lgkmcnt(0)
	v_cvt_pk_bf16_f32 v4, v12, v10
	v_lshl_add_u64 v[26:27], v[8:9], 0, v[26:27]
	v_or_b32_e32 v10, s6, v46
	v_cvt_pk_bf16_f32 v5, v14, v16
	v_cvt_pk_bf16_f32 v6, v18, v20
	v_cvt_pk_bf16_f32 v7, v22, v24
	global_store_dwordx4 v[26:27], v[4:7], off sc1
	v_or_b32_e32 v26, s6, v47
	v_ashrrev_i32_e32 v27, 31, v26
	v_cvt_pk_bf16_f32 v4, v13, v11
	v_ashrrev_i32_e32 v11, 31, v10
	v_lshlrev_b64 v[10:11], 11, v[10:11]
	v_lshl_add_u64 v[10:11], v[8:9], 0, v[10:11]
	v_cvt_pk_bf16_f32 v5, v15, v17
	v_cvt_pk_bf16_f32 v6, v19, v21
	v_cvt_pk_bf16_f32 v7, v23, v25
	global_store_dwordx4 v[10:11], v[4:7], off sc1
	ds_read2_b32 v[10:11], v49 offset0:16 offset1:24
	ds_read2_b32 v[12:13], v49 offset0:49 offset1:57
	ds_read2_b32 v[14:15], v49 offset0:82 offset1:90
	ds_read2_b32 v[16:17], v49 offset0:115 offset1:123
	ds_read2_b32 v[18:19], v49 offset0:148 offset1:156
	ds_read2_b32 v[20:21], v49 offset0:181 offset1:189
	ds_read2_b32 v[22:23], v49 offset0:214 offset1:222
	ds_read2_b32 v[24:25], v49 offset0:247 offset1:255
	v_lshlrev_b64 v[26:27], 11, v[26:27]
	s_waitcnt lgkmcnt(6)
	v_cvt_pk_bf16_f32 v4, v10, v12
	v_lshl_add_u64 v[26:27], v[8:9], 0, v[26:27]
	v_or_b32_e32 v10, s6, v48
	s_waitcnt lgkmcnt(4)
	v_cvt_pk_bf16_f32 v5, v14, v16
	s_waitcnt lgkmcnt(2)
	v_cvt_pk_bf16_f32 v6, v18, v20
	s_waitcnt lgkmcnt(0)
	v_cvt_pk_bf16_f32 v7, v22, v24
	global_store_dwordx4 v[26:27], v[4:7], off sc1
	s_nop 1
	v_cvt_pk_bf16_f32 v4, v11, v13
	v_ashrrev_i32_e32 v11, 31, v10
	v_lshlrev_b64 v[10:11], 11, v[10:11]
	v_lshl_add_u64 v[8:9], v[8:9], 0, v[10:11]
	v_cvt_pk_bf16_f32 v5, v15, v17
	v_cvt_pk_bf16_f32 v6, v19, v21
	v_cvt_pk_bf16_f32 v7, v23, v25
	global_store_dwordx4 v[8:9], v[4:7], off sc1
	s_waitcnt lgkmcnt(0)
	s_branch .LBB0_477

; #define GAS __attribute__((address_space(1)))
; __device__ __forceinline__ void transpose_item(const float* W, int K, int N, bf16* WT, int drow0, int kb, int n0, LAS float* scr, int lane) {
;     const int k0 = 64 * kb; const int c4 = 4 * (lane & 7); const bool ok = (n0 + c4) < N;
;     f32x4 v[8];
; #pragma unroll
;     for (int i = 0; i < 8; ++i) { const int kk = 8 * i + (lane >> 3); v[i] = ok ? *(const f32x4*)(W + (size_t)(k0 + kk) * N + n0 + c4) : (f32x4){0.f, 0.f, 0.f, 0.f}; }
; #pragma unroll
;     for (int i = 0; i < 8; ++i) { const int kk = 8 * i + (lane >> 3); LAS float* d = scr + kk * 33 + c4; d[0] = v[i][0]; d[1] = v[i][1]; d[2] = v[i][2]; d[3] = v[i][3]; }
;     LDS_WAIT(); asm volatile("" ::: "memory");
;     const int c = lane & 7;
; #pragma unroll
;     for (int j = 0; j < 4; ++j) { const int n = (lane >> 3) + 8 * j; const LAS float* s = scr + (8 * c) * 33 + n;
;         v4u o; o.x = pk2(s[0 * 33], s[1 * 33]); o.y = pk2(s[2 * 33], s[3 * 33]); o.z = pk2(s[4 * 33], s[5 * 33]); o.w = pk2(s[6 * 33], s[7 * 33]);
;         *(GAS v4u*)(WT + (size_t)(drow0 + n) * K + k0 + 8 * c) = o; }
;     LDS_WAIT(); asm volatile("" ::: "memory");
; }
; __device__ __forceinline__ void convert_item(const In& I, unsigned char* ws, int it, LAS float* scr, int lane) {
;     ...
;     int r = it;
;     if (r < T0) { const int f = r / I_FFN; r -= f * I_FFN;
;         if (r < 2 * I_G) { const int up = r >= I_G; r -= up * I_G; const int kb = r / 88, nb = r % 88;
;             transpose_item((up ? I.w_up : I.w_gate) + (size_t)f * D * FF, D, FF, Wgu + (size_t)f * NGU * D, 256 * (nb >> 2) + 32 * (nb & 3) + 128 * up, kb, 32 * nb, scr, lane); }
;         else { r -= 2 * I_G; const int kb = r / 32, nb = r % 32; transpose_item(I.w_down + (size_t)f * FF * D, FF, D, Wd + (size_t)f * D * FF, 32 * nb, kb, 32 * nb, scr, lane); }
;         return; }
;     r -= T0;
;     if (r < 2 * I_NIN) { const int j = r / I_NIN; r -= j * I_NIN; const int kb = r / 88, nb = r % 88;
;         transpose_item(I.nsa_w_in + (size_t)j * D * NSA_IN, D, NSA_IN, Wnin + (size_t)j * NSA_IN_PAD * D, 32 * nb, kb, 32 * nb, scr, lane); return; }
;     r -= 2 * I_NIN;
;     if (r < 2 * I_SQ) { const int j = r / I_SQ; r -= j * I_SQ; const int kb = r / 32, nb = r % 32;
;         transpose_item(I.nsa_w_out + (size_t)j * D * D, D, D, Wnout + (size_t)j * D * D, 32 * nb, kb, 32 * nb, scr, lane); return; }
;     r -= 2 * I_SQ;
.LBB0_540:
	s_add_i32 s30, s14, s16
	s_add_i32 s34, s30, 0xa800
	s_cmp_gt_i32 s34, 0x83ff
	s_mov_b64 s[2:3], -1
	s_cbranch_scc0 .LBB0_594
	s_cmpk_gt_u32 s34, 0x8eff
	s_cbranch_scc0 .LBB0_575
	s_cmpk_gt_u32 s34, 0x92ff
	s_cbranch_scc0 .LBB0_572
	s_cmpk_gt_u32 s34, 0x9fff
	s_cbranch_scc0 .LBB0_553
	s_cmpk_gt_u32 s34, 0xa3ff
	s_cbranch_scc0 .LBB0_550
	s_cmpk_gt_u32 s34, 0xa7ff
	s_cbranch_scc0 .LBB0_547
	s_lshr_b32 s68, s30, 3
	v_readlane_b32 s40, v253, 16
	s_lshl_b64 s[2:3], s[68:69], 16
	v_readlane_b32 s44, v253, 20
	v_readlane_b32 s45, v253, 21
	s_add_u32 s5, s44, s2
	s_addc_u32 s6, s45, s3
	s_lshl_b64 s[2:3], s[68:69], 15
	s_add_u32 s7, s26, s2
	s_addc_u32 s8, s27, s3
	s_and_b32 s4, s33, 32
	s_and_b32 s9, s33, 0xc0
	s_lshl_b32 s2, s4, 2
	s_add_u32 s2, s5, s2
	v_or_b32_e32 v2, s9, v37
	s_addc_u32 s3, s6, 0
	v_lshlrev_b32_e32 v4, 2, v36
	v_mov_b32_e32 v5, v3
	v_lshl_add_u64 v[4:5], s[2:3], 0, v[4:5]
	v_lshlrev_b32_e32 v6, 8, v2
	v_mov_b32_e32 v7, v3
	v_lshl_add_u64 v[28:29], v[4:5], 0, v[6:7]
	global_load_dwordx4 v[4:7], v[28:29], off nt
	global_load_dwordx4 v[8:11], v[28:29], off offset:2048 nt
	v_add_co_u32_e32 v16, vcc, s84, v28
	s_movk_i32 s2, 0x3000
	s_nop 0
	v_addc_co_u32_e32 v17, vcc, 0, v29, vcc
	v_add_co_u32_e32 v24, vcc, s74, v28
	v_add_u32_e32 v2, v39, v44
	s_nop 0
	v_addc_co_u32_e32 v25, vcc, 0, v29, vcc
	global_load_dwordx4 v[12:15], v[24:25], off offset:-4096 nt
	s_nop 0
	global_load_dwordx4 v[16:19], v[16:17], off offset:2048 nt
	s_nop 0
	global_load_dwordx4 v[20:23], v[24:25], off nt
	s_nop 0
	global_load_dwordx4 v[24:27], v[24:25], off offset:2048 nt
	v_add_co_u32_e32 v32, vcc, s2, v28
	s_lshl_b32 s2, s9, 1
	s_nop 0
	v_addc_co_u32_e32 v33, vcc, 0, v29, vcc
	global_load_dwordx4 v[28:31], v[32:33], off nt
	s_nop 0
	global_load_dwordx4 v[32:35], v[32:33], off offset:2048 nt
	s_add_u32 s2, s7, s2
	s_addc_u32 s3, s8, 0
	v_readlane_b32 s41, v253, 17
	v_readlane_b32 s42, v253, 18
	v_readlane_b32 s43, v253, 19
	v_readlane_b32 s46, v253, 22
	v_readlane_b32 s47, v253, 23
	v_readlane_b32 s48, v253, 24
	v_readlane_b32 s49, v253, 25
	v_readlane_b32 s50, v253, 26
	v_readlane_b32 s51, v253, 27
	v_readlane_b32 s52, v253, 28
	v_readlane_b32 s53, v253, 29
	v_readlane_b32 s54, v253, 30
	v_readlane_b32 s55, v253, 31
	s_waitcnt vmcnt(0)
	ds_write2_b32 v2, v4, v5 offset1:1
	ds_write2_b32 v2, v6, v7 offset0:2 offset1:3
	v_add_u32_e32 v4, 0x420, v2
	ds_write2_b32 v4, v8, v9 offset1:1
	v_add_u32_e32 v4, 0x428, v2
	ds_write2_b32 v4, v10, v11 offset1:1
	v_add_u32_e32 v4, 0x840, v2
	v_mov_b32_e32 v5, v3
	ds_write2_b32 v4, v12, v13 offset1:1
	v_add_u32_e32 v4, 0x848, v2
	ds_write2_b32 v4, v14, v15 offset1:1
	v_add_u32_e32 v4, 0xc60, v2
	ds_write2_b32 v4, v16, v17 offset1:1
	v_add_u32_e32 v4, 0xc68, v2
	ds_write2_b32 v4, v18, v19 offset1:1
	v_add_u32_e32 v4, 0x1080, v2
	ds_write2_b32 v4, v20, v21 offset1:1
	v_add_u32_e32 v4, 0x1088, v2
	ds_write2_b32 v4, v22, v23 offset1:1
	v_add_u32_e32 v4, 0x14a0, v2
	ds_write2_b32 v4, v24, v25 offset1:1
	v_add_u32_e32 v4, 0x14a8, v2
	ds_write2_b32 v4, v26, v27 offset1:1
	v_add_u32_e32 v4, 0x18c0, v2
	ds_write2_b32 v4, v28, v29 offset1:1
	v_add_u32_e32 v4, 0x18c8, v2
	ds_write2_b32 v4, v30, v31 offset1:1
	v_add_u32_e32 v4, 0x1ce0, v2
	v_add_u32_e32 v2, 0x1ce8, v2
	ds_write2_b32 v4, v32, v33 offset1:1
	ds_write2_b32 v2, v34, v35 offset1:1
	s_waitcnt lgkmcnt(0)
	ds_read2_b32 v[10:11], v48 offset0:33 offset1:41
	ds_read2_b32 v[12:13], v48 offset1:8
	ds_read2_b32 v[14:15], v48 offset0:66 offset1:74
	ds_read2_b32 v[16:17], v48 offset0:99 offset1:107
	ds_read2_b32 v[18:19], v48 offset0:132 offset1:140
	ds_read2_b32 v[20:21], v48 offset0:165 offset1:173
	ds_read2_b32 v[22:23], v48 offset0:198 offset1:206
	ds_read2_b32 v[24:25], v48 offset0:231 offset1:239
	v_lshlrev_b32_e32 v4, 1, v38
	v_or_b32_e32 v2, s4, v37
	v_lshl_add_u64 v[8:9], s[2:3], 0, v[4:5]
	v_lshlrev_b32_e32 v26, 9, v2
	v_mov_b32_e32 v27, v3
	s_waitcnt lgkmcnt(0)
	v_cvt_pk_bf16_f32 v4, v12, v10
	v_lshl_add_u64 v[26:27], v[8:9], 0, v[26:27]
	v_or_b32_e32 v2, s4, v45
	v_cvt_pk_bf16_f32 v5, v14, v16
	v_cvt_pk_bf16_f32 v6, v18, v20
	v_cvt_pk_bf16_f32 v7, v22, v24
	global_store_dwordx4 v[26:27], v[4:7], off sc1
	v_lshlrev_b32_e32 v10, 9, v2
	v_or_b32_e32 v2, s4, v46
	v_cvt_pk_bf16_f32 v4, v13, v11
	v_mov_b32_e32 v11, v3
	v_lshl_add_u64 v[10:11], v[8:9], 0, v[10:11]
	v_cvt_pk_bf16_f32 v5, v15, v17
	v_cvt_pk_bf16_f32 v6, v19, v21
	v_cvt_pk_bf16_f32 v7, v23, v25
	global_store_dwordx4 v[10:11], v[4:7], off sc1
	ds_read2_b32 v[10:11], v48 offset0:16 offset1:24
	ds_read2_b32 v[12:13], v48 offset0:49 offset1:57
	ds_read2_b32 v[14:15], v48 offset0:82 offset1:90
	ds_read2_b32 v[16:17], v48 offset0:115 offset1:123
	ds_read2_b32 v[18:19], v48 offset0:148 offset1:156
	ds_read2_b32 v[20:21], v48 offset0:181 offset1:189
	ds_read2_b32 v[22:23], v48 offset0:214 offset1:222
	ds_read2_b32 v[24:25], v48 offset0:247 offset1:255
	v_lshlrev_b32_e32 v26, 9, v2
	v_mov_b32_e32 v27, v3
	s_waitcnt lgkmcnt(6)
	v_cvt_pk_bf16_f32 v4, v10, v12
	v_lshl_add_u64 v[26:27], v[8:9], 0, v[26:27]
	v_or_b32_e32 v2, s4, v47
	s_waitcnt lgkmcnt(4)
	v_cvt_pk_bf16_f32 v5, v14, v16
	s_waitcnt lgkmcnt(2)
	v_cvt_pk_bf16_f32 v6, v18, v20
	s_waitcnt lgkmcnt(0)
	v_cvt_pk_bf16_f32 v7, v22, v24
	global_store_dwordx4 v[26:27], v[4:7], off sc1
	v_lshlrev_b32_e32 v10, 9, v2
	s_mov_b64 s[2:3], 0
	v_cvt_pk_bf16_f32 v4, v11, v13
	v_mov_b32_e32 v11, v3
	v_lshl_add_u64 v[8:9], v[8:9], 0, v[10:11]
	v_cvt_pk_bf16_f32 v5, v15, v17
	v_cvt_pk_bf16_f32 v6, v19, v21
	v_cvt_pk_bf16_f32 v7, v23, v25
	global_store_dwordx4 v[8:9], v[4:7], off sc1
	s_waitcnt lgkmcnt(0)
; #define GAS __attribute__((address_space(1)))
; #define LAS __attribute__((address_space(3)))
; #define LDS_WAIT() asm volatile("s_waitcnt lgkmcnt(0)" ::: "memory")
; __device__ __forceinline__ unsigned pk2(float lo, float hi) { unsigned r; asm("v_cvt_pk_bf16_f32 %0, %1, %2" : "=v"(r) : "v"(lo), "v"(hi)); return r; }
; __device__ __forceinline__ void transpose_item(const float* W, int K, int N, bf16* WT, int drow0, int kb, int n0, LAS float* scr, int lane) {
;     const int k0 = 64 * kb; const int c4 = 4 * (lane & 7); const bool ok = (n0 + c4) < N;
;     f32x4 v[8];
; #pragma unroll
;     for (int i = 0; i < 8; ++i) { const int kk = 8 * i + (lane >> 3); v[i] = ok ? *(const f32x4*)(W + (size_t)(k0 + kk) * N + n0 + c4) : (f32x4){0.f, 0.f, 0.f, 0.f}; }
; #pragma unroll
;     for (int i = 0; i < 8; ++i) { const int kk = 8 * i + (lane >> 3); LAS float* d = scr + kk * 33 + c4; d[0] = v[i][0]; d[1] = v[i][1]; d[2] = v[i][2]; d[3] = v[i][3]; }
;     LDS_WAIT(); asm volatile("" ::: "memory");
;     const int c = lane & 7;
; #pragma unroll
;     for (int j = 0; j < 4; ++j) { const int n = (lane >> 3) + 8 * j; const LAS float* s = scr + (8 * c) * 33 + n;
;         v4u o; o.x = pk2(s[0 * 33], s[1 * 33]); o.y = pk2(s[2 * 33], s[3 * 33]); o.z = pk2(s[4 * 33], s[5 * 33]); o.w = pk2(s[6 * 33], s[7 * 33]);
;         *(GAS v4u*)(WT + (size_t)(drow0 + n) * K + k0 + 8 * c) = o; }
;     LDS_WAIT(); asm volatile("" ::: "memory");
; }
; __device__ __forceinline__ void convert_item(const In& I, unsigned char* ws, int it, LAS float* scr, int lane) {
;     ...
;     if (r < 4 * I_W1) { const int jk = r / I_W1; r -= jk * I_W1; const int kb = r / 8, nb = r % 8;
;         transpose_item(I.nsa_w1 + (size_t)jk * 2048 * 256, 2048, 256, W1t + (size_t)jk * 256 * 2048, 32 * nb, kb, 32 * nb, scr, lane); return; }
.LBB0_547:
	s_andn2_b64 vcc, exec, s[2:3]
	s_cbranch_vccnz .LBB0_549
	s_add_i32 s2, s30, 0x400
	s_lshr_b32 s68, s2, 8
	s_lshl_b64 s[2:3], s[68:69], 21
	v_readlane_b32 s40, v253, 16
	v_readlane_b32 s41, v253, 17
	s_add_u32 s4, s40, s2
	s_addc_u32 s5, s41, s3
	s_lshl_b64 s[2:3], s[68:69], 20
	s_add_u32 s6, s24, s2
	s_addc_u32 s3, s25, s3
	s_and_b32 s2, s33, 0xe0
	s_and_b32 s7, s31, 0x7c0
	s_lshl_b32 s8, s2, 2
	s_add_u32 s4, s4, s8
	v_or_b32_e32 v6, s7, v37
	s_addc_u32 s5, s5, 0
	v_lshlrev_b32_e32 v2, 2, v36
	v_lshl_add_u64 v[4:5], s[4:5], 0, v[2:3]
	v_lshlrev_b32_e32 v2, 10, v6
	v_lshl_add_u64 v[32:33], v[4:5], 0, v[2:3]
	v_add_co_u32_e32 v8, vcc, s74, v32
	global_load_dwordx4 v[4:7], v[32:33], off nt
	s_nop 0
	v_addc_co_u32_e32 v9, vcc, 0, v33, vcc
	s_movk_i32 s4, 0x4000
	global_load_dwordx4 v[8:11], v[8:9], off nt
	v_add_co_u32_e32 v12, vcc, s4, v32
	s_movk_i32 s4, 0x6000
	s_nop 0
	v_addc_co_u32_e32 v13, vcc, 0, v33, vcc
	global_load_dwordx4 v[12:15], v[12:13], off nt
	v_add_co_u32_e32 v16, vcc, s4, v32
	s_mov_b32 s4, 0xa000
	s_nop 0
	v_addc_co_u32_e32 v17, vcc, 0, v33, vcc
	global_load_dwordx4 v[16:19], v[16:17], off nt
	v_add_co_u32_e32 v20, vcc, s81, v32
	v_add_u32_e32 v2, v39, v44
	s_nop 0
	v_addc_co_u32_e32 v21, vcc, 0, v33, vcc
	global_load_dwordx4 v[20:23], v[20:21], off nt
	v_add_co_u32_e32 v24, vcc, s4, v32
	s_mov_b32 s4, 0xc000
	s_nop 0
	v_addc_co_u32_e32 v25, vcc, 0, v33, vcc
	global_load_dwordx4 v[24:27], v[24:25], off nt
	v_add_co_u32_e32 v28, vcc, s4, v32
	s_mov_b32 s4, 0xe000
	s_nop 0
	v_addc_co_u32_e32 v29, vcc, 0, v33, vcc
	global_load_dwordx4 v[28:31], v[28:29], off nt
	v_add_co_u32_e32 v32, vcc, s4, v32
	s_lshl_b32 s4, s7, 1
	s_nop 0
	v_addc_co_u32_e32 v33, vcc, 0, v33, vcc
	global_load_dwordx4 v[32:35], v[32:33], off nt
	s_add_u32 s4, s6, s4
	s_addc_u32 s5, s3, 0
	v_readlane_b32 s42, v253, 18
	v_readlane_b32 s43, v253, 19
	v_readlane_b32 s44, v253, 20
	v_readlane_b32 s45, v253, 21
	v_readlane_b32 s46, v253, 22
	v_readlane_b32 s47, v253, 23
	v_readlane_b32 s48, v253, 24
	v_readlane_b32 s49, v253, 25
	v_readlane_b32 s50, v253, 26
	v_readlane_b32 s51, v253, 27
	v_readlane_b32 s52, v253, 28
	v_readlane_b32 s53, v253, 29
	v_readlane_b32 s54, v253, 30
	v_readlane_b32 s55, v253, 31
	s_waitcnt vmcnt(0)
	ds_write2_b32 v2, v4, v5 offset1:1
	ds_write2_b32 v2, v6, v7 offset0:2 offset1:3
	v_add_u32_e32 v4, 0x420, v2
	ds_write2_b32 v4, v8, v9 offset1:1
	v_add_u32_e32 v4, 0x428, v2
	ds_write2_b32 v4, v10, v11 offset1:1
	v_add_u32_e32 v4, 0x840, v2
	ds_write2_b32 v4, v12, v13 offset1:1
	v_add_u32_e32 v4, 0x848, v2
	ds_write2_b32 v4, v14, v15 offset1:1
	v_add_u32_e32 v4, 0xc60, v2
	ds_write2_b32 v4, v16, v17 offset1:1
	v_add_u32_e32 v4, 0xc68, v2
	ds_write2_b32 v4, v18, v19 offset1:1
	v_add_u32_e32 v4, 0x1080, v2
	ds_write2_b32 v4, v20, v21 offset1:1
	v_add_u32_e32 v4, 0x1088, v2
	ds_write2_b32 v4, v22, v23 offset1:1
	v_add_u32_e32 v4, 0x14a0, v2
	ds_write2_b32 v4, v24, v25 offset1:1
	v_add_u32_e32 v4, 0x14a8, v2
	ds_write2_b32 v4, v26, v27 offset1:1
	v_add_u32_e32 v4, 0x18c0, v2
	ds_write2_b32 v4, v28, v29 offset1:1
	v_add_u32_e32 v4, 0x18c8, v2
	ds_write2_b32 v4, v30, v31 offset1:1
	v_add_u32_e32 v4, 0x1ce0, v2
	v_add_u32_e32 v2, 0x1ce8, v2
	ds_write2_b32 v4, v32, v33 offset1:1
	ds_write2_b32 v2, v34, v35 offset1:1
	s_waitcnt lgkmcnt(0)
	ds_read2_b32 v[10:11], v48 offset0:33 offset1:41
	ds_read2_b32 v[12:13], v48 offset1:8
	ds_read2_b32 v[14:15], v48 offset0:66 offset1:74
	ds_read2_b32 v[16:17], v48 offset0:99 offset1:107
	ds_read2_b32 v[18:19], v48 offset0:132 offset1:140
	ds_read2_b32 v[20:21], v48 offset0:165 offset1:173
	ds_read2_b32 v[22:23], v48 offset0:198 offset1:206
	ds_read2_b32 v[24:25], v48 offset0:231 offset1:239
	v_lshlrev_b32_e32 v2, 1, v38
	v_lshl_add_u64 v[8:9], s[4:5], 0, v[2:3]
	v_or_b32_e32 v2, s2, v37
	v_lshlrev_b32_e32 v2, 12, v2
	s_waitcnt lgkmcnt(0)
	v_cvt_pk_bf16_f32 v4, v12, v10
	v_lshl_add_u64 v[26:27], v[8:9], 0, v[2:3]
	v_or_b32_e32 v2, s2, v45
	v_cvt_pk_bf16_f32 v5, v14, v16
	v_cvt_pk_bf16_f32 v6, v18, v20
	v_cvt_pk_bf16_f32 v7, v22, v24
	global_store_dwordx4 v[26:27], v[4:7], off sc1
	v_lshlrev_b32_e32 v10, 12, v2
	v_or_b32_e32 v2, s2, v46
	v_cvt_pk_bf16_f32 v4, v13, v11
	v_mov_b32_e32 v11, v3
	v_lshl_add_u64 v[10:11], v[8:9], 0, v[10:11]
	v_cvt_pk_bf16_f32 v5, v15, v17
	v_cvt_pk_bf16_f32 v6, v19, v21
	v_cvt_pk_bf16_f32 v7, v23, v25
	global_store_dwordx4 v[10:11], v[4:7], off sc1
	ds_read2_b32 v[10:11], v48 offset0:16 offset1:24
	ds_read2_b32 v[12:13], v48 offset0:49 offset1:57
	ds_read2_b32 v[14:15], v48 offset0:82 offset1:90
	ds_read2_b32 v[16:17], v48 offset0:115 offset1:123
	ds_read2_b32 v[18:19], v48 offset0:148 offset1:156
	ds_read2_b32 v[20:21], v48 offset0:181 offset1:189
	ds_read2_b32 v[22:23], v48 offset0:214 offset1:222
	ds_read2_b32 v[24:25], v48 offset0:247 offset1:255
	v_lshlrev_b32_e32 v26, 12, v2
	v_mov_b32_e32 v27, v3
	s_waitcnt lgkmcnt(6)
	v_cvt_pk_bf16_f32 v4, v10, v12
	v_lshl_add_u64 v[26:27], v[8:9], 0, v[26:27]
	v_or_b32_e32 v2, s2, v47
	s_waitcnt lgkmcnt(4)
	v_cvt_pk_bf16_f32 v5, v14, v16
	s_waitcnt lgkmcnt(2)
	v_cvt_pk_bf16_f32 v6, v18, v20
	s_waitcnt lgkmcnt(0)
	v_cvt_pk_bf16_f32 v7, v22, v24
	global_store_dwordx4 v[26:27], v[4:7], off sc1
	v_lshlrev_b32_e32 v10, 12, v2
	s_nop 0
	v_cvt_pk_bf16_f32 v4, v11, v13
	v_mov_b32_e32 v11, v3
	v_lshl_add_u64 v[8:9], v[8:9], 0, v[10:11]
	v_cvt_pk_bf16_f32 v5, v15, v17
	v_cvt_pk_bf16_f32 v6, v19, v21
	v_cvt_pk_bf16_f32 v7, v23, v25
	global_store_dwordx4 v[8:9], v[4:7], off sc1
	s_waitcnt lgkmcnt(0)

; #define GAS __attribute__((address_space(1)))
; #define LAS __attribute__((address_space(3)))
; #define LDS_WAIT() asm volatile("s_waitcnt lgkmcnt(0)" ::: "memory")
; __device__ __forceinline__ unsigned pk2(float lo, float hi) { unsigned r; asm("v_cvt_pk_bf16_f32 %0, %1, %2" : "=v"(r) : "v"(lo), "v"(hi)); return r; }
; __device__ __forceinline__ void transpose_item(const float* W, int K, int N, bf16* WT, int drow0, int kb, int n0, LAS float* scr, int lane) {
;     const int k0 = 64 * kb; const int c4 = 4 * (lane & 7); const bool ok = (n0 + c4) < N;
;     f32x4 v[8];
; #pragma unroll
;     for (int i = 0; i < 8; ++i) { const int kk = 8 * i + (lane >> 3); v[i] = ok ? *(const f32x4*)(W + (size_t)(k0 + kk) * N + n0 + c4) : (f32x4){0.f, 0.f, 0.f, 0.f}; }
; #pragma unroll
;     for (int i = 0; i < 8; ++i) { const int kk = 8 * i + (lane >> 3); LAS float* d = scr + kk * 33 + c4; d[0] = v[i][0]; d[1] = v[i][1]; d[2] = v[i][2]; d[3] = v[i][3]; }
;     LDS_WAIT(); asm volatile("" ::: "memory");
;     const int c = lane & 7;
; #pragma unroll
;     for (int j = 0; j < 4; ++j) { const int n = (lane >> 3) + 8 * j; const LAS float* s = scr + (8 * c) * 33 + n;
;         v4u o; o.x = pk2(s[0 * 33], s[1 * 33]); o.y = pk2(s[2 * 33], s[3 * 33]); o.z = pk2(s[4 * 33], s[5 * 33]); o.w = pk2(s[6 * 33], s[7 * 33]);
;         *(GAS v4u*)(WT + (size_t)(drow0 + n) * K + k0 + 8 * c) = o; }
;     LDS_WAIT(); asm volatile("" ::: "memory");
; }
; __device__ __forceinline__ void convert_item(const In& I, unsigned char* ws, int it, LAS float* scr, int lane) {
;     ...
;     if (r < 2 * I_SQ) { const int j = r / I_SQ; r -= j * I_SQ; const int kb = r / 32, nb = r % 32;
;         transpose_item(I.fox_w_out + (size_t)j * D * D, D, D, Wfout + (size_t)j * D * D, 32 * nb, kb, 32 * nb, scr, lane); return; }
.LBB0_550:
	s_andn2_b64 vcc, exec, s[2:3]
	s_cbranch_vccnz .LBB0_552
	s_add_i32 s2, s30, 0x800
	s_lshr_b32 s68, s2, 9
	v_readlane_b32 s40, v253, 16
	s_lshl_b64 s[2:3], s[68:69], 22
	v_readlane_b32 s52, v253, 28
	v_readlane_b32 s53, v253, 29
	s_add_u32 s4, s52, s2
	s_addc_u32 s5, s53, s3
	s_lshl_b64 s[2:3], s[68:69], 21
	s_add_u32 s6, s22, s2
	v_readlane_b32 s7, v253, 52
	s_addc_u32 s3, s23, s3
	s_add_i32 s7, s7, s15
	s_and_b32 s2, s33, 0x3e0
	s_addk_i32 s7, 0x1900
	s_and_b32 s7, s7, 0x3c0
	s_lshl_b32 s8, s2, 2
	s_add_u32 s4, s4, s8
	v_or_b32_e32 v6, s7, v37
	s_addc_u32 s5, s5, 0
	v_lshlrev_b32_e32 v2, 2, v36
	v_lshl_add_u64 v[4:5], s[4:5], 0, v[2:3]
	v_lshlrev_b32_e32 v2, 12, v6
	v_lshl_add_u64 v[32:33], v[4:5], 0, v[2:3]
	v_add_co_u32_e32 v8, vcc, s81, v32
	global_load_dwordx4 v[4:7], v[32:33], off nt
	s_nop 0
	v_addc_co_u32_e32 v9, vcc, 0, v33, vcc
	global_load_dwordx4 v[8:11], v[8:9], off nt
	v_add_co_u32_e32 v12, vcc, s79, v32
	v_add_u32_e32 v2, v39, v44
	s_nop 0
	v_addc_co_u32_e32 v13, vcc, 0, v33, vcc
	global_load_dwordx4 v[12:15], v[12:13], off nt
	v_add_co_u32_e32 v16, vcc, s80, v32
	s_lshl_b32 s4, s7, 1
	s_nop 0
	v_addc_co_u32_e32 v17, vcc, 0, v33, vcc
	global_load_dwordx4 v[16:19], v[16:17], off nt
	v_add_co_u32_e32 v20, vcc, s85, v32
	s_add_u32 s4, s6, s4
	s_nop 0
	v_addc_co_u32_e32 v21, vcc, 0, v33, vcc
	global_load_dwordx4 v[20:23], v[20:21], off nt
	v_add_co_u32_e32 v24, vcc, s86, v32
	s_addc_u32 s5, s3, 0
	s_nop 0
	v_addc_co_u32_e32 v25, vcc, 0, v33, vcc
	global_load_dwordx4 v[24:27], v[24:25], off nt
	v_add_co_u32_e32 v28, vcc, s87, v32
	v_readlane_b32 s41, v253, 17
	s_nop 0
	v_addc_co_u32_e32 v29, vcc, 0, v33, vcc
	global_load_dwordx4 v[28:31], v[28:29], off nt
	v_add_co_u32_e32 v32, vcc, s89, v32
	v_readlane_b32 s42, v253, 18
	s_nop 0
	v_addc_co_u32_e32 v33, vcc, 0, v33, vcc
	global_load_dwordx4 v[32:35], v[32:33], off nt
	v_readlane_b32 s43, v253, 19
	v_readlane_b32 s44, v253, 20
	v_readlane_b32 s45, v253, 21
	v_readlane_b32 s46, v253, 22
	v_readlane_b32 s47, v253, 23
	v_readlane_b32 s48, v253, 24
	v_readlane_b32 s49, v253, 25
	v_readlane_b32 s50, v253, 26
	v_readlane_b32 s51, v253, 27
	v_readlane_b32 s54, v253, 30
	v_readlane_b32 s55, v253, 31
	s_waitcnt vmcnt(0)
	ds_write2_b32 v2, v4, v5 offset1:1
	ds_write2_b32 v2, v6, v7 offset0:2 offset1:3
	v_add_u32_e32 v4, 0x420, v2
	ds_write2_b32 v4, v8, v9 offset1:1
	v_add_u32_e32 v4, 0x428, v2
	ds_write2_b32 v4, v10, v11 offset1:1
	v_add_u32_e32 v4, 0x840, v2
	ds_write2_b32 v4, v12, v13 offset1:1
	v_add_u32_e32 v4, 0x848, v2
	ds_write2_b32 v4, v14, v15 offset1:1
	v_add_u32_e32 v4, 0xc60, v2
	ds_write2_b32 v4, v16, v17 offset1:1
	v_add_u32_e32 v4, 0xc68, v2
	ds_write2_b32 v4, v18, v19 offset1:1
	v_add_u32_e32 v4, 0x1080, v2
	ds_write2_b32 v4, v20, v21 offset1:1
	v_add_u32_e32 v4, 0x1088, v2
	ds_write2_b32 v4, v22, v23 offset1:1
	v_add_u32_e32 v4, 0x14a0, v2
	ds_write2_b32 v4, v24, v25 offset1:1
	v_add_u32_e32 v4, 0x14a8, v2
	ds_write2_b32 v4, v26, v27 offset1:1
	v_add_u32_e32 v4, 0x18c0, v2
	ds_write2_b32 v4, v28, v29 offset1:1
	v_add_u32_e32 v4, 0x18c8, v2
	ds_write2_b32 v4, v30, v31 offset1:1
	v_add_u32_e32 v4, 0x1ce0, v2
	v_add_u32_e32 v2, 0x1ce8, v2
	ds_write2_b32 v4, v32, v33 offset1:1
	ds_write2_b32 v2, v34, v35 offset1:1
	s_waitcnt lgkmcnt(0)
	ds_read2_b32 v[10:11], v48 offset0:33 offset1:41
	ds_read2_b32 v[12:13], v48 offset1:8
	v_lshlrev_b32_e32 v2, 1, v38
	ds_read2_b32 v[14:15], v48 offset0:66 offset1:74
	ds_read2_b32 v[16:17], v48 offset0:99 offset1:107
	ds_read2_b32 v[18:19], v48 offset0:132 offset1:140
	ds_read2_b32 v[20:21], v48 offset0:165 offset1:173
	ds_read2_b32 v[22:23], v48 offset0:198 offset1:206
	ds_read2_b32 v[24:25], v48 offset0:231 offset1:239
	v_lshl_add_u64 v[8:9], s[4:5], 0, v[2:3]
	v_or_b32_e32 v2, s2, v37
	v_lshlrev_b32_e32 v2, 11, v2
	v_lshl_add_u64 v[26:27], v[8:9], 0, v[2:3]
	v_or_b32_e32 v2, s2, v45
	s_waitcnt lgkmcnt(0)
	v_cvt_pk_bf16_f32 v4, v12, v10
	v_lshlrev_b32_e32 v2, 11, v2
	v_cvt_pk_bf16_f32 v5, v14, v16
	v_cvt_pk_bf16_f32 v6, v18, v20
	v_cvt_pk_bf16_f32 v7, v22, v24
	global_store_dwordx4 v[26:27], v[4:7], off sc1
	s_nop 1
	v_cvt_pk_bf16_f32 v4, v13, v11
	v_lshl_add_u64 v[10:11], v[8:9], 0, v[2:3]
	v_cvt_pk_bf16_f32 v5, v15, v17
	v_cvt_pk_bf16_f32 v6, v19, v21
	v_cvt_pk_bf16_f32 v7, v23, v25
	global_store_dwordx4 v[10:11], v[4:7], off sc1
	ds_read2_b32 v[10:11], v48 offset0:16 offset1:24
	ds_read2_b32 v[12:13], v48 offset0:49 offset1:57
	ds_read2_b32 v[14:15], v48 offset0:82 offset1:90
	ds_read2_b32 v[16:17], v48 offset0:115 offset1:123
	ds_read2_b32 v[18:19], v48 offset0:148 offset1:156
	ds_read2_b32 v[20:21], v48 offset0:181 offset1:189
	ds_read2_b32 v[22:23], v48 offset0:214 offset1:222
	ds_read2_b32 v[24:25], v48 offset0:247 offset1:255
	v_or_b32_e32 v2, s2, v46
	v_lshlrev_b32_e32 v2, 11, v2
	v_lshl_add_u64 v[26:27], v[8:9], 0, v[2:3]
	v_or_b32_e32 v2, s2, v47
	v_lshlrev_b32_e32 v2, 11, v2
	s_waitcnt lgkmcnt(6)
	v_cvt_pk_bf16_f32 v4, v10, v12
	s_waitcnt lgkmcnt(4)
	v_cvt_pk_bf16_f32 v5, v14, v16
	s_waitcnt lgkmcnt(2)
	v_cvt_pk_bf16_f32 v6, v18, v20
	s_waitcnt lgkmcnt(0)
	v_cvt_pk_bf16_f32 v7, v22, v24
	v_lshl_add_u64 v[8:9], v[8:9], 0, v[2:3]
	global_store_dwordx4 v[26:27], v[4:7], off sc1
	s_nop 1
	v_cvt_pk_bf16_f32 v4, v11, v13
	v_cvt_pk_bf16_f32 v5, v15, v17
	v_cvt_pk_bf16_f32 v6, v19, v21
	v_cvt_pk_bf16_f32 v7, v23, v25
	global_store_dwordx4 v[8:9], v[4:7], off sc1
	s_waitcnt lgkmcnt(0)

; #define GAS __attribute__((address_space(1)))
; #define LAS __attribute__((address_space(3)))
; #define LDS_WAIT() asm volatile("s_waitcnt lgkmcnt(0)" ::: "memory")
; __device__ __forceinline__ unsigned pk2(float lo, float hi) { unsigned r; asm("v_cvt_pk_bf16_f32 %0, %1, %2" : "=v"(r) : "v"(lo), "v"(hi)); return r; }
; __device__ __forceinline__ void transpose_item(const float* W, int K, int N, bf16* WT, int drow0, int kb, int n0, LAS float* scr, int lane) {
;     const int k0 = 64 * kb; const int c4 = 4 * (lane & 7); const bool ok = (n0 + c4) < N;
;     f32x4 v[8];
; #pragma unroll
;     for (int i = 0; i < 8; ++i) { const int kk = 8 * i + (lane >> 3); v[i] = ok ? *(const f32x4*)(W + (size_t)(k0 + kk) * N + n0 + c4) : (f32x4){0.f, 0.f, 0.f, 0.f}; }
; #pragma unroll
;     for (int i = 0; i < 8; ++i) { const int kk = 8 * i + (lane >> 3); LAS float* d = scr + kk * 33 + c4; d[0] = v[i][0]; d[1] = v[i][1]; d[2] = v[i][2]; d[3] = v[i][3]; }
;     LDS_WAIT(); asm volatile("" ::: "memory");
;     const int c = lane & 7;
; #pragma unroll
;     for (int j = 0; j < 4; ++j) { const int n = (lane >> 3) + 8 * j; const LAS float* s = scr + (8 * c) * 33 + n;
;         v4u o; o.x = pk2(s[0 * 33], s[1 * 33]); o.y = pk2(s[2 * 33], s[3 * 33]); o.z = pk2(s[4 * 33], s[5 * 33]); o.w = pk2(s[6 * 33], s[7 * 33]);
;         *(GAS v4u*)(WT + (size_t)(drow0 + n) * K + k0 + 8 * c) = o; }
;     LDS_WAIT(); asm volatile("" ::: "memory");
; }
; __device__ __forceinline__ void convert_item(const In& I, unsigned char* ws, int it, LAS float* scr, int lane) {
;     ...
;     if (r < 2 * I_SQ) { const int j = r / I_SQ; r -= j * I_SQ; const int kb = r / 32, nb = r % 32;
;         transpose_item(I.nsa_w_out + (size_t)j * D * D, D, D, Wnout + (size_t)j * D * D, 32 * nb, kb, 32 * nb, scr, lane); return; }
.LBB0_572:
	s_andn2_b64 vcc, exec, s[2:3]
	s_cbranch_vccnz .LBB0_574
	s_add_i32 s2, s30, 0x1900
	s_lshr_b32 s68, s2, 9
	v_readlane_b32 s40, v253, 16
	s_lshl_b64 s[2:3], s[68:69], 22
	v_readlane_b32 s46, v253, 22
	v_readlane_b32 s47, v253, 23
	s_add_u32 s4, s46, s2
	s_addc_u32 s5, s47, s3
	s_lshl_b64 s[2:3], s[68:69], 21
	s_add_u32 s6, s18, s2
	v_readlane_b32 s7, v253, 52
	s_addc_u32 s3, s19, s3
	s_add_i32 s7, s7, s15
	s_and_b32 s2, s33, 0x3e0
	s_add_i32 s7, s7, 0xfffefb00
	s_and_b32 s7, s7, 0x3c0
	s_lshl_b32 s8, s2, 2
	s_add_u32 s4, s4, s8
	v_or_b32_e32 v6, s7, v37
	s_addc_u32 s5, s5, 0
	v_lshlrev_b32_e32 v2, 2, v36
	v_lshl_add_u64 v[4:5], s[4:5], 0, v[2:3]
	v_lshlrev_b32_e32 v2, 12, v6
	v_lshl_add_u64 v[32:33], v[4:5], 0, v[2:3]
	v_add_co_u32_e32 v8, vcc, s81, v32
	global_load_dwordx4 v[4:7], v[32:33], off nt
	s_nop 0
	v_addc_co_u32_e32 v9, vcc, 0, v33, vcc
	global_load_dwordx4 v[8:11], v[8:9], off nt
	v_add_co_u32_e32 v12, vcc, s79, v32
	v_add_u32_e32 v2, v39, v44
	s_nop 0
	v_addc_co_u32_e32 v13, vcc, 0, v33, vcc
	global_load_dwordx4 v[12:15], v[12:13], off nt
	v_add_co_u32_e32 v16, vcc, s80, v32
	s_lshl_b32 s4, s7, 1
	s_nop 0
	v_addc_co_u32_e32 v17, vcc, 0, v33, vcc
	global_load_dwordx4 v[16:19], v[16:17], off nt
	v_add_co_u32_e32 v20, vcc, s85, v32
	s_add_u32 s4, s6, s4
	s_nop 0
	v_addc_co_u32_e32 v21, vcc, 0, v33, vcc
	global_load_dwordx4 v[20:23], v[20:21], off nt
	v_add_co_u32_e32 v24, vcc, s86, v32
	s_addc_u32 s5, s3, 0
	s_nop 0
	v_addc_co_u32_e32 v25, vcc, 0, v33, vcc
	global_load_dwordx4 v[24:27], v[24:25], off nt
	v_add_co_u32_e32 v28, vcc, s87, v32
	v_readlane_b32 s41, v253, 17
	s_nop 0
	v_addc_co_u32_e32 v29, vcc, 0, v33, vcc
	global_load_dwordx4 v[28:31], v[28:29], off nt
	v_add_co_u32_e32 v32, vcc, s89, v32
	v_readlane_b32 s42, v253, 18
	s_nop 0
	v_addc_co_u32_e32 v33, vcc, 0, v33, vcc
	global_load_dwordx4 v[32:35], v[32:33], off nt
	v_readlane_b32 s43, v253, 19
	v_readlane_b32 s44, v253, 20
	v_readlane_b32 s45, v253, 21
	v_readlane_b32 s48, v253, 24
	v_readlane_b32 s49, v253, 25
	v_readlane_b32 s50, v253, 26
	v_readlane_b32 s51, v253, 27
	v_readlane_b32 s52, v253, 28
	v_readlane_b32 s53, v253, 29
	v_readlane_b32 s54, v253, 30
	v_readlane_b32 s55, v253, 31
	s_waitcnt vmcnt(0)
	ds_write2_b32 v2, v4, v5 offset1:1
	ds_write2_b32 v2, v6, v7 offset0:2 offset1:3
	v_add_u32_e32 v4, 0x420, v2
	ds_write2_b32 v4, v8, v9 offset1:1
	v_add_u32_e32 v4, 0x428, v2
	ds_write2_b32 v4, v10, v11 offset1:1
	v_add_u32_e32 v4, 0x840, v2
	ds_write2_b32 v4, v12, v13 offset1:1
	v_add_u32_e32 v4, 0x848, v2
	ds_write2_b32 v4, v14, v15 offset1:1
	v_add_u32_e32 v4, 0xc60, v2
	ds_write2_b32 v4, v16, v17 offset1:1
	v_add_u32_e32 v4, 0xc68, v2
	ds_write2_b32 v4, v18, v19 offset1:1
	v_add_u32_e32 v4, 0x1080, v2
	ds_write2_b32 v4, v20, v21 offset1:1
	v_add_u32_e32 v4, 0x1088, v2
	ds_write2_b32 v4, v22, v23 offset1:1
	v_add_u32_e32 v4, 0x14a0, v2
	ds_write2_b32 v4, v24, v25 offset1:1
	v_add_u32_e32 v4, 0x14a8, v2
	ds_write2_b32 v4, v26, v27 offset1:1
	v_add_u32_e32 v4, 0x18c0, v2
	ds_write2_b32 v4, v28, v29 offset1:1
	v_add_u32_e32 v4, 0x18c8, v2
	ds_write2_b32 v4, v30, v31 offset1:1
	v_add_u32_e32 v4, 0x1ce0, v2
	v_add_u32_e32 v2, 0x1ce8, v2
	ds_write2_b32 v4, v32, v33 offset1:1
	ds_write2_b32 v2, v34, v35 offset1:1
	s_waitcnt lgkmcnt(0)
	ds_read2_b32 v[10:11], v48 offset0:33 offset1:41
	ds_read2_b32 v[12:13], v48 offset1:8
	v_lshlrev_b32_e32 v2, 1, v38
	ds_read2_b32 v[14:15], v48 offset0:66 offset1:74
	ds_read2_b32 v[16:17], v48 offset0:99 offset1:107
	ds_read2_b32 v[18:19], v48 offset0:132 offset1:140
	ds_read2_b32 v[20:21], v48 offset0:165 offset1:173
	ds_read2_b32 v[22:23], v48 offset0:198 offset1:206
	ds_read2_b32 v[24:25], v48 offset0:231 offset1:239
	v_lshl_add_u64 v[8:9], s[4:5], 0, v[2:3]
	v_or_b32_e32 v2, s2, v37
	v_lshlrev_b32_e32 v2, 11, v2
	v_lshl_add_u64 v[26:27], v[8:9], 0, v[2:3]
	v_or_b32_e32 v2, s2, v45
	s_waitcnt lgkmcnt(0)
	v_cvt_pk_bf16_f32 v4, v12, v10
	v_lshlrev_b32_e32 v2, 11, v2
	v_cvt_pk_bf16_f32 v5, v14, v16
	v_cvt_pk_bf16_f32 v6, v18, v20
	v_cvt_pk_bf16_f32 v7, v22, v24
	global_store_dwordx4 v[26:27], v[4:7], off sc1
	s_nop 1
	v_cvt_pk_bf16_f32 v4, v13, v11
	v_lshl_add_u64 v[10:11], v[8:9], 0, v[2:3]
	v_cvt_pk_bf16_f32 v5, v15, v17
	v_cvt_pk_bf16_f32 v6, v19, v21
	v_cvt_pk_bf16_f32 v7, v23, v25
	global_store_dwordx4 v[10:11], v[4:7], off sc1
	ds_read2_b32 v[10:11], v48 offset0:16 offset1:24
	ds_read2_b32 v[12:13], v48 offset0:49 offset1:57
	ds_read2_b32 v[14:15], v48 offset0:82 offset1:90
	ds_read2_b32 v[16:17], v48 offset0:115 offset1:123
	ds_read2_b32 v[18:19], v48 offset0:148 offset1:156
	ds_read2_b32 v[20:21], v48 offset0:181 offset1:189
	ds_read2_b32 v[22:23], v48 offset0:214 offset1:222
	ds_read2_b32 v[24:25], v48 offset0:247 offset1:255
	v_or_b32_e32 v2, s2, v46
	v_lshlrev_b32_e32 v2, 11, v2
	v_lshl_add_u64 v[26:27], v[8:9], 0, v[2:3]
	v_or_b32_e32 v2, s2, v47
	v_lshlrev_b32_e32 v2, 11, v2
	s_waitcnt lgkmcnt(6)
	v_cvt_pk_bf16_f32 v4, v10, v12
	s_waitcnt lgkmcnt(4)
	v_cvt_pk_bf16_f32 v5, v14, v16
	s_waitcnt lgkmcnt(2)
	v_cvt_pk_bf16_f32 v6, v18, v20
	s_waitcnt lgkmcnt(0)
	v_cvt_pk_bf16_f32 v7, v22, v24
	v_lshl_add_u64 v[8:9], v[8:9], 0, v[2:3]
	global_store_dwordx4 v[26:27], v[4:7], off sc1
	s_nop 1
	v_cvt_pk_bf16_f32 v4, v11, v13
	v_cvt_pk_bf16_f32 v5, v15, v17
	v_cvt_pk_bf16_f32 v6, v19, v21
	v_cvt_pk_bf16_f32 v7, v23, v25
	global_store_dwordx4 v[8:9], v[4:7], off sc1
	s_waitcnt lgkmcnt(0)

; #define GAS __attribute__((address_space(1)))
; #define LAS __attribute__((address_space(3)))
; #define LDS_WAIT() asm volatile("s_waitcnt lgkmcnt(0)" ::: "memory")
; __device__ __forceinline__ unsigned pk2(float lo, float hi) { unsigned r; asm("v_cvt_pk_bf16_f32 %0, %1, %2" : "=v"(r) : "v"(lo), "v"(hi)); return r; }
; __device__ __forceinline__ void transpose_item(const float* W, int K, int N, bf16* WT, int drow0, int kb, int n0, LAS float* scr, int lane) {
;     const int k0 = 64 * kb; const int c4 = 4 * (lane & 7); const bool ok = (n0 + c4) < N;
;     f32x4 v[8];
; #pragma unroll
;     for (int i = 0; i < 8; ++i) { const int kk = 8 * i + (lane >> 3); v[i] = ok ? *(const f32x4*)(W + (size_t)(k0 + kk) * N + n0 + c4) : (f32x4){0.f, 0.f, 0.f, 0.f}; }
; #pragma unroll
;     for (int i = 0; i < 8; ++i) { const int kk = 8 * i + (lane >> 3); LAS float* d = scr + kk * 33 + c4; d[0] = v[i][0]; d[1] = v[i][1]; d[2] = v[i][2]; d[3] = v[i][3]; }
;     LDS_WAIT(); asm volatile("" ::: "memory");
;     const int c = lane & 7;
; #pragma unroll
;     for (int j = 0; j < 4; ++j) { const int n = (lane >> 3) + 8 * j; const LAS float* s = scr + (8 * c) * 33 + n;
;         v4u o; o.x = pk2(s[0 * 33], s[1 * 33]); o.y = pk2(s[2 * 33], s[3 * 33]); o.z = pk2(s[4 * 33], s[5 * 33]); o.w = pk2(s[6 * 33], s[7 * 33]);
;         *(GAS v4u*)(WT + (size_t)(drow0 + n) * K + k0 + 8 * c) = o; }
;     LDS_WAIT(); asm volatile("" ::: "memory");
; }
; __device__ __forceinline__ void convert_item(const In& I, unsigned char* ws, int it, LAS float* scr, int lane) {
;     ...
;     if (r < T0) { const int f = r / I_FFN; r -= f * I_FFN;
;         if (r < 2 * I_G) { const int up = r >= I_G; r -= up * I_G; const int kb = r / 88, nb = r % 88;
;             transpose_item((up ? I.w_up : I.w_gate) + (size_t)f * D * FF, D, FF, Wgu + (size_t)f * NGU * D, 256 * (nb >> 2) + 32 * (nb & 3) + 128 * up, kb, 32 * nb, scr, lane); }
;         else { r -= 2 * I_G; const int kb = r / 32, nb = r % 32; transpose_item(I.w_down + (size_t)f * FF * D, FF, D, Wd + (size_t)f * D * FF, 32 * nb, kb, 32 * nb, scr, lane); }
.LBB0_594:
	s_andn2_b64 vcc, exec, s[2:3]
	s_cbranch_vccnz .LBB0_539
	s_mul_hi_i32 s2, s34, 0x3e0f83e1
	s_lshr_b32 s3, s2, 31
	s_ashr_i32 s6, s2, 10
	s_add_i32 s6, s6, s3
	s_mul_i32 s2, s6, 0xffffef80
	s_add_i32 s7, s30, s2
	s_add_i32 s7, s7, 0xa800
	v_add_u32_e32 v8, v39, v44
	s_mov_b64 s[2:3], -1
	s_cmpk_gt_i32 s7, 0xaff
	s_mul_hi_i32 s4, s6, 0xb00000
	s_mul_i32 s5, s6, 0xb00000
	v_lshlrev_b32_e32 v2, 2, v36
	v_add_u32_e32 v9, 0x420, v8
	v_add_u32_e32 v10, 0x428, v8
	v_add_u32_e32 v11, 0x840, v8
	v_add_u32_e32 v12, 0x848, v8
	v_add_u32_e32 v13, 0xc60, v8
	v_add_u32_e32 v14, 0xc68, v8
	v_add_u32_e32 v15, 0x1080, v8
	v_add_u32_e32 v16, 0x1088, v8
	v_add_u32_e32 v17, 0x14a0, v8
	v_add_u32_e32 v18, 0x14a8, v8
	v_add_u32_e32 v19, 0x18c0, v8
	v_add_u32_e32 v20, 0x18c8, v8
	v_add_u32_e32 v21, 0x1ce0, v8
	v_add_u32_e32 v22, 0x1ce8, v8
	v_lshlrev_b32_e32 v4, 1, v38
	s_cbranch_scc0 .LBB0_597
	v_readlane_b32 s40, v253, 0
	v_readlane_b32 s48, v253, 8
	v_readlane_b32 s49, v253, 9
	s_add_u32 s3, s48, s5
	s_addc_u32 s9, s49, s4
	s_mul_i32 s8, s6, 0x580000
	s_mul_hi_i32 s2, s6, 0x580000
	s_add_u32 s10, s1, s8
	v_readlane_b32 s34, v253, 52
	s_addc_u32 s11, s12, s2
	s_mul_i32 s8, s6, 0xffffdf00
	s_add_i32 s34, s34, s15
	s_add_i32 s8, s34, s8
	s_addk_i32 s8, 0x1900
	s_and_b32 s2, s33, 0x3e0
	s_andn2_b32 s8, s8, 63
	s_add_i32 s68, s8, 0xffffea00
	s_lshl_b32 s8, s2, 2
	v_or_b32_e32 v6, s68, v37
	s_add_u32 s8, s3, s8
	s_addc_u32 s9, s9, 0
	v_ashrrev_i32_e32 v7, 31, v6
	v_lshl_add_u64 v[62:63], s[8:9], 0, v[2:3]
	v_lshlrev_b64 v[24:25], 12, v[6:7]
	v_or_b32_e32 v28, 8, v6
	v_lshl_add_u64 v[24:25], v[62:63], 0, v[24:25]
	v_ashrrev_i32_e32 v29, 31, v28
	global_load_dwordx4 v[24:27], v[24:25], off nt
	v_lshlrev_b64 v[28:29], 12, v[28:29]
	v_or_b32_e32 v32, 16, v6
	v_lshl_add_u64 v[28:29], v[62:63], 0, v[28:29]
	v_ashrrev_i32_e32 v33, 31, v32
	global_load_dwordx4 v[28:31], v[28:29], off nt
	v_lshlrev_b64 v[32:33], 12, v[32:33]
	v_or_b32_e32 v40, 24, v6
	v_lshl_add_u64 v[32:33], v[62:63], 0, v[32:33]
	v_ashrrev_i32_e32 v41, 31, v40
	global_load_dwordx4 v[32:35], v[32:33], off nt
	v_lshlrev_b64 v[40:41], 12, v[40:41]
	v_or_b32_e32 v50, 32, v6
	v_lshl_add_u64 v[40:41], v[62:63], 0, v[40:41]
	v_ashrrev_i32_e32 v51, 31, v50
	global_load_dwordx4 v[40:43], v[40:41], off nt
	v_lshlrev_b64 v[50:51], 12, v[50:51]
	v_or_b32_e32 v54, 40, v6
	v_lshl_add_u64 v[50:51], v[62:63], 0, v[50:51]
	v_ashrrev_i32_e32 v55, 31, v54
	global_load_dwordx4 v[50:53], v[50:51], off nt
	v_lshlrev_b64 v[54:55], 12, v[54:55]
	v_or_b32_e32 v58, 48, v6
	v_lshl_add_u64 v[54:55], v[62:63], 0, v[54:55]
	v_ashrrev_i32_e32 v59, 31, v58
	global_load_dwordx4 v[54:57], v[54:55], off nt
	v_lshlrev_b64 v[58:59], 12, v[58:59]
	v_or_b32_e32 v6, 56, v6
	v_lshl_add_u64 v[58:59], v[62:63], 0, v[58:59]
	v_ashrrev_i32_e32 v7, 31, v6
	global_load_dwordx4 v[58:61], v[58:59], off nt
	v_lshlrev_b64 v[6:7], 12, v[6:7]
	v_lshl_add_u64 v[6:7], v[62:63], 0, v[6:7]
	global_load_dwordx4 v[62:65], v[6:7], off nt
	s_lshl_b64 s[8:9], s[68:69], 1
	s_add_u32 s8, s10, s8
	s_addc_u32 s9, s11, s9
	v_mov_b32_e32 v5, v3
	v_lshl_add_u64 v[6:7], s[8:9], 0, v[4:5]
	v_or_b32_e32 v5, s2, v37
	v_readlane_b32 s41, v253, 1
	v_readlane_b32 s42, v253, 2
	v_readlane_b32 s43, v253, 3
	v_readlane_b32 s44, v253, 4
	v_readlane_b32 s45, v253, 5
	v_readlane_b32 s46, v253, 6
	v_readlane_b32 s47, v253, 7
	v_readlane_b32 s50, v253, 10
	v_readlane_b32 s51, v253, 11
	v_readlane_b32 s52, v253, 12
	v_readlane_b32 s53, v253, 13
	v_readlane_b32 s54, v253, 14
	v_readlane_b32 s55, v253, 15
	s_waitcnt vmcnt(0)
	ds_write2_b32 v8, v24, v25 offset1:1
	ds_write2_b32 v8, v26, v27 offset0:2 offset1:3
	ds_write2_b32 v9, v28, v29 offset1:1
	ds_write2_b32 v10, v30, v31 offset1:1
	ds_write2_b32 v11, v32, v33 offset1:1
	ds_write2_b32 v12, v34, v35 offset1:1
	ds_write2_b32 v13, v40, v41 offset1:1
	ds_write2_b32 v14, v42, v43 offset1:1
	ds_write2_b32 v15, v50, v51 offset1:1
	ds_write2_b32 v16, v52, v53 offset1:1
	ds_write2_b32 v17, v54, v55 offset1:1
	ds_write2_b32 v18, v56, v57 offset1:1
	ds_write2_b32 v19, v58, v59 offset1:1
	ds_write2_b32 v20, v60, v61 offset1:1
	ds_write2_b32 v21, v62, v63 offset1:1
	ds_write2_b32 v22, v64, v65 offset1:1
	s_waitcnt lgkmcnt(0)
	ds_read2_b32 v[28:29], v48 offset0:33 offset1:41
	ds_read2_b32 v[30:31], v48 offset1:8
	ds_read2_b32 v[32:33], v48 offset0:66 offset1:74
	ds_read2_b32 v[34:35], v48 offset0:99 offset1:107
	ds_read2_b32 v[40:41], v48 offset0:132 offset1:140
	ds_read2_b32 v[42:43], v48 offset0:165 offset1:173
	ds_read2_b32 v[50:51], v48 offset0:198 offset1:206
	ds_read2_b32 v[52:53], v48 offset0:231 offset1:239
	v_mul_u32_u24_e32 v54, 0x1600, v5
	v_mov_b32_e32 v55, v3
	s_waitcnt lgkmcnt(0)
	v_cvt_pk_bf16_f32 v24, v30, v28
	v_lshl_add_u64 v[54:55], v[6:7], 0, v[54:55]
	v_or_b32_e32 v5, s2, v45
	v_cvt_pk_bf16_f32 v25, v32, v34
	v_cvt_pk_bf16_f32 v26, v40, v42
	v_cvt_pk_bf16_f32 v27, v50, v52
	global_store_dwordx4 v[54:55], v[24:27], off sc1
	v_mul_u32_u24_e32 v28, 0x1600, v5
	v_or_b32_e32 v5, s2, v46
	v_cvt_pk_bf16_f32 v24, v31, v29
	v_mov_b32_e32 v29, v3
	v_lshl_add_u64 v[28:29], v[6:7], 0, v[28:29]
	v_cvt_pk_bf16_f32 v25, v33, v35
	v_cvt_pk_bf16_f32 v26, v41, v43
	v_cvt_pk_bf16_f32 v27, v51, v53
	global_store_dwordx4 v[28:29], v[24:27], off sc1
	ds_read2_b32 v[28:29], v48 offset0:16 offset1:24
	ds_read2_b32 v[30:31], v48 offset0:49 offset1:57
	ds_read2_b32 v[32:33], v48 offset0:82 offset1:90
	ds_read2_b32 v[34:35], v48 offset0:115 offset1:123
	ds_read2_b32 v[40:41], v48 offset0:148 offset1:156
	ds_read2_b32 v[42:43], v48 offset0:181 offset1:189
	ds_read2_b32 v[50:51], v48 offset0:214 offset1:222
	ds_read2_b32 v[52:53], v48 offset0:247 offset1:255
	v_mul_u32_u24_e32 v54, 0x1600, v5
	v_mov_b32_e32 v55, v3
	s_waitcnt lgkmcnt(6)
	v_cvt_pk_bf16_f32 v24, v28, v30
	v_lshl_add_u64 v[54:55], v[6:7], 0, v[54:55]
	v_or_b32_e32 v5, s2, v47
	s_waitcnt lgkmcnt(4)
	v_cvt_pk_bf16_f32 v25, v32, v34
	s_waitcnt lgkmcnt(2)
	v_cvt_pk_bf16_f32 v26, v40, v42
	s_waitcnt lgkmcnt(0)
	v_cvt_pk_bf16_f32 v27, v50, v52
	global_store_dwordx4 v[54:55], v[24:27], off sc1
	v_mul_u32_u24_e32 v28, 0x1600, v5
	s_mov_b64 s[2:3], 0
	v_cvt_pk_bf16_f32 v24, v29, v31
	v_mov_b32_e32 v29, v3
	v_lshl_add_u64 v[6:7], v[6:7], 0, v[28:29]
	v_cvt_pk_bf16_f32 v25, v33, v35
	v_cvt_pk_bf16_f32 v26, v41, v43
	v_cvt_pk_bf16_f32 v27, v51, v53
	global_store_dwordx4 v[6:7], v[24:27], off sc1
	s_waitcnt lgkmcnt(0)
; #define GAS __attribute__((address_space(1)))
; #define LAS __attribute__((address_space(3)))
; #define LDS_WAIT() asm volatile("s_waitcnt lgkmcnt(0)" ::: "memory")
; __device__ __forceinline__ unsigned pk2(float lo, float hi) { unsigned r; asm("v_cvt_pk_bf16_f32 %0, %1, %2" : "=v"(r) : "v"(lo), "v"(hi)); return r; }
; __device__ __forceinline__ void transpose_item(const float* W, int K, int N, bf16* WT, int drow0, int kb, int n0, LAS float* scr, int lane) {
;     const int k0 = 64 * kb; const int c4 = 4 * (lane & 7); const bool ok = (n0 + c4) < N;
;     f32x4 v[8];
; #pragma unroll
;     for (int i = 0; i < 8; ++i) { const int kk = 8 * i + (lane >> 3); v[i] = ok ? *(const f32x4*)(W + (size_t)(k0 + kk) * N + n0 + c4) : (f32x4){0.f, 0.f, 0.f, 0.f}; }
; #pragma unroll
;     for (int i = 0; i < 8; ++i) { const int kk = 8 * i + (lane >> 3); LAS float* d = scr + kk * 33 + c4; d[0] = v[i][0]; d[1] = v[i][1]; d[2] = v[i][2]; d[3] = v[i][3]; }
;     LDS_WAIT(); asm volatile("" ::: "memory");
;     const int c = lane & 7;
; #pragma unroll
;     for (int j = 0; j < 4; ++j) { const int n = (lane >> 3) + 8 * j; const LAS float* s = scr + (8 * c) * 33 + n;
;         v4u o; o.x = pk2(s[0 * 33], s[1 * 33]); o.y = pk2(s[2 * 33], s[3 * 33]); o.z = pk2(s[4 * 33], s[5 * 33]); o.w = pk2(s[6 * 33], s[7 * 33]);
;         *(GAS v4u*)(WT + (size_t)(drow0 + n) * K + k0 + 8 * c) = o; }
;     LDS_WAIT(); asm volatile("" ::: "memory");
; }
; __device__ __forceinline__ void convert_item(const In& I, unsigned char* ws, int it, LAS float* scr, int lane) {
;     ...
;     if (r < T0) { const int f = r / I_FFN; r -= f * I_FFN;
;         if (r < 2 * I_G) { const int up = r >= I_G; r -= up * I_G; const int kb = r / 88, nb = r % 88;
;             transpose_item((up ? I.w_up : I.w_gate) + (size_t)f * D * FF, D, FF, Wgu + (size_t)f * NGU * D, 256 * (nb >> 2) + 32 * (nb & 3) + 128 * up, kb, 32 * nb, scr, lane); }
.LBB0_597:
	s_andn2_b64 vcc, exec, s[2:3]
	s_cbranch_vccnz .LBB0_539
	s_cmpk_gt_i32 s7, 0x57f
	v_readlane_b32 s40, v253, 0
	s_cselect_b32 s2, 0xfffffa80, 0
	s_mulk_i32 s6, 0x1080
	v_readlane_b32 s44, v253, 4
	v_readlane_b32 s45, v253, 5
	v_readlane_b32 s46, v253, 6
	v_readlane_b32 s47, v253, 7
	s_cselect_b32 s3, 0x80, 0
	s_cselect_b32 s7, s46, s44
	s_cselect_b32 s8, s47, s45
	s_sub_i32 s2, s2, s6
	s_add_i32 s2, s30, s2
	s_add_i32 s2, s2, 0xa800
	s_mul_hi_i32 s6, s2, 0x2e8ba2e9
	s_lshr_b32 s9, s6, 31
	s_ashr_i32 s6, s6, 4
	s_add_i32 s6, s6, s9
	s_mul_i32 s9, s6, 0x58
	s_sub_i32 s2, s2, s9
	s_add_u32 s7, s7, s5
	s_addc_u32 s8, s8, s4
	s_add_u32 s9, s28, s5
	s_addc_u32 s10, s29, s4
	s_lshl_b32 s4, s2, 6
	s_and_b32 s5, s4, 0xffffff00
	s_lshl_b32 s4, s2, 5
	s_and_b32 s2, s4, 0x60
	s_or_b32 s2, s2, s3
	s_or_b32 s2, s2, s5
	s_ashr_i32 s5, s4, 31
	s_lshl_b32 s6, s6, 6
	s_lshl_b64 s[4:5], s[4:5], 2
	s_add_u32 s4, s7, s4
	s_addc_u32 s5, s8, s5
	v_or_b32_e32 v5, s6, v37
	v_lshl_add_u64 v[6:7], s[4:5], 0, v[2:3]
	s_movk_i32 s3, 0x2c00
	v_mad_i64_i32 v[24:25], s[4:5], v5, s3, v[6:7]
	global_load_dwordx4 v[24:27], v[24:25], off nt
	v_or_b32_e32 v2, 8, v5
	v_mad_i64_i32 v[28:29], s[4:5], v2, s3, v[6:7]
	global_load_dwordx4 v[28:31], v[28:29], off nt
	v_or_b32_e32 v2, 16, v5
	v_mad_i64_i32 v[32:33], s[4:5], v2, s3, v[6:7]
	global_load_dwordx4 v[32:35], v[32:33], off nt
	v_or_b32_e32 v2, 24, v5
	v_mad_i64_i32 v[40:41], s[4:5], v2, s3, v[6:7]
	global_load_dwordx4 v[40:43], v[40:41], off nt
	v_or_b32_e32 v2, 32, v5
	v_mad_i64_i32 v[50:51], s[4:5], v2, s3, v[6:7]
	global_load_dwordx4 v[50:53], v[50:51], off nt
	v_or_b32_e32 v2, 40, v5
	v_mad_i64_i32 v[54:55], s[4:5], v2, s3, v[6:7]
	global_load_dwordx4 v[54:57], v[54:55], off nt
	v_or_b32_e32 v2, 48, v5
	v_mad_i64_i32 v[58:59], s[4:5], v2, s3, v[6:7]
	global_load_dwordx4 v[58:61], v[58:59], off nt
	v_or_b32_e32 v2, 56, v5
	v_mad_i64_i32 v[6:7], s[4:5], v2, s3, v[6:7]
	global_load_dwordx4 v[62:65], v[6:7], off nt
	s_ashr_i32 s7, s6, 31
	s_lshl_b64 s[4:5], s[6:7], 1
	s_add_u32 s4, s9, s4
	s_addc_u32 s5, s10, s5
	v_mov_b32_e32 v5, v3
	v_lshl_add_u64 v[4:5], s[4:5], 0, v[4:5]
	v_readlane_b32 s41, v253, 1
	v_readlane_b32 s42, v253, 2
	v_readlane_b32 s43, v253, 3
	v_readlane_b32 s48, v253, 8
	v_readlane_b32 s49, v253, 9
	v_readlane_b32 s50, v253, 10
	v_readlane_b32 s51, v253, 11
	v_readlane_b32 s52, v253, 12
	v_readlane_b32 s53, v253, 13
	v_readlane_b32 s54, v253, 14
	v_readlane_b32 s55, v253, 15
	s_waitcnt vmcnt(0)
	ds_write2_b32 v8, v24, v25 offset1:1
	ds_write2_b32 v8, v26, v27 offset0:2 offset1:3
	ds_write2_b32 v9, v28, v29 offset1:1
	ds_write2_b32 v10, v30, v31 offset1:1
	ds_write2_b32 v11, v32, v33 offset1:1
	ds_write2_b32 v12, v34, v35 offset1:1
	ds_write2_b32 v13, v40, v41 offset1:1
	ds_write2_b32 v14, v42, v43 offset1:1
	ds_write2_b32 v15, v50, v51 offset1:1
	ds_write2_b32 v16, v52, v53 offset1:1
	ds_write2_b32 v17, v54, v55 offset1:1
	ds_write2_b32 v18, v56, v57 offset1:1
	ds_write2_b32 v19, v58, v59 offset1:1
	ds_write2_b32 v20, v60, v61 offset1:1
	ds_write2_b32 v21, v62, v63 offset1:1
	ds_write2_b32 v22, v64, v65 offset1:1
	s_waitcnt lgkmcnt(0)
	ds_read2_b32 v[10:11], v48 offset0:33 offset1:41
	ds_read2_b32 v[12:13], v48 offset1:8
	ds_read2_b32 v[14:15], v48 offset0:66 offset1:74
	ds_read2_b32 v[16:17], v48 offset0:99 offset1:107
	ds_read2_b32 v[18:19], v48 offset0:132 offset1:140
	ds_read2_b32 v[20:21], v48 offset0:165 offset1:173
	ds_read2_b32 v[22:23], v48 offset0:198 offset1:206
	ds_read2_b32 v[24:25], v48 offset0:231 offset1:239
	v_or_b32_e32 v26, s2, v37
	v_ashrrev_i32_e32 v27, 31, v26
	v_lshlrev_b64 v[26:27], 11, v[26:27]
	s_waitcnt lgkmcnt(0)
	v_cvt_pk_bf16_f32 v6, v12, v10
	v_lshl_add_u64 v[26:27], v[4:5], 0, v[26:27]
	v_or_b32_e32 v10, s2, v45
	v_cvt_pk_bf16_f32 v7, v14, v16
	v_cvt_pk_bf16_f32 v8, v18, v20
	v_cvt_pk_bf16_f32 v9, v22, v24
	global_store_dwordx4 v[26:27], v[6:9], off sc1
	v_or_b32_e32 v26, s2, v46
	v_ashrrev_i32_e32 v27, 31, v26
	v_cvt_pk_bf16_f32 v6, v13, v11
	v_ashrrev_i32_e32 v11, 31, v10
	v_lshlrev_b64 v[10:11], 11, v[10:11]
	v_lshl_add_u64 v[10:11], v[4:5], 0, v[10:11]
	v_cvt_pk_bf16_f32 v7, v15, v17
	v_cvt_pk_bf16_f32 v8, v19, v21
	v_cvt_pk_bf16_f32 v9, v23, v25
	global_store_dwordx4 v[10:11], v[6:9], off sc1
	ds_read2_b32 v[10:11], v48 offset0:16 offset1:24
	ds_read2_b32 v[12:13], v48 offset0:49 offset1:57
	ds_read2_b32 v[14:15], v48 offset0:82 offset1:90
	ds_read2_b32 v[16:17], v48 offset0:115 offset1:123
	ds_read2_b32 v[18:19], v48 offset0:148 offset1:156
	ds_read2_b32 v[20:21], v48 offset0:181 offset1:189
	ds_read2_b32 v[22:23], v48 offset0:214 offset1:222
	ds_read2_b32 v[24:25], v48 offset0:247 offset1:255
	v_lshlrev_b64 v[26:27], 11, v[26:27]
	s_waitcnt lgkmcnt(6)
	v_cvt_pk_bf16_f32 v6, v10, v12
	v_lshl_add_u64 v[26:27], v[4:5], 0, v[26:27]
	v_or_b32_e32 v10, s2, v47
	s_waitcnt lgkmcnt(4)
	v_cvt_pk_bf16_f32 v7, v14, v16
	s_waitcnt lgkmcnt(2)
	v_cvt_pk_bf16_f32 v8, v18, v20
	s_waitcnt lgkmcnt(0)
	v_cvt_pk_bf16_f32 v9, v22, v24
	global_store_dwordx4 v[26:27], v[6:9], off sc1
	s_nop 1
	v_cvt_pk_bf16_f32 v6, v11, v13
	v_ashrrev_i32_e32 v11, 31, v10
	v_lshlrev_b64 v[10:11], 11, v[10:11]
	v_lshl_add_u64 v[4:5], v[4:5], 0, v[10:11]
	v_cvt_pk_bf16_f32 v7, v15, v17
	v_cvt_pk_bf16_f32 v8, v19, v21
	v_cvt_pk_bf16_f32 v9, v23, v25
	global_store_dwordx4 v[4:5], v[6:9], off sc1
	s_waitcnt lgkmcnt(0)
	s_branch .LBB0_539
